# v27 + kernel-wide removal of dead zero-inits ahead of cvt_pk_fp8 lo/hi pairs (314 VALU in GEMM epilogues and prologue)
# speedup vs baseline: 1.0092x; 1.0055x over previous
; #define GAS __attribute__((address_space(1)))
; __device__ __forceinline__ unsigned f2bf(float f) { unsigned u = __builtin_bit_cast(unsigned, f); return (u + 0x7fffu + ((u >> 16) & 1u)) >> 16; }
; __device__ __forceinline__ unsigned pk2(float lo, float hi) { return f2bf(lo) | (f2bf(hi) << 16); }
; __global__ void __launch_bounds__(NWAVES * 64, 2) mk_fwd(Args args) {
;     ...
;         for (int m = gw; m < MTOK; m += NGW) {
;             const GAS f32x4* xr = (const GAS f32x4*)(x + (size_t)m * DMODEL) + lane;
;             f32x4 v[16]; float s = 0.f;
; #pragma unroll
;             for (int j = 0; j < 16; ++j) { v[j] = __builtin_nontemporal_load(xr + 64 * j); s += (v[j].x * v[j].x + v[j].y * v[j].y) + (v[j].z * v[j].z + v[j].w * v[j].w); }
;             s = wave_sum(s);
;             if (lane == 0) SS0[m] = s;
;             GAS v2u* o8 = (GAS v2u*)(XB + (size_t)m * DMODEL) + lane; GAS unsigned* o4 = (GAS unsigned*)(X8 + (size_t)m * DMODEL) + lane;
; #pragma unroll
;             for (int j = 0; j < 16; ++j) { v2u w; w.x = pk2(v[j].x, v[j].y); w.y = pk2(v[j].z, v[j].w); o8[64 * j] = w; o4[64 * j] = pg8::pk4_fp8(v[j].x, v[j].y, v[j].z, v[j].w); }
.LBB0_43:
	s_or_b64 exec, exec, s[12:13]
	v_and_b32_sdwa v88, v65, v84 dst_sel:DWORD dst_unused:UNUSED_PAD src0_sel:WORD_1 src1_sel:DWORD
	v_and_b32_sdwa v76, v64, v84 dst_sel:DWORD dst_unused:UNUSED_PAD src0_sel:WORD_1 src1_sel:DWORD
	v_and_b32_sdwa v89, v63, v84 dst_sel:DWORD dst_unused:UNUSED_PAD src0_sel:WORD_1 src1_sel:DWORD
	v_add3_u32 v88, v65, v88, s20
	s_waitcnt lgkmcnt(0)
	v_lshl_add_u64 v[74:75], s[78:79], 0, v[70:71]
	v_and_b32_sdwa v77, v62, v84 dst_sel:DWORD dst_unused:UNUSED_PAD src0_sel:WORD_1 src1_sel:DWORD
	v_add3_u32 v76, v64, v76, s20
	v_add3_u32 v89, v63, v89, s20
	v_and_b32_e32 v88, 0xffff0000, v88
	v_add3_u32 v77, v62, v77, s20
	v_and_b32_e32 v90, 0xffff0000, v89
	v_or_b32_sdwa v89, v88, v76 dst_sel:DWORD dst_unused:UNUSED_PAD src0_sel:DWORD src1_sel:WORD_1
	v_add_co_u32_e32 v76, vcc, s21, v74
	v_or_b32_sdwa v88, v90, v77 dst_sel:DWORD dst_unused:UNUSED_PAD src0_sel:DWORD src1_sel:WORD_1
	s_nop 0
	v_addc_co_u32_e32 v77, vcc, 0, v75, vcc
	v_add_co_u32_e32 v74, vcc, s24, v74
	v_max_f32_e32 v62, v62, v62
	s_nop 0
	v_addc_co_u32_e32 v75, vcc, 0, v75, vcc
	v_max_f32_e32 v63, v63, v63
	global_store_dwordx2 v[74:75], v[88:89], off offset:-4096
	v_med3_f32 v62, v62, s22, v85
	v_med3_f32 v63, v63, s22, v85
	v_cvt_pk_fp8_f32 v88, v62, v63
	v_max_f32_e32 v64, v64, v64
	v_max_f32_e32 v63, v65, v65
	v_med3_f32 v62, v64, s22, v85
	v_med3_f32 v63, v63, s22, v85
	v_lshl_add_u64 v[86:87], s[78:79], 0, v[68:69]
	v_cvt_pk_fp8_f32 v88, v62, v63 op_sel:[0,0,1]
	v_add_co_u32_e32 v62, vcc, s23, v86
	v_and_b32_sdwa v65, v54, v84 dst_sel:DWORD dst_unused:UNUSED_PAD src0_sel:WORD_1 src1_sel:DWORD
	s_nop 0
	v_addc_co_u32_e32 v63, vcc, 0, v87, vcc
	v_and_b32_sdwa v87, v55, v84 dst_sel:DWORD dst_unused:UNUSED_PAD src0_sel:WORD_1 src1_sel:DWORD
	v_add3_u32 v65, v54, v65, s20
	v_add3_u32 v87, v55, v87, s20
	v_max_f32_e32 v54, v54, v54
	v_max_f32_e32 v55, v55, v55
	global_store_dword v[62:63], v88, off
	v_med3_f32 v54, v54, s22, v85
	v_med3_f32 v55, v55, s22, v85
	v_cvt_pk_fp8_f32 v88, v54, v55
	v_and_b32_sdwa v64, v56, v84 dst_sel:DWORD dst_unused:UNUSED_PAD src0_sel:WORD_1 src1_sel:DWORD
	v_add3_u32 v64, v56, v64, s20
	v_max_f32_e32 v56, v56, v56
	v_max_f32_e32 v55, v57, v57
	v_and_b32_sdwa v86, v57, v84 dst_sel:DWORD dst_unused:UNUSED_PAD src0_sel:WORD_1 src1_sel:DWORD
	v_med3_f32 v54, v56, s22, v85
	v_med3_f32 v55, v55, s22, v85
	v_add3_u32 v86, v57, v86, s20
	v_cvt_pk_fp8_f32 v88, v54, v55 op_sel:[0,0,1]
	v_and_b32_e32 v86, 0xffff0000, v86
	v_and_b32_e32 v87, 0xffff0000, v87
	v_or_b32_sdwa v55, v86, v64 dst_sel:DWORD dst_unused:UNUSED_PAD src0_sel:DWORD src1_sel:WORD_1
	v_or_b32_sdwa v54, v87, v65 dst_sel:DWORD dst_unused:UNUSED_PAD src0_sel:DWORD src1_sel:WORD_1
	global_store_dwordx2 v[76:77], v[54:55], off offset:512
	global_store_dword v[62:63], v88, off offset:256
	v_and_b32_sdwa v55, v58, v84 dst_sel:DWORD dst_unused:UNUSED_PAD src0_sel:WORD_1 src1_sel:DWORD
	v_and_b32_sdwa v57, v59, v84 dst_sel:DWORD dst_unused:UNUSED_PAD src0_sel:WORD_1 src1_sel:DWORD
	v_add3_u32 v56, v58, v55, s20
	v_add3_u32 v57, v59, v57, s20
	v_max_f32_e32 v58, v58, v58
	v_max_f32_e32 v59, v59, v59
	v_med3_f32 v58, v58, s22, v85
	v_med3_f32 v59, v59, s22, v85
	v_cvt_pk_fp8_f32 v64, v58, v59
	v_and_b32_sdwa v54, v60, v84 dst_sel:DWORD dst_unused:UNUSED_PAD src0_sel:WORD_1 src1_sel:DWORD
	v_add3_u32 v54, v60, v54, s20
	v_max_f32_e32 v60, v60, v60
	v_max_f32_e32 v59, v61, v61
	v_and_b32_sdwa v55, v61, v84 dst_sel:DWORD dst_unused:UNUSED_PAD src0_sel:WORD_1 src1_sel:DWORD
	v_med3_f32 v58, v60, s22, v85
	v_med3_f32 v59, v59, s22, v85
	v_add3_u32 v55, v61, v55, s20
	v_cvt_pk_fp8_f32 v64, v58, v59 op_sel:[0,0,1]
	v_and_b32_e32 v55, 0xffff0000, v55
	v_and_b32_e32 v57, 0xffff0000, v57
	v_or_b32_sdwa v55, v55, v54 dst_sel:DWORD dst_unused:UNUSED_PAD src0_sel:DWORD src1_sel:WORD_1
	v_or_b32_sdwa v54, v57, v56 dst_sel:DWORD dst_unused:UNUSED_PAD src0_sel:DWORD src1_sel:WORD_1
	global_store_dwordx2 v[76:77], v[54:55], off offset:1024
	global_store_dword v[62:63], v64, off offset:512
	v_and_b32_sdwa v55, v50, v84 dst_sel:DWORD dst_unused:UNUSED_PAD src0_sel:WORD_1 src1_sel:DWORD
	v_and_b32_sdwa v57, v51, v84 dst_sel:DWORD dst_unused:UNUSED_PAD src0_sel:WORD_1 src1_sel:DWORD
	v_add3_u32 v55, v50, v55, s20
	v_add3_u32 v57, v51, v57, s20
	v_max_f32_e32 v50, v50, v50
	v_max_f32_e32 v51, v51, v51
	v_med3_f32 v50, v50, s22, v85
	v_med3_f32 v51, v51, s22, v85
	v_cvt_pk_fp8_f32 v58, v50, v51
	v_and_b32_sdwa v54, v52, v84 dst_sel:DWORD dst_unused:UNUSED_PAD src0_sel:WORD_1 src1_sel:DWORD
	v_add3_u32 v54, v52, v54, s20
	v_max_f32_e32 v52, v52, v52
	v_max_f32_e32 v51, v53, v53
	v_and_b32_sdwa v56, v53, v84 dst_sel:DWORD dst_unused:UNUSED_PAD src0_sel:WORD_1 src1_sel:DWORD
	v_med3_f32 v50, v52, s22, v85
	v_med3_f32 v51, v51, s22, v85
	v_add3_u32 v56, v53, v56, s20
	v_cvt_pk_fp8_f32 v58, v50, v51 op_sel:[0,0,1]
	v_and_b32_e32 v56, 0xffff0000, v56
	v_and_b32_e32 v57, 0xffff0000, v57
	v_or_b32_sdwa v51, v56, v54 dst_sel:DWORD dst_unused:UNUSED_PAD src0_sel:DWORD src1_sel:WORD_1
	v_or_b32_sdwa v50, v57, v55 dst_sel:DWORD dst_unused:UNUSED_PAD src0_sel:DWORD src1_sel:WORD_1
	global_store_dwordx2 v[76:77], v[50:51], off offset:1536
	global_store_dword v[62:63], v58, off offset:768
	v_and_b32_sdwa v51, v46, v84 dst_sel:DWORD dst_unused:UNUSED_PAD src0_sel:WORD_1 src1_sel:DWORD
	v_and_b32_sdwa v53, v47, v84 dst_sel:DWORD dst_unused:UNUSED_PAD src0_sel:WORD_1 src1_sel:DWORD
	v_add3_u32 v51, v46, v51, s20
	v_add3_u32 v53, v47, v53, s20
	v_max_f32_e32 v46, v46, v46
	v_max_f32_e32 v47, v47, v47
	v_med3_f32 v46, v46, s22, v85
	v_med3_f32 v47, v47, s22, v85
	v_cvt_pk_fp8_f32 v54, v46, v47
; #define GAS __attribute__((address_space(1)))
; __device__ __forceinline__ unsigned f2bf(float f) { unsigned u = __builtin_bit_cast(unsigned, f); return (u + 0x7fffu + ((u >> 16) & 1u)) >> 16; }
; __device__ __forceinline__ unsigned pk2(float lo, float hi) { return f2bf(lo) | (f2bf(hi) << 16); }
; __global__ void __launch_bounds__(NWAVES * 64, 2) mk_fwd(Args args) {
;     ...
;             GAS v2u* o8 = (GAS v2u*)(XB + (size_t)m * DMODEL) + lane; GAS unsigned* o4 = (GAS unsigned*)(X8 + (size_t)m * DMODEL) + lane;
; #pragma unroll
;             for (int j = 0; j < 16; ++j) { v2u w; w.x = pk2(v[j].x, v[j].y); w.y = pk2(v[j].z, v[j].w); o8[64 * j] = w; o4[64 * j] = pg8::pk4_fp8(v[j].x, v[j].y, v[j].z, v[j].w); }
	v_and_b32_sdwa v50, v48, v84 dst_sel:DWORD dst_unused:UNUSED_PAD src0_sel:WORD_1 src1_sel:DWORD
	v_add3_u32 v50, v48, v50, s20
	v_max_f32_e32 v48, v48, v48
	v_max_f32_e32 v47, v49, v49
	v_and_b32_sdwa v52, v49, v84 dst_sel:DWORD dst_unused:UNUSED_PAD src0_sel:WORD_1 src1_sel:DWORD
	v_med3_f32 v46, v48, s22, v85
	v_med3_f32 v47, v47, s22, v85
	v_add3_u32 v52, v49, v52, s20
	v_cvt_pk_fp8_f32 v54, v46, v47 op_sel:[0,0,1]
	v_and_b32_e32 v52, 0xffff0000, v52
	v_and_b32_e32 v53, 0xffff0000, v53
	v_or_b32_sdwa v47, v52, v50 dst_sel:DWORD dst_unused:UNUSED_PAD src0_sel:DWORD src1_sel:WORD_1
	v_or_b32_sdwa v46, v53, v51 dst_sel:DWORD dst_unused:UNUSED_PAD src0_sel:DWORD src1_sel:WORD_1
	global_store_dwordx2 v[76:77], v[46:47], off offset:2048
	global_store_dword v[62:63], v54, off offset:1024
	v_and_b32_sdwa v47, v42, v84 dst_sel:DWORD dst_unused:UNUSED_PAD src0_sel:WORD_1 src1_sel:DWORD
	v_and_b32_sdwa v49, v43, v84 dst_sel:DWORD dst_unused:UNUSED_PAD src0_sel:WORD_1 src1_sel:DWORD
	v_add3_u32 v47, v42, v47, s20
	v_add3_u32 v49, v43, v49, s20
	v_max_f32_e32 v42, v42, v42
	v_max_f32_e32 v43, v43, v43
	v_med3_f32 v42, v42, s22, v85
	v_med3_f32 v43, v43, s22, v85
	v_cvt_pk_fp8_f32 v50, v42, v43
	v_and_b32_sdwa v46, v44, v84 dst_sel:DWORD dst_unused:UNUSED_PAD src0_sel:WORD_1 src1_sel:DWORD
	v_add3_u32 v46, v44, v46, s20
	v_max_f32_e32 v44, v44, v44
	v_max_f32_e32 v43, v45, v45
	v_and_b32_sdwa v48, v45, v84 dst_sel:DWORD dst_unused:UNUSED_PAD src0_sel:WORD_1 src1_sel:DWORD
	v_med3_f32 v42, v44, s22, v85
	v_med3_f32 v43, v43, s22, v85
	v_add3_u32 v48, v45, v48, s20
	v_cvt_pk_fp8_f32 v50, v42, v43 op_sel:[0,0,1]
	v_and_b32_e32 v48, 0xffff0000, v48
	v_and_b32_e32 v49, 0xffff0000, v49
	v_or_b32_sdwa v43, v48, v46 dst_sel:DWORD dst_unused:UNUSED_PAD src0_sel:DWORD src1_sel:WORD_1
	v_or_b32_sdwa v42, v49, v47 dst_sel:DWORD dst_unused:UNUSED_PAD src0_sel:DWORD src1_sel:WORD_1
	global_store_dwordx2 v[76:77], v[42:43], off offset:2560
	global_store_dword v[62:63], v50, off offset:1280
	v_and_b32_sdwa v43, v38, v84 dst_sel:DWORD dst_unused:UNUSED_PAD src0_sel:WORD_1 src1_sel:DWORD
	v_and_b32_sdwa v45, v39, v84 dst_sel:DWORD dst_unused:UNUSED_PAD src0_sel:WORD_1 src1_sel:DWORD
	v_add3_u32 v43, v38, v43, s20
	v_add3_u32 v45, v39, v45, s20
	v_max_f32_e32 v38, v38, v38
	v_max_f32_e32 v39, v39, v39
	v_med3_f32 v38, v38, s22, v85
	v_med3_f32 v39, v39, s22, v85
	v_cvt_pk_fp8_f32 v46, v38, v39
	v_and_b32_sdwa v42, v40, v84 dst_sel:DWORD dst_unused:UNUSED_PAD src0_sel:WORD_1 src1_sel:DWORD
	v_add3_u32 v42, v40, v42, s20
	v_max_f32_e32 v40, v40, v40
	v_max_f32_e32 v39, v41, v41
	v_and_b32_sdwa v44, v41, v84 dst_sel:DWORD dst_unused:UNUSED_PAD src0_sel:WORD_1 src1_sel:DWORD
	v_med3_f32 v38, v40, s22, v85
	v_med3_f32 v39, v39, s22, v85
	v_add3_u32 v44, v41, v44, s20
	v_cvt_pk_fp8_f32 v46, v38, v39 op_sel:[0,0,1]
	v_and_b32_e32 v44, 0xffff0000, v44
	v_and_b32_e32 v45, 0xffff0000, v45
	v_or_b32_sdwa v39, v44, v42 dst_sel:DWORD dst_unused:UNUSED_PAD src0_sel:DWORD src1_sel:WORD_1
	v_or_b32_sdwa v38, v45, v43 dst_sel:DWORD dst_unused:UNUSED_PAD src0_sel:DWORD src1_sel:WORD_1
	global_store_dwordx2 v[76:77], v[38:39], off offset:3072
	global_store_dword v[62:63], v46, off offset:1536
	v_and_b32_sdwa v39, v34, v84 dst_sel:DWORD dst_unused:UNUSED_PAD src0_sel:WORD_1 src1_sel:DWORD
	v_and_b32_sdwa v41, v35, v84 dst_sel:DWORD dst_unused:UNUSED_PAD src0_sel:WORD_1 src1_sel:DWORD
	v_add3_u32 v39, v34, v39, s20
	v_add3_u32 v41, v35, v41, s20
	v_max_f32_e32 v34, v34, v34
	v_max_f32_e32 v35, v35, v35
	v_med3_f32 v34, v34, s22, v85
	v_med3_f32 v35, v35, s22, v85
	v_cvt_pk_fp8_f32 v42, v34, v35
	v_and_b32_sdwa v38, v36, v84 dst_sel:DWORD dst_unused:UNUSED_PAD src0_sel:WORD_1 src1_sel:DWORD
	v_add3_u32 v38, v36, v38, s20
	v_max_f32_e32 v36, v36, v36
	v_max_f32_e32 v35, v37, v37
	v_and_b32_sdwa v40, v37, v84 dst_sel:DWORD dst_unused:UNUSED_PAD src0_sel:WORD_1 src1_sel:DWORD
	v_med3_f32 v34, v36, s22, v85
	v_med3_f32 v35, v35, s22, v85
	v_add3_u32 v40, v37, v40, s20
	v_cvt_pk_fp8_f32 v42, v34, v35 op_sel:[0,0,1]
	v_and_b32_e32 v40, 0xffff0000, v40
	v_and_b32_e32 v41, 0xffff0000, v41
	v_or_b32_sdwa v35, v40, v38 dst_sel:DWORD dst_unused:UNUSED_PAD src0_sel:DWORD src1_sel:WORD_1
	v_or_b32_sdwa v34, v41, v39 dst_sel:DWORD dst_unused:UNUSED_PAD src0_sel:DWORD src1_sel:WORD_1
	global_store_dwordx2 v[76:77], v[34:35], off offset:3584
	global_store_dword v[62:63], v42, off offset:1792
	v_and_b32_sdwa v35, v30, v84 dst_sel:DWORD dst_unused:UNUSED_PAD src0_sel:WORD_1 src1_sel:DWORD
	v_and_b32_sdwa v37, v31, v84 dst_sel:DWORD dst_unused:UNUSED_PAD src0_sel:WORD_1 src1_sel:DWORD
	v_add3_u32 v35, v30, v35, s20
	v_add3_u32 v37, v31, v37, s20
	v_max_f32_e32 v30, v30, v30
	v_max_f32_e32 v31, v31, v31
	v_med3_f32 v30, v30, s22, v85
	v_med3_f32 v31, v31, s22, v85
	v_cvt_pk_fp8_f32 v38, v30, v31
	v_and_b32_sdwa v34, v32, v84 dst_sel:DWORD dst_unused:UNUSED_PAD src0_sel:WORD_1 src1_sel:DWORD
	v_add3_u32 v34, v32, v34, s20
	v_max_f32_e32 v32, v32, v32
	v_max_f32_e32 v31, v33, v33
	v_and_b32_sdwa v36, v33, v84 dst_sel:DWORD dst_unused:UNUSED_PAD src0_sel:WORD_1 src1_sel:DWORD
	v_med3_f32 v30, v32, s22, v85
	v_med3_f32 v31, v31, s22, v85
	v_add3_u32 v36, v33, v36, s20
	v_cvt_pk_fp8_f32 v38, v30, v31 op_sel:[0,0,1]
	v_and_b32_e32 v36, 0xffff0000, v36
	v_and_b32_e32 v37, 0xffff0000, v37
	v_or_b32_sdwa v31, v36, v34 dst_sel:DWORD dst_unused:UNUSED_PAD src0_sel:DWORD src1_sel:WORD_1
	v_or_b32_sdwa v30, v37, v35 dst_sel:DWORD dst_unused:UNUSED_PAD src0_sel:DWORD src1_sel:WORD_1
	global_store_dwordx2 v[74:75], v[30:31], off
	global_store_dword v[62:63], v38, off offset:2048
; #define GAS __attribute__((address_space(1)))
; __device__ __forceinline__ unsigned f2bf(float f) { unsigned u = __builtin_bit_cast(unsigned, f); return (u + 0x7fffu + ((u >> 16) & 1u)) >> 16; }
; __device__ __forceinline__ unsigned pk2(float lo, float hi) { return f2bf(lo) | (f2bf(hi) << 16); }
; __global__ void __launch_bounds__(NWAVES * 64, 2) mk_fwd(Args args) {
;     ...
;             GAS v2u* o8 = (GAS v2u*)(XB + (size_t)m * DMODEL) + lane; GAS unsigned* o4 = (GAS unsigned*)(X8 + (size_t)m * DMODEL) + lane;
; #pragma unroll
;             for (int j = 0; j < 16; ++j) { v2u w; w.x = pk2(v[j].x, v[j].y); w.y = pk2(v[j].z, v[j].w); o8[64 * j] = w; o4[64 * j] = pg8::pk4_fp8(v[j].x, v[j].y, v[j].z, v[j].w); }
	v_and_b32_sdwa v31, v22, v84 dst_sel:DWORD dst_unused:UNUSED_PAD src0_sel:WORD_1 src1_sel:DWORD
	v_and_b32_sdwa v33, v23, v84 dst_sel:DWORD dst_unused:UNUSED_PAD src0_sel:WORD_1 src1_sel:DWORD
	v_add3_u32 v31, v22, v31, s20
	v_add3_u32 v33, v23, v33, s20
	v_max_f32_e32 v22, v22, v22
	v_max_f32_e32 v23, v23, v23
	v_med3_f32 v22, v22, s22, v85
	v_med3_f32 v23, v23, s22, v85
	v_cvt_pk_fp8_f32 v34, v22, v23
	v_and_b32_sdwa v30, v24, v84 dst_sel:DWORD dst_unused:UNUSED_PAD src0_sel:WORD_1 src1_sel:DWORD
	v_add3_u32 v30, v24, v30, s20
	v_max_f32_e32 v24, v24, v24
	v_max_f32_e32 v23, v25, v25
	v_and_b32_sdwa v32, v25, v84 dst_sel:DWORD dst_unused:UNUSED_PAD src0_sel:WORD_1 src1_sel:DWORD
	v_med3_f32 v22, v24, s22, v85
	v_med3_f32 v23, v23, s22, v85
	v_add3_u32 v32, v25, v32, s20
	v_cvt_pk_fp8_f32 v34, v22, v23 op_sel:[0,0,1]
	v_and_b32_e32 v32, 0xffff0000, v32
	v_and_b32_e32 v33, 0xffff0000, v33
	v_or_b32_sdwa v23, v32, v30 dst_sel:DWORD dst_unused:UNUSED_PAD src0_sel:DWORD src1_sel:WORD_1
	v_or_b32_sdwa v22, v33, v31 dst_sel:DWORD dst_unused:UNUSED_PAD src0_sel:DWORD src1_sel:WORD_1
	global_store_dwordx2 v[74:75], v[22:23], off offset:512
	global_store_dword v[62:63], v34, off offset:2304
	v_and_b32_sdwa v23, v14, v84 dst_sel:DWORD dst_unused:UNUSED_PAD src0_sel:WORD_1 src1_sel:DWORD
	v_and_b32_sdwa v25, v15, v84 dst_sel:DWORD dst_unused:UNUSED_PAD src0_sel:WORD_1 src1_sel:DWORD
	v_add3_u32 v23, v14, v23, s20
	v_add3_u32 v25, v15, v25, s20
	v_max_f32_e32 v14, v14, v14
	v_max_f32_e32 v15, v15, v15
	v_med3_f32 v14, v14, s22, v85
	v_med3_f32 v15, v15, s22, v85
	v_cvt_pk_fp8_f32 v30, v14, v15
	v_and_b32_sdwa v22, v16, v84 dst_sel:DWORD dst_unused:UNUSED_PAD src0_sel:WORD_1 src1_sel:DWORD
	v_add3_u32 v22, v16, v22, s20
	v_max_f32_e32 v16, v16, v16
	v_max_f32_e32 v15, v17, v17
	v_and_b32_sdwa v24, v17, v84 dst_sel:DWORD dst_unused:UNUSED_PAD src0_sel:WORD_1 src1_sel:DWORD
	v_med3_f32 v14, v16, s22, v85
	v_med3_f32 v15, v15, s22, v85
	v_add3_u32 v24, v17, v24, s20
	v_cvt_pk_fp8_f32 v30, v14, v15 op_sel:[0,0,1]
	v_and_b32_e32 v24, 0xffff0000, v24
	v_and_b32_e32 v25, 0xffff0000, v25
	v_or_b32_sdwa v15, v24, v22 dst_sel:DWORD dst_unused:UNUSED_PAD src0_sel:DWORD src1_sel:WORD_1
	v_or_b32_sdwa v14, v25, v23 dst_sel:DWORD dst_unused:UNUSED_PAD src0_sel:DWORD src1_sel:WORD_1
	global_store_dwordx2 v[74:75], v[14:15], off offset:1024
	global_store_dword v[62:63], v30, off offset:2560
	v_and_b32_sdwa v15, v6, v84 dst_sel:DWORD dst_unused:UNUSED_PAD src0_sel:WORD_1 src1_sel:DWORD
	v_and_b32_sdwa v17, v7, v84 dst_sel:DWORD dst_unused:UNUSED_PAD src0_sel:WORD_1 src1_sel:DWORD
	v_add3_u32 v15, v6, v15, s20
	v_add3_u32 v17, v7, v17, s20
	v_max_f32_e32 v6, v6, v6
	v_max_f32_e32 v7, v7, v7
	v_med3_f32 v6, v6, s22, v85
	v_med3_f32 v7, v7, s22, v85
	v_cvt_pk_fp8_f32 v22, v6, v7
	v_and_b32_sdwa v14, v8, v84 dst_sel:DWORD dst_unused:UNUSED_PAD src0_sel:WORD_1 src1_sel:DWORD
	v_and_b32_sdwa v16, v9, v84 dst_sel:DWORD dst_unused:UNUSED_PAD src0_sel:WORD_1 src1_sel:DWORD
	v_add3_u32 v14, v8, v14, s20
	v_add3_u32 v16, v9, v16, s20
	v_max_f32_e32 v8, v8, v8
	v_max_f32_e32 v7, v9, v9
	v_and_b32_e32 v16, 0xffff0000, v16
	v_and_b32_e32 v17, 0xffff0000, v17
	v_med3_f32 v6, v8, s22, v85
	v_med3_f32 v7, v7, s22, v85
	v_cvt_pk_fp8_f32 v22, v6, v7 op_sel:[0,0,1]
	v_or_b32_sdwa v7, v16, v14 dst_sel:DWORD dst_unused:UNUSED_PAD src0_sel:DWORD src1_sel:WORD_1
	v_or_b32_sdwa v6, v17, v15 dst_sel:DWORD dst_unused:UNUSED_PAD src0_sel:DWORD src1_sel:WORD_1
	v_max_f32_e32 v14, v26, v26
	v_max_f32_e32 v15, v27, v27
	v_med3_f32 v14, v14, s22, v85
	v_med3_f32 v15, v15, s22, v85
	v_cvt_pk_fp8_f32 v17, v14, v15
	global_store_dwordx2 v[74:75], v[6:7], off offset:1536
	global_store_dword v[62:63], v22, off offset:2816
	v_and_b32_sdwa v7, v26, v84 dst_sel:DWORD dst_unused:UNUSED_PAD src0_sel:WORD_1 src1_sel:DWORD
	v_max_f32_e32 v16, v28, v28
	v_max_f32_e32 v15, v29, v29
	v_add3_u32 v8, v26, v7, s20
	v_and_b32_sdwa v7, v29, v84 dst_sel:DWORD dst_unused:UNUSED_PAD src0_sel:WORD_1 src1_sel:DWORD
	v_and_b32_sdwa v9, v27, v84 dst_sel:DWORD dst_unused:UNUSED_PAD src0_sel:WORD_1 src1_sel:DWORD
	v_med3_f32 v14, v16, s22, v85
	v_med3_f32 v15, v15, s22, v85
	v_and_b32_sdwa v6, v28, v84 dst_sel:DWORD dst_unused:UNUSED_PAD src0_sel:WORD_1 src1_sel:DWORD
; #define GAS __attribute__((address_space(1)))
; __device__ __forceinline__ unsigned f2bf(float f) { unsigned u = __builtin_bit_cast(unsigned, f); return (u + 0x7fffu + ((u >> 16) & 1u)) >> 16; }
; __device__ __forceinline__ unsigned pk2(float lo, float hi) { return f2bf(lo) | (f2bf(hi) << 16); }
; __global__ void __launch_bounds__(NWAVES * 64, 2) mk_fwd(Args args) {
;     ...
;             GAS v2u* o8 = (GAS v2u*)(XB + (size_t)m * DMODEL) + lane; GAS unsigned* o4 = (GAS unsigned*)(X8 + (size_t)m * DMODEL) + lane;
; #pragma unroll
;             for (int j = 0; j < 16; ++j) { v2u w; w.x = pk2(v[j].x, v[j].y); w.y = pk2(v[j].z, v[j].w); o8[64 * j] = w; o4[64 * j] = pg8::pk4_fp8(v[j].x, v[j].y, v[j].z, v[j].w); }
	v_add3_u32 v7, v29, v7, s20
	v_add3_u32 v9, v27, v9, s20
	v_cvt_pk_fp8_f32 v17, v14, v15 op_sel:[0,0,1]
	v_add3_u32 v6, v28, v6, s20
	v_and_b32_e32 v7, 0xffff0000, v7
	v_and_b32_e32 v9, 0xffff0000, v9
	v_or_b32_sdwa v7, v7, v6 dst_sel:DWORD dst_unused:UNUSED_PAD src0_sel:DWORD src1_sel:WORD_1
	v_or_b32_sdwa v6, v9, v8 dst_sel:DWORD dst_unused:UNUSED_PAD src0_sel:DWORD src1_sel:WORD_1
	v_max_f32_e32 v14, v18, v18
	v_max_f32_e32 v15, v19, v19
	global_store_dwordx2 v[74:75], v[6:7], off offset:2048
	global_store_dword v[62:63], v17, off offset:3072
	v_med3_f32 v14, v14, s22, v85
	v_med3_f32 v15, v15, s22, v85
	v_cvt_pk_fp8_f32 v17, v14, v15
	v_and_b32_sdwa v7, v18, v84 dst_sel:DWORD dst_unused:UNUSED_PAD src0_sel:WORD_1 src1_sel:DWORD
	v_max_f32_e32 v16, v20, v20
	v_max_f32_e32 v15, v21, v21
	v_add3_u32 v8, v18, v7, s20
	v_and_b32_sdwa v7, v21, v84 dst_sel:DWORD dst_unused:UNUSED_PAD src0_sel:WORD_1 src1_sel:DWORD
	v_and_b32_sdwa v9, v19, v84 dst_sel:DWORD dst_unused:UNUSED_PAD src0_sel:WORD_1 src1_sel:DWORD
	v_med3_f32 v14, v16, s22, v85
	v_med3_f32 v15, v15, s22, v85
	v_and_b32_sdwa v6, v20, v84 dst_sel:DWORD dst_unused:UNUSED_PAD src0_sel:WORD_1 src1_sel:DWORD
	v_add3_u32 v7, v21, v7, s20
	v_add3_u32 v9, v19, v9, s20
	v_cvt_pk_fp8_f32 v17, v14, v15 op_sel:[0,0,1]
	v_add3_u32 v6, v20, v6, s20
	v_and_b32_e32 v7, 0xffff0000, v7
	v_and_b32_e32 v9, 0xffff0000, v9
	v_or_b32_sdwa v7, v7, v6 dst_sel:DWORD dst_unused:UNUSED_PAD src0_sel:DWORD src1_sel:WORD_1
	v_or_b32_sdwa v6, v9, v8 dst_sel:DWORD dst_unused:UNUSED_PAD src0_sel:DWORD src1_sel:WORD_1
	global_store_dwordx2 v[74:75], v[6:7], off offset:2560
	global_store_dword v[62:63], v17, off offset:3328
	v_and_b32_sdwa v7, v10, v84 dst_sel:DWORD dst_unused:UNUSED_PAD src0_sel:WORD_1 src1_sel:DWORD
	v_and_b32_sdwa v9, v11, v84 dst_sel:DWORD dst_unused:UNUSED_PAD src0_sel:WORD_1 src1_sel:DWORD
	v_add3_u32 v8, v10, v7, s20
	v_add3_u32 v9, v11, v9, s20
	v_max_f32_e32 v10, v10, v10
	v_max_f32_e32 v11, v11, v11
	v_med3_f32 v10, v10, s22, v85
	v_med3_f32 v11, v11, s22, v85
	v_cvt_pk_fp8_f32 v14, v10, v11
	v_and_b32_sdwa v6, v12, v84 dst_sel:DWORD dst_unused:UNUSED_PAD src0_sel:WORD_1 src1_sel:DWORD
	v_add3_u32 v6, v12, v6, s20
	v_max_f32_e32 v12, v12, v12
	v_max_f32_e32 v11, v13, v13
	v_and_b32_sdwa v7, v13, v84 dst_sel:DWORD dst_unused:UNUSED_PAD src0_sel:WORD_1 src1_sel:DWORD
	v_med3_f32 v10, v12, s22, v85
	v_med3_f32 v11, v11, s22, v85
	v_add3_u32 v7, v13, v7, s20
	v_cvt_pk_fp8_f32 v14, v10, v11 op_sel:[0,0,1]
	v_and_b32_e32 v7, 0xffff0000, v7
	v_and_b32_e32 v9, 0xffff0000, v9
	v_or_b32_sdwa v7, v7, v6 dst_sel:DWORD dst_unused:UNUSED_PAD src0_sel:DWORD src1_sel:WORD_1
	v_or_b32_sdwa v6, v9, v8 dst_sel:DWORD dst_unused:UNUSED_PAD src0_sel:DWORD src1_sel:WORD_1
	global_store_dwordx2 v[74:75], v[6:7], off offset:3072
	global_store_dword v[62:63], v14, off offset:3584
	v_and_b32_sdwa v7, v2, v84 dst_sel:DWORD dst_unused:UNUSED_PAD src0_sel:WORD_1 src1_sel:DWORD
	v_and_b32_sdwa v9, v3, v84 dst_sel:DWORD dst_unused:UNUSED_PAD src0_sel:WORD_1 src1_sel:DWORD
	v_add3_u32 v7, v2, v7, s20
	v_add3_u32 v9, v3, v9, s20
	v_max_f32_e32 v2, v2, v2
	v_max_f32_e32 v3, v3, v3
	v_med3_f32 v2, v2, s22, v85
	v_med3_f32 v3, v3, s22, v85
	v_cvt_pk_fp8_f32 v10, v2, v3
	v_and_b32_sdwa v6, v4, v84 dst_sel:DWORD dst_unused:UNUSED_PAD src0_sel:WORD_1 src1_sel:DWORD
	v_add3_u32 v6, v4, v6, s20
	v_max_f32_e32 v4, v4, v4
	v_max_f32_e32 v3, v5, v5
	v_and_b32_sdwa v8, v5, v84 dst_sel:DWORD dst_unused:UNUSED_PAD src0_sel:WORD_1 src1_sel:DWORD
	v_med3_f32 v2, v4, s22, v85
	v_med3_f32 v3, v3, s22, v85
	s_add_i32 s25, s25, s84
	v_add3_u32 v8, v5, v8, s20
	v_cvt_pk_fp8_f32 v10, v2, v3 op_sel:[0,0,1]
	s_add_u32 s14, s14, s4
	v_and_b32_e32 v8, 0xffff0000, v8
	v_and_b32_e32 v9, 0xffff0000, v9
	s_addc_u32 s15, s15, s5
	v_or_b32_sdwa v3, v8, v6 dst_sel:DWORD dst_unused:UNUSED_PAD src0_sel:DWORD src1_sel:WORD_1
	v_or_b32_sdwa v2, v9, v7 dst_sel:DWORD dst_unused:UNUSED_PAD src0_sel:DWORD src1_sel:WORD_1
	v_lshl_add_u64 v[68:69], v[68:69], 0, s[6:7]
	v_lshl_add_u64 v[70:71], v[70:71], 0, s[8:9]
	s_cmpk_gt_i32 s25, 0x3fff
	v_lshl_add_u64 v[72:73], v[72:73], 0, s[10:11]
	global_store_dwordx2 v[74:75], v[2:3], off offset:3584
	global_store_dword v[62:63], v10, off offset:3840
	s_cbranch_scc1 .LBB0_46

; #define GAS __attribute__((address_space(1)))
; __device__ __forceinline__ float wave_sum(float v) {
; #pragma unroll
;     for (int o = 1; o < 64; o <<= 1) v += __shfl_xor(v, o);
;     return v;
; __global__ void __launch_bounds__(NWAVES * 64, 2) mk_fwd(Args args) {
;     ...
;         for (int m = gw; m < BATCH * MEMLEN; m += NGW) {
;             const GAS f32x4* xr = (const GAS f32x4*)(mem + (size_t)m * DMODEL) + lane;
;             const GAS f32x4* gr = (const GAS f32x4*)ln_mem_g + lane;
;             f32x4 v[16]; float s = 0.f;
; #pragma unroll
;             for (int j = 0; j < 16; ++j) { v[j] = xr[64 * j]; s += (v[j].x * v[j].x + v[j].y * v[j].y) + (v[j].z * v[j].z + v[j].w * v[j].w); }
;             const float rs = rsqrtf(wave_sum(s) * (1.0f / DMODEL) + 1e-5f);
.LBB0_48:
	v_add_co_u32_e64 v18, s[0:1], s6, v66
	v_add_co_u32_e32 v84, vcc, 0xffffd000, v66
	s_nop 0
	v_addc_co_u32_e64 v19, s[0:1], -1, v67, s[0:1]
	v_add_co_u32_e64 v20, s[0:1], s7, v66
	global_load_dwordx4 v[2:5], v[66:67], off offset:-3072
	s_nop 0
	v_addc_co_u32_e64 v21, s[0:1], -1, v67, s[0:1]
	global_load_dwordx4 v[14:17], v[66:67], off offset:-2048
	global_load_dwordx4 v[10:13], v[66:67], off offset:-1024
	global_load_dwordx4 v[6:9], v[66:67], off
	global_load_dwordx4 v[42:45], v[56:57], off
	global_load_dwordx4 v[50:53], v[18:19], off offset:-3072
	global_load_dwordx4 v[38:41], v[18:19], off offset:-1024
	global_load_dwordx4 v[46:49], v[18:19], off offset:-2048
	global_load_dwordx4 v[34:37], v[18:19], off
	global_load_dwordx4 v[26:29], v[20:21], off offset:-2048
	global_load_dwordx4 v[30:33], v[20:21], off offset:-3072
	global_load_dwordx4 v[22:25], v[20:21], off offset:-1024
	s_nop 0
	global_load_dwordx4 v[18:21], v[66:67], off offset:-4096
	v_addc_co_u32_e32 v85, vcc, -1, v67, vcc
	global_load_dwordx4 v[96:99], v[84:85], off offset:-3072
	global_load_dwordx4 v[100:103], v[84:85], off offset:-2048
	global_load_dwordx4 v[104:107], v[84:85], off
	global_load_dwordx4 v[108:111], v[84:85], off offset:-1024
	v_mov_b32_e32 v151, 0
	v_mov_b32_e32 v153, 0
	s_add_i32 s0, s10, 0x4000
	s_ashr_i32 s1, s0, 31
	s_lshl_b64 s[0:1], s[0:1], 12
	v_lshl_add_u64 v[84:85], v[54:55], 0, s[0:1]
	v_mov_b32_e32 v156, 0
	v_mov_b32_e32 v157, 0
	s_add_i32 s10, s10, s84
	v_lshl_add_u64 v[66:67], v[66:67], 0, s[4:5]
	s_cmpk_gt_i32 s10, 0x3ff
	s_waitcnt vmcnt(11)
	v_pk_mul_f32 v[118:119], v[52:53], v[52:53]
	v_pk_mul_f32 v[120:121], v[50:51], v[50:51]
	s_waitcnt vmcnt(9)
	v_mul_f32_e32 v122, v47, v47
	v_pk_mul_f32 v[94:95], v[16:17], v[16:17]
	v_pk_mul_f32 v[112:113], v[14:15], v[14:15]
	v_mul_f32_e32 v114, v11, v11
	v_mul_f32_e32 v116, v13, v13
	v_mul_f32_e32 v141, v8, v8
	v_mul_f32_e32 v164, v9, v9
	v_mul_f32_e32 v124, v49, v49
	s_waitcnt vmcnt(8)
	v_pk_mul_f32 v[126:127], v[36:37], v[36:37]
	v_pk_mul_f32 v[128:129], v[34:35], v[34:35]
	s_waitcnt vmcnt(6)
	v_mul_f32_e32 v130, v31, v31
	v_mul_f32_e32 v132, v33, v33
	s_waitcnt vmcnt(5)
	v_pk_mul_f32 v[134:135], v[24:25], v[24:25]
	v_pk_mul_f32 v[136:137], v[22:23], v[22:23]
	s_waitcnt vmcnt(4)
	v_mul_f32_e32 v138, v19, v19
	v_mul_f32_e32 v140, v21, v21
	v_pk_mov_b32 v[142:143], v[112:113], v[94:95] op_sel:[1,0]
	v_mov_b32_e32 v113, v95
	v_pk_fma_f32 v[94:95], v[10:11], v[10:11], v[114:115] op_sel_hi:[1,1,0]
	v_pk_fma_f32 v[114:115], v[12:13], v[12:13], v[116:117] op_sel_hi:[1,1,0]
	s_waitcnt vmcnt(3)
	v_pk_mul_f32 v[116:117], v[98:99], v[98:99]
	v_pk_mul_f32 v[144:145], v[96:97], v[96:97]
	s_waitcnt vmcnt(2)
	v_pk_mul_f32 v[146:147], v[102:103], v[102:103]
	v_pk_mul_f32 v[148:149], v[100:101], v[100:101]
	v_pk_mov_b32 v[154:155], v[120:121], v[118:119] op_sel:[1,0]
	v_mov_b32_e32 v121, v119
	v_pk_fma_f32 v[118:119], v[46:47], v[46:47], v[122:123] op_sel_hi:[1,1,0]
	v_pk_fma_f32 v[122:123], v[48:49], v[48:49], v[124:125] op_sel_hi:[1,1,0]
	v_pk_mov_b32 v[124:125], v[128:129], v[126:127] op_sel:[1,0]
	v_mov_b32_e32 v129, v127
	v_pk_fma_f32 v[126:127], v[30:31], v[30:31], v[130:131] op_sel_hi:[1,1,0]
	v_pk_fma_f32 v[130:131], v[32:33], v[32:33], v[132:133] op_sel_hi:[1,1,0]
	v_pk_mov_b32 v[132:133], v[136:137], v[134:135] op_sel:[1,0]
	v_mov_b32_e32 v137, v135
	v_pk_fma_f32 v[134:135], v[18:19], v[18:19], v[138:139] op_sel_hi:[1,1,0]
	v_pk_fma_f32 v[138:139], v[20:21], v[20:21], v[140:141] op_sel_hi:[1,1,0]
	v_mov_b32_e32 v95, v141
	v_mov_b32_e32 v115, v164
	v_pk_mov_b32 v[140:141], v[144:145], v[116:117] op_sel:[1,0]
	v_mov_b32_e32 v145, v117
	v_pk_mov_b32 v[116:117], v[148:149], v[146:147] op_sel:[1,0]
	v_mov_b32_e32 v149, v147
	s_waitcnt vmcnt(0)
	v_mul_f32_e32 v150, v109, v109
	v_mul_f32_e32 v152, v111, v111
	v_pk_add_f32 v[94:95], v[94:95], v[114:115]
	v_pk_add_f32 v[114:115], v[140:141], v[144:145]
	v_pk_add_f32 v[116:117], v[116:117], v[148:149]
	v_mul_f32_e32 v167, v40, v40
	v_mul_f32_e32 v168, v41, v41
	v_mul_f32_e32 v171, v28, v28
	v_mul_f32_e32 v172, v29, v29
	v_mul_f32_e32 v173, v104, v104
	v_mul_f32_e32 v174, v105, v105
	v_mul_f32_e32 v175, v106, v106
	v_mul_f32_e32 v176, v107, v107
	v_pk_add_f32 v[112:113], v[142:143], v[112:113]
	v_pk_fma_f32 v[142:143], v[108:109], v[108:109], v[150:151] op_sel_hi:[1,1,0]
	v_pk_fma_f32 v[146:147], v[110:111], v[110:111], v[152:153] op_sel_hi:[1,1,0]
	v_pk_add_f32 v[114:115], v[114:115], v[114:115] op_sel:[0,1] op_sel_hi:[1,0]
	v_pk_add_f32 v[116:117], v[116:117], v[116:117] op_sel:[0,1] op_sel_hi:[1,0]
	v_mov_b32_e32 v119, v167
	v_mov_b32_e32 v123, v168
	v_pk_add_f32 v[124:125], v[124:125], v[128:129]
	v_mov_b32_e32 v127, v171
	v_mov_b32_e32 v131, v172
	v_mov_b32_e32 v143, v175
	v_mov_b32_e32 v147, v176
	v_mov_b32_e32 v115, v173
	v_mov_b32_e32 v117, v174
	v_pk_add_f32 v[118:119], v[118:119], v[122:123]
	v_pk_add_f32 v[122:123], v[124:125], v[124:125] op_sel:[0,1] op_sel_hi:[1,0]
	v_pk_add_f32 v[124:125], v[126:127], v[130:131]
	v_pk_add_f32 v[130:131], v[142:143], v[146:147]
	v_pk_add_f32 v[114:115], v[114:115], v[116:117]
	v_pk_add_f32 v[120:121], v[154:155], v[120:121]
	v_pk_add_f32 v[114:115], v[114:115], v[130:131]
	v_mul_f32_e32 v165, v38, v38
	v_mul_f32_e32 v166, v39, v39
	v_pk_add_f32 v[120:121], v[120:121], v[120:121] op_sel:[0,1] op_sel_hi:[1,0]
	v_pk_add_f32 v[114:115], v[114:115], v[114:115] op_sel:[0,1] op_sel_hi:[1,0]
	v_mov_b32_e32 v121, v166
	v_mov_b32_e32 v115, v165
	v_pk_add_f32 v[114:115], v[114:115], v[120:121]
	v_mul_f32_e32 v169, v26, v26
	v_pk_add_f32 v[114:115], v[114:115], v[118:119]
	v_mul_f32_e32 v170, v27, v27
	v_pk_add_f32 v[114:115], v[114:115], v[114:115] op_sel:[0,1] op_sel_hi:[1,0]
	v_mov_b32_e32 v123, v170
	v_mov_b32_e32 v115, v169
	v_pk_add_f32 v[114:115], v[114:115], v[122:123]
	v_pk_add_f32 v[128:129], v[132:133], v[136:137]
	v_pk_add_f32 v[114:115], v[114:115], v[124:125]
	v_mul_f32_e32 v158, v2, v2
	v_mul_f32_e32 v159, v3, v3
	v_mul_f32_e32 v160, v4, v4
	v_mul_f32_e32 v161, v5, v5
	v_pk_add_f32 v[126:127], v[128:129], v[128:129] op_sel:[0,1] op_sel_hi:[1,0]
	v_pk_add_f32 v[114:115], v[114:115], v[114:115] op_sel:[0,1] op_sel_hi:[1,0]
	v_mov_b32_e32 v135, v160
	v_mov_b32_e32 v139, v161
	v_mov_b32_e32 v127, v159
	v_mov_b32_e32 v115, v158
	v_pk_add_f32 v[128:129], v[134:135], v[138:139]
	v_pk_add_f32 v[114:115], v[114:115], v[126:127]
	v_mul_f32_e32 v162, v6, v6
	v_pk_add_f32 v[114:115], v[114:115], v[128:129]
	v_mul_f32_e32 v163, v7, v7
	v_pk_add_f32 v[112:113], v[112:113], v[112:113] op_sel:[0,1] op_sel_hi:[1,0]
	v_pk_add_f32 v[114:115], v[114:115], v[114:115] op_sel:[0,1] op_sel_hi:[1,0]
	v_mov_b32_e32 v113, v163
	v_mov_b32_e32 v115, v162
	v_pk_add_f32 v[112:113], v[114:115], v[112:113]
	s_nop 0
	v_pk_add_f32 v[94:95], v[112:113], v[94:95]
	s_nop 0
	v_add_f32_e32 v94, v94, v95
	ds_bpermute_b32 v95, v86, v94
	s_waitcnt lgkmcnt(0)
; #define GAS __attribute__((address_space(1)))
; __device__ __forceinline__ float wave_sum(float v) {
; #pragma unroll
;     for (int o = 1; o < 64; o <<= 1) v += __shfl_xor(v, o);
;     return v;
; __global__ void __launch_bounds__(NWAVES * 64, 2) mk_fwd(Args args) {
;     ...
;             const float rs = rsqrtf(wave_sum(s) * (1.0f / DMODEL) + 1e-5f);
;             GAS unsigned* o4 = (GAS unsigned*)(XB8 + (size_t)(MTOK + m) * DMODEL) + lane;
; #pragma unroll
;             for (int j = 0; j < 16; ++j) { const f32x4 g = gr[64 * j]; o4[64 * j] = pg8::pk4_fp8(v[j].x * rs * g.x, v[j].y * rs * g.y, v[j].z * rs * g.z, v[j].w * rs * g.w); }
	v_add_f32_e32 v94, v94, v95
	ds_bpermute_b32 v95, v87, v94
	s_waitcnt lgkmcnt(0)
	v_add_f32_e32 v94, v94, v95
	ds_bpermute_b32 v95, v88, v94
	s_waitcnt lgkmcnt(0)
	v_add_f32_e32 v94, v94, v95
	ds_bpermute_b32 v95, v89, v94
	s_waitcnt lgkmcnt(0)
	v_add_f32_e32 v94, v94, v95
	ds_bpermute_b32 v95, v90, v94
	s_waitcnt lgkmcnt(0)
	v_add_f32_e32 v94, v94, v95
	ds_bpermute_b32 v95, v91, v94
	s_waitcnt lgkmcnt(0)
	v_add_f32_e32 v94, v94, v95
	v_fmamk_f32 v94, v94, 0x39800000, v92
	v_mul_f32_e32 v95, 0x4b800000, v94
	v_cmp_gt_f32_e32 vcc, s8, v94
	s_nop 1
	v_cndmask_b32_e32 v94, v94, v95, vcc
	v_rsq_f32_e32 v94, v94
	s_nop 0
	v_mul_f32_e32 v95, 0x45800000, v94
	v_cndmask_b32_e32 v94, v94, v95, vcc
	v_mul_f32_e32 v95, v94, v96
	v_mul_f32_e32 v96, v94, v97
	v_mul_f32_e32 v42, v42, v95
	v_mul_f32_e32 v43, v43, v96
	v_med3_f32 v42, v42, s9, v93
	v_med3_f32 v43, v43, s9, v93
	v_cvt_pk_fp8_f32 v151, v42, v43
	v_mul_f32_e32 v97, v94, v98
	v_mul_f32_e32 v98, v94, v99
	v_mul_f32_e32 v44, v44, v97
	v_mul_f32_e32 v45, v45, v98
	v_med3_f32 v44, v44, s9, v93
	v_med3_f32 v45, v45, s9, v93
	v_cvt_pk_fp8_f32 v151, v44, v45 op_sel:[0,0,1]
	v_mul_f32_e32 v99, v94, v100
	v_mul_f32_e32 v100, v94, v101
	v_mul_f32_e32 v101, v94, v102
	global_store_dword v[84:85], v151, off
	global_load_dwordx4 v[42:45], v[56:57], off offset:1024
	v_mul_f32_e32 v102, v94, v103
	v_mul_f32_e32 v103, v94, v108
	v_mul_f32_e32 v108, v94, v109
	v_mul_f32_e32 v109, v94, v110
	v_mul_f32_e32 v110, v94, v111
	v_mul_f32_e32 v95, v94, v104
	v_mul_f32_e32 v96, v94, v105
	v_mul_f32_e32 v97, v94, v106
	v_mul_f32_e32 v98, v94, v107
	v_mul_f32_e32 v50, v94, v50
	v_mul_f32_e32 v51, v94, v51
	v_mul_f32_e32 v52, v94, v52
	v_mul_f32_e32 v53, v94, v53
	v_mul_f32_e32 v46, v94, v46
	v_mul_f32_e32 v47, v94, v47
	v_mul_f32_e32 v48, v94, v48
	v_mul_f32_e32 v49, v94, v49
	v_mul_f32_e32 v38, v94, v38
	v_mul_f32_e32 v39, v94, v39
	v_mul_f32_e32 v40, v94, v40
	v_mul_f32_e32 v41, v94, v41
	v_mul_f32_e32 v34, v94, v34
	v_mul_f32_e32 v35, v94, v35
	v_mul_f32_e32 v36, v94, v36
	v_mul_f32_e32 v37, v94, v37
	v_mul_f32_e32 v30, v94, v30
	v_mul_f32_e32 v31, v94, v31
	v_mul_f32_e32 v32, v94, v32
	v_mul_f32_e32 v33, v94, v33
	v_mul_f32_e32 v26, v94, v26
	v_mul_f32_e32 v27, v94, v27
	v_mul_f32_e32 v28, v94, v28
	v_mul_f32_e32 v29, v94, v29
	v_mul_f32_e32 v22, v94, v22
	v_mul_f32_e32 v23, v94, v23
	v_mul_f32_e32 v24, v94, v24
	v_mul_f32_e32 v25, v94, v25
	v_mul_f32_e32 v18, v94, v18
	v_mul_f32_e32 v19, v94, v19
	v_mul_f32_e32 v20, v94, v20
	v_mul_f32_e32 v21, v94, v21
	v_mul_f32_e32 v2, v94, v2
	v_mul_f32_e32 v3, v94, v3
	v_mul_f32_e32 v4, v94, v4
	v_mul_f32_e32 v5, v94, v5
	v_mul_f32_e32 v14, v94, v14
	v_mul_f32_e32 v15, v94, v15
	v_mul_f32_e32 v16, v94, v16
	v_mul_f32_e32 v17, v94, v17
	v_mul_f32_e32 v10, v94, v10
	v_mul_f32_e32 v11, v94, v11
	v_mul_f32_e32 v12, v94, v12
	v_mul_f32_e32 v13, v94, v13
	v_mul_f32_e32 v6, v94, v6
	v_mul_f32_e32 v7, v94, v7
	v_mul_f32_e32 v8, v94, v8
	v_mul_f32_e32 v9, v94, v9
	s_waitcnt vmcnt(0)
	v_mul_f32_e32 v42, v42, v99
	v_mul_f32_e32 v43, v43, v100
	v_med3_f32 v42, v42, s9, v93
	v_med3_f32 v43, v43, s9, v93
	v_cvt_pk_fp8_f32 v153, v42, v43
	v_mul_f32_e32 v44, v44, v101
	v_mul_f32_e32 v45, v45, v102
	v_med3_f32 v44, v44, s9, v93
	v_med3_f32 v45, v45, s9, v93
	v_cvt_pk_fp8_f32 v153, v44, v45 op_sel:[0,0,1]
	global_store_dword v[84:85], v153, off offset:256
	global_load_dwordx4 v[42:45], v[56:57], off offset:2048
	s_waitcnt vmcnt(0)
	v_mul_f32_e32 v42, v42, v103
	v_mul_f32_e32 v43, v43, v108
	v_med3_f32 v42, v42, s9, v93
	v_med3_f32 v43, v43, s9, v93
	v_cvt_pk_fp8_f32 v156, v42, v43
	v_mul_f32_e32 v44, v44, v109
	v_mul_f32_e32 v45, v45, v110
	v_med3_f32 v44, v44, s9, v93
	v_med3_f32 v45, v45, s9, v93
	v_cvt_pk_fp8_f32 v156, v44, v45 op_sel:[0,0,1]
	global_store_dword v[84:85], v156, off offset:512
	global_load_dwordx4 v[42:45], v[56:57], off offset:3072
	s_waitcnt vmcnt(0)
	v_mul_f32_e32 v42, v42, v95
	v_mul_f32_e32 v43, v43, v96
	v_med3_f32 v42, v42, s9, v93
	v_med3_f32 v43, v43, s9, v93
	v_cvt_pk_fp8_f32 v157, v42, v43
	v_mul_f32_e32 v44, v44, v97
	v_mul_f32_e32 v45, v45, v98
	v_med3_f32 v44, v44, s9, v93
	v_med3_f32 v45, v45, s9, v93
	v_cvt_pk_fp8_f32 v157, v44, v45 op_sel:[0,0,1]
	global_store_dword v[84:85], v157, off offset:768
	global_load_dwordx4 v[42:45], v[58:59], off
	s_waitcnt vmcnt(0)
	v_mul_f32_e32 v42, v42, v50
	v_mul_f32_e32 v43, v43, v51
	v_med3_f32 v42, v42, s9, v93
	v_med3_f32 v43, v43, s9, v93
	v_cvt_pk_fp8_f32 v95, v42, v43
	v_mul_f32_e32 v44, v44, v52
	v_mul_f32_e32 v45, v45, v53
	v_med3_f32 v44, v44, s9, v93
	v_med3_f32 v45, v45, s9, v93
	v_cvt_pk_fp8_f32 v95, v44, v45 op_sel:[0,0,1]
	global_store_dword v[84:85], v95, off offset:1024
	global_load_dwordx4 v[42:45], v[60:61], off
	s_waitcnt vmcnt(0)
; #define GAS __attribute__((address_space(1)))
; __device__ __forceinline__ unsigned pk4_fp8(float a, float b, float c, float d) {
;     a = fminf(fmaxf(a, -448.f), 448.f); b = fminf(fmaxf(b, -448.f), 448.f); c = fminf(fmaxf(c, -448.f), 448.f); d = fminf(fmaxf(d, -448.f), 448.f);
;     int w = 0; w = __builtin_amdgcn_cvt_pk_fp8_f32(a, b, w, false); w = __builtin_amdgcn_cvt_pk_fp8_f32(c, d, w, true); return (unsigned)w;
; __global__ void __launch_bounds__(NWAVES * 64, 2) mk_fwd(Args args) {
;     ...
;             GAS unsigned* o4 = (GAS unsigned*)(XB8 + (size_t)(MTOK + m) * DMODEL) + lane;
; #pragma unroll
;             for (int j = 0; j < 16; ++j) { const f32x4 g = gr[64 * j]; o4[64 * j] = pg8::pk4_fp8(v[j].x * rs * g.x, v[j].y * rs * g.y, v[j].z * rs * g.z, v[j].w * rs * g.w); }
	v_mul_f32_e32 v42, v42, v46
	v_mul_f32_e32 v43, v43, v47
	v_med3_f32 v42, v42, s9, v93
	v_med3_f32 v43, v43, s9, v93
	v_cvt_pk_fp8_f32 v50, v42, v43
	v_mul_f32_e32 v44, v44, v48
	v_mul_f32_e32 v45, v45, v49
	v_med3_f32 v44, v44, s9, v93
	v_med3_f32 v45, v45, s9, v93
	v_cvt_pk_fp8_f32 v50, v44, v45 op_sel:[0,0,1]
	global_store_dword v[84:85], v50, off offset:1280
	global_load_dwordx4 v[42:45], v[62:63], off
	s_waitcnt vmcnt(0)
	v_mul_f32_e32 v38, v42, v38
	v_mul_f32_e32 v39, v43, v39
	v_med3_f32 v38, v38, s9, v93
	v_med3_f32 v39, v39, s9, v93
	v_cvt_pk_fp8_f32 v46, v38, v39
	v_mul_f32_e32 v40, v44, v40
	v_mul_f32_e32 v41, v45, v41
	v_med3_f32 v40, v40, s9, v93
	v_med3_f32 v41, v41, s9, v93
	v_cvt_pk_fp8_f32 v46, v40, v41 op_sel:[0,0,1]
	global_store_dword v[84:85], v46, off offset:1536
	global_load_dwordx4 v[38:41], v[64:65], off
	s_waitcnt vmcnt(0)
	v_mul_f32_e32 v34, v38, v34
	v_mul_f32_e32 v35, v39, v35
	v_med3_f32 v34, v34, s9, v93
	v_med3_f32 v35, v35, s9, v93
	v_cvt_pk_fp8_f32 v42, v34, v35
	v_mul_f32_e32 v36, v40, v36
	v_mul_f32_e32 v37, v41, v37
	v_med3_f32 v36, v36, s9, v93
	v_med3_f32 v37, v37, s9, v93
	v_cvt_pk_fp8_f32 v42, v36, v37 op_sel:[0,0,1]
	global_store_dword v[84:85], v42, off offset:1792
	global_load_dwordx4 v[34:37], v[68:69], off
	s_waitcnt vmcnt(0)
	v_mul_f32_e32 v30, v34, v30
	v_mul_f32_e32 v31, v35, v31
	v_med3_f32 v30, v30, s9, v93
	v_med3_f32 v31, v31, s9, v93
	v_cvt_pk_fp8_f32 v38, v30, v31
	v_mul_f32_e32 v32, v36, v32
	v_mul_f32_e32 v33, v37, v33
	v_med3_f32 v32, v32, s9, v93
	v_med3_f32 v33, v33, s9, v93
	v_cvt_pk_fp8_f32 v38, v32, v33 op_sel:[0,0,1]
	global_store_dword v[84:85], v38, off offset:2048
	global_load_dwordx4 v[30:33], v[70:71], off
	s_waitcnt vmcnt(0)
	v_mul_f32_e32 v26, v30, v26
	v_mul_f32_e32 v27, v31, v27
	v_med3_f32 v26, v26, s9, v93
	v_med3_f32 v27, v27, s9, v93
	v_cvt_pk_fp8_f32 v34, v26, v27
	v_mul_f32_e32 v28, v32, v28
	v_mul_f32_e32 v29, v33, v29
	v_med3_f32 v28, v28, s9, v93
	v_med3_f32 v29, v29, s9, v93
	v_cvt_pk_fp8_f32 v34, v28, v29 op_sel:[0,0,1]
	global_store_dword v[84:85], v34, off offset:2304
	global_load_dwordx4 v[26:29], v[72:73], off
	s_waitcnt vmcnt(0)
	v_mul_f32_e32 v22, v26, v22
	v_mul_f32_e32 v23, v27, v23
	v_med3_f32 v22, v22, s9, v93
	v_med3_f32 v23, v23, s9, v93
	v_cvt_pk_fp8_f32 v30, v22, v23
	v_mul_f32_e32 v24, v28, v24
	v_mul_f32_e32 v25, v29, v25
	v_med3_f32 v24, v24, s9, v93
	v_med3_f32 v25, v25, s9, v93
	v_cvt_pk_fp8_f32 v30, v24, v25 op_sel:[0,0,1]
	global_store_dword v[84:85], v30, off offset:2560
	global_load_dwordx4 v[22:25], v[74:75], off
	s_waitcnt vmcnt(0)
	v_mul_f32_e32 v18, v22, v18
	v_mul_f32_e32 v19, v23, v19
	v_med3_f32 v18, v18, s9, v93
	v_med3_f32 v19, v19, s9, v93
	v_cvt_pk_fp8_f32 v26, v18, v19
	v_mul_f32_e32 v20, v24, v20
	v_mul_f32_e32 v21, v25, v21
	v_med3_f32 v20, v20, s9, v93
	v_med3_f32 v21, v21, s9, v93
	v_cvt_pk_fp8_f32 v26, v20, v21 op_sel:[0,0,1]
	global_store_dword v[84:85], v26, off offset:2816
	global_load_dwordx4 v[18:21], v[76:77], off
	s_waitcnt vmcnt(0)
	v_mul_f32_e32 v2, v18, v2
	v_mul_f32_e32 v3, v19, v3
	v_med3_f32 v2, v2, s9, v93
	v_med3_f32 v3, v3, s9, v93
	v_cvt_pk_fp8_f32 v22, v2, v3
	v_mul_f32_e32 v4, v20, v4
	v_mul_f32_e32 v5, v21, v5
	v_med3_f32 v4, v4, s9, v93
	v_med3_f32 v5, v5, s9, v93
	v_cvt_pk_fp8_f32 v22, v4, v5 op_sel:[0,0,1]
	global_store_dword v[84:85], v22, off offset:3072
	global_load_dwordx4 v[2:5], v[78:79], off
	s_waitcnt vmcnt(0)
	v_mul_f32_e32 v2, v2, v14
	v_mul_f32_e32 v3, v3, v15
	v_med3_f32 v2, v2, s9, v93
	v_med3_f32 v3, v3, s9, v93
	v_cvt_pk_fp8_f32 v18, v2, v3
	v_mul_f32_e32 v4, v4, v16
	v_mul_f32_e32 v5, v5, v17
	v_med3_f32 v4, v4, s9, v93
	v_med3_f32 v5, v5, s9, v93
	v_cvt_pk_fp8_f32 v18, v4, v5 op_sel:[0,0,1]
	global_store_dword v[84:85], v18, off offset:3328
	global_load_dwordx4 v[2:5], v[80:81], off
	s_waitcnt vmcnt(0)
	v_mul_f32_e32 v2, v2, v10
	v_mul_f32_e32 v3, v3, v11
	v_med3_f32 v2, v2, s9, v93
	v_med3_f32 v3, v3, s9, v93
	v_cvt_pk_fp8_f32 v14, v2, v3
	v_mul_f32_e32 v4, v4, v12
	v_mul_f32_e32 v5, v5, v13
	v_med3_f32 v4, v4, s9, v93
	v_med3_f32 v5, v5, s9, v93
	v_cvt_pk_fp8_f32 v14, v4, v5 op_sel:[0,0,1]
	global_store_dword v[84:85], v14, off offset:3584
	global_load_dwordx4 v[2:5], v[82:83], off
	s_waitcnt vmcnt(0)
	v_mul_f32_e32 v2, v2, v6
	v_mul_f32_e32 v3, v3, v7
	v_med3_f32 v2, v2, s9, v93
	v_med3_f32 v3, v3, s9, v93
	v_cvt_pk_fp8_f32 v10, v2, v3
	v_mul_f32_e32 v4, v4, v8
	v_mul_f32_e32 v2, v5, v9
	v_med3_f32 v3, v4, s9, v93
	v_med3_f32 v2, v2, s9, v93
	v_cvt_pk_fp8_f32 v10, v3, v2 op_sel:[0,0,1]
	global_store_dword v[84:85], v10, off offset:3840
	s_cbranch_scc0 .LBB0_48

; __device__ __forceinline__ unsigned pk4_fp8(float a, float b, float c, float d) {
;     a = fminf(fmaxf(a, -448.f), 448.f); b = fminf(fmaxf(b, -448.f), 448.f); c = fminf(fmaxf(c, -448.f), 448.f); d = fminf(fmaxf(d, -448.f), 448.f);
;     int w = 0; w = __builtin_amdgcn_cvt_pk_fp8_f32(a, b, w, false); w = __builtin_amdgcn_cvt_pk_fp8_f32(c, d, w, true); return (unsigned)w;
;     __device__ __forceinline__ void operator()(const f32x4 (&acc)[2][2][4][2], const Unit& u, int wr, int wc, int fr, int fq) const {
;     ...
;                     if (g == 1) {
;                         unsigned char* d8 = (unsigned char*)(QKV + (size_t)g * 4 * 16 * 4096 * 128) + ((((size_t)b * 16 + head) * 4096 + s) * 128 + (wc >> 1) * 64 + (fq & 1) * 32 + ((wc & 1) * 2 + (fq >> 1)) * 8);
;                         u32x2 w8; w8.x = pk4_fp8(v0[0] * 16.f, v0[1] * 16.f, v0[2] * 16.f, v0[3] * 16.f); w8.y = pk4_fp8(v1[0] * 16.f, v1[1] * 16.f, v1[2] * 16.f, v1[3] * 16.f);
;                         *(u32x2*)d8 = w8;
;                     } else if (g == 3 || g == 4) {
;                         unsigned char* d8 = (unsigned char*)(QKV + (size_t)g * 4 * 16 * 4096 * 128) + ((((size_t)b * 16 + head) * 4096 + s) * 128 + wc * 32 + 8 * fq);
;                         u32x2 w8; w8.x = pk4_fp8(v0[0] * 16.f, v0[1] * 16.f, v0[2] * 16.f, v0[3] * 16.f); w8.y = pk4_fp8(v1[0] * 16.f, v1[1] * 16.f, v1[2] * 16.f, v1[3] * 16.f);
;                         *(u32x2*)d8 = w8;
.LBB0_189:
	s_andn2_b64 vcc, exec, s[16:17]
	s_cbranch_vccnz .LBB0_191
	v_mul_f32_e32 v128, 0x41800000, v182
	v_mul_f32_e32 v129, 0x41800000, v183
	v_med3_f32 v180, v128, s69, v198
	v_med3_f32 v129, v129, s69, v198
	v_cvt_pk_fp8_f32 v128, v180, v129
	v_mul_f32_e32 v172, 0x41800000, v178
	v_mul_f32_e32 v173, 0x41800000, v179
	v_med3_f32 v172, v172, s69, v198
	v_med3_f32 v173, v173, s69, v198
	v_cvt_pk_fp8_f32 v128, v172, v173 op_sel:[0,0,1]
	v_mul_f32_e32 v129, 0x41800000, v174
	v_mul_f32_e32 v172, 0x41800000, v175
	v_med3_f32 v181, v129, s69, v198
	v_med3_f32 v172, v172, s69, v198
	v_cvt_pk_fp8_f32 v129, v181, v172
	s_lshl_b32 s16, s45, 1
	v_readlane_b32 s50, v253, 46
	v_mul_f32_e32 v173, 0x41800000, v170
	v_mul_f32_e32 v180, 0x41800000, v171
	v_readlane_b32 s51, v253, 47
	s_add_u32 s16, s50, s16
	v_lshl_add_u64 v[126:127], v[122:123], 0, s[28:29]
	v_med3_f32 v173, v173, s69, v198
	v_med3_f32 v180, v180, s69, v198
	s_addc_u32 s17, s51, 0
	v_lshlrev_b64 v[126:127], 7, v[126:127]
	v_cvt_pk_fp8_f32 v129, v173, v180 op_sel:[0,0,1]
	v_lshl_add_u64 v[126:127], s[16:17], 0, v[126:127]
	v_lshl_add_u64 v[126:127], v[126:127], 0, s[34:35]
	v_lshl_add_u64 v[126:127], v[126:127], 0, v[154:155]
	global_store_dwordx2 v[126:127], v[128:129], off

; __device__ __forceinline__ unsigned pk4_fp8(float a, float b, float c, float d) {
;     a = fminf(fmaxf(a, -448.f), 448.f); b = fminf(fmaxf(b, -448.f), 448.f); c = fminf(fmaxf(c, -448.f), 448.f); d = fminf(fmaxf(d, -448.f), 448.f);
;     int w = 0; w = __builtin_amdgcn_cvt_pk_fp8_f32(a, b, w, false); w = __builtin_amdgcn_cvt_pk_fp8_f32(c, d, w, true); return (unsigned)w;
;     __device__ __forceinline__ void operator()(const f32x4 (&acc)[2][2][4][2], const Unit& u, int wr, int wc, int fr, int fq) const {
;     ...
;                     if (g == 1) {
;                         unsigned char* d8 = (unsigned char*)(QKV + (size_t)g * 4 * 16 * 4096 * 128) + ((((size_t)b * 16 + head) * 4096 + s) * 128 + (wc >> 1) * 64 + (fq & 1) * 32 + ((wc & 1) * 2 + (fq >> 1)) * 8);
;                         u32x2 w8; w8.x = pk4_fp8(v0[0] * 16.f, v0[1] * 16.f, v0[2] * 16.f, v0[3] * 16.f); w8.y = pk4_fp8(v1[0] * 16.f, v1[1] * 16.f, v1[2] * 16.f, v1[3] * 16.f);
;                         *(u32x2*)d8 = w8;
;                     } else if (g == 3 || g == 4) {
;                         unsigned char* d8 = (unsigned char*)(QKV + (size_t)g * 4 * 16 * 4096 * 128) + ((((size_t)b * 16 + head) * 4096 + s) * 128 + wc * 32 + 8 * fq);
;                         u32x2 w8; w8.x = pk4_fp8(v0[0] * 16.f, v0[1] * 16.f, v0[2] * 16.f, v0[3] * 16.f); w8.y = pk4_fp8(v1[0] * 16.f, v1[1] * 16.f, v1[2] * 16.f, v1[3] * 16.f);
;                         *(u32x2*)d8 = w8;
.LBB0_192:
	s_andn2_b64 vcc, exec, s[16:17]
	s_cbranch_vccnz .LBB0_194
	v_mul_f32_e32 v128, 0x41800000, v182
	v_mul_f32_e32 v129, 0x41800000, v183
	v_med3_f32 v180, v128, s69, v198
	v_med3_f32 v129, v129, s69, v198
	v_cvt_pk_fp8_f32 v128, v180, v129
	v_mul_f32_e32 v172, 0x41800000, v178
	v_mul_f32_e32 v173, 0x41800000, v179
	v_med3_f32 v172, v172, s69, v198
	v_med3_f32 v173, v173, s69, v198
	v_cvt_pk_fp8_f32 v128, v172, v173 op_sel:[0,0,1]
	v_mul_f32_e32 v129, 0x41800000, v174
	v_mul_f32_e32 v172, 0x41800000, v175
	v_med3_f32 v181, v129, s69, v198
	v_med3_f32 v172, v172, s69, v198
	v_cvt_pk_fp8_f32 v129, v181, v172
	v_mul_f32_e32 v173, 0x41800000, v170
	v_mul_f32_e32 v180, 0x41800000, v171
	v_med3_f32 v173, v173, s69, v198
	v_med3_f32 v180, v180, s69, v198
	v_cvt_pk_fp8_f32 v129, v173, v180 op_sel:[0,0,1]
	v_lshl_add_u64 v[126:127], v[122:123], 0, s[28:29]
	v_lshlrev_b64 v[126:127], 7, v[126:127]
	v_lshl_add_u64 v[126:127], v[160:161], 0, v[126:127]
	global_store_dwordx2 v[126:127], v[128:129], off

; __device__ __forceinline__ unsigned pk4_fp8(float a, float b, float c, float d) {
;     a = fminf(fmaxf(a, -448.f), 448.f); b = fminf(fmaxf(b, -448.f), 448.f); c = fminf(fmaxf(c, -448.f), 448.f); d = fminf(fmaxf(d, -448.f), 448.f);
;     int w = 0; w = __builtin_amdgcn_cvt_pk_fp8_f32(a, b, w, false); w = __builtin_amdgcn_cvt_pk_fp8_f32(c, d, w, true); return (unsigned)w;
;     __device__ __forceinline__ void operator()(const f32x4 (&acc)[2][2][4][2], const Unit& u, int wr, int wc, int fr, int fq) const {
;     ...
;                     if (g == 1) {
;                         unsigned char* d8 = (unsigned char*)(QKV + (size_t)g * 4 * 16 * 4096 * 128) + ((((size_t)b * 16 + head) * 4096 + s) * 128 + (wc >> 1) * 64 + (fq & 1) * 32 + ((wc & 1) * 2 + (fq >> 1)) * 8);
;                         u32x2 w8; w8.x = pk4_fp8(v0[0] * 16.f, v0[1] * 16.f, v0[2] * 16.f, v0[3] * 16.f); w8.y = pk4_fp8(v1[0] * 16.f, v1[1] * 16.f, v1[2] * 16.f, v1[3] * 16.f);
;                         *(u32x2*)d8 = w8;
;                     } else if (g == 3 || g == 4) {
;                         unsigned char* d8 = (unsigned char*)(QKV + (size_t)g * 4 * 16 * 4096 * 128) + ((((size_t)b * 16 + head) * 4096 + s) * 128 + wc * 32 + 8 * fq);
;                         u32x2 w8; w8.x = pk4_fp8(v0[0] * 16.f, v0[1] * 16.f, v0[2] * 16.f, v0[3] * 16.f); w8.y = pk4_fp8(v1[0] * 16.f, v1[1] * 16.f, v1[2] * 16.f, v1[3] * 16.f);
;                         *(u32x2*)d8 = w8;
.LBB0_204:
	s_andn2_b64 vcc, exec, s[56:57]
	s_cbranch_vccnz .LBB0_206
	v_mul_f32_e32 v116, 0x41800000, v184
	v_mul_f32_e32 v117, 0x41800000, v185
	v_med3_f32 v120, v116, s69, v198
	v_med3_f32 v117, v117, s69, v198
	v_cvt_pk_fp8_f32 v116, v120, v117
	v_mul_f32_e32 v118, 0x41800000, v180
	v_mul_f32_e32 v119, 0x41800000, v181
	v_med3_f32 v118, v118, s69, v198
	v_med3_f32 v119, v119, s69, v198
	v_cvt_pk_fp8_f32 v116, v118, v119 op_sel:[0,0,1]
	v_mul_f32_e32 v117, 0x41800000, v176
	v_mul_f32_e32 v118, 0x41800000, v177
	v_med3_f32 v121, v117, s69, v198
	v_med3_f32 v118, v118, s69, v198
	v_cvt_pk_fp8_f32 v117, v121, v118
	s_lshl_b32 s56, s45, 1
	v_readlane_b32 s58, v253, 46
	v_mul_f32_e32 v119, 0x41800000, v172
	v_mul_f32_e32 v120, 0x41800000, v173
	v_readlane_b32 s59, v253, 47
	s_add_u32 s56, s58, s56
	v_lshl_add_u64 v[114:115], v[122:123], 0, s[50:51]
	v_med3_f32 v119, v119, s69, v198
	v_med3_f32 v120, v120, s69, v198
	s_addc_u32 s57, s59, 0
	v_lshlrev_b64 v[114:115], 7, v[114:115]
	v_cvt_pk_fp8_f32 v117, v119, v120 op_sel:[0,0,1]
	v_lshl_add_u64 v[114:115], s[56:57], 0, v[114:115]
	v_lshl_add_u64 v[114:115], v[114:115], 0, s[34:35]
	v_lshl_add_u64 v[114:115], v[114:115], 0, v[154:155]
	global_store_dwordx2 v[114:115], v[116:117], off

; __device__ __forceinline__ unsigned pk4_fp8(float a, float b, float c, float d) {
;     a = fminf(fmaxf(a, -448.f), 448.f); b = fminf(fmaxf(b, -448.f), 448.f); c = fminf(fmaxf(c, -448.f), 448.f); d = fminf(fmaxf(d, -448.f), 448.f);
;     int w = 0; w = __builtin_amdgcn_cvt_pk_fp8_f32(a, b, w, false); w = __builtin_amdgcn_cvt_pk_fp8_f32(c, d, w, true); return (unsigned)w;
;     __device__ __forceinline__ void operator()(const f32x4 (&acc)[2][2][4][2], const Unit& u, int wr, int wc, int fr, int fq) const {
;     ...
;                     if (g == 1) {
;                         unsigned char* d8 = (unsigned char*)(QKV + (size_t)g * 4 * 16 * 4096 * 128) + ((((size_t)b * 16 + head) * 4096 + s) * 128 + (wc >> 1) * 64 + (fq & 1) * 32 + ((wc & 1) * 2 + (fq >> 1)) * 8);
;                         u32x2 w8; w8.x = pk4_fp8(v0[0] * 16.f, v0[1] * 16.f, v0[2] * 16.f, v0[3] * 16.f); w8.y = pk4_fp8(v1[0] * 16.f, v1[1] * 16.f, v1[2] * 16.f, v1[3] * 16.f);
;                         *(u32x2*)d8 = w8;
;                     } else if (g == 3 || g == 4) {
;                         unsigned char* d8 = (unsigned char*)(QKV + (size_t)g * 4 * 16 * 4096 * 128) + ((((size_t)b * 16 + head) * 4096 + s) * 128 + wc * 32 + 8 * fq);
;                         u32x2 w8; w8.x = pk4_fp8(v0[0] * 16.f, v0[1] * 16.f, v0[2] * 16.f, v0[3] * 16.f); w8.y = pk4_fp8(v1[0] * 16.f, v1[1] * 16.f, v1[2] * 16.f, v1[3] * 16.f);
;                         *(u32x2*)d8 = w8;
.LBB0_207:
	s_andn2_b64 vcc, exec, s[58:59]
	s_cbranch_vccnz .LBB0_209
	v_mul_f32_e32 v116, 0x41800000, v184
	v_mul_f32_e32 v117, 0x41800000, v185
	v_med3_f32 v120, v116, s69, v198
	v_med3_f32 v117, v117, s69, v198
	v_cvt_pk_fp8_f32 v116, v120, v117
	v_mul_f32_e32 v118, 0x41800000, v180
	v_mul_f32_e32 v119, 0x41800000, v181
	v_med3_f32 v118, v118, s69, v198
	v_med3_f32 v119, v119, s69, v198
	v_cvt_pk_fp8_f32 v116, v118, v119 op_sel:[0,0,1]
	v_mul_f32_e32 v117, 0x41800000, v176
	v_mul_f32_e32 v118, 0x41800000, v177
	v_med3_f32 v121, v117, s69, v198
	v_med3_f32 v118, v118, s69, v198
	v_cvt_pk_fp8_f32 v117, v121, v118
	v_mul_f32_e32 v119, 0x41800000, v172
	v_mul_f32_e32 v120, 0x41800000, v173
	v_med3_f32 v119, v119, s69, v198
	v_med3_f32 v120, v120, s69, v198
	v_cvt_pk_fp8_f32 v117, v119, v120 op_sel:[0,0,1]
	v_lshl_add_u64 v[114:115], v[122:123], 0, s[50:51]
	v_lshlrev_b64 v[114:115], 7, v[114:115]
	v_lshl_add_u64 v[114:115], v[160:161], 0, v[114:115]
	global_store_dwordx2 v[114:115], v[116:117], off

; __device__ __forceinline__ unsigned pk4_fp8(float a, float b, float c, float d) {
;     a = fminf(fmaxf(a, -448.f), 448.f); b = fminf(fmaxf(b, -448.f), 448.f); c = fminf(fmaxf(c, -448.f), 448.f); d = fminf(fmaxf(d, -448.f), 448.f);
;     int w = 0; w = __builtin_amdgcn_cvt_pk_fp8_f32(a, b, w, false); w = __builtin_amdgcn_cvt_pk_fp8_f32(c, d, w, true); return (unsigned)w;
;     __device__ __forceinline__ void operator()(const f32x4 (&acc)[2][2][4][2], const Unit& u, int wr, int wc, int fr, int fq) const {
;     ...
;                     if (g == 1) {
;                         unsigned char* d8 = (unsigned char*)(QKV + (size_t)g * 4 * 16 * 4096 * 128) + ((((size_t)b * 16 + head) * 4096 + s) * 128 + (wc >> 1) * 64 + (fq & 1) * 32 + ((wc & 1) * 2 + (fq >> 1)) * 8);
;                         u32x2 w8; w8.x = pk4_fp8(v0[0] * 16.f, v0[1] * 16.f, v0[2] * 16.f, v0[3] * 16.f); w8.y = pk4_fp8(v1[0] * 16.f, v1[1] * 16.f, v1[2] * 16.f, v1[3] * 16.f);
;                         *(u32x2*)d8 = w8;
;                     } else if (g == 3 || g == 4) {
;                         unsigned char* d8 = (unsigned char*)(QKV + (size_t)g * 4 * 16 * 4096 * 128) + ((((size_t)b * 16 + head) * 4096 + s) * 128 + wc * 32 + 8 * fq);
;                         u32x2 w8; w8.x = pk4_fp8(v0[0] * 16.f, v0[1] * 16.f, v0[2] * 16.f, v0[3] * 16.f); w8.y = pk4_fp8(v1[0] * 16.f, v1[1] * 16.f, v1[2] * 16.f, v1[3] * 16.f);
;                         *(u32x2*)d8 = w8;
.LBB0_227:
	s_andn2_b64 vcc, exec, s[56:57]
	s_cbranch_vccnz .LBB0_229
	v_mul_f32_e32 v112, 0x41800000, v142
	v_mul_f32_e32 v113, 0x41800000, v143
	v_med3_f32 v140, v112, s69, v198
	v_med3_f32 v113, v113, s69, v198
	v_cvt_pk_fp8_f32 v112, v140, v113
	v_mul_f32_e32 v132, 0x41800000, v138
	v_mul_f32_e32 v133, 0x41800000, v139
	v_med3_f32 v132, v132, s69, v198
	v_med3_f32 v133, v133, s69, v198
	v_cvt_pk_fp8_f32 v112, v132, v133 op_sel:[0,0,1]
	v_mul_f32_e32 v113, 0x41800000, v134
	v_mul_f32_e32 v132, 0x41800000, v135
	v_med3_f32 v141, v113, s69, v198
	v_med3_f32 v132, v132, s69, v198
	v_cvt_pk_fp8_f32 v113, v141, v132
	s_lshl_b32 s56, s45, 1
	v_readlane_b32 s58, v253, 46
	v_mul_f32_e32 v133, 0x41800000, v130
	v_mul_f32_e32 v140, 0x41800000, v131
	v_readlane_b32 s59, v253, 47
	s_add_u32 s56, s58, s56
	v_lshl_add_u64 v[110:111], v[106:107], 0, s[28:29]
	v_med3_f32 v133, v133, s69, v198
	v_med3_f32 v140, v140, s69, v198
	s_addc_u32 s57, s59, 0
	v_lshlrev_b64 v[110:111], 7, v[110:111]
	v_cvt_pk_fp8_f32 v113, v133, v140 op_sel:[0,0,1]
	v_lshl_add_u64 v[110:111], s[56:57], 0, v[110:111]
	v_lshl_add_u64 v[110:111], v[110:111], 0, s[34:35]
	v_lshl_add_u64 v[110:111], v[110:111], 0, v[154:155]
	global_store_dwordx2 v[110:111], v[112:113], off

; __device__ __forceinline__ unsigned pk4_fp8(float a, float b, float c, float d) {
;     a = fminf(fmaxf(a, -448.f), 448.f); b = fminf(fmaxf(b, -448.f), 448.f); c = fminf(fmaxf(c, -448.f), 448.f); d = fminf(fmaxf(d, -448.f), 448.f);
;     int w = 0; w = __builtin_amdgcn_cvt_pk_fp8_f32(a, b, w, false); w = __builtin_amdgcn_cvt_pk_fp8_f32(c, d, w, true); return (unsigned)w;
;     __device__ __forceinline__ void operator()(const f32x4 (&acc)[2][2][4][2], const Unit& u, int wr, int wc, int fr, int fq) const {
;     ...
;                     if (g == 1) {
;                         unsigned char* d8 = (unsigned char*)(QKV + (size_t)g * 4 * 16 * 4096 * 128) + ((((size_t)b * 16 + head) * 4096 + s) * 128 + (wc >> 1) * 64 + (fq & 1) * 32 + ((wc & 1) * 2 + (fq >> 1)) * 8);
;                         u32x2 w8; w8.x = pk4_fp8(v0[0] * 16.f, v0[1] * 16.f, v0[2] * 16.f, v0[3] * 16.f); w8.y = pk4_fp8(v1[0] * 16.f, v1[1] * 16.f, v1[2] * 16.f, v1[3] * 16.f);
;                         *(u32x2*)d8 = w8;
;                     } else if (g == 3 || g == 4) {
;                         unsigned char* d8 = (unsigned char*)(QKV + (size_t)g * 4 * 16 * 4096 * 128) + ((((size_t)b * 16 + head) * 4096 + s) * 128 + wc * 32 + 8 * fq);
;                         u32x2 w8; w8.x = pk4_fp8(v0[0] * 16.f, v0[1] * 16.f, v0[2] * 16.f, v0[3] * 16.f); w8.y = pk4_fp8(v1[0] * 16.f, v1[1] * 16.f, v1[2] * 16.f, v1[3] * 16.f);
;                         *(u32x2*)d8 = w8;
.LBB0_230:
	s_andn2_b64 vcc, exec, s[56:57]
	s_cbranch_vccnz .LBB0_232
	v_mul_f32_e32 v112, 0x41800000, v142
	v_mul_f32_e32 v113, 0x41800000, v143
	v_med3_f32 v140, v112, s69, v198
	v_med3_f32 v113, v113, s69, v198
	v_cvt_pk_fp8_f32 v112, v140, v113
	v_mul_f32_e32 v132, 0x41800000, v138
	v_mul_f32_e32 v133, 0x41800000, v139
	v_med3_f32 v132, v132, s69, v198
	v_med3_f32 v133, v133, s69, v198
	v_cvt_pk_fp8_f32 v112, v132, v133 op_sel:[0,0,1]
	v_mul_f32_e32 v113, 0x41800000, v134
	v_mul_f32_e32 v132, 0x41800000, v135
	v_med3_f32 v141, v113, s69, v198
	v_med3_f32 v132, v132, s69, v198
	v_cvt_pk_fp8_f32 v113, v141, v132
	v_mul_f32_e32 v133, 0x41800000, v130
	v_mul_f32_e32 v140, 0x41800000, v131
	v_med3_f32 v133, v133, s69, v198
	v_med3_f32 v140, v140, s69, v198
	v_cvt_pk_fp8_f32 v113, v133, v140 op_sel:[0,0,1]
	v_lshl_add_u64 v[110:111], v[106:107], 0, s[28:29]
	v_lshlrev_b64 v[110:111], 7, v[110:111]
	v_lshl_add_u64 v[110:111], v[160:161], 0, v[110:111]
	global_store_dwordx2 v[110:111], v[112:113], off

; __device__ __forceinline__ unsigned pk4_fp8(float a, float b, float c, float d) {
;     a = fminf(fmaxf(a, -448.f), 448.f); b = fminf(fmaxf(b, -448.f), 448.f); c = fminf(fmaxf(c, -448.f), 448.f); d = fminf(fmaxf(d, -448.f), 448.f);
;     int w = 0; w = __builtin_amdgcn_cvt_pk_fp8_f32(a, b, w, false); w = __builtin_amdgcn_cvt_pk_fp8_f32(c, d, w, true); return (unsigned)w;
;     __device__ __forceinline__ void operator()(const f32x4 (&acc)[2][2][4][2], const Unit& u, int wr, int wc, int fr, int fq) const {
;     ...
;                     if (g == 1) {
;                         unsigned char* d8 = (unsigned char*)(QKV + (size_t)g * 4 * 16 * 4096 * 128) + ((((size_t)b * 16 + head) * 4096 + s) * 128 + (wc >> 1) * 64 + (fq & 1) * 32 + ((wc & 1) * 2 + (fq >> 1)) * 8);
;                         u32x2 w8; w8.x = pk4_fp8(v0[0] * 16.f, v0[1] * 16.f, v0[2] * 16.f, v0[3] * 16.f); w8.y = pk4_fp8(v1[0] * 16.f, v1[1] * 16.f, v1[2] * 16.f, v1[3] * 16.f);
;                         *(u32x2*)d8 = w8;
;                     } else if (g == 3 || g == 4) {
;                         unsigned char* d8 = (unsigned char*)(QKV + (size_t)g * 4 * 16 * 4096 * 128) + ((((size_t)b * 16 + head) * 4096 + s) * 128 + wc * 32 + 8 * fq);
;                         u32x2 w8; w8.x = pk4_fp8(v0[0] * 16.f, v0[1] * 16.f, v0[2] * 16.f, v0[3] * 16.f); w8.y = pk4_fp8(v1[0] * 16.f, v1[1] * 16.f, v1[2] * 16.f, v1[3] * 16.f);
;                         *(u32x2*)d8 = w8;
.LBB0_242:
	s_andn2_b64 vcc, exec, s[56:57]
	s_cbranch_vccnz .LBB0_244
	v_mul_f32_e32 v100, 0x41800000, v144
	v_mul_f32_e32 v101, 0x41800000, v145
	v_med3_f32 v104, v100, s69, v198
	v_med3_f32 v101, v101, s69, v198
	v_cvt_pk_fp8_f32 v100, v104, v101
	v_mul_f32_e32 v102, 0x41800000, v140
	v_mul_f32_e32 v103, 0x41800000, v141
	v_med3_f32 v102, v102, s69, v198
	v_med3_f32 v103, v103, s69, v198
	v_cvt_pk_fp8_f32 v100, v102, v103 op_sel:[0,0,1]
	v_mul_f32_e32 v101, 0x41800000, v136
	v_mul_f32_e32 v102, 0x41800000, v137
	v_med3_f32 v105, v101, s69, v198
	v_med3_f32 v102, v102, s69, v198
	v_cvt_pk_fp8_f32 v101, v105, v102
	s_lshl_b32 s56, s45, 1
	v_readlane_b32 s58, v253, 46
	v_mul_f32_e32 v103, 0x41800000, v132
	v_mul_f32_e32 v104, 0x41800000, v133
	v_readlane_b32 s59, v253, 47
	s_add_u32 s56, s58, s56
	v_lshl_add_u64 v[98:99], v[106:107], 0, s[50:51]
	v_med3_f32 v103, v103, s69, v198
	v_med3_f32 v104, v104, s69, v198
	s_addc_u32 s57, s59, 0
	v_lshlrev_b64 v[98:99], 7, v[98:99]
	v_cvt_pk_fp8_f32 v101, v103, v104 op_sel:[0,0,1]
	v_lshl_add_u64 v[98:99], s[56:57], 0, v[98:99]
	v_lshl_add_u64 v[98:99], v[98:99], 0, s[34:35]
	v_lshl_add_u64 v[98:99], v[98:99], 0, v[154:155]
	global_store_dwordx2 v[98:99], v[100:101], off

; __device__ __forceinline__ unsigned pk4_fp8(float a, float b, float c, float d) {
;     a = fminf(fmaxf(a, -448.f), 448.f); b = fminf(fmaxf(b, -448.f), 448.f); c = fminf(fmaxf(c, -448.f), 448.f); d = fminf(fmaxf(d, -448.f), 448.f);
;     int w = 0; w = __builtin_amdgcn_cvt_pk_fp8_f32(a, b, w, false); w = __builtin_amdgcn_cvt_pk_fp8_f32(c, d, w, true); return (unsigned)w;
;     __device__ __forceinline__ void operator()(const f32x4 (&acc)[2][2][4][2], const Unit& u, int wr, int wc, int fr, int fq) const {
;     ...
;                     if (g == 1) {
;                         unsigned char* d8 = (unsigned char*)(QKV + (size_t)g * 4 * 16 * 4096 * 128) + ((((size_t)b * 16 + head) * 4096 + s) * 128 + (wc >> 1) * 64 + (fq & 1) * 32 + ((wc & 1) * 2 + (fq >> 1)) * 8);
;                         u32x2 w8; w8.x = pk4_fp8(v0[0] * 16.f, v0[1] * 16.f, v0[2] * 16.f, v0[3] * 16.f); w8.y = pk4_fp8(v1[0] * 16.f, v1[1] * 16.f, v1[2] * 16.f, v1[3] * 16.f);
;                         *(u32x2*)d8 = w8;
;                     } else if (g == 3 || g == 4) {
;                         unsigned char* d8 = (unsigned char*)(QKV + (size_t)g * 4 * 16 * 4096 * 128) + ((((size_t)b * 16 + head) * 4096 + s) * 128 + wc * 32 + 8 * fq);
;                         u32x2 w8; w8.x = pk4_fp8(v0[0] * 16.f, v0[1] * 16.f, v0[2] * 16.f, v0[3] * 16.f); w8.y = pk4_fp8(v1[0] * 16.f, v1[1] * 16.f, v1[2] * 16.f, v1[3] * 16.f);
;                         *(u32x2*)d8 = w8;
.LBB0_245:
	s_andn2_b64 vcc, exec, s[56:57]
	s_cbranch_vccnz .LBB0_247
	v_mul_f32_e32 v100, 0x41800000, v144
	v_mul_f32_e32 v101, 0x41800000, v145
	v_med3_f32 v104, v100, s69, v198
	v_med3_f32 v101, v101, s69, v198
	v_cvt_pk_fp8_f32 v100, v104, v101
	v_mul_f32_e32 v102, 0x41800000, v140
	v_mul_f32_e32 v103, 0x41800000, v141
	v_med3_f32 v102, v102, s69, v198
	v_med3_f32 v103, v103, s69, v198
	v_cvt_pk_fp8_f32 v100, v102, v103 op_sel:[0,0,1]
	v_mul_f32_e32 v101, 0x41800000, v136
	v_mul_f32_e32 v102, 0x41800000, v137
	v_med3_f32 v105, v101, s69, v198
	v_med3_f32 v102, v102, s69, v198
	v_cvt_pk_fp8_f32 v101, v105, v102
	v_mul_f32_e32 v103, 0x41800000, v132
	v_mul_f32_e32 v104, 0x41800000, v133
	v_med3_f32 v103, v103, s69, v198
	v_med3_f32 v104, v104, s69, v198
	v_cvt_pk_fp8_f32 v101, v103, v104 op_sel:[0,0,1]
	v_lshl_add_u64 v[98:99], v[106:107], 0, s[50:51]
	v_lshlrev_b64 v[98:99], 7, v[98:99]
	v_lshl_add_u64 v[98:99], v[160:161], 0, v[98:99]
	global_store_dwordx2 v[98:99], v[100:101], off

; __device__ __forceinline__ unsigned pk4_fp8(float a, float b, float c, float d) {
;     a = fminf(fmaxf(a, -448.f), 448.f); b = fminf(fmaxf(b, -448.f), 448.f); c = fminf(fmaxf(c, -448.f), 448.f); d = fminf(fmaxf(d, -448.f), 448.f);
;     int w = 0; w = __builtin_amdgcn_cvt_pk_fp8_f32(a, b, w, false); w = __builtin_amdgcn_cvt_pk_fp8_f32(c, d, w, true); return (unsigned)w;
;     __device__ __forceinline__ void operator()(const f32x4 (&acc)[2][2][4][2], const Unit& u, int wr, int wc, int fr, int fq) const {
;     ...
;                     if (g == 1) {
;                         unsigned char* d8 = (unsigned char*)(QKV + (size_t)g * 4 * 16 * 4096 * 128) + ((((size_t)b * 16 + head) * 4096 + s) * 128 + (wc >> 1) * 64 + (fq & 1) * 32 + ((wc & 1) * 2 + (fq >> 1)) * 8);
;                         u32x2 w8; w8.x = pk4_fp8(v0[0] * 16.f, v0[1] * 16.f, v0[2] * 16.f, v0[3] * 16.f); w8.y = pk4_fp8(v1[0] * 16.f, v1[1] * 16.f, v1[2] * 16.f, v1[3] * 16.f);
;                         *(u32x2*)d8 = w8;
;                     } else if (g == 3 || g == 4) {
;                         unsigned char* d8 = (unsigned char*)(QKV + (size_t)g * 4 * 16 * 4096 * 128) + ((((size_t)b * 16 + head) * 4096 + s) * 128 + wc * 32 + 8 * fq);
;                         u32x2 w8; w8.x = pk4_fp8(v0[0] * 16.f, v0[1] * 16.f, v0[2] * 16.f, v0[3] * 16.f); w8.y = pk4_fp8(v1[0] * 16.f, v1[1] * 16.f, v1[2] * 16.f, v1[3] * 16.f);
;                         *(u32x2*)d8 = w8;
.LBB0_265:
	s_andn2_b64 vcc, exec, s[56:57]
	s_cbranch_vccnz .LBB0_267
	v_mul_f32_e32 v96, 0x41800000, v126
	v_mul_f32_e32 v97, 0x41800000, v127
	v_med3_f32 v124, v96, s69, v198
	v_med3_f32 v97, v97, s69, v198
	v_cvt_pk_fp8_f32 v96, v124, v97
	v_mul_f32_e32 v116, 0x41800000, v122
	v_mul_f32_e32 v117, 0x41800000, v123
	v_med3_f32 v116, v116, s69, v198
	v_med3_f32 v117, v117, s69, v198
	v_cvt_pk_fp8_f32 v96, v116, v117 op_sel:[0,0,1]
	v_mul_f32_e32 v97, 0x41800000, v118
	v_mul_f32_e32 v116, 0x41800000, v119
	v_med3_f32 v125, v97, s69, v198
	v_med3_f32 v116, v116, s69, v198
	v_cvt_pk_fp8_f32 v97, v125, v116
	s_lshl_b32 s56, s45, 1
	v_readlane_b32 s58, v253, 46
	v_mul_f32_e32 v117, 0x41800000, v114
	v_mul_f32_e32 v124, 0x41800000, v115
	v_readlane_b32 s59, v253, 47
	s_add_u32 s56, s58, s56
	v_lshl_add_u64 v[94:95], v[90:91], 0, s[28:29]
	v_med3_f32 v117, v117, s69, v198
	v_med3_f32 v124, v124, s69, v198
	s_addc_u32 s57, s59, 0
	v_lshlrev_b64 v[94:95], 7, v[94:95]
	v_cvt_pk_fp8_f32 v97, v117, v124 op_sel:[0,0,1]
	v_lshl_add_u64 v[94:95], s[56:57], 0, v[94:95]
	v_lshl_add_u64 v[94:95], v[94:95], 0, s[34:35]
	v_lshl_add_u64 v[94:95], v[94:95], 0, v[154:155]
	global_store_dwordx2 v[94:95], v[96:97], off

; __device__ __forceinline__ unsigned pk4_fp8(float a, float b, float c, float d) {
;     a = fminf(fmaxf(a, -448.f), 448.f); b = fminf(fmaxf(b, -448.f), 448.f); c = fminf(fmaxf(c, -448.f), 448.f); d = fminf(fmaxf(d, -448.f), 448.f);
;     int w = 0; w = __builtin_amdgcn_cvt_pk_fp8_f32(a, b, w, false); w = __builtin_amdgcn_cvt_pk_fp8_f32(c, d, w, true); return (unsigned)w;
;     __device__ __forceinline__ void operator()(const f32x4 (&acc)[2][2][4][2], const Unit& u, int wr, int wc, int fr, int fq) const {
;     ...
;                     if (g == 1) {
;                         unsigned char* d8 = (unsigned char*)(QKV + (size_t)g * 4 * 16 * 4096 * 128) + ((((size_t)b * 16 + head) * 4096 + s) * 128 + (wc >> 1) * 64 + (fq & 1) * 32 + ((wc & 1) * 2 + (fq >> 1)) * 8);
;                         u32x2 w8; w8.x = pk4_fp8(v0[0] * 16.f, v0[1] * 16.f, v0[2] * 16.f, v0[3] * 16.f); w8.y = pk4_fp8(v1[0] * 16.f, v1[1] * 16.f, v1[2] * 16.f, v1[3] * 16.f);
;                         *(u32x2*)d8 = w8;
;                     } else if (g == 3 || g == 4) {
;                         unsigned char* d8 = (unsigned char*)(QKV + (size_t)g * 4 * 16 * 4096 * 128) + ((((size_t)b * 16 + head) * 4096 + s) * 128 + wc * 32 + 8 * fq);
;                         u32x2 w8; w8.x = pk4_fp8(v0[0] * 16.f, v0[1] * 16.f, v0[2] * 16.f, v0[3] * 16.f); w8.y = pk4_fp8(v1[0] * 16.f, v1[1] * 16.f, v1[2] * 16.f, v1[3] * 16.f);
;                         *(u32x2*)d8 = w8;
.LBB0_268:
	s_andn2_b64 vcc, exec, s[56:57]
	s_cbranch_vccnz .LBB0_270
	v_mul_f32_e32 v96, 0x41800000, v126
	v_mul_f32_e32 v97, 0x41800000, v127
	v_med3_f32 v124, v96, s69, v198
	v_med3_f32 v97, v97, s69, v198
	v_cvt_pk_fp8_f32 v96, v124, v97
	v_mul_f32_e32 v116, 0x41800000, v122
	v_mul_f32_e32 v117, 0x41800000, v123
	v_med3_f32 v116, v116, s69, v198
	v_med3_f32 v117, v117, s69, v198
	v_cvt_pk_fp8_f32 v96, v116, v117 op_sel:[0,0,1]
	v_mul_f32_e32 v97, 0x41800000, v118
	v_mul_f32_e32 v116, 0x41800000, v119
	v_med3_f32 v125, v97, s69, v198
	v_med3_f32 v116, v116, s69, v198
	v_cvt_pk_fp8_f32 v97, v125, v116
	v_mul_f32_e32 v117, 0x41800000, v114
	v_mul_f32_e32 v124, 0x41800000, v115
	v_med3_f32 v117, v117, s69, v198
	v_med3_f32 v124, v124, s69, v198
	v_cvt_pk_fp8_f32 v97, v117, v124 op_sel:[0,0,1]
	v_lshl_add_u64 v[94:95], v[90:91], 0, s[28:29]
	v_lshlrev_b64 v[94:95], 7, v[94:95]
	v_lshl_add_u64 v[94:95], v[160:161], 0, v[94:95]
	global_store_dwordx2 v[94:95], v[96:97], off

; __device__ __forceinline__ unsigned pk4_fp8(float a, float b, float c, float d) {
;     a = fminf(fmaxf(a, -448.f), 448.f); b = fminf(fmaxf(b, -448.f), 448.f); c = fminf(fmaxf(c, -448.f), 448.f); d = fminf(fmaxf(d, -448.f), 448.f);
;     int w = 0; w = __builtin_amdgcn_cvt_pk_fp8_f32(a, b, w, false); w = __builtin_amdgcn_cvt_pk_fp8_f32(c, d, w, true); return (unsigned)w;
;     __device__ __forceinline__ void operator()(const f32x4 (&acc)[2][2][4][2], const Unit& u, int wr, int wc, int fr, int fq) const {
;     ...
;                     if (g == 1) {
;                         unsigned char* d8 = (unsigned char*)(QKV + (size_t)g * 4 * 16 * 4096 * 128) + ((((size_t)b * 16 + head) * 4096 + s) * 128 + (wc >> 1) * 64 + (fq & 1) * 32 + ((wc & 1) * 2 + (fq >> 1)) * 8);
;                         u32x2 w8; w8.x = pk4_fp8(v0[0] * 16.f, v0[1] * 16.f, v0[2] * 16.f, v0[3] * 16.f); w8.y = pk4_fp8(v1[0] * 16.f, v1[1] * 16.f, v1[2] * 16.f, v1[3] * 16.f);
;                         *(u32x2*)d8 = w8;
;                     } else if (g == 3 || g == 4) {
;                         unsigned char* d8 = (unsigned char*)(QKV + (size_t)g * 4 * 16 * 4096 * 128) + ((((size_t)b * 16 + head) * 4096 + s) * 128 + wc * 32 + 8 * fq);
;                         u32x2 w8; w8.x = pk4_fp8(v0[0] * 16.f, v0[1] * 16.f, v0[2] * 16.f, v0[3] * 16.f); w8.y = pk4_fp8(v1[0] * 16.f, v1[1] * 16.f, v1[2] * 16.f, v1[3] * 16.f);
;                         *(u32x2*)d8 = w8;
.LBB0_280:
	s_andn2_b64 vcc, exec, s[56:57]
	s_cbranch_vccnz .LBB0_282
	v_mul_f32_e32 v84, 0x41800000, v128
	v_mul_f32_e32 v85, 0x41800000, v129
	v_med3_f32 v88, v84, s69, v198
	v_med3_f32 v85, v85, s69, v198
	v_cvt_pk_fp8_f32 v84, v88, v85
	v_mul_f32_e32 v86, 0x41800000, v124
	v_mul_f32_e32 v87, 0x41800000, v125
	v_med3_f32 v86, v86, s69, v198
	v_med3_f32 v87, v87, s69, v198
	v_cvt_pk_fp8_f32 v84, v86, v87 op_sel:[0,0,1]
	v_mul_f32_e32 v85, 0x41800000, v120
	v_mul_f32_e32 v86, 0x41800000, v121
	v_med3_f32 v89, v85, s69, v198
	v_med3_f32 v86, v86, s69, v198
	v_cvt_pk_fp8_f32 v85, v89, v86
	s_lshl_b32 s56, s45, 1
	v_readlane_b32 s58, v253, 46
	v_mul_f32_e32 v87, 0x41800000, v116
	v_mul_f32_e32 v88, 0x41800000, v117
	v_readlane_b32 s59, v253, 47
	s_add_u32 s56, s58, s56
	v_lshl_add_u64 v[82:83], v[90:91], 0, s[50:51]
	v_med3_f32 v87, v87, s69, v198
	v_med3_f32 v88, v88, s69, v198
	s_addc_u32 s57, s59, 0
	v_lshlrev_b64 v[82:83], 7, v[82:83]
	v_cvt_pk_fp8_f32 v85, v87, v88 op_sel:[0,0,1]
	v_lshl_add_u64 v[82:83], s[56:57], 0, v[82:83]
	v_lshl_add_u64 v[82:83], v[82:83], 0, s[34:35]
	v_lshl_add_u64 v[82:83], v[82:83], 0, v[154:155]
	global_store_dwordx2 v[82:83], v[84:85], off

; __device__ __forceinline__ unsigned pk4_fp8(float a, float b, float c, float d) {
;     a = fminf(fmaxf(a, -448.f), 448.f); b = fminf(fmaxf(b, -448.f), 448.f); c = fminf(fmaxf(c, -448.f), 448.f); d = fminf(fmaxf(d, -448.f), 448.f);
;     int w = 0; w = __builtin_amdgcn_cvt_pk_fp8_f32(a, b, w, false); w = __builtin_amdgcn_cvt_pk_fp8_f32(c, d, w, true); return (unsigned)w;
;     __device__ __forceinline__ void operator()(const f32x4 (&acc)[2][2][4][2], const Unit& u, int wr, int wc, int fr, int fq) const {
;     ...
;                     if (g == 1) {
;                         unsigned char* d8 = (unsigned char*)(QKV + (size_t)g * 4 * 16 * 4096 * 128) + ((((size_t)b * 16 + head) * 4096 + s) * 128 + (wc >> 1) * 64 + (fq & 1) * 32 + ((wc & 1) * 2 + (fq >> 1)) * 8);
;                         u32x2 w8; w8.x = pk4_fp8(v0[0] * 16.f, v0[1] * 16.f, v0[2] * 16.f, v0[3] * 16.f); w8.y = pk4_fp8(v1[0] * 16.f, v1[1] * 16.f, v1[2] * 16.f, v1[3] * 16.f);
;                         *(u32x2*)d8 = w8;
;                     } else if (g == 3 || g == 4) {
;                         unsigned char* d8 = (unsigned char*)(QKV + (size_t)g * 4 * 16 * 4096 * 128) + ((((size_t)b * 16 + head) * 4096 + s) * 128 + wc * 32 + 8 * fq);
;                         u32x2 w8; w8.x = pk4_fp8(v0[0] * 16.f, v0[1] * 16.f, v0[2] * 16.f, v0[3] * 16.f); w8.y = pk4_fp8(v1[0] * 16.f, v1[1] * 16.f, v1[2] * 16.f, v1[3] * 16.f);
;                         *(u32x2*)d8 = w8;
.LBB0_283:
	s_andn2_b64 vcc, exec, s[56:57]
	s_cbranch_vccnz .LBB0_285
	v_mul_f32_e32 v84, 0x41800000, v128
	v_mul_f32_e32 v85, 0x41800000, v129
	v_med3_f32 v88, v84, s69, v198
	v_med3_f32 v85, v85, s69, v198
	v_cvt_pk_fp8_f32 v84, v88, v85
	v_mul_f32_e32 v86, 0x41800000, v124
	v_mul_f32_e32 v87, 0x41800000, v125
	v_med3_f32 v86, v86, s69, v198
	v_med3_f32 v87, v87, s69, v198
	v_cvt_pk_fp8_f32 v84, v86, v87 op_sel:[0,0,1]
	v_mul_f32_e32 v85, 0x41800000, v120
	v_mul_f32_e32 v86, 0x41800000, v121
	v_med3_f32 v89, v85, s69, v198
	v_med3_f32 v86, v86, s69, v198
	v_cvt_pk_fp8_f32 v85, v89, v86
	v_mul_f32_e32 v87, 0x41800000, v116
	v_mul_f32_e32 v88, 0x41800000, v117
	v_med3_f32 v87, v87, s69, v198
	v_med3_f32 v88, v88, s69, v198
	v_cvt_pk_fp8_f32 v85, v87, v88 op_sel:[0,0,1]
	v_lshl_add_u64 v[82:83], v[90:91], 0, s[50:51]
	v_lshlrev_b64 v[82:83], 7, v[82:83]
	v_lshl_add_u64 v[82:83], v[160:161], 0, v[82:83]
	global_store_dwordx2 v[82:83], v[84:85], off

; __device__ __forceinline__ unsigned pk4_fp8(float a, float b, float c, float d) {
;     a = fminf(fmaxf(a, -448.f), 448.f); b = fminf(fmaxf(b, -448.f), 448.f); c = fminf(fmaxf(c, -448.f), 448.f); d = fminf(fmaxf(d, -448.f), 448.f);
;     int w = 0; w = __builtin_amdgcn_cvt_pk_fp8_f32(a, b, w, false); w = __builtin_amdgcn_cvt_pk_fp8_f32(c, d, w, true); return (unsigned)w;
;     __device__ __forceinline__ void operator()(const f32x4 (&acc)[2][2][4][2], const Unit& u, int wr, int wc, int fr, int fq) const {
;     ...
;                     if (g == 1) {
;                         unsigned char* d8 = (unsigned char*)(QKV + (size_t)g * 4 * 16 * 4096 * 128) + ((((size_t)b * 16 + head) * 4096 + s) * 128 + (wc >> 1) * 64 + (fq & 1) * 32 + ((wc & 1) * 2 + (fq >> 1)) * 8);
;                         u32x2 w8; w8.x = pk4_fp8(v0[0] * 16.f, v0[1] * 16.f, v0[2] * 16.f, v0[3] * 16.f); w8.y = pk4_fp8(v1[0] * 16.f, v1[1] * 16.f, v1[2] * 16.f, v1[3] * 16.f);
;                         *(u32x2*)d8 = w8;
;                     } else if (g == 3 || g == 4) {
;                         unsigned char* d8 = (unsigned char*)(QKV + (size_t)g * 4 * 16 * 4096 * 128) + ((((size_t)b * 16 + head) * 4096 + s) * 128 + wc * 32 + 8 * fq);
;                         u32x2 w8; w8.x = pk4_fp8(v0[0] * 16.f, v0[1] * 16.f, v0[2] * 16.f, v0[3] * 16.f); w8.y = pk4_fp8(v1[0] * 16.f, v1[1] * 16.f, v1[2] * 16.f, v1[3] * 16.f);
;                         *(u32x2*)d8 = w8;
.LBB0_303:
	s_andn2_b64 vcc, exec, s[56:57]
	s_cbranch_vccnz .LBB0_305
	v_mul_f32_e32 v80, 0x41800000, v110
	v_mul_f32_e32 v81, 0x41800000, v111
	v_med3_f32 v108, v80, s69, v198
	v_med3_f32 v81, v81, s69, v198
	v_cvt_pk_fp8_f32 v80, v108, v81
	v_mul_f32_e32 v100, 0x41800000, v106
	v_mul_f32_e32 v101, 0x41800000, v107
	v_med3_f32 v100, v100, s69, v198
	v_med3_f32 v101, v101, s69, v198
	v_cvt_pk_fp8_f32 v80, v100, v101 op_sel:[0,0,1]
	v_mul_f32_e32 v81, 0x41800000, v102
	v_mul_f32_e32 v100, 0x41800000, v103
	v_med3_f32 v109, v81, s69, v198
	v_med3_f32 v100, v100, s69, v198
	v_cvt_pk_fp8_f32 v81, v109, v100
	s_lshl_b32 s56, s45, 1
	v_readlane_b32 s58, v253, 46
	v_mul_f32_e32 v101, 0x41800000, v98
	v_mul_f32_e32 v108, 0x41800000, v99
	v_readlane_b32 s59, v253, 47
	s_add_u32 s56, s58, s56
	v_lshl_add_u64 v[78:79], v[74:75], 0, s[28:29]
	v_med3_f32 v101, v101, s69, v198
	v_med3_f32 v108, v108, s69, v198
	s_addc_u32 s57, s59, 0
	v_lshlrev_b64 v[78:79], 7, v[78:79]
	v_cvt_pk_fp8_f32 v81, v101, v108 op_sel:[0,0,1]
	v_lshl_add_u64 v[78:79], s[56:57], 0, v[78:79]
	v_lshl_add_u64 v[78:79], v[78:79], 0, s[34:35]
	v_lshl_add_u64 v[78:79], v[78:79], 0, v[154:155]
	global_store_dwordx2 v[78:79], v[80:81], off

; __device__ __forceinline__ unsigned pk4_fp8(float a, float b, float c, float d) {
;     a = fminf(fmaxf(a, -448.f), 448.f); b = fminf(fmaxf(b, -448.f), 448.f); c = fminf(fmaxf(c, -448.f), 448.f); d = fminf(fmaxf(d, -448.f), 448.f);
;     int w = 0; w = __builtin_amdgcn_cvt_pk_fp8_f32(a, b, w, false); w = __builtin_amdgcn_cvt_pk_fp8_f32(c, d, w, true); return (unsigned)w;
;     __device__ __forceinline__ void operator()(const f32x4 (&acc)[2][2][4][2], const Unit& u, int wr, int wc, int fr, int fq) const {
;     ...
;                     if (g == 1) {
;                         unsigned char* d8 = (unsigned char*)(QKV + (size_t)g * 4 * 16 * 4096 * 128) + ((((size_t)b * 16 + head) * 4096 + s) * 128 + (wc >> 1) * 64 + (fq & 1) * 32 + ((wc & 1) * 2 + (fq >> 1)) * 8);
;                         u32x2 w8; w8.x = pk4_fp8(v0[0] * 16.f, v0[1] * 16.f, v0[2] * 16.f, v0[3] * 16.f); w8.y = pk4_fp8(v1[0] * 16.f, v1[1] * 16.f, v1[2] * 16.f, v1[3] * 16.f);
;                         *(u32x2*)d8 = w8;
;                     } else if (g == 3 || g == 4) {
;                         unsigned char* d8 = (unsigned char*)(QKV + (size_t)g * 4 * 16 * 4096 * 128) + ((((size_t)b * 16 + head) * 4096 + s) * 128 + wc * 32 + 8 * fq);
;                         u32x2 w8; w8.x = pk4_fp8(v0[0] * 16.f, v0[1] * 16.f, v0[2] * 16.f, v0[3] * 16.f); w8.y = pk4_fp8(v1[0] * 16.f, v1[1] * 16.f, v1[2] * 16.f, v1[3] * 16.f);
;                         *(u32x2*)d8 = w8;
.LBB0_306:
	s_andn2_b64 vcc, exec, s[56:57]
	s_cbranch_vccnz .LBB0_308
	v_mul_f32_e32 v80, 0x41800000, v110
	v_mul_f32_e32 v81, 0x41800000, v111
	v_med3_f32 v108, v80, s69, v198
	v_med3_f32 v81, v81, s69, v198
	v_cvt_pk_fp8_f32 v80, v108, v81
	v_mul_f32_e32 v100, 0x41800000, v106
	v_mul_f32_e32 v101, 0x41800000, v107
	v_med3_f32 v100, v100, s69, v198
	v_med3_f32 v101, v101, s69, v198
	v_cvt_pk_fp8_f32 v80, v100, v101 op_sel:[0,0,1]
	v_mul_f32_e32 v81, 0x41800000, v102
	v_mul_f32_e32 v100, 0x41800000, v103
	v_med3_f32 v109, v81, s69, v198
	v_med3_f32 v100, v100, s69, v198
	v_cvt_pk_fp8_f32 v81, v109, v100
	v_mul_f32_e32 v101, 0x41800000, v98
	v_mul_f32_e32 v108, 0x41800000, v99
	v_med3_f32 v101, v101, s69, v198
	v_med3_f32 v108, v108, s69, v198
	v_cvt_pk_fp8_f32 v81, v101, v108 op_sel:[0,0,1]
	v_lshl_add_u64 v[78:79], v[74:75], 0, s[28:29]
	v_lshlrev_b64 v[78:79], 7, v[78:79]
	v_lshl_add_u64 v[78:79], v[160:161], 0, v[78:79]
	global_store_dwordx2 v[78:79], v[80:81], off

; __device__ __forceinline__ unsigned pk4_fp8(float a, float b, float c, float d) {
;     a = fminf(fmaxf(a, -448.f), 448.f); b = fminf(fmaxf(b, -448.f), 448.f); c = fminf(fmaxf(c, -448.f), 448.f); d = fminf(fmaxf(d, -448.f), 448.f);
;     int w = 0; w = __builtin_amdgcn_cvt_pk_fp8_f32(a, b, w, false); w = __builtin_amdgcn_cvt_pk_fp8_f32(c, d, w, true); return (unsigned)w;
;     __device__ __forceinline__ void operator()(const f32x4 (&acc)[2][2][4][2], const Unit& u, int wr, int wc, int fr, int fq) const {
;     ...
;                     if (g == 1) {
;                         unsigned char* d8 = (unsigned char*)(QKV + (size_t)g * 4 * 16 * 4096 * 128) + ((((size_t)b * 16 + head) * 4096 + s) * 128 + (wc >> 1) * 64 + (fq & 1) * 32 + ((wc & 1) * 2 + (fq >> 1)) * 8);
;                         u32x2 w8; w8.x = pk4_fp8(v0[0] * 16.f, v0[1] * 16.f, v0[2] * 16.f, v0[3] * 16.f); w8.y = pk4_fp8(v1[0] * 16.f, v1[1] * 16.f, v1[2] * 16.f, v1[3] * 16.f);
;                         *(u32x2*)d8 = w8;
;                     } else if (g == 3 || g == 4) {
;                         unsigned char* d8 = (unsigned char*)(QKV + (size_t)g * 4 * 16 * 4096 * 128) + ((((size_t)b * 16 + head) * 4096 + s) * 128 + wc * 32 + 8 * fq);
;                         u32x2 w8; w8.x = pk4_fp8(v0[0] * 16.f, v0[1] * 16.f, v0[2] * 16.f, v0[3] * 16.f); w8.y = pk4_fp8(v1[0] * 16.f, v1[1] * 16.f, v1[2] * 16.f, v1[3] * 16.f);
;                         *(u32x2*)d8 = w8;
.LBB0_318:
	s_andn2_b64 vcc, exec, s[56:57]
	s_cbranch_vccnz .LBB0_320
	v_mul_f32_e32 v68, 0x41800000, v112
	v_mul_f32_e32 v69, 0x41800000, v113
	v_med3_f32 v72, v68, s69, v198
	v_med3_f32 v69, v69, s69, v198
	v_cvt_pk_fp8_f32 v68, v72, v69
	v_mul_f32_e32 v70, 0x41800000, v108
	v_mul_f32_e32 v71, 0x41800000, v109
	v_med3_f32 v70, v70, s69, v198
	v_med3_f32 v71, v71, s69, v198
	v_cvt_pk_fp8_f32 v68, v70, v71 op_sel:[0,0,1]
	v_mul_f32_e32 v69, 0x41800000, v104
	v_mul_f32_e32 v70, 0x41800000, v105
	v_med3_f32 v73, v69, s69, v198
	v_med3_f32 v70, v70, s69, v198
	v_cvt_pk_fp8_f32 v69, v73, v70
	s_lshl_b32 s56, s45, 1
	v_readlane_b32 s58, v253, 46
	v_mul_f32_e32 v71, 0x41800000, v100
	v_mul_f32_e32 v72, 0x41800000, v101
	v_readlane_b32 s59, v253, 47
	s_add_u32 s56, s58, s56
	v_lshl_add_u64 v[66:67], v[74:75], 0, s[50:51]
	v_med3_f32 v71, v71, s69, v198
	v_med3_f32 v72, v72, s69, v198
	s_addc_u32 s57, s59, 0
	v_lshlrev_b64 v[66:67], 7, v[66:67]
	v_cvt_pk_fp8_f32 v69, v71, v72 op_sel:[0,0,1]
	v_lshl_add_u64 v[66:67], s[56:57], 0, v[66:67]
	v_lshl_add_u64 v[66:67], v[66:67], 0, s[34:35]
	v_lshl_add_u64 v[66:67], v[66:67], 0, v[154:155]
	global_store_dwordx2 v[66:67], v[68:69], off

; __device__ __forceinline__ unsigned pk4_fp8(float a, float b, float c, float d) {
;     a = fminf(fmaxf(a, -448.f), 448.f); b = fminf(fmaxf(b, -448.f), 448.f); c = fminf(fmaxf(c, -448.f), 448.f); d = fminf(fmaxf(d, -448.f), 448.f);
;     int w = 0; w = __builtin_amdgcn_cvt_pk_fp8_f32(a, b, w, false); w = __builtin_amdgcn_cvt_pk_fp8_f32(c, d, w, true); return (unsigned)w;
;     __device__ __forceinline__ void operator()(const f32x4 (&acc)[2][2][4][2], const Unit& u, int wr, int wc, int fr, int fq) const {
;     ...
;                     if (g == 1) {
;                         unsigned char* d8 = (unsigned char*)(QKV + (size_t)g * 4 * 16 * 4096 * 128) + ((((size_t)b * 16 + head) * 4096 + s) * 128 + (wc >> 1) * 64 + (fq & 1) * 32 + ((wc & 1) * 2 + (fq >> 1)) * 8);
;                         u32x2 w8; w8.x = pk4_fp8(v0[0] * 16.f, v0[1] * 16.f, v0[2] * 16.f, v0[3] * 16.f); w8.y = pk4_fp8(v1[0] * 16.f, v1[1] * 16.f, v1[2] * 16.f, v1[3] * 16.f);
;                         *(u32x2*)d8 = w8;
;                     } else if (g == 3 || g == 4) {
;                         unsigned char* d8 = (unsigned char*)(QKV + (size_t)g * 4 * 16 * 4096 * 128) + ((((size_t)b * 16 + head) * 4096 + s) * 128 + wc * 32 + 8 * fq);
;                         u32x2 w8; w8.x = pk4_fp8(v0[0] * 16.f, v0[1] * 16.f, v0[2] * 16.f, v0[3] * 16.f); w8.y = pk4_fp8(v1[0] * 16.f, v1[1] * 16.f, v1[2] * 16.f, v1[3] * 16.f);
;                         *(u32x2*)d8 = w8;
.LBB0_321:
	s_andn2_b64 vcc, exec, s[56:57]
	s_cbranch_vccnz .LBB0_323
	v_mul_f32_e32 v68, 0x41800000, v112
	v_mul_f32_e32 v69, 0x41800000, v113
	v_med3_f32 v72, v68, s69, v198
	v_med3_f32 v69, v69, s69, v198
	v_cvt_pk_fp8_f32 v68, v72, v69
	v_mul_f32_e32 v70, 0x41800000, v108
	v_mul_f32_e32 v71, 0x41800000, v109
	v_med3_f32 v70, v70, s69, v198
	v_med3_f32 v71, v71, s69, v198
	v_cvt_pk_fp8_f32 v68, v70, v71 op_sel:[0,0,1]
	v_mul_f32_e32 v69, 0x41800000, v104
	v_mul_f32_e32 v70, 0x41800000, v105
	v_med3_f32 v73, v69, s69, v198
	v_med3_f32 v70, v70, s69, v198
	v_cvt_pk_fp8_f32 v69, v73, v70
	v_mul_f32_e32 v71, 0x41800000, v100
	v_mul_f32_e32 v72, 0x41800000, v101
	v_med3_f32 v71, v71, s69, v198
	v_med3_f32 v72, v72, s69, v198
	v_cvt_pk_fp8_f32 v69, v71, v72 op_sel:[0,0,1]
	v_lshl_add_u64 v[66:67], v[74:75], 0, s[50:51]
	v_lshlrev_b64 v[66:67], 7, v[66:67]
	v_lshl_add_u64 v[66:67], v[160:161], 0, v[66:67]
	global_store_dwordx2 v[66:67], v[68:69], off

; __device__ __forceinline__ unsigned pk4_fp8(float a, float b, float c, float d) {
;     a = fminf(fmaxf(a, -448.f), 448.f); b = fminf(fmaxf(b, -448.f), 448.f); c = fminf(fmaxf(c, -448.f), 448.f); d = fminf(fmaxf(d, -448.f), 448.f);
;     int w = 0; w = __builtin_amdgcn_cvt_pk_fp8_f32(a, b, w, false); w = __builtin_amdgcn_cvt_pk_fp8_f32(c, d, w, true); return (unsigned)w;
;     __device__ __forceinline__ void operator()(const f32x4 (&acc)[2][2][4][2], const Unit& u, int wr, int wc, int fr, int fq) const {
;     ...
;                     if (g == 1) {
;                         unsigned char* d8 = (unsigned char*)(QKV + (size_t)g * 4 * 16 * 4096 * 128) + ((((size_t)b * 16 + head) * 4096 + s) * 128 + (wc >> 1) * 64 + (fq & 1) * 32 + ((wc & 1) * 2 + (fq >> 1)) * 8);
;                         u32x2 w8; w8.x = pk4_fp8(v0[0] * 16.f, v0[1] * 16.f, v0[2] * 16.f, v0[3] * 16.f); w8.y = pk4_fp8(v1[0] * 16.f, v1[1] * 16.f, v1[2] * 16.f, v1[3] * 16.f);
;                         *(u32x2*)d8 = w8;
;                     } else if (g == 3 || g == 4) {
;                         unsigned char* d8 = (unsigned char*)(QKV + (size_t)g * 4 * 16 * 4096 * 128) + ((((size_t)b * 16 + head) * 4096 + s) * 128 + wc * 32 + 8 * fq);
;                         u32x2 w8; w8.x = pk4_fp8(v0[0] * 16.f, v0[1] * 16.f, v0[2] * 16.f, v0[3] * 16.f); w8.y = pk4_fp8(v1[0] * 16.f, v1[1] * 16.f, v1[2] * 16.f, v1[3] * 16.f);
;                         *(u32x2*)d8 = w8;
.LBB0_341:
	s_andn2_b64 vcc, exec, s[56:57]
	s_cbranch_vccnz .LBB0_343
	v_mul_f32_e32 v64, 0x41800000, v94
	v_mul_f32_e32 v65, 0x41800000, v95
	v_med3_f32 v92, v64, s69, v198
	v_med3_f32 v65, v65, s69, v198
	v_cvt_pk_fp8_f32 v64, v92, v65
	v_mul_f32_e32 v84, 0x41800000, v90
	v_mul_f32_e32 v85, 0x41800000, v91
	v_med3_f32 v84, v84, s69, v198
	v_med3_f32 v85, v85, s69, v198
	v_cvt_pk_fp8_f32 v64, v84, v85 op_sel:[0,0,1]
	v_mul_f32_e32 v65, 0x41800000, v86
	v_mul_f32_e32 v84, 0x41800000, v87
	v_med3_f32 v93, v65, s69, v198
	v_med3_f32 v84, v84, s69, v198
	v_cvt_pk_fp8_f32 v65, v93, v84
	s_lshl_b32 s56, s45, 1
	v_readlane_b32 s58, v253, 46
	v_mul_f32_e32 v85, 0x41800000, v82
	v_mul_f32_e32 v92, 0x41800000, v83
	v_readlane_b32 s59, v253, 47
	s_add_u32 s56, s58, s56
	v_lshl_add_u64 v[62:63], v[58:59], 0, s[28:29]
	v_med3_f32 v85, v85, s69, v198
	v_med3_f32 v92, v92, s69, v198
	s_addc_u32 s57, s59, 0
	v_lshlrev_b64 v[62:63], 7, v[62:63]
	v_cvt_pk_fp8_f32 v65, v85, v92 op_sel:[0,0,1]
	v_lshl_add_u64 v[62:63], s[56:57], 0, v[62:63]
	v_lshl_add_u64 v[62:63], v[62:63], 0, s[34:35]
	v_lshl_add_u64 v[62:63], v[62:63], 0, v[154:155]
	global_store_dwordx2 v[62:63], v[64:65], off

; __device__ __forceinline__ unsigned pk4_fp8(float a, float b, float c, float d) {
;     a = fminf(fmaxf(a, -448.f), 448.f); b = fminf(fmaxf(b, -448.f), 448.f); c = fminf(fmaxf(c, -448.f), 448.f); d = fminf(fmaxf(d, -448.f), 448.f);
;     int w = 0; w = __builtin_amdgcn_cvt_pk_fp8_f32(a, b, w, false); w = __builtin_amdgcn_cvt_pk_fp8_f32(c, d, w, true); return (unsigned)w;
;     __device__ __forceinline__ void operator()(const f32x4 (&acc)[2][2][4][2], const Unit& u, int wr, int wc, int fr, int fq) const {
;     ...
;                     if (g == 1) {
;                         unsigned char* d8 = (unsigned char*)(QKV + (size_t)g * 4 * 16 * 4096 * 128) + ((((size_t)b * 16 + head) * 4096 + s) * 128 + (wc >> 1) * 64 + (fq & 1) * 32 + ((wc & 1) * 2 + (fq >> 1)) * 8);
;                         u32x2 w8; w8.x = pk4_fp8(v0[0] * 16.f, v0[1] * 16.f, v0[2] * 16.f, v0[3] * 16.f); w8.y = pk4_fp8(v1[0] * 16.f, v1[1] * 16.f, v1[2] * 16.f, v1[3] * 16.f);
;                         *(u32x2*)d8 = w8;
;                     } else if (g == 3 || g == 4) {
;                         unsigned char* d8 = (unsigned char*)(QKV + (size_t)g * 4 * 16 * 4096 * 128) + ((((size_t)b * 16 + head) * 4096 + s) * 128 + wc * 32 + 8 * fq);
;                         u32x2 w8; w8.x = pk4_fp8(v0[0] * 16.f, v0[1] * 16.f, v0[2] * 16.f, v0[3] * 16.f); w8.y = pk4_fp8(v1[0] * 16.f, v1[1] * 16.f, v1[2] * 16.f, v1[3] * 16.f);
;                         *(u32x2*)d8 = w8;
.LBB0_344:
	s_andn2_b64 vcc, exec, s[56:57]
	s_cbranch_vccnz .LBB0_346
	v_mul_f32_e32 v64, 0x41800000, v94
	v_mul_f32_e32 v65, 0x41800000, v95
	v_med3_f32 v92, v64, s69, v198
	v_med3_f32 v65, v65, s69, v198
	v_cvt_pk_fp8_f32 v64, v92, v65
	v_mul_f32_e32 v84, 0x41800000, v90
	v_mul_f32_e32 v85, 0x41800000, v91
	v_med3_f32 v84, v84, s69, v198
	v_med3_f32 v85, v85, s69, v198
	v_cvt_pk_fp8_f32 v64, v84, v85 op_sel:[0,0,1]
	v_mul_f32_e32 v65, 0x41800000, v86
	v_mul_f32_e32 v84, 0x41800000, v87
	v_med3_f32 v93, v65, s69, v198
	v_med3_f32 v84, v84, s69, v198
	v_cvt_pk_fp8_f32 v65, v93, v84
	v_mul_f32_e32 v85, 0x41800000, v82
	v_mul_f32_e32 v92, 0x41800000, v83
	v_med3_f32 v85, v85, s69, v198
	v_med3_f32 v92, v92, s69, v198
	v_cvt_pk_fp8_f32 v65, v85, v92 op_sel:[0,0,1]
	v_lshl_add_u64 v[62:63], v[58:59], 0, s[28:29]
	v_lshlrev_b64 v[62:63], 7, v[62:63]
	v_lshl_add_u64 v[62:63], v[160:161], 0, v[62:63]
	global_store_dwordx2 v[62:63], v[64:65], off

; __device__ __forceinline__ unsigned pk4_fp8(float a, float b, float c, float d) {
;     a = fminf(fmaxf(a, -448.f), 448.f); b = fminf(fmaxf(b, -448.f), 448.f); c = fminf(fmaxf(c, -448.f), 448.f); d = fminf(fmaxf(d, -448.f), 448.f);
;     int w = 0; w = __builtin_amdgcn_cvt_pk_fp8_f32(a, b, w, false); w = __builtin_amdgcn_cvt_pk_fp8_f32(c, d, w, true); return (unsigned)w;
;     __device__ __forceinline__ void operator()(const f32x4 (&acc)[2][2][4][2], const Unit& u, int wr, int wc, int fr, int fq) const {
;     ...
;                     if (g == 1) {
;                         unsigned char* d8 = (unsigned char*)(QKV + (size_t)g * 4 * 16 * 4096 * 128) + ((((size_t)b * 16 + head) * 4096 + s) * 128 + (wc >> 1) * 64 + (fq & 1) * 32 + ((wc & 1) * 2 + (fq >> 1)) * 8);
;                         u32x2 w8; w8.x = pk4_fp8(v0[0] * 16.f, v0[1] * 16.f, v0[2] * 16.f, v0[3] * 16.f); w8.y = pk4_fp8(v1[0] * 16.f, v1[1] * 16.f, v1[2] * 16.f, v1[3] * 16.f);
;                         *(u32x2*)d8 = w8;
;                     } else if (g == 3 || g == 4) {
;                         unsigned char* d8 = (unsigned char*)(QKV + (size_t)g * 4 * 16 * 4096 * 128) + ((((size_t)b * 16 + head) * 4096 + s) * 128 + wc * 32 + 8 * fq);
;                         u32x2 w8; w8.x = pk4_fp8(v0[0] * 16.f, v0[1] * 16.f, v0[2] * 16.f, v0[3] * 16.f); w8.y = pk4_fp8(v1[0] * 16.f, v1[1] * 16.f, v1[2] * 16.f, v1[3] * 16.f);
;                         *(u32x2*)d8 = w8;
.LBB0_356:
	s_andn2_b64 vcc, exec, s[56:57]
	s_cbranch_vccnz .LBB0_358
	v_mul_f32_e32 v52, 0x41800000, v96
	v_mul_f32_e32 v53, 0x41800000, v97
	v_med3_f32 v56, v52, s69, v198
	v_med3_f32 v53, v53, s69, v198
	v_cvt_pk_fp8_f32 v52, v56, v53
	v_mul_f32_e32 v54, 0x41800000, v92
	v_mul_f32_e32 v55, 0x41800000, v93
	v_med3_f32 v54, v54, s69, v198
	v_med3_f32 v55, v55, s69, v198
	v_cvt_pk_fp8_f32 v52, v54, v55 op_sel:[0,0,1]
	v_mul_f32_e32 v53, 0x41800000, v88
	v_mul_f32_e32 v54, 0x41800000, v89
	v_med3_f32 v57, v53, s69, v198
	v_med3_f32 v54, v54, s69, v198
	v_cvt_pk_fp8_f32 v53, v57, v54
	s_lshl_b32 s56, s45, 1
	v_readlane_b32 s58, v253, 46
	v_mul_f32_e32 v55, 0x41800000, v84
	v_mul_f32_e32 v56, 0x41800000, v85
	v_readlane_b32 s59, v253, 47
	s_add_u32 s56, s58, s56
	v_lshl_add_u64 v[50:51], v[58:59], 0, s[50:51]
	v_med3_f32 v55, v55, s69, v198
	v_med3_f32 v56, v56, s69, v198
	s_addc_u32 s57, s59, 0
	v_lshlrev_b64 v[50:51], 7, v[50:51]
	v_cvt_pk_fp8_f32 v53, v55, v56 op_sel:[0,0,1]
	v_lshl_add_u64 v[50:51], s[56:57], 0, v[50:51]
	v_lshl_add_u64 v[50:51], v[50:51], 0, s[34:35]
	v_lshl_add_u64 v[50:51], v[50:51], 0, v[154:155]
	global_store_dwordx2 v[50:51], v[52:53], off

; __device__ __forceinline__ unsigned pk4_fp8(float a, float b, float c, float d) {
;     a = fminf(fmaxf(a, -448.f), 448.f); b = fminf(fmaxf(b, -448.f), 448.f); c = fminf(fmaxf(c, -448.f), 448.f); d = fminf(fmaxf(d, -448.f), 448.f);
;     int w = 0; w = __builtin_amdgcn_cvt_pk_fp8_f32(a, b, w, false); w = __builtin_amdgcn_cvt_pk_fp8_f32(c, d, w, true); return (unsigned)w;
;     __device__ __forceinline__ void operator()(const f32x4 (&acc)[2][2][4][2], const Unit& u, int wr, int wc, int fr, int fq) const {
;     ...
;                     if (g == 1) {
;                         unsigned char* d8 = (unsigned char*)(QKV + (size_t)g * 4 * 16 * 4096 * 128) + ((((size_t)b * 16 + head) * 4096 + s) * 128 + (wc >> 1) * 64 + (fq & 1) * 32 + ((wc & 1) * 2 + (fq >> 1)) * 8);
;                         u32x2 w8; w8.x = pk4_fp8(v0[0] * 16.f, v0[1] * 16.f, v0[2] * 16.f, v0[3] * 16.f); w8.y = pk4_fp8(v1[0] * 16.f, v1[1] * 16.f, v1[2] * 16.f, v1[3] * 16.f);
;                         *(u32x2*)d8 = w8;
;                     } else if (g == 3 || g == 4) {
;                         unsigned char* d8 = (unsigned char*)(QKV + (size_t)g * 4 * 16 * 4096 * 128) + ((((size_t)b * 16 + head) * 4096 + s) * 128 + wc * 32 + 8 * fq);
;                         u32x2 w8; w8.x = pk4_fp8(v0[0] * 16.f, v0[1] * 16.f, v0[2] * 16.f, v0[3] * 16.f); w8.y = pk4_fp8(v1[0] * 16.f, v1[1] * 16.f, v1[2] * 16.f, v1[3] * 16.f);
;                         *(u32x2*)d8 = w8;
.LBB0_359:
	s_andn2_b64 vcc, exec, s[56:57]
	s_cbranch_vccnz .LBB0_361
	v_mul_f32_e32 v52, 0x41800000, v96
	v_mul_f32_e32 v53, 0x41800000, v97
	v_med3_f32 v56, v52, s69, v198
	v_med3_f32 v53, v53, s69, v198
	v_cvt_pk_fp8_f32 v52, v56, v53
	v_mul_f32_e32 v54, 0x41800000, v92
	v_mul_f32_e32 v55, 0x41800000, v93
	v_med3_f32 v54, v54, s69, v198
	v_med3_f32 v55, v55, s69, v198
	v_cvt_pk_fp8_f32 v52, v54, v55 op_sel:[0,0,1]
	v_mul_f32_e32 v53, 0x41800000, v88
	v_mul_f32_e32 v54, 0x41800000, v89
	v_med3_f32 v57, v53, s69, v198
	v_med3_f32 v54, v54, s69, v198
	v_cvt_pk_fp8_f32 v53, v57, v54
	v_mul_f32_e32 v55, 0x41800000, v84
	v_mul_f32_e32 v56, 0x41800000, v85
	v_med3_f32 v55, v55, s69, v198
	v_med3_f32 v56, v56, s69, v198
	v_cvt_pk_fp8_f32 v53, v55, v56 op_sel:[0,0,1]
	v_lshl_add_u64 v[50:51], v[58:59], 0, s[50:51]
	v_lshlrev_b64 v[50:51], 7, v[50:51]
	v_lshl_add_u64 v[50:51], v[160:161], 0, v[50:51]
	global_store_dwordx2 v[50:51], v[52:53], off

; __device__ __forceinline__ unsigned pk4_fp8(float a, float b, float c, float d) {
;     a = fminf(fmaxf(a, -448.f), 448.f); b = fminf(fmaxf(b, -448.f), 448.f); c = fminf(fmaxf(c, -448.f), 448.f); d = fminf(fmaxf(d, -448.f), 448.f);
;     int w = 0; w = __builtin_amdgcn_cvt_pk_fp8_f32(a, b, w, false); w = __builtin_amdgcn_cvt_pk_fp8_f32(c, d, w, true); return (unsigned)w;
;     __device__ __forceinline__ void operator()(const f32x4 (&acc)[2][2][4][2], const Unit& u, int wr, int wc, int fr, int fq) const {
;     ...
;                     if (g == 1) {
;                         unsigned char* d8 = (unsigned char*)(QKV + (size_t)g * 4 * 16 * 4096 * 128) + ((((size_t)b * 16 + head) * 4096 + s) * 128 + (wc >> 1) * 64 + (fq & 1) * 32 + ((wc & 1) * 2 + (fq >> 1)) * 8);
;                         u32x2 w8; w8.x = pk4_fp8(v0[0] * 16.f, v0[1] * 16.f, v0[2] * 16.f, v0[3] * 16.f); w8.y = pk4_fp8(v1[0] * 16.f, v1[1] * 16.f, v1[2] * 16.f, v1[3] * 16.f);
;                         *(u32x2*)d8 = w8;
;                     } else if (g == 3 || g == 4) {
;                         unsigned char* d8 = (unsigned char*)(QKV + (size_t)g * 4 * 16 * 4096 * 128) + ((((size_t)b * 16 + head) * 4096 + s) * 128 + wc * 32 + 8 * fq);
;                         u32x2 w8; w8.x = pk4_fp8(v0[0] * 16.f, v0[1] * 16.f, v0[2] * 16.f, v0[3] * 16.f); w8.y = pk4_fp8(v1[0] * 16.f, v1[1] * 16.f, v1[2] * 16.f, v1[3] * 16.f);
;                         *(u32x2*)d8 = w8;
.LBB0_379:
	s_andn2_b64 vcc, exec, s[56:57]
	s_cbranch_vccnz .LBB0_381
	v_mul_f32_e32 v48, 0x41800000, v78
	v_mul_f32_e32 v49, 0x41800000, v79
	v_med3_f32 v76, v48, s69, v198
	v_med3_f32 v49, v49, s69, v198
	v_cvt_pk_fp8_f32 v48, v76, v49
	v_mul_f32_e32 v68, 0x41800000, v74
	v_mul_f32_e32 v69, 0x41800000, v75
	v_med3_f32 v68, v68, s69, v198
	v_med3_f32 v69, v69, s69, v198
	v_cvt_pk_fp8_f32 v48, v68, v69 op_sel:[0,0,1]
	v_mul_f32_e32 v49, 0x41800000, v70
	v_mul_f32_e32 v68, 0x41800000, v71
	v_med3_f32 v77, v49, s69, v198
	v_med3_f32 v68, v68, s69, v198
	v_cvt_pk_fp8_f32 v49, v77, v68
	s_lshl_b32 s56, s45, 1
	v_readlane_b32 s58, v253, 46
	v_mul_f32_e32 v69, 0x41800000, v66
	v_mul_f32_e32 v76, 0x41800000, v67
	v_readlane_b32 s59, v253, 47
	s_add_u32 s56, s58, s56
	v_lshl_add_u64 v[46:47], v[42:43], 0, s[28:29]
	v_med3_f32 v69, v69, s69, v198
	v_med3_f32 v76, v76, s69, v198
	s_addc_u32 s57, s59, 0
	v_lshlrev_b64 v[46:47], 7, v[46:47]
	v_cvt_pk_fp8_f32 v49, v69, v76 op_sel:[0,0,1]
	v_lshl_add_u64 v[46:47], s[56:57], 0, v[46:47]
	v_lshl_add_u64 v[46:47], v[46:47], 0, s[34:35]
	v_lshl_add_u64 v[46:47], v[46:47], 0, v[154:155]
	global_store_dwordx2 v[46:47], v[48:49], off

; __device__ __forceinline__ unsigned pk4_fp8(float a, float b, float c, float d) {
;     a = fminf(fmaxf(a, -448.f), 448.f); b = fminf(fmaxf(b, -448.f), 448.f); c = fminf(fmaxf(c, -448.f), 448.f); d = fminf(fmaxf(d, -448.f), 448.f);
;     int w = 0; w = __builtin_amdgcn_cvt_pk_fp8_f32(a, b, w, false); w = __builtin_amdgcn_cvt_pk_fp8_f32(c, d, w, true); return (unsigned)w;
;     __device__ __forceinline__ void operator()(const f32x4 (&acc)[2][2][4][2], const Unit& u, int wr, int wc, int fr, int fq) const {
;     ...
;                     if (g == 1) {
;                         unsigned char* d8 = (unsigned char*)(QKV + (size_t)g * 4 * 16 * 4096 * 128) + ((((size_t)b * 16 + head) * 4096 + s) * 128 + (wc >> 1) * 64 + (fq & 1) * 32 + ((wc & 1) * 2 + (fq >> 1)) * 8);
;                         u32x2 w8; w8.x = pk4_fp8(v0[0] * 16.f, v0[1] * 16.f, v0[2] * 16.f, v0[3] * 16.f); w8.y = pk4_fp8(v1[0] * 16.f, v1[1] * 16.f, v1[2] * 16.f, v1[3] * 16.f);
;                         *(u32x2*)d8 = w8;
;                     } else if (g == 3 || g == 4) {
;                         unsigned char* d8 = (unsigned char*)(QKV + (size_t)g * 4 * 16 * 4096 * 128) + ((((size_t)b * 16 + head) * 4096 + s) * 128 + wc * 32 + 8 * fq);
;                         u32x2 w8; w8.x = pk4_fp8(v0[0] * 16.f, v0[1] * 16.f, v0[2] * 16.f, v0[3] * 16.f); w8.y = pk4_fp8(v1[0] * 16.f, v1[1] * 16.f, v1[2] * 16.f, v1[3] * 16.f);
;                         *(u32x2*)d8 = w8;
.LBB0_382:
	s_andn2_b64 vcc, exec, s[56:57]
	s_cbranch_vccnz .LBB0_384
	v_mul_f32_e32 v48, 0x41800000, v78
	v_mul_f32_e32 v49, 0x41800000, v79
	v_med3_f32 v76, v48, s69, v198
	v_med3_f32 v49, v49, s69, v198
	v_cvt_pk_fp8_f32 v48, v76, v49
	v_mul_f32_e32 v68, 0x41800000, v74
	v_mul_f32_e32 v69, 0x41800000, v75
	v_med3_f32 v68, v68, s69, v198
	v_med3_f32 v69, v69, s69, v198
	v_cvt_pk_fp8_f32 v48, v68, v69 op_sel:[0,0,1]
	v_mul_f32_e32 v49, 0x41800000, v70
	v_mul_f32_e32 v68, 0x41800000, v71
	v_med3_f32 v77, v49, s69, v198
	v_med3_f32 v68, v68, s69, v198
	v_cvt_pk_fp8_f32 v49, v77, v68
	v_mul_f32_e32 v69, 0x41800000, v66
	v_mul_f32_e32 v76, 0x41800000, v67
	v_med3_f32 v69, v69, s69, v198
	v_med3_f32 v76, v76, s69, v198
	v_cvt_pk_fp8_f32 v49, v69, v76 op_sel:[0,0,1]
	v_lshl_add_u64 v[46:47], v[42:43], 0, s[28:29]
	v_lshlrev_b64 v[46:47], 7, v[46:47]
	v_lshl_add_u64 v[46:47], v[160:161], 0, v[46:47]
	global_store_dwordx2 v[46:47], v[48:49], off

; __device__ __forceinline__ unsigned pk4_fp8(float a, float b, float c, float d) {
;     a = fminf(fmaxf(a, -448.f), 448.f); b = fminf(fmaxf(b, -448.f), 448.f); c = fminf(fmaxf(c, -448.f), 448.f); d = fminf(fmaxf(d, -448.f), 448.f);
;     int w = 0; w = __builtin_amdgcn_cvt_pk_fp8_f32(a, b, w, false); w = __builtin_amdgcn_cvt_pk_fp8_f32(c, d, w, true); return (unsigned)w;
;     __device__ __forceinline__ void operator()(const f32x4 (&acc)[2][2][4][2], const Unit& u, int wr, int wc, int fr, int fq) const {
;     ...
;                     if (g == 1) {
;                         unsigned char* d8 = (unsigned char*)(QKV + (size_t)g * 4 * 16 * 4096 * 128) + ((((size_t)b * 16 + head) * 4096 + s) * 128 + (wc >> 1) * 64 + (fq & 1) * 32 + ((wc & 1) * 2 + (fq >> 1)) * 8);
;                         u32x2 w8; w8.x = pk4_fp8(v0[0] * 16.f, v0[1] * 16.f, v0[2] * 16.f, v0[3] * 16.f); w8.y = pk4_fp8(v1[0] * 16.f, v1[1] * 16.f, v1[2] * 16.f, v1[3] * 16.f);
;                         *(u32x2*)d8 = w8;
;                     } else if (g == 3 || g == 4) {
;                         unsigned char* d8 = (unsigned char*)(QKV + (size_t)g * 4 * 16 * 4096 * 128) + ((((size_t)b * 16 + head) * 4096 + s) * 128 + wc * 32 + 8 * fq);
;                         u32x2 w8; w8.x = pk4_fp8(v0[0] * 16.f, v0[1] * 16.f, v0[2] * 16.f, v0[3] * 16.f); w8.y = pk4_fp8(v1[0] * 16.f, v1[1] * 16.f, v1[2] * 16.f, v1[3] * 16.f);
;                         *(u32x2*)d8 = w8;
.LBB0_394:
	s_andn2_b64 vcc, exec, s[56:57]
	s_cbranch_vccnz .LBB0_396
	v_mul_f32_e32 v36, 0x41800000, v80
	v_mul_f32_e32 v37, 0x41800000, v81
	v_med3_f32 v40, v36, s69, v198
	v_med3_f32 v37, v37, s69, v198
	v_cvt_pk_fp8_f32 v36, v40, v37
	v_mul_f32_e32 v38, 0x41800000, v76
	v_mul_f32_e32 v39, 0x41800000, v77
	v_med3_f32 v38, v38, s69, v198
	v_med3_f32 v39, v39, s69, v198
	v_cvt_pk_fp8_f32 v36, v38, v39 op_sel:[0,0,1]
	v_mul_f32_e32 v37, 0x41800000, v72
	v_mul_f32_e32 v38, 0x41800000, v73
	v_med3_f32 v41, v37, s69, v198
	v_med3_f32 v38, v38, s69, v198
	v_cvt_pk_fp8_f32 v37, v41, v38
	s_lshl_b32 s56, s45, 1
	v_readlane_b32 s58, v253, 46
	v_mul_f32_e32 v39, 0x41800000, v68
	v_mul_f32_e32 v40, 0x41800000, v69
	v_readlane_b32 s59, v253, 47
	s_add_u32 s56, s58, s56
	v_lshl_add_u64 v[34:35], v[42:43], 0, s[50:51]
	v_med3_f32 v39, v39, s69, v198
	v_med3_f32 v40, v40, s69, v198
	s_addc_u32 s57, s59, 0
	v_lshlrev_b64 v[34:35], 7, v[34:35]
	v_cvt_pk_fp8_f32 v37, v39, v40 op_sel:[0,0,1]
	v_lshl_add_u64 v[34:35], s[56:57], 0, v[34:35]
	v_lshl_add_u64 v[34:35], v[34:35], 0, s[34:35]
	v_lshl_add_u64 v[34:35], v[34:35], 0, v[154:155]
	global_store_dwordx2 v[34:35], v[36:37], off

; __device__ __forceinline__ unsigned pk4_fp8(float a, float b, float c, float d) {
;     a = fminf(fmaxf(a, -448.f), 448.f); b = fminf(fmaxf(b, -448.f), 448.f); c = fminf(fmaxf(c, -448.f), 448.f); d = fminf(fmaxf(d, -448.f), 448.f);
;     int w = 0; w = __builtin_amdgcn_cvt_pk_fp8_f32(a, b, w, false); w = __builtin_amdgcn_cvt_pk_fp8_f32(c, d, w, true); return (unsigned)w;
;     __device__ __forceinline__ void operator()(const f32x4 (&acc)[2][2][4][2], const Unit& u, int wr, int wc, int fr, int fq) const {
;     ...
;                     if (g == 1) {
;                         unsigned char* d8 = (unsigned char*)(QKV + (size_t)g * 4 * 16 * 4096 * 128) + ((((size_t)b * 16 + head) * 4096 + s) * 128 + (wc >> 1) * 64 + (fq & 1) * 32 + ((wc & 1) * 2 + (fq >> 1)) * 8);
;                         u32x2 w8; w8.x = pk4_fp8(v0[0] * 16.f, v0[1] * 16.f, v0[2] * 16.f, v0[3] * 16.f); w8.y = pk4_fp8(v1[0] * 16.f, v1[1] * 16.f, v1[2] * 16.f, v1[3] * 16.f);
;                         *(u32x2*)d8 = w8;
;                     } else if (g == 3 || g == 4) {
;                         unsigned char* d8 = (unsigned char*)(QKV + (size_t)g * 4 * 16 * 4096 * 128) + ((((size_t)b * 16 + head) * 4096 + s) * 128 + wc * 32 + 8 * fq);
;                         u32x2 w8; w8.x = pk4_fp8(v0[0] * 16.f, v0[1] * 16.f, v0[2] * 16.f, v0[3] * 16.f); w8.y = pk4_fp8(v1[0] * 16.f, v1[1] * 16.f, v1[2] * 16.f, v1[3] * 16.f);
;                         *(u32x2*)d8 = w8;
.LBB0_397:
	s_andn2_b64 vcc, exec, s[56:57]
	s_cbranch_vccnz .LBB0_399
	v_mul_f32_e32 v36, 0x41800000, v80
	v_mul_f32_e32 v37, 0x41800000, v81
	v_med3_f32 v40, v36, s69, v198
	v_med3_f32 v37, v37, s69, v198
	v_cvt_pk_fp8_f32 v36, v40, v37
	v_mul_f32_e32 v38, 0x41800000, v76
	v_mul_f32_e32 v39, 0x41800000, v77
	v_med3_f32 v38, v38, s69, v198
	v_med3_f32 v39, v39, s69, v198
	v_cvt_pk_fp8_f32 v36, v38, v39 op_sel:[0,0,1]
	v_mul_f32_e32 v37, 0x41800000, v72
	v_mul_f32_e32 v38, 0x41800000, v73
	v_med3_f32 v41, v37, s69, v198
	v_med3_f32 v38, v38, s69, v198
	v_cvt_pk_fp8_f32 v37, v41, v38
	v_mul_f32_e32 v39, 0x41800000, v68
	v_mul_f32_e32 v40, 0x41800000, v69
	v_med3_f32 v39, v39, s69, v198
	v_med3_f32 v40, v40, s69, v198
	v_cvt_pk_fp8_f32 v37, v39, v40 op_sel:[0,0,1]
	v_lshl_add_u64 v[34:35], v[42:43], 0, s[50:51]
	v_lshlrev_b64 v[34:35], 7, v[34:35]
	v_lshl_add_u64 v[34:35], v[160:161], 0, v[34:35]
	global_store_dwordx2 v[34:35], v[36:37], off

; __device__ __forceinline__ unsigned pk4_fp8(float a, float b, float c, float d) {
;     a = fminf(fmaxf(a, -448.f), 448.f); b = fminf(fmaxf(b, -448.f), 448.f); c = fminf(fmaxf(c, -448.f), 448.f); d = fminf(fmaxf(d, -448.f), 448.f);
;     int w = 0; w = __builtin_amdgcn_cvt_pk_fp8_f32(a, b, w, false); w = __builtin_amdgcn_cvt_pk_fp8_f32(c, d, w, true); return (unsigned)w;
;     __device__ __forceinline__ void operator()(const f32x4 (&acc)[2][2][4][2], const Unit& u, int wr, int wc, int fr, int fq) const {
;     ...
;                     if (g == 1) {
;                         unsigned char* d8 = (unsigned char*)(QKV + (size_t)g * 4 * 16 * 4096 * 128) + ((((size_t)b * 16 + head) * 4096 + s) * 128 + (wc >> 1) * 64 + (fq & 1) * 32 + ((wc & 1) * 2 + (fq >> 1)) * 8);
;                         u32x2 w8; w8.x = pk4_fp8(v0[0] * 16.f, v0[1] * 16.f, v0[2] * 16.f, v0[3] * 16.f); w8.y = pk4_fp8(v1[0] * 16.f, v1[1] * 16.f, v1[2] * 16.f, v1[3] * 16.f);
;                         *(u32x2*)d8 = w8;
;                     } else if (g == 3 || g == 4) {
;                         unsigned char* d8 = (unsigned char*)(QKV + (size_t)g * 4 * 16 * 4096 * 128) + ((((size_t)b * 16 + head) * 4096 + s) * 128 + wc * 32 + 8 * fq);
;                         u32x2 w8; w8.x = pk4_fp8(v0[0] * 16.f, v0[1] * 16.f, v0[2] * 16.f, v0[3] * 16.f); w8.y = pk4_fp8(v1[0] * 16.f, v1[1] * 16.f, v1[2] * 16.f, v1[3] * 16.f);
;                         *(u32x2*)d8 = w8;
.LBB0_417:
	s_andn2_b64 vcc, exec, s[56:57]
	s_cbranch_vccnz .LBB0_419
	v_mul_f32_e32 v32, 0x41800000, v62
	v_mul_f32_e32 v33, 0x41800000, v63
	v_med3_f32 v60, v32, s69, v198
	v_med3_f32 v33, v33, s69, v198
	v_cvt_pk_fp8_f32 v32, v60, v33
	v_mul_f32_e32 v52, 0x41800000, v58
	v_mul_f32_e32 v53, 0x41800000, v59
	v_med3_f32 v52, v52, s69, v198
	v_med3_f32 v53, v53, s69, v198
	v_cvt_pk_fp8_f32 v32, v52, v53 op_sel:[0,0,1]
	v_mul_f32_e32 v33, 0x41800000, v54
	v_mul_f32_e32 v52, 0x41800000, v55
	v_med3_f32 v61, v33, s69, v198
	v_med3_f32 v52, v52, s69, v198
	v_cvt_pk_fp8_f32 v33, v61, v52
	s_lshl_b32 s56, s45, 1
	v_readlane_b32 s58, v253, 46
	v_mul_f32_e32 v53, 0x41800000, v50
	v_mul_f32_e32 v60, 0x41800000, v51
	v_readlane_b32 s59, v253, 47
	s_add_u32 s56, s58, s56
	v_lshl_add_u64 v[30:31], v[26:27], 0, s[28:29]
	v_med3_f32 v53, v53, s69, v198
	v_med3_f32 v60, v60, s69, v198
	s_addc_u32 s57, s59, 0
	v_lshlrev_b64 v[30:31], 7, v[30:31]
	v_cvt_pk_fp8_f32 v33, v53, v60 op_sel:[0,0,1]
	v_lshl_add_u64 v[30:31], s[56:57], 0, v[30:31]
	v_lshl_add_u64 v[30:31], v[30:31], 0, s[34:35]
	v_lshl_add_u64 v[30:31], v[30:31], 0, v[154:155]
	global_store_dwordx2 v[30:31], v[32:33], off

; __device__ __forceinline__ unsigned pk4_fp8(float a, float b, float c, float d) {
;     a = fminf(fmaxf(a, -448.f), 448.f); b = fminf(fmaxf(b, -448.f), 448.f); c = fminf(fmaxf(c, -448.f), 448.f); d = fminf(fmaxf(d, -448.f), 448.f);
;     int w = 0; w = __builtin_amdgcn_cvt_pk_fp8_f32(a, b, w, false); w = __builtin_amdgcn_cvt_pk_fp8_f32(c, d, w, true); return (unsigned)w;
; }
;     __device__ __forceinline__ void operator()(const f32x4 (&acc)[2][2][4][2], const Unit& u, int wr, int wc, int fr, int fq) const {
;     ...
;                     if (g == 1) {
;                         unsigned char* d8 = (unsigned char*)(QKV + (size_t)g * 4 * 16 * 4096 * 128) + ((((size_t)b * 16 + head) * 4096 + s) * 128 + (wc >> 1) * 64 + (fq & 1) * 32 + ((wc & 1) * 2 + (fq >> 1)) * 8);
;                         u32x2 w8; w8.x = pk4_fp8(v0[0] * 16.f, v0[1] * 16.f, v0[2] * 16.f, v0[3] * 16.f); w8.y = pk4_fp8(v1[0] * 16.f, v1[1] * 16.f, v1[2] * 16.f, v1[3] * 16.f);
;                         *(u32x2*)d8 = w8;
;                     } else if (g == 3 || g == 4) {
;                         unsigned char* d8 = (unsigned char*)(QKV + (size_t)g * 4 * 16 * 4096 * 128) + ((((size_t)b * 16 + head) * 4096 + s) * 128 + wc * 32 + 8 * fq);
;                         u32x2 w8; w8.x = pk4_fp8(v0[0] * 16.f, v0[1] * 16.f, v0[2] * 16.f, v0[3] * 16.f); w8.y = pk4_fp8(v1[0] * 16.f, v1[1] * 16.f, v1[2] * 16.f, v1[3] * 16.f);
;                         *(u32x2*)d8 = w8;
.LBB0_420:
	s_andn2_b64 vcc, exec, s[56:57]
	s_cbranch_vccnz .LBB0_422
	v_mul_f32_e32 v32, 0x41800000, v62
	v_mul_f32_e32 v33, 0x41800000, v63
	v_med3_f32 v60, v32, s69, v198
	v_med3_f32 v33, v33, s69, v198
	v_cvt_pk_fp8_f32 v32, v60, v33
	v_mul_f32_e32 v52, 0x41800000, v58
	v_mul_f32_e32 v53, 0x41800000, v59
	v_med3_f32 v52, v52, s69, v198
	v_med3_f32 v53, v53, s69, v198
	v_cvt_pk_fp8_f32 v32, v52, v53 op_sel:[0,0,1]
	v_mul_f32_e32 v33, 0x41800000, v54
	v_mul_f32_e32 v52, 0x41800000, v55
	v_med3_f32 v61, v33, s69, v198
	v_med3_f32 v52, v52, s69, v198
	v_cvt_pk_fp8_f32 v33, v61, v52
	v_mul_f32_e32 v53, 0x41800000, v50
	v_mul_f32_e32 v60, 0x41800000, v51
	v_med3_f32 v53, v53, s69, v198
	v_med3_f32 v60, v60, s69, v198
	v_cvt_pk_fp8_f32 v33, v53, v60 op_sel:[0,0,1]
	v_lshl_add_u64 v[30:31], v[26:27], 0, s[28:29]
	v_lshlrev_b64 v[30:31], 7, v[30:31]
	v_lshl_add_u64 v[30:31], v[160:161], 0, v[30:31]
	global_store_dwordx2 v[30:31], v[32:33], off

; __device__ __forceinline__ unsigned pk4_fp8(float a, float b, float c, float d) {
;     a = fminf(fmaxf(a, -448.f), 448.f); b = fminf(fmaxf(b, -448.f), 448.f); c = fminf(fmaxf(c, -448.f), 448.f); d = fminf(fmaxf(d, -448.f), 448.f);
;     int w = 0; w = __builtin_amdgcn_cvt_pk_fp8_f32(a, b, w, false); w = __builtin_amdgcn_cvt_pk_fp8_f32(c, d, w, true); return (unsigned)w;
; }
;     __device__ __forceinline__ void operator()(const f32x4 (&acc)[2][2][4][2], const Unit& u, int wr, int wc, int fr, int fq) const {
;     ...
;                     } else if (g == 3 || g == 4) {
;                         unsigned char* d8 = (unsigned char*)(QKV + (size_t)g * 4 * 16 * 4096 * 128) + ((((size_t)b * 16 + head) * 4096 + s) * 128 + wc * 32 + 8 * fq);
;                         u32x2 w8; w8.x = pk4_fp8(v0[0] * 16.f, v0[1] * 16.f, v0[2] * 16.f, v0[3] * 16.f); w8.y = pk4_fp8(v1[0] * 16.f, v1[1] * 16.f, v1[2] * 16.f, v1[3] * 16.f);
;                         *(u32x2*)d8 = w8;
.LBB0_432:
	s_andn2_b64 vcc, exec, s[56:57]
	s_cbranch_vccnz .LBB0_434
	v_mul_f32_e32 v20, 0x41800000, v64
	v_mul_f32_e32 v21, 0x41800000, v65
	v_med3_f32 v24, v20, s69, v198
	v_med3_f32 v21, v21, s69, v198
	v_cvt_pk_fp8_f32 v20, v24, v21
	v_mul_f32_e32 v22, 0x41800000, v60
	v_mul_f32_e32 v23, 0x41800000, v61
	v_med3_f32 v22, v22, s69, v198
	v_med3_f32 v23, v23, s69, v198
	v_cvt_pk_fp8_f32 v20, v22, v23 op_sel:[0,0,1]
	v_mul_f32_e32 v21, 0x41800000, v56
	v_mul_f32_e32 v22, 0x41800000, v57
	v_med3_f32 v25, v21, s69, v198
	v_med3_f32 v22, v22, s69, v198
	v_cvt_pk_fp8_f32 v21, v25, v22
	s_lshl_b32 s56, s45, 1
	v_readlane_b32 s58, v253, 46
	v_mul_f32_e32 v23, 0x41800000, v52
	v_mul_f32_e32 v24, 0x41800000, v53
	v_readlane_b32 s59, v253, 47
	s_add_u32 s56, s58, s56
	v_lshl_add_u64 v[18:19], v[26:27], 0, s[50:51]
	v_med3_f32 v23, v23, s69, v198
	v_med3_f32 v24, v24, s69, v198
	s_addc_u32 s57, s59, 0
	v_lshlrev_b64 v[18:19], 7, v[18:19]
	v_cvt_pk_fp8_f32 v21, v23, v24 op_sel:[0,0,1]
	v_lshl_add_u64 v[18:19], s[56:57], 0, v[18:19]
	v_lshl_add_u64 v[18:19], v[18:19], 0, s[34:35]
	v_lshl_add_u64 v[18:19], v[18:19], 0, v[154:155]
	global_store_dwordx2 v[18:19], v[20:21], off

; __device__ __forceinline__ unsigned pk4_fp8(float a, float b, float c, float d) {
;     a = fminf(fmaxf(a, -448.f), 448.f); b = fminf(fmaxf(b, -448.f), 448.f); c = fminf(fmaxf(c, -448.f), 448.f); d = fminf(fmaxf(d, -448.f), 448.f);
;     int w = 0; w = __builtin_amdgcn_cvt_pk_fp8_f32(a, b, w, false); w = __builtin_amdgcn_cvt_pk_fp8_f32(c, d, w, true); return (unsigned)w;
; }
;     __device__ __forceinline__ void operator()(const f32x4 (&acc)[2][2][4][2], const Unit& u, int wr, int wc, int fr, int fq) const {
;     ...
;                     if (g == 1) {
;                         unsigned char* d8 = (unsigned char*)(QKV + (size_t)g * 4 * 16 * 4096 * 128) + ((((size_t)b * 16 + head) * 4096 + s) * 128 + (wc >> 1) * 64 + (fq & 1) * 32 + ((wc & 1) * 2 + (fq >> 1)) * 8);
;                         u32x2 w8; w8.x = pk4_fp8(v0[0] * 16.f, v0[1] * 16.f, v0[2] * 16.f, v0[3] * 16.f); w8.y = pk4_fp8(v1[0] * 16.f, v1[1] * 16.f, v1[2] * 16.f, v1[3] * 16.f);
;                         *(u32x2*)d8 = w8;
;                     } else if (g == 3 || g == 4) {
;                         unsigned char* d8 = (unsigned char*)(QKV + (size_t)g * 4 * 16 * 4096 * 128) + ((((size_t)b * 16 + head) * 4096 + s) * 128 + wc * 32 + 8 * fq);
;                         u32x2 w8; w8.x = pk4_fp8(v0[0] * 16.f, v0[1] * 16.f, v0[2] * 16.f, v0[3] * 16.f); w8.y = pk4_fp8(v1[0] * 16.f, v1[1] * 16.f, v1[2] * 16.f, v1[3] * 16.f);
;                         *(u32x2*)d8 = w8;
.LBB0_435:
	s_andn2_b64 vcc, exec, s[56:57]
	s_cbranch_vccnz .LBB0_437
	v_mul_f32_e32 v20, 0x41800000, v64
	v_mul_f32_e32 v21, 0x41800000, v65
	v_med3_f32 v24, v20, s69, v198
	v_med3_f32 v21, v21, s69, v198
	v_cvt_pk_fp8_f32 v20, v24, v21
	v_mul_f32_e32 v22, 0x41800000, v60
	v_mul_f32_e32 v23, 0x41800000, v61
	v_med3_f32 v22, v22, s69, v198
	v_med3_f32 v23, v23, s69, v198
	v_cvt_pk_fp8_f32 v20, v22, v23 op_sel:[0,0,1]
	v_mul_f32_e32 v21, 0x41800000, v56
	v_mul_f32_e32 v22, 0x41800000, v57
	v_med3_f32 v25, v21, s69, v198
	v_med3_f32 v22, v22, s69, v198
	v_cvt_pk_fp8_f32 v21, v25, v22
	v_mul_f32_e32 v23, 0x41800000, v52
	v_mul_f32_e32 v24, 0x41800000, v53
	v_med3_f32 v23, v23, s69, v198
	v_med3_f32 v24, v24, s69, v198
	v_cvt_pk_fp8_f32 v21, v23, v24 op_sel:[0,0,1]
	v_lshl_add_u64 v[18:19], v[26:27], 0, s[50:51]
	v_lshlrev_b64 v[18:19], 7, v[18:19]
	v_lshl_add_u64 v[18:19], v[160:161], 0, v[18:19]
	global_store_dwordx2 v[18:19], v[20:21], off

; __device__ __forceinline__ unsigned pk4_fp8(float a, float b, float c, float d) {
;     a = fminf(fmaxf(a, -448.f), 448.f); b = fminf(fmaxf(b, -448.f), 448.f); c = fminf(fmaxf(c, -448.f), 448.f); d = fminf(fmaxf(d, -448.f), 448.f);
;     int w = 0; w = __builtin_amdgcn_cvt_pk_fp8_f32(a, b, w, false); w = __builtin_amdgcn_cvt_pk_fp8_f32(c, d, w, true); return (unsigned)w;
; }
;     __device__ __forceinline__ void operator()(const f32x4 (&acc)[2][2][4][2], const Unit& u, int wr, int wc, int fr, int fq) const {
;     ...
;                     } else if (g == 3 || g == 4) {
;                         unsigned char* d8 = (unsigned char*)(QKV + (size_t)g * 4 * 16 * 4096 * 128) + ((((size_t)b * 16 + head) * 4096 + s) * 128 + wc * 32 + 8 * fq);
;                         u32x2 w8; w8.x = pk4_fp8(v0[0] * 16.f, v0[1] * 16.f, v0[2] * 16.f, v0[3] * 16.f); w8.y = pk4_fp8(v1[0] * 16.f, v1[1] * 16.f, v1[2] * 16.f, v1[3] * 16.f);
;                         *(u32x2*)d8 = w8;
.LBB0_455:
	s_andn2_b64 vcc, exec, s[52:53]
	s_cbranch_vccnz .LBB0_457
	v_mul_f32_e32 v42, 0x41800000, v14
	v_mul_f32_e32 v43, 0x41800000, v15
	v_med3_f32 v46, v42, s69, v198
	v_med3_f32 v43, v43, s69, v198
	v_cvt_pk_fp8_f32 v42, v46, v43
	v_mul_f32_e32 v44, 0x41800000, v16
	v_mul_f32_e32 v45, 0x41800000, v17
	v_med3_f32 v44, v44, s69, v198
	v_med3_f32 v45, v45, s69, v198
	v_cvt_pk_fp8_f32 v42, v44, v45 op_sel:[0,0,1]
	v_mul_f32_e32 v43, 0x41800000, v10
	v_mul_f32_e32 v44, 0x41800000, v11
	v_med3_f32 v47, v43, s69, v198
	v_med3_f32 v44, v44, s69, v198
	v_cvt_pk_fp8_f32 v43, v47, v44
	s_lshl_b32 s52, s45, 1
	v_readlane_b32 s54, v253, 46
	v_mul_f32_e32 v45, 0x41800000, v12
	v_mul_f32_e32 v46, 0x41800000, v13
	v_readlane_b32 s55, v253, 47
	s_add_u32 s52, s54, s52
	v_lshl_add_u64 v[40:41], v[34:35], 0, s[28:29]
	v_med3_f32 v45, v45, s69, v198
	v_med3_f32 v46, v46, s69, v198
	s_addc_u32 s53, s55, 0
	v_lshlrev_b64 v[40:41], 7, v[40:41]
	v_cvt_pk_fp8_f32 v43, v45, v46 op_sel:[0,0,1]
	v_lshl_add_u64 v[40:41], s[52:53], 0, v[40:41]
	v_lshl_add_u64 v[40:41], v[40:41], 0, s[34:35]
	v_lshl_add_u64 v[40:41], v[40:41], 0, v[154:155]
	global_store_dwordx2 v[40:41], v[42:43], off

; __device__ __forceinline__ unsigned pk4_fp8(float a, float b, float c, float d) {
;     a = fminf(fmaxf(a, -448.f), 448.f); b = fminf(fmaxf(b, -448.f), 448.f); c = fminf(fmaxf(c, -448.f), 448.f); d = fminf(fmaxf(d, -448.f), 448.f);
;     int w = 0; w = __builtin_amdgcn_cvt_pk_fp8_f32(a, b, w, false); w = __builtin_amdgcn_cvt_pk_fp8_f32(c, d, w, true); return (unsigned)w;
; }
;     __device__ __forceinline__ void operator()(const f32x4 (&acc)[2][2][4][2], const Unit& u, int wr, int wc, int fr, int fq) const {
;     ...
;                     if (g == 1) {
;                         unsigned char* d8 = (unsigned char*)(QKV + (size_t)g * 4 * 16 * 4096 * 128) + ((((size_t)b * 16 + head) * 4096 + s) * 128 + (wc >> 1) * 64 + (fq & 1) * 32 + ((wc & 1) * 2 + (fq >> 1)) * 8);
;                         u32x2 w8; w8.x = pk4_fp8(v0[0] * 16.f, v0[1] * 16.f, v0[2] * 16.f, v0[3] * 16.f); w8.y = pk4_fp8(v1[0] * 16.f, v1[1] * 16.f, v1[2] * 16.f, v1[3] * 16.f);
;                         *(u32x2*)d8 = w8;
;                     } else if (g == 3 || g == 4) {
;                         unsigned char* d8 = (unsigned char*)(QKV + (size_t)g * 4 * 16 * 4096 * 128) + ((((size_t)b * 16 + head) * 4096 + s) * 128 + wc * 32 + 8 * fq);
;                         u32x2 w8; w8.x = pk4_fp8(v0[0] * 16.f, v0[1] * 16.f, v0[2] * 16.f, v0[3] * 16.f); w8.y = pk4_fp8(v1[0] * 16.f, v1[1] * 16.f, v1[2] * 16.f, v1[3] * 16.f);
;                         *(u32x2*)d8 = w8;
.LBB0_458:
	s_andn2_b64 vcc, exec, s[52:53]
	s_cbranch_vccnz .LBB0_460
	v_mul_f32_e32 v42, 0x41800000, v14
	v_mul_f32_e32 v43, 0x41800000, v15
	v_med3_f32 v46, v42, s69, v198
	v_med3_f32 v43, v43, s69, v198
	v_cvt_pk_fp8_f32 v42, v46, v43
	v_mul_f32_e32 v44, 0x41800000, v16
	v_mul_f32_e32 v45, 0x41800000, v17
	v_med3_f32 v44, v44, s69, v198
	v_med3_f32 v45, v45, s69, v198
	v_cvt_pk_fp8_f32 v42, v44, v45 op_sel:[0,0,1]
	v_mul_f32_e32 v43, 0x41800000, v10
	v_mul_f32_e32 v44, 0x41800000, v11
	v_med3_f32 v47, v43, s69, v198
	v_med3_f32 v44, v44, s69, v198
	v_cvt_pk_fp8_f32 v43, v47, v44
	v_mul_f32_e32 v45, 0x41800000, v12
	v_mul_f32_e32 v46, 0x41800000, v13
	v_med3_f32 v45, v45, s69, v198
	v_med3_f32 v46, v46, s69, v198
	v_cvt_pk_fp8_f32 v43, v45, v46 op_sel:[0,0,1]
	v_lshl_add_u64 v[40:41], v[34:35], 0, s[28:29]
	v_lshlrev_b64 v[40:41], 7, v[40:41]
	v_lshl_add_u64 v[40:41], v[160:161], 0, v[40:41]
	global_store_dwordx2 v[40:41], v[42:43], off

; __device__ __forceinline__ unsigned pk4_fp8(float a, float b, float c, float d) {
;     a = fminf(fmaxf(a, -448.f), 448.f); b = fminf(fmaxf(b, -448.f), 448.f); c = fminf(fmaxf(c, -448.f), 448.f); d = fminf(fmaxf(d, -448.f), 448.f);
;     int w = 0; w = __builtin_amdgcn_cvt_pk_fp8_f32(a, b, w, false); w = __builtin_amdgcn_cvt_pk_fp8_f32(c, d, w, true); return (unsigned)w;
; }
;     __device__ __forceinline__ void operator()(const f32x4 (&acc)[2][2][4][2], const Unit& u, int wr, int wc, int fr, int fq) const {
;     ...
;                     } else if (g == 3 || g == 4) {
;                         unsigned char* d8 = (unsigned char*)(QKV + (size_t)g * 4 * 16 * 4096 * 128) + ((((size_t)b * 16 + head) * 4096 + s) * 128 + wc * 32 + 8 * fq);
;                         u32x2 w8; w8.x = pk4_fp8(v0[0] * 16.f, v0[1] * 16.f, v0[2] * 16.f, v0[3] * 16.f); w8.y = pk4_fp8(v1[0] * 16.f, v1[1] * 16.f, v1[2] * 16.f, v1[3] * 16.f);
;                         *(u32x2*)d8 = w8;
.LBB0_473:
	s_andn2_b64 vcc, exec, s[12:13]
	s_cbranch_vccnz .LBB0_475
	v_mul_f32_e32 v20, 0x41800000, v6
	v_mul_f32_e32 v21, 0x41800000, v7
	v_med3_f32 v24, v20, s69, v198
	v_med3_f32 v21, v21, s69, v198
	v_cvt_pk_fp8_f32 v20, v24, v21
	v_mul_f32_e32 v22, 0x41800000, v8
	v_mul_f32_e32 v23, 0x41800000, v9
	v_med3_f32 v22, v22, s69, v198
	v_med3_f32 v23, v23, s69, v198
	v_cvt_pk_fp8_f32 v20, v22, v23 op_sel:[0,0,1]
	v_mul_f32_e32 v21, 0x41800000, v2
	v_mul_f32_e32 v22, 0x41800000, v3
	v_med3_f32 v25, v21, s69, v198
	v_med3_f32 v22, v22, s69, v198
	v_cvt_pk_fp8_f32 v21, v25, v22
	s_lshl_b32 s12, s45, 1
	v_readlane_b32 s14, v253, 46
	v_mul_f32_e32 v23, 0x41800000, v4
	v_mul_f32_e32 v24, 0x41800000, v5
	v_readlane_b32 s15, v253, 47
	s_add_u32 s12, s14, s12
	v_lshl_add_u64 v[18:19], v[34:35], 0, s[50:51]
	v_med3_f32 v23, v23, s69, v198
	v_med3_f32 v24, v24, s69, v198
	s_addc_u32 s13, s15, 0
	v_lshlrev_b64 v[18:19], 7, v[18:19]
	v_cvt_pk_fp8_f32 v21, v23, v24 op_sel:[0,0,1]
	v_lshl_add_u64 v[18:19], s[12:13], 0, v[18:19]
	v_lshl_add_u64 v[18:19], v[18:19], 0, s[34:35]
	v_lshl_add_u64 v[18:19], v[18:19], 0, v[154:155]
	global_store_dwordx2 v[18:19], v[20:21], off

; __device__ __forceinline__ unsigned pk4_fp8(float a, float b, float c, float d) {
;     a = fminf(fmaxf(a, -448.f), 448.f); b = fminf(fmaxf(b, -448.f), 448.f); c = fminf(fmaxf(c, -448.f), 448.f); d = fminf(fmaxf(d, -448.f), 448.f);
;     int w = 0; w = __builtin_amdgcn_cvt_pk_fp8_f32(a, b, w, false); w = __builtin_amdgcn_cvt_pk_fp8_f32(c, d, w, true); return (unsigned)w;
; }
;     __device__ __forceinline__ void operator()(const f32x4 (&acc)[2][2][4][2], const Unit& u, int wr, int wc, int fr, int fq) const {
;     ...
;                     if (g == 1) {
;                         unsigned char* d8 = (unsigned char*)(QKV + (size_t)g * 4 * 16 * 4096 * 128) + ((((size_t)b * 16 + head) * 4096 + s) * 128 + (wc >> 1) * 64 + (fq & 1) * 32 + ((wc & 1) * 2 + (fq >> 1)) * 8);
;                         u32x2 w8; w8.x = pk4_fp8(v0[0] * 16.f, v0[1] * 16.f, v0[2] * 16.f, v0[3] * 16.f); w8.y = pk4_fp8(v1[0] * 16.f, v1[1] * 16.f, v1[2] * 16.f, v1[3] * 16.f);
;                         *(u32x2*)d8 = w8;
;                     } else if (g == 3 || g == 4) {
;                         unsigned char* d8 = (unsigned char*)(QKV + (size_t)g * 4 * 16 * 4096 * 128) + ((((size_t)b * 16 + head) * 4096 + s) * 128 + wc * 32 + 8 * fq);
;                         u32x2 w8; w8.x = pk4_fp8(v0[0] * 16.f, v0[1] * 16.f, v0[2] * 16.f, v0[3] * 16.f); w8.y = pk4_fp8(v1[0] * 16.f, v1[1] * 16.f, v1[2] * 16.f, v1[3] * 16.f);
;                         *(u32x2*)d8 = w8;
.LBB0_476:
	v_mul_f32_e32 v20, 0x41800000, v6
	v_mul_f32_e32 v21, 0x41800000, v7
	v_med3_f32 v24, v20, s69, v198
	v_med3_f32 v21, v21, s69, v198
	v_cvt_pk_fp8_f32 v20, v24, v21
	v_mul_f32_e32 v22, 0x41800000, v8
	v_mul_f32_e32 v23, 0x41800000, v9
	v_med3_f32 v22, v22, s69, v198
	v_med3_f32 v23, v23, s69, v198
	v_cvt_pk_fp8_f32 v20, v22, v23 op_sel:[0,0,1]
	v_mul_f32_e32 v21, 0x41800000, v2
	v_mul_f32_e32 v22, 0x41800000, v3
	v_med3_f32 v25, v21, s69, v198
	v_med3_f32 v22, v22, s69, v198
	v_cvt_pk_fp8_f32 v21, v25, v22
	v_mul_f32_e32 v23, 0x41800000, v4
	v_mul_f32_e32 v24, 0x41800000, v5
	v_med3_f32 v23, v23, s69, v198
	v_med3_f32 v24, v24, s69, v198
	v_cvt_pk_fp8_f32 v21, v23, v24 op_sel:[0,0,1]
	v_lshl_add_u64 v[18:19], v[34:35], 0, s[50:51]
	v_lshlrev_b64 v[18:19], 7, v[18:19]
	v_lshl_add_u64 v[18:19], v[160:161], 0, v[18:19]
	global_store_dwordx2 v[18:19], v[20:21], off
	s_and_b64 vcc, exec, s[10:11]
	s_cbranch_vccz .LBB0_470

; __device__ __forceinline__ unsigned pk4_fp8(float a, float b, float c, float d) {
;     a = fminf(fmaxf(a, -448.f), 448.f); b = fminf(fmaxf(b, -448.f), 448.f); c = fminf(fmaxf(c, -448.f), 448.f); d = fminf(fmaxf(d, -448.f), 448.f);
;     int w = 0; w = __builtin_amdgcn_cvt_pk_fp8_f32(a, b, w, false); w = __builtin_amdgcn_cvt_pk_fp8_f32(c, d, w, true); return (unsigned)w;
; }
;     __device__ __forceinline__ void operator()(const f32x4 (&acc)[2][2][4][2], const Unit& u, int wr, int wc, int fr, int fq) const {
;     ...
;                     } else if (g == 3 || g == 4) {
;                         unsigned char* d8 = (unsigned char*)(QKV + (size_t)g * 4 * 16 * 4096 * 128) + ((((size_t)b * 16 + head) * 4096 + s) * 128 + wc * 32 + 8 * fq);
;                         u32x2 w8; w8.x = pk4_fp8(v0[0] * 16.f, v0[1] * 16.f, v0[2] * 16.f, v0[3] * 16.f); w8.y = pk4_fp8(v1[0] * 16.f, v1[1] * 16.f, v1[2] * 16.f, v1[3] * 16.f);
;                         *(u32x2*)d8 = w8;
.LBB0_555:
	s_andn2_b64 vcc, exec, s[14:15]
	s_cbranch_vccnz .LBB0_557
	v_mul_f32_e32 v28, 0x41800000, v30
	v_mul_f32_e32 v29, 0x41800000, v31
	v_med3_f32 v158, v28, s67, v206
	v_med3_f32 v29, v29, s67, v206
	v_cvt_pk_fp8_f32 v28, v158, v29
	v_mul_f32_e32 v32, 0x41800000, v26
	v_mul_f32_e32 v33, 0x41800000, v27
	v_med3_f32 v32, v32, s67, v206
	v_med3_f32 v33, v33, s67, v206
	v_cvt_pk_fp8_f32 v28, v32, v33 op_sel:[0,0,1]
	v_mul_f32_e32 v29, 0x41800000, v22
	v_mul_f32_e32 v32, 0x41800000, v23
	v_med3_f32 v159, v29, s67, v206
	v_med3_f32 v32, v32, s67, v206
	v_cvt_pk_fp8_f32 v29, v159, v32
	s_lshl_b32 s14, s41, 1
	v_readlane_b32 s46, v253, 46
	v_mul_f32_e32 v33, 0x41800000, v18
	v_mul_f32_e32 v158, 0x41800000, v19
	v_readlane_b32 s47, v253, 47
	s_add_u32 s14, s46, s14
	v_lshl_add_u64 v[20:21], v[154:155], 0, s[24:25]
	v_med3_f32 v33, v33, s67, v206
	v_med3_f32 v158, v158, s67, v206
	s_addc_u32 s15, s47, 0
	v_lshlrev_b64 v[20:21], 7, v[20:21]
	v_cvt_pk_fp8_f32 v29, v33, v158 op_sel:[0,0,1]
	v_lshl_add_u64 v[20:21], s[14:15], 0, v[20:21]
	v_lshl_add_u64 v[20:21], v[20:21], 0, s[28:29]
	v_lshl_add_u64 v[20:21], v[20:21], 0, v[170:171]
	global_store_dwordx2 v[20:21], v[28:29], off

; __device__ __forceinline__ unsigned pk4_fp8(float a, float b, float c, float d) {
;     a = fminf(fmaxf(a, -448.f), 448.f); b = fminf(fmaxf(b, -448.f), 448.f); c = fminf(fmaxf(c, -448.f), 448.f); d = fminf(fmaxf(d, -448.f), 448.f);
;     int w = 0; w = __builtin_amdgcn_cvt_pk_fp8_f32(a, b, w, false); w = __builtin_amdgcn_cvt_pk_fp8_f32(c, d, w, true); return (unsigned)w;
; }
;     __device__ __forceinline__ void operator()(const f32x4 (&acc)[2][2][4][2], const Unit& u, int wr, int wc, int fr, int fq) const {
;     ...
;                     if (g == 1) {
;                         unsigned char* d8 = (unsigned char*)(QKV + (size_t)g * 4 * 16 * 4096 * 128) + ((((size_t)b * 16 + head) * 4096 + s) * 128 + (wc >> 1) * 64 + (fq & 1) * 32 + ((wc & 1) * 2 + (fq >> 1)) * 8);
;                         u32x2 w8; w8.x = pk4_fp8(v0[0] * 16.f, v0[1] * 16.f, v0[2] * 16.f, v0[3] * 16.f); w8.y = pk4_fp8(v1[0] * 16.f, v1[1] * 16.f, v1[2] * 16.f, v1[3] * 16.f);
;                         *(u32x2*)d8 = w8;
;                     } else if (g == 3 || g == 4) {
;                         unsigned char* d8 = (unsigned char*)(QKV + (size_t)g * 4 * 16 * 4096 * 128) + ((((size_t)b * 16 + head) * 4096 + s) * 128 + wc * 32 + 8 * fq);
;                         u32x2 w8; w8.x = pk4_fp8(v0[0] * 16.f, v0[1] * 16.f, v0[2] * 16.f, v0[3] * 16.f); w8.y = pk4_fp8(v1[0] * 16.f, v1[1] * 16.f, v1[2] * 16.f, v1[3] * 16.f);
;                         *(u32x2*)d8 = w8;
.LBB0_558:
	s_andn2_b64 vcc, exec, s[14:15]
	s_cbranch_vccnz .LBB0_560
	v_mul_f32_e32 v28, 0x41800000, v30
	v_mul_f32_e32 v29, 0x41800000, v31
	v_med3_f32 v158, v28, s67, v206
	v_med3_f32 v29, v29, s67, v206
	v_cvt_pk_fp8_f32 v28, v158, v29
	v_mul_f32_e32 v32, 0x41800000, v26
	v_mul_f32_e32 v33, 0x41800000, v27
	v_med3_f32 v32, v32, s67, v206
	v_med3_f32 v33, v33, s67, v206
	v_cvt_pk_fp8_f32 v28, v32, v33 op_sel:[0,0,1]
	v_mul_f32_e32 v29, 0x41800000, v22
	v_mul_f32_e32 v32, 0x41800000, v23
	v_med3_f32 v159, v29, s67, v206
	v_med3_f32 v32, v32, s67, v206
	v_cvt_pk_fp8_f32 v29, v159, v32
	v_mul_f32_e32 v33, 0x41800000, v18
	v_mul_f32_e32 v158, 0x41800000, v19
	v_med3_f32 v33, v33, s67, v206
	v_med3_f32 v158, v158, s67, v206
	v_cvt_pk_fp8_f32 v29, v33, v158 op_sel:[0,0,1]
	v_lshl_add_u64 v[20:21], v[154:155], 0, s[24:25]
	v_lshlrev_b64 v[20:21], 7, v[20:21]
	v_lshl_add_u64 v[20:21], v[176:177], 0, v[20:21]
	global_store_dwordx2 v[20:21], v[28:29], off

; __device__ __forceinline__ unsigned pk4_fp8(float a, float b, float c, float d) {
;     a = fminf(fmaxf(a, -448.f), 448.f); b = fminf(fmaxf(b, -448.f), 448.f); c = fminf(fmaxf(c, -448.f), 448.f); d = fminf(fmaxf(d, -448.f), 448.f);
;     int w = 0; w = __builtin_amdgcn_cvt_pk_fp8_f32(a, b, w, false); w = __builtin_amdgcn_cvt_pk_fp8_f32(c, d, w, true); return (unsigned)w;
; }
;     __device__ __forceinline__ void operator()(const f32x4 (&acc)[2][2][4][2], const Unit& u, int wr, int wc, int fr, int fq) const {
;     ...
;                     } else if (g == 3 || g == 4) {
;                         unsigned char* d8 = (unsigned char*)(QKV + (size_t)g * 4 * 16 * 4096 * 128) + ((((size_t)b * 16 + head) * 4096 + s) * 128 + wc * 32 + 8 * fq);
;                         u32x2 w8; w8.x = pk4_fp8(v0[0] * 16.f, v0[1] * 16.f, v0[2] * 16.f, v0[3] * 16.f); w8.y = pk4_fp8(v1[0] * 16.f, v1[1] * 16.f, v1[2] * 16.f, v1[3] * 16.f);
;                         *(u32x2*)d8 = w8;
.LBB0_570:
	s_andn2_b64 vcc, exec, s[52:53]
	s_cbranch_vccnz .LBB0_572
	v_mul_f32_e32 v4, 0x41800000, v32
	v_mul_f32_e32 v5, 0x41800000, v33
	v_med3_f32 v8, v4, s67, v206
	v_med3_f32 v5, v5, s67, v206
	v_cvt_pk_fp8_f32 v4, v8, v5
	v_mul_f32_e32 v6, 0x41800000, v28
	v_mul_f32_e32 v7, 0x41800000, v29
	v_med3_f32 v6, v6, s67, v206
	v_med3_f32 v7, v7, s67, v206
	v_cvt_pk_fp8_f32 v4, v6, v7 op_sel:[0,0,1]
	v_mul_f32_e32 v5, 0x41800000, v24
	v_mul_f32_e32 v6, 0x41800000, v25
	v_med3_f32 v9, v5, s67, v206
	v_med3_f32 v6, v6, s67, v206
	v_cvt_pk_fp8_f32 v5, v9, v6
	s_lshl_b32 s52, s41, 1
	v_readlane_b32 s54, v253, 46
	v_mul_f32_e32 v7, 0x41800000, v20
	v_mul_f32_e32 v8, 0x41800000, v21
	v_readlane_b32 s55, v253, 47
	s_add_u32 s52, s54, s52
	v_lshl_add_u64 v[2:3], v[154:155], 0, s[46:47]
	v_med3_f32 v7, v7, s67, v206
	v_med3_f32 v8, v8, s67, v206
	s_addc_u32 s53, s55, 0
	v_lshlrev_b64 v[2:3], 7, v[2:3]
	v_cvt_pk_fp8_f32 v5, v7, v8 op_sel:[0,0,1]
	v_lshl_add_u64 v[2:3], s[52:53], 0, v[2:3]
	v_lshl_add_u64 v[2:3], v[2:3], 0, s[28:29]
	v_lshl_add_u64 v[2:3], v[2:3], 0, v[170:171]
	global_store_dwordx2 v[2:3], v[4:5], off

; __device__ __forceinline__ unsigned pk4_fp8(float a, float b, float c, float d) {
;     a = fminf(fmaxf(a, -448.f), 448.f); b = fminf(fmaxf(b, -448.f), 448.f); c = fminf(fmaxf(c, -448.f), 448.f); d = fminf(fmaxf(d, -448.f), 448.f);
;     int w = 0; w = __builtin_amdgcn_cvt_pk_fp8_f32(a, b, w, false); w = __builtin_amdgcn_cvt_pk_fp8_f32(c, d, w, true); return (unsigned)w;
; }
;     __device__ __forceinline__ void operator()(const f32x4 (&acc)[2][2][4][2], const Unit& u, int wr, int wc, int fr, int fq) const {
;     ...
;                     if (g == 1) {
;                         unsigned char* d8 = (unsigned char*)(QKV + (size_t)g * 4 * 16 * 4096 * 128) + ((((size_t)b * 16 + head) * 4096 + s) * 128 + (wc >> 1) * 64 + (fq & 1) * 32 + ((wc & 1) * 2 + (fq >> 1)) * 8);
;                         u32x2 w8; w8.x = pk4_fp8(v0[0] * 16.f, v0[1] * 16.f, v0[2] * 16.f, v0[3] * 16.f); w8.y = pk4_fp8(v1[0] * 16.f, v1[1] * 16.f, v1[2] * 16.f, v1[3] * 16.f);
;                         *(u32x2*)d8 = w8;
;                     } else if (g == 3 || g == 4) {
;                         unsigned char* d8 = (unsigned char*)(QKV + (size_t)g * 4 * 16 * 4096 * 128) + ((((size_t)b * 16 + head) * 4096 + s) * 128 + wc * 32 + 8 * fq);
;                         u32x2 w8; w8.x = pk4_fp8(v0[0] * 16.f, v0[1] * 16.f, v0[2] * 16.f, v0[3] * 16.f); w8.y = pk4_fp8(v1[0] * 16.f, v1[1] * 16.f, v1[2] * 16.f, v1[3] * 16.f);
;                         *(u32x2*)d8 = w8;
.LBB0_573:
	s_andn2_b64 vcc, exec, s[54:55]
	s_cbranch_vccnz .LBB0_575
	v_mul_f32_e32 v4, 0x41800000, v32
	v_mul_f32_e32 v5, 0x41800000, v33
	v_med3_f32 v8, v4, s67, v206
	v_med3_f32 v5, v5, s67, v206
	v_cvt_pk_fp8_f32 v4, v8, v5
	v_mul_f32_e32 v6, 0x41800000, v28
	v_mul_f32_e32 v7, 0x41800000, v29
	v_med3_f32 v6, v6, s67, v206
	v_med3_f32 v7, v7, s67, v206
	v_cvt_pk_fp8_f32 v4, v6, v7 op_sel:[0,0,1]
	v_mul_f32_e32 v5, 0x41800000, v24
	v_mul_f32_e32 v6, 0x41800000, v25
	v_med3_f32 v9, v5, s67, v206
	v_med3_f32 v6, v6, s67, v206
	v_cvt_pk_fp8_f32 v5, v9, v6
	v_mul_f32_e32 v7, 0x41800000, v20
	v_mul_f32_e32 v8, 0x41800000, v21
	v_med3_f32 v7, v7, s67, v206
	v_med3_f32 v8, v8, s67, v206
	v_cvt_pk_fp8_f32 v5, v7, v8 op_sel:[0,0,1]
	v_lshl_add_u64 v[2:3], v[154:155], 0, s[46:47]
	v_lshlrev_b64 v[2:3], 7, v[2:3]
	v_lshl_add_u64 v[2:3], v[176:177], 0, v[2:3]
	global_store_dwordx2 v[2:3], v[4:5], off

; __device__ __forceinline__ unsigned pk4_fp8(float a, float b, float c, float d) {
;     a = fminf(fmaxf(a, -448.f), 448.f); b = fminf(fmaxf(b, -448.f), 448.f); c = fminf(fmaxf(c, -448.f), 448.f); d = fminf(fmaxf(d, -448.f), 448.f);
;     int w = 0; w = __builtin_amdgcn_cvt_pk_fp8_f32(a, b, w, false); w = __builtin_amdgcn_cvt_pk_fp8_f32(c, d, w, true); return (unsigned)w;
; }
;     __device__ __forceinline__ void operator()(const f32x4 (&acc)[2][2][4][2], const Unit& u, int wr, int wc, int fr, int fq) const {
;     ...
;                     } else if (g == 3 || g == 4) {
;                         unsigned char* d8 = (unsigned char*)(QKV + (size_t)g * 4 * 16 * 4096 * 128) + ((((size_t)b * 16 + head) * 4096 + s) * 128 + wc * 32 + 8 * fq);
;                         u32x2 w8; w8.x = pk4_fp8(v0[0] * 16.f, v0[1] * 16.f, v0[2] * 16.f, v0[3] * 16.f); w8.y = pk4_fp8(v1[0] * 16.f, v1[1] * 16.f, v1[2] * 16.f, v1[3] * 16.f);
;                         *(u32x2*)d8 = w8;
.LBB0_593:
	s_andn2_b64 vcc, exec, s[52:53]
	s_cbranch_vccnz .LBB0_595
	v_mul_f32_e32 v154, 0x41800000, v142
	v_mul_f32_e32 v155, 0x41800000, v143
	v_med3_f32 v158, v154, s67, v206
	v_med3_f32 v155, v155, s67, v206
	v_cvt_pk_fp8_f32 v154, v158, v155
	v_mul_f32_e32 v156, 0x41800000, v144
	v_mul_f32_e32 v157, 0x41800000, v145
	v_med3_f32 v156, v156, s67, v206
	v_med3_f32 v157, v157, s67, v206
	v_cvt_pk_fp8_f32 v154, v156, v157 op_sel:[0,0,1]
	v_mul_f32_e32 v155, 0x41800000, v138
	v_mul_f32_e32 v156, 0x41800000, v139
	v_med3_f32 v159, v155, s67, v206
	v_med3_f32 v156, v156, s67, v206
	v_cvt_pk_fp8_f32 v155, v159, v156
	s_lshl_b32 s52, s41, 1
	v_readlane_b32 s54, v253, 46
	v_mul_f32_e32 v157, 0x41800000, v140
	v_mul_f32_e32 v158, 0x41800000, v141
	v_readlane_b32 s55, v253, 47
	s_add_u32 s52, s54, s52
	v_lshl_add_u64 v[152:153], v[146:147], 0, s[24:25]
	v_med3_f32 v157, v157, s67, v206
	v_med3_f32 v158, v158, s67, v206
	s_addc_u32 s53, s55, 0
	v_lshlrev_b64 v[152:153], 7, v[152:153]
	v_cvt_pk_fp8_f32 v155, v157, v158 op_sel:[0,0,1]
	v_lshl_add_u64 v[152:153], s[52:53], 0, v[152:153]
	v_lshl_add_u64 v[152:153], v[152:153], 0, s[28:29]
	v_lshl_add_u64 v[152:153], v[152:153], 0, v[170:171]
	global_store_dwordx2 v[152:153], v[154:155], off

; __device__ __forceinline__ unsigned pk4_fp8(float a, float b, float c, float d) {
;     a = fminf(fmaxf(a, -448.f), 448.f); b = fminf(fmaxf(b, -448.f), 448.f); c = fminf(fmaxf(c, -448.f), 448.f); d = fminf(fmaxf(d, -448.f), 448.f);
;     int w = 0; w = __builtin_amdgcn_cvt_pk_fp8_f32(a, b, w, false); w = __builtin_amdgcn_cvt_pk_fp8_f32(c, d, w, true); return (unsigned)w;
; }
;     __device__ __forceinline__ void operator()(const f32x4 (&acc)[2][2][4][2], const Unit& u, int wr, int wc, int fr, int fq) const {
;     ...
;                     if (g == 1) {
;                         unsigned char* d8 = (unsigned char*)(QKV + (size_t)g * 4 * 16 * 4096 * 128) + ((((size_t)b * 16 + head) * 4096 + s) * 128 + (wc >> 1) * 64 + (fq & 1) * 32 + ((wc & 1) * 2 + (fq >> 1)) * 8);
;                         u32x2 w8; w8.x = pk4_fp8(v0[0] * 16.f, v0[1] * 16.f, v0[2] * 16.f, v0[3] * 16.f); w8.y = pk4_fp8(v1[0] * 16.f, v1[1] * 16.f, v1[2] * 16.f, v1[3] * 16.f);
;                         *(u32x2*)d8 = w8;
;                     } else if (g == 3 || g == 4) {
;                         unsigned char* d8 = (unsigned char*)(QKV + (size_t)g * 4 * 16 * 4096 * 128) + ((((size_t)b * 16 + head) * 4096 + s) * 128 + wc * 32 + 8 * fq);
;                         u32x2 w8; w8.x = pk4_fp8(v0[0] * 16.f, v0[1] * 16.f, v0[2] * 16.f, v0[3] * 16.f); w8.y = pk4_fp8(v1[0] * 16.f, v1[1] * 16.f, v1[2] * 16.f, v1[3] * 16.f);
;                         *(u32x2*)d8 = w8;
.LBB0_596:
	s_andn2_b64 vcc, exec, s[52:53]
	s_cbranch_vccnz .LBB0_598
	v_mul_f32_e32 v154, 0x41800000, v142
	v_mul_f32_e32 v155, 0x41800000, v143
	v_med3_f32 v158, v154, s67, v206
	v_med3_f32 v155, v155, s67, v206
	v_cvt_pk_fp8_f32 v154, v158, v155
	v_mul_f32_e32 v156, 0x41800000, v144
	v_mul_f32_e32 v157, 0x41800000, v145
	v_med3_f32 v156, v156, s67, v206
	v_med3_f32 v157, v157, s67, v206
	v_cvt_pk_fp8_f32 v154, v156, v157 op_sel:[0,0,1]
	v_mul_f32_e32 v155, 0x41800000, v138
	v_mul_f32_e32 v156, 0x41800000, v139
	v_med3_f32 v159, v155, s67, v206
	v_med3_f32 v156, v156, s67, v206
	v_cvt_pk_fp8_f32 v155, v159, v156
	v_mul_f32_e32 v157, 0x41800000, v140
	v_mul_f32_e32 v158, 0x41800000, v141
	v_med3_f32 v157, v157, s67, v206
	v_med3_f32 v158, v158, s67, v206
	v_cvt_pk_fp8_f32 v155, v157, v158 op_sel:[0,0,1]
	v_lshl_add_u64 v[152:153], v[146:147], 0, s[24:25]
	v_lshlrev_b64 v[152:153], 7, v[152:153]
	v_lshl_add_u64 v[152:153], v[176:177], 0, v[152:153]
	global_store_dwordx2 v[152:153], v[154:155], off

; __device__ __forceinline__ unsigned pk4_fp8(float a, float b, float c, float d) {
;     a = fminf(fmaxf(a, -448.f), 448.f); b = fminf(fmaxf(b, -448.f), 448.f); c = fminf(fmaxf(c, -448.f), 448.f); d = fminf(fmaxf(d, -448.f), 448.f);
;     int w = 0; w = __builtin_amdgcn_cvt_pk_fp8_f32(a, b, w, false); w = __builtin_amdgcn_cvt_pk_fp8_f32(c, d, w, true); return (unsigned)w;
; }
;     __device__ __forceinline__ void operator()(const f32x4 (&acc)[2][2][4][2], const Unit& u, int wr, int wc, int fr, int fq) const {
;     ...
;                     } else if (g == 3 || g == 4) {
;                         unsigned char* d8 = (unsigned char*)(QKV + (size_t)g * 4 * 16 * 4096 * 128) + ((((size_t)b * 16 + head) * 4096 + s) * 128 + wc * 32 + 8 * fq);
;                         u32x2 w8; w8.x = pk4_fp8(v0[0] * 16.f, v0[1] * 16.f, v0[2] * 16.f, v0[3] * 16.f); w8.y = pk4_fp8(v1[0] * 16.f, v1[1] * 16.f, v1[2] * 16.f, v1[3] * 16.f);
;                         *(u32x2*)d8 = w8;
.LBB0_608:
	s_andn2_b64 vcc, exec, s[52:53]
	s_cbranch_vccnz .LBB0_610
	v_mul_f32_e32 v4, 0x41800000, v134
	v_mul_f32_e32 v5, 0x41800000, v135
	v_med3_f32 v8, v4, s67, v206
	v_med3_f32 v5, v5, s67, v206
	v_cvt_pk_fp8_f32 v4, v8, v5
	v_mul_f32_e32 v6, 0x41800000, v136
	v_mul_f32_e32 v7, 0x41800000, v137
	v_med3_f32 v6, v6, s67, v206
	v_med3_f32 v7, v7, s67, v206
	v_cvt_pk_fp8_f32 v4, v6, v7 op_sel:[0,0,1]
	v_mul_f32_e32 v5, 0x41800000, v130
	v_mul_f32_e32 v6, 0x41800000, v131
	v_med3_f32 v9, v5, s67, v206
	v_med3_f32 v6, v6, s67, v206
	v_cvt_pk_fp8_f32 v5, v9, v6
	s_lshl_b32 s52, s41, 1
	v_readlane_b32 s54, v253, 46
	v_mul_f32_e32 v7, 0x41800000, v132
	v_mul_f32_e32 v8, 0x41800000, v133
	v_readlane_b32 s55, v253, 47
	s_add_u32 s52, s54, s52
	v_lshl_add_u64 v[2:3], v[146:147], 0, s[46:47]
	v_med3_f32 v7, v7, s67, v206
	v_med3_f32 v8, v8, s67, v206
	s_addc_u32 s53, s55, 0
	v_lshlrev_b64 v[2:3], 7, v[2:3]
	v_cvt_pk_fp8_f32 v5, v7, v8 op_sel:[0,0,1]
	v_lshl_add_u64 v[2:3], s[52:53], 0, v[2:3]
	v_lshl_add_u64 v[2:3], v[2:3], 0, s[28:29]
	v_lshl_add_u64 v[2:3], v[2:3], 0, v[170:171]
	global_store_dwordx2 v[2:3], v[4:5], off

; __device__ __forceinline__ unsigned pk4_fp8(float a, float b, float c, float d) {
;     a = fminf(fmaxf(a, -448.f), 448.f); b = fminf(fmaxf(b, -448.f), 448.f); c = fminf(fmaxf(c, -448.f), 448.f); d = fminf(fmaxf(d, -448.f), 448.f);
;     int w = 0; w = __builtin_amdgcn_cvt_pk_fp8_f32(a, b, w, false); w = __builtin_amdgcn_cvt_pk_fp8_f32(c, d, w, true); return (unsigned)w;
; }
;     __device__ __forceinline__ void operator()(const f32x4 (&acc)[2][2][4][2], const Unit& u, int wr, int wc, int fr, int fq) const {
;     ...
;                     if (g == 1) {
;                         unsigned char* d8 = (unsigned char*)(QKV + (size_t)g * 4 * 16 * 4096 * 128) + ((((size_t)b * 16 + head) * 4096 + s) * 128 + (wc >> 1) * 64 + (fq & 1) * 32 + ((wc & 1) * 2 + (fq >> 1)) * 8);
;                         u32x2 w8; w8.x = pk4_fp8(v0[0] * 16.f, v0[1] * 16.f, v0[2] * 16.f, v0[3] * 16.f); w8.y = pk4_fp8(v1[0] * 16.f, v1[1] * 16.f, v1[2] * 16.f, v1[3] * 16.f);
;                         *(u32x2*)d8 = w8;
;                     } else if (g == 3 || g == 4) {
;                         unsigned char* d8 = (unsigned char*)(QKV + (size_t)g * 4 * 16 * 4096 * 128) + ((((size_t)b * 16 + head) * 4096 + s) * 128 + wc * 32 + 8 * fq);
;                         u32x2 w8; w8.x = pk4_fp8(v0[0] * 16.f, v0[1] * 16.f, v0[2] * 16.f, v0[3] * 16.f); w8.y = pk4_fp8(v1[0] * 16.f, v1[1] * 16.f, v1[2] * 16.f, v1[3] * 16.f);
;                         *(u32x2*)d8 = w8;
.LBB0_611:
	s_andn2_b64 vcc, exec, s[52:53]
	s_cbranch_vccnz .LBB0_613
	v_mul_f32_e32 v4, 0x41800000, v134
	v_mul_f32_e32 v5, 0x41800000, v135
	v_med3_f32 v8, v4, s67, v206
	v_med3_f32 v5, v5, s67, v206
	v_cvt_pk_fp8_f32 v4, v8, v5
	v_mul_f32_e32 v6, 0x41800000, v136
	v_mul_f32_e32 v7, 0x41800000, v137
	v_med3_f32 v6, v6, s67, v206
	v_med3_f32 v7, v7, s67, v206
	v_cvt_pk_fp8_f32 v4, v6, v7 op_sel:[0,0,1]
	v_mul_f32_e32 v5, 0x41800000, v130
	v_mul_f32_e32 v6, 0x41800000, v131
	v_med3_f32 v9, v5, s67, v206
	v_med3_f32 v6, v6, s67, v206
	v_cvt_pk_fp8_f32 v5, v9, v6
	v_mul_f32_e32 v7, 0x41800000, v132
	v_mul_f32_e32 v8, 0x41800000, v133
	v_med3_f32 v7, v7, s67, v206
	v_med3_f32 v8, v8, s67, v206
	v_cvt_pk_fp8_f32 v5, v7, v8 op_sel:[0,0,1]
	v_lshl_add_u64 v[2:3], v[146:147], 0, s[46:47]
	v_lshlrev_b64 v[2:3], 7, v[2:3]
	v_lshl_add_u64 v[2:3], v[176:177], 0, v[2:3]
	global_store_dwordx2 v[2:3], v[4:5], off

; __device__ __forceinline__ unsigned pk4_fp8(float a, float b, float c, float d) {
;     a = fminf(fmaxf(a, -448.f), 448.f); b = fminf(fmaxf(b, -448.f), 448.f); c = fminf(fmaxf(c, -448.f), 448.f); d = fminf(fmaxf(d, -448.f), 448.f);
;     int w = 0; w = __builtin_amdgcn_cvt_pk_fp8_f32(a, b, w, false); w = __builtin_amdgcn_cvt_pk_fp8_f32(c, d, w, true); return (unsigned)w;
; }
;     __device__ __forceinline__ void operator()(const f32x4 (&acc)[2][2][4][2], const Unit& u, int wr, int wc, int fr, int fq) const {
;     ...
;                     } else if (g == 3 || g == 4) {
;                         unsigned char* d8 = (unsigned char*)(QKV + (size_t)g * 4 * 16 * 4096 * 128) + ((((size_t)b * 16 + head) * 4096 + s) * 128 + wc * 32 + 8 * fq);
;                         u32x2 w8; w8.x = pk4_fp8(v0[0] * 16.f, v0[1] * 16.f, v0[2] * 16.f, v0[3] * 16.f); w8.y = pk4_fp8(v1[0] * 16.f, v1[1] * 16.f, v1[2] * 16.f, v1[3] * 16.f);
;                         *(u32x2*)d8 = w8;
.LBB0_631:
	s_andn2_b64 vcc, exec, s[52:53]
	s_cbranch_vccnz .LBB0_633
	v_mul_f32_e32 v154, 0x41800000, v126
	v_mul_f32_e32 v155, 0x41800000, v127
	v_med3_f32 v158, v154, s67, v206
	v_med3_f32 v155, v155, s67, v206
	v_cvt_pk_fp8_f32 v154, v158, v155
	v_mul_f32_e32 v156, 0x41800000, v128
	v_mul_f32_e32 v157, 0x41800000, v129
	v_med3_f32 v156, v156, s67, v206
	v_med3_f32 v157, v157, s67, v206
	v_cvt_pk_fp8_f32 v154, v156, v157 op_sel:[0,0,1]
	v_mul_f32_e32 v155, 0x41800000, v122
	v_mul_f32_e32 v156, 0x41800000, v123
	v_med3_f32 v159, v155, s67, v206
	v_med3_f32 v156, v156, s67, v206
	v_cvt_pk_fp8_f32 v155, v159, v156
	s_lshl_b32 s52, s41, 1
	v_readlane_b32 s54, v253, 46
	v_mul_f32_e32 v157, 0x41800000, v124
	v_mul_f32_e32 v158, 0x41800000, v125
	v_readlane_b32 s55, v253, 47
	s_add_u32 s52, s54, s52
	v_lshl_add_u64 v[152:153], v[146:147], 0, s[24:25]
	v_med3_f32 v157, v157, s67, v206
	v_med3_f32 v158, v158, s67, v206
	s_addc_u32 s53, s55, 0
	v_lshlrev_b64 v[152:153], 7, v[152:153]
	v_cvt_pk_fp8_f32 v155, v157, v158 op_sel:[0,0,1]
	v_lshl_add_u64 v[152:153], s[52:53], 0, v[152:153]
	v_lshl_add_u64 v[152:153], v[152:153], 0, s[28:29]
	v_lshl_add_u64 v[152:153], v[152:153], 0, v[170:171]
	global_store_dwordx2 v[152:153], v[154:155], off

; __device__ __forceinline__ unsigned pk4_fp8(float a, float b, float c, float d) {
;     a = fminf(fmaxf(a, -448.f), 448.f); b = fminf(fmaxf(b, -448.f), 448.f); c = fminf(fmaxf(c, -448.f), 448.f); d = fminf(fmaxf(d, -448.f), 448.f);
;     int w = 0; w = __builtin_amdgcn_cvt_pk_fp8_f32(a, b, w, false); w = __builtin_amdgcn_cvt_pk_fp8_f32(c, d, w, true); return (unsigned)w;
; }
;     __device__ __forceinline__ void operator()(const f32x4 (&acc)[2][2][4][2], const Unit& u, int wr, int wc, int fr, int fq) const {
;     ...
;                     if (g == 1) {
;                         unsigned char* d8 = (unsigned char*)(QKV + (size_t)g * 4 * 16 * 4096 * 128) + ((((size_t)b * 16 + head) * 4096 + s) * 128 + (wc >> 1) * 64 + (fq & 1) * 32 + ((wc & 1) * 2 + (fq >> 1)) * 8);
;                         u32x2 w8; w8.x = pk4_fp8(v0[0] * 16.f, v0[1] * 16.f, v0[2] * 16.f, v0[3] * 16.f); w8.y = pk4_fp8(v1[0] * 16.f, v1[1] * 16.f, v1[2] * 16.f, v1[3] * 16.f);
;                         *(u32x2*)d8 = w8;
;                     } else if (g == 3 || g == 4) {
;                         unsigned char* d8 = (unsigned char*)(QKV + (size_t)g * 4 * 16 * 4096 * 128) + ((((size_t)b * 16 + head) * 4096 + s) * 128 + wc * 32 + 8 * fq);
;                         u32x2 w8; w8.x = pk4_fp8(v0[0] * 16.f, v0[1] * 16.f, v0[2] * 16.f, v0[3] * 16.f); w8.y = pk4_fp8(v1[0] * 16.f, v1[1] * 16.f, v1[2] * 16.f, v1[3] * 16.f);
;                         *(u32x2*)d8 = w8;
.LBB0_634:
	s_andn2_b64 vcc, exec, s[52:53]
	s_cbranch_vccnz .LBB0_636
	v_mul_f32_e32 v154, 0x41800000, v126
	v_mul_f32_e32 v155, 0x41800000, v127
	v_med3_f32 v158, v154, s67, v206
	v_med3_f32 v155, v155, s67, v206
	v_cvt_pk_fp8_f32 v154, v158, v155
	v_mul_f32_e32 v156, 0x41800000, v128
	v_mul_f32_e32 v157, 0x41800000, v129
	v_med3_f32 v156, v156, s67, v206
	v_med3_f32 v157, v157, s67, v206
	v_cvt_pk_fp8_f32 v154, v156, v157 op_sel:[0,0,1]
	v_mul_f32_e32 v155, 0x41800000, v122
	v_mul_f32_e32 v156, 0x41800000, v123
	v_med3_f32 v159, v155, s67, v206
	v_med3_f32 v156, v156, s67, v206
	v_cvt_pk_fp8_f32 v155, v159, v156
	v_mul_f32_e32 v157, 0x41800000, v124
	v_mul_f32_e32 v158, 0x41800000, v125
	v_med3_f32 v157, v157, s67, v206
	v_med3_f32 v158, v158, s67, v206
	v_cvt_pk_fp8_f32 v155, v157, v158 op_sel:[0,0,1]
	v_lshl_add_u64 v[152:153], v[146:147], 0, s[24:25]
	v_lshlrev_b64 v[152:153], 7, v[152:153]
	v_lshl_add_u64 v[152:153], v[176:177], 0, v[152:153]
	global_store_dwordx2 v[152:153], v[154:155], off

; __device__ __forceinline__ unsigned pk4_fp8(float a, float b, float c, float d) {
;     a = fminf(fmaxf(a, -448.f), 448.f); b = fminf(fmaxf(b, -448.f), 448.f); c = fminf(fmaxf(c, -448.f), 448.f); d = fminf(fmaxf(d, -448.f), 448.f);
;     int w = 0; w = __builtin_amdgcn_cvt_pk_fp8_f32(a, b, w, false); w = __builtin_amdgcn_cvt_pk_fp8_f32(c, d, w, true); return (unsigned)w;
; }
;     __device__ __forceinline__ void operator()(const f32x4 (&acc)[2][2][4][2], const Unit& u, int wr, int wc, int fr, int fq) const {
;     ...
;                     } else if (g == 3 || g == 4) {
;                         unsigned char* d8 = (unsigned char*)(QKV + (size_t)g * 4 * 16 * 4096 * 128) + ((((size_t)b * 16 + head) * 4096 + s) * 128 + wc * 32 + 8 * fq);
;                         u32x2 w8; w8.x = pk4_fp8(v0[0] * 16.f, v0[1] * 16.f, v0[2] * 16.f, v0[3] * 16.f); w8.y = pk4_fp8(v1[0] * 16.f, v1[1] * 16.f, v1[2] * 16.f, v1[3] * 16.f);
;                         *(u32x2*)d8 = w8;
.LBB0_646:
	s_andn2_b64 vcc, exec, s[52:53]
	s_cbranch_vccnz .LBB0_648
	v_mul_f32_e32 v4, 0x41800000, v118
	v_mul_f32_e32 v5, 0x41800000, v119
	v_med3_f32 v8, v4, s67, v206
	v_med3_f32 v5, v5, s67, v206
	v_cvt_pk_fp8_f32 v4, v8, v5
	v_mul_f32_e32 v6, 0x41800000, v120
	v_mul_f32_e32 v7, 0x41800000, v121
	v_med3_f32 v6, v6, s67, v206
	v_med3_f32 v7, v7, s67, v206
	v_cvt_pk_fp8_f32 v4, v6, v7 op_sel:[0,0,1]
	v_mul_f32_e32 v5, 0x41800000, v114
	v_mul_f32_e32 v6, 0x41800000, v115
	v_med3_f32 v9, v5, s67, v206
	v_med3_f32 v6, v6, s67, v206
	v_cvt_pk_fp8_f32 v5, v9, v6
	s_lshl_b32 s52, s41, 1
	v_readlane_b32 s54, v253, 46
	v_mul_f32_e32 v7, 0x41800000, v116
	v_mul_f32_e32 v8, 0x41800000, v117
	v_readlane_b32 s55, v253, 47
	s_add_u32 s52, s54, s52
	v_lshl_add_u64 v[2:3], v[146:147], 0, s[46:47]
	v_med3_f32 v7, v7, s67, v206
	v_med3_f32 v8, v8, s67, v206
	s_addc_u32 s53, s55, 0
	v_lshlrev_b64 v[2:3], 7, v[2:3]
	v_cvt_pk_fp8_f32 v5, v7, v8 op_sel:[0,0,1]
	v_lshl_add_u64 v[2:3], s[52:53], 0, v[2:3]
	v_lshl_add_u64 v[2:3], v[2:3], 0, s[28:29]
	v_lshl_add_u64 v[2:3], v[2:3], 0, v[170:171]
	global_store_dwordx2 v[2:3], v[4:5], off

; __device__ __forceinline__ unsigned pk4_fp8(float a, float b, float c, float d) {
;     a = fminf(fmaxf(a, -448.f), 448.f); b = fminf(fmaxf(b, -448.f), 448.f); c = fminf(fmaxf(c, -448.f), 448.f); d = fminf(fmaxf(d, -448.f), 448.f);
;     int w = 0; w = __builtin_amdgcn_cvt_pk_fp8_f32(a, b, w, false); w = __builtin_amdgcn_cvt_pk_fp8_f32(c, d, w, true); return (unsigned)w;
; }
;     __device__ __forceinline__ void operator()(const f32x4 (&acc)[2][2][4][2], const Unit& u, int wr, int wc, int fr, int fq) const {
;     ...
;                     if (g == 1) {
;                         unsigned char* d8 = (unsigned char*)(QKV + (size_t)g * 4 * 16 * 4096 * 128) + ((((size_t)b * 16 + head) * 4096 + s) * 128 + (wc >> 1) * 64 + (fq & 1) * 32 + ((wc & 1) * 2 + (fq >> 1)) * 8);
;                         u32x2 w8; w8.x = pk4_fp8(v0[0] * 16.f, v0[1] * 16.f, v0[2] * 16.f, v0[3] * 16.f); w8.y = pk4_fp8(v1[0] * 16.f, v1[1] * 16.f, v1[2] * 16.f, v1[3] * 16.f);
;                         *(u32x2*)d8 = w8;
;                     } else if (g == 3 || g == 4) {
;                         unsigned char* d8 = (unsigned char*)(QKV + (size_t)g * 4 * 16 * 4096 * 128) + ((((size_t)b * 16 + head) * 4096 + s) * 128 + wc * 32 + 8 * fq);
;                         u32x2 w8; w8.x = pk4_fp8(v0[0] * 16.f, v0[1] * 16.f, v0[2] * 16.f, v0[3] * 16.f); w8.y = pk4_fp8(v1[0] * 16.f, v1[1] * 16.f, v1[2] * 16.f, v1[3] * 16.f);
;                         *(u32x2*)d8 = w8;
.LBB0_649:
	s_andn2_b64 vcc, exec, s[52:53]
	s_cbranch_vccnz .LBB0_651
	v_mul_f32_e32 v4, 0x41800000, v118
	v_mul_f32_e32 v5, 0x41800000, v119
	v_med3_f32 v8, v4, s67, v206
	v_med3_f32 v5, v5, s67, v206
	v_cvt_pk_fp8_f32 v4, v8, v5
	v_mul_f32_e32 v6, 0x41800000, v120
	v_mul_f32_e32 v7, 0x41800000, v121
	v_med3_f32 v6, v6, s67, v206
	v_med3_f32 v7, v7, s67, v206
	v_cvt_pk_fp8_f32 v4, v6, v7 op_sel:[0,0,1]
	v_mul_f32_e32 v5, 0x41800000, v114
	v_mul_f32_e32 v6, 0x41800000, v115
	v_med3_f32 v9, v5, s67, v206
	v_med3_f32 v6, v6, s67, v206
	v_cvt_pk_fp8_f32 v5, v9, v6
	v_mul_f32_e32 v7, 0x41800000, v116
	v_mul_f32_e32 v8, 0x41800000, v117
	v_med3_f32 v7, v7, s67, v206
	v_med3_f32 v8, v8, s67, v206
	v_cvt_pk_fp8_f32 v5, v7, v8 op_sel:[0,0,1]
	v_lshl_add_u64 v[2:3], v[146:147], 0, s[46:47]
	v_lshlrev_b64 v[2:3], 7, v[2:3]
	v_lshl_add_u64 v[2:3], v[176:177], 0, v[2:3]
	global_store_dwordx2 v[2:3], v[4:5], off

; __device__ __forceinline__ unsigned pk4_fp8(float a, float b, float c, float d) {
;     a = fminf(fmaxf(a, -448.f), 448.f); b = fminf(fmaxf(b, -448.f), 448.f); c = fminf(fmaxf(c, -448.f), 448.f); d = fminf(fmaxf(d, -448.f), 448.f);
;     int w = 0; w = __builtin_amdgcn_cvt_pk_fp8_f32(a, b, w, false); w = __builtin_amdgcn_cvt_pk_fp8_f32(c, d, w, true); return (unsigned)w;
; }
;     __device__ __forceinline__ void operator()(const f32x4 (&acc)[2][2][4][2], const Unit& u, int wr, int wc, int fr, int fq) const {
;     ...
;                     } else if (g == 3 || g == 4) {
;                         unsigned char* d8 = (unsigned char*)(QKV + (size_t)g * 4 * 16 * 4096 * 128) + ((((size_t)b * 16 + head) * 4096 + s) * 128 + wc * 32 + 8 * fq);
;                         u32x2 w8; w8.x = pk4_fp8(v0[0] * 16.f, v0[1] * 16.f, v0[2] * 16.f, v0[3] * 16.f); w8.y = pk4_fp8(v1[0] * 16.f, v1[1] * 16.f, v1[2] * 16.f, v1[3] * 16.f);
;                         *(u32x2*)d8 = w8;
.LBB0_669:
	s_andn2_b64 vcc, exec, s[52:53]
	s_cbranch_vccnz .LBB0_671
	v_mul_f32_e32 v154, 0x41800000, v110
	v_mul_f32_e32 v155, 0x41800000, v111
	v_med3_f32 v158, v154, s67, v206
	v_med3_f32 v155, v155, s67, v206
	v_cvt_pk_fp8_f32 v154, v158, v155
	v_mul_f32_e32 v156, 0x41800000, v112
	v_mul_f32_e32 v157, 0x41800000, v113
	v_med3_f32 v156, v156, s67, v206
	v_med3_f32 v157, v157, s67, v206
	v_cvt_pk_fp8_f32 v154, v156, v157 op_sel:[0,0,1]
	v_mul_f32_e32 v155, 0x41800000, v106
	v_mul_f32_e32 v156, 0x41800000, v107
	v_med3_f32 v159, v155, s67, v206
	v_med3_f32 v156, v156, s67, v206
	v_cvt_pk_fp8_f32 v155, v159, v156
	s_lshl_b32 s52, s41, 1
	v_readlane_b32 s54, v253, 46
	v_mul_f32_e32 v157, 0x41800000, v108
	v_mul_f32_e32 v158, 0x41800000, v109
	v_readlane_b32 s55, v253, 47
	s_add_u32 s52, s54, s52
	v_lshl_add_u64 v[152:153], v[146:147], 0, s[24:25]
	v_med3_f32 v157, v157, s67, v206
	v_med3_f32 v158, v158, s67, v206
	s_addc_u32 s53, s55, 0
	v_lshlrev_b64 v[152:153], 7, v[152:153]
	v_cvt_pk_fp8_f32 v155, v157, v158 op_sel:[0,0,1]
	v_lshl_add_u64 v[152:153], s[52:53], 0, v[152:153]
	v_lshl_add_u64 v[152:153], v[152:153], 0, s[28:29]
	v_lshl_add_u64 v[152:153], v[152:153], 0, v[170:171]
	global_store_dwordx2 v[152:153], v[154:155], off

; __device__ __forceinline__ unsigned pk4_fp8(float a, float b, float c, float d) {
;     a = fminf(fmaxf(a, -448.f), 448.f); b = fminf(fmaxf(b, -448.f), 448.f); c = fminf(fmaxf(c, -448.f), 448.f); d = fminf(fmaxf(d, -448.f), 448.f);
;     int w = 0; w = __builtin_amdgcn_cvt_pk_fp8_f32(a, b, w, false); w = __builtin_amdgcn_cvt_pk_fp8_f32(c, d, w, true); return (unsigned)w;
; }
;     __device__ __forceinline__ void operator()(const f32x4 (&acc)[2][2][4][2], const Unit& u, int wr, int wc, int fr, int fq) const {
;     ...
;                     if (g == 1) {
;                         unsigned char* d8 = (unsigned char*)(QKV + (size_t)g * 4 * 16 * 4096 * 128) + ((((size_t)b * 16 + head) * 4096 + s) * 128 + (wc >> 1) * 64 + (fq & 1) * 32 + ((wc & 1) * 2 + (fq >> 1)) * 8);
;                         u32x2 w8; w8.x = pk4_fp8(v0[0] * 16.f, v0[1] * 16.f, v0[2] * 16.f, v0[3] * 16.f); w8.y = pk4_fp8(v1[0] * 16.f, v1[1] * 16.f, v1[2] * 16.f, v1[3] * 16.f);
;                         *(u32x2*)d8 = w8;
;                     } else if (g == 3 || g == 4) {
;                         unsigned char* d8 = (unsigned char*)(QKV + (size_t)g * 4 * 16 * 4096 * 128) + ((((size_t)b * 16 + head) * 4096 + s) * 128 + wc * 32 + 8 * fq);
;                         u32x2 w8; w8.x = pk4_fp8(v0[0] * 16.f, v0[1] * 16.f, v0[2] * 16.f, v0[3] * 16.f); w8.y = pk4_fp8(v1[0] * 16.f, v1[1] * 16.f, v1[2] * 16.f, v1[3] * 16.f);
;                         *(u32x2*)d8 = w8;
.LBB0_672:
	s_andn2_b64 vcc, exec, s[52:53]
	s_cbranch_vccnz .LBB0_674
	v_mul_f32_e32 v154, 0x41800000, v110
	v_mul_f32_e32 v155, 0x41800000, v111
	v_med3_f32 v158, v154, s67, v206
	v_med3_f32 v155, v155, s67, v206
	v_cvt_pk_fp8_f32 v154, v158, v155
	v_mul_f32_e32 v156, 0x41800000, v112
	v_mul_f32_e32 v157, 0x41800000, v113
	v_med3_f32 v156, v156, s67, v206
	v_med3_f32 v157, v157, s67, v206
	v_cvt_pk_fp8_f32 v154, v156, v157 op_sel:[0,0,1]
	v_mul_f32_e32 v155, 0x41800000, v106
	v_mul_f32_e32 v156, 0x41800000, v107
	v_med3_f32 v159, v155, s67, v206
	v_med3_f32 v156, v156, s67, v206
	v_cvt_pk_fp8_f32 v155, v159, v156
	v_mul_f32_e32 v157, 0x41800000, v108
	v_mul_f32_e32 v158, 0x41800000, v109
	v_med3_f32 v157, v157, s67, v206
	v_med3_f32 v158, v158, s67, v206
	v_cvt_pk_fp8_f32 v155, v157, v158 op_sel:[0,0,1]
	v_lshl_add_u64 v[152:153], v[146:147], 0, s[24:25]
	v_lshlrev_b64 v[152:153], 7, v[152:153]
	v_lshl_add_u64 v[152:153], v[176:177], 0, v[152:153]
	global_store_dwordx2 v[152:153], v[154:155], off

; __device__ __forceinline__ unsigned pk4_fp8(float a, float b, float c, float d) {
;     a = fminf(fmaxf(a, -448.f), 448.f); b = fminf(fmaxf(b, -448.f), 448.f); c = fminf(fmaxf(c, -448.f), 448.f); d = fminf(fmaxf(d, -448.f), 448.f);
;     int w = 0; w = __builtin_amdgcn_cvt_pk_fp8_f32(a, b, w, false); w = __builtin_amdgcn_cvt_pk_fp8_f32(c, d, w, true); return (unsigned)w;
; }
;     __device__ __forceinline__ void operator()(const f32x4 (&acc)[2][2][4][2], const Unit& u, int wr, int wc, int fr, int fq) const {
;     ...
;                     } else if (g == 3 || g == 4) {
;                         unsigned char* d8 = (unsigned char*)(QKV + (size_t)g * 4 * 16 * 4096 * 128) + ((((size_t)b * 16 + head) * 4096 + s) * 128 + wc * 32 + 8 * fq);
;                         u32x2 w8; w8.x = pk4_fp8(v0[0] * 16.f, v0[1] * 16.f, v0[2] * 16.f, v0[3] * 16.f); w8.y = pk4_fp8(v1[0] * 16.f, v1[1] * 16.f, v1[2] * 16.f, v1[3] * 16.f);
;                         *(u32x2*)d8 = w8;
.LBB0_684:
	s_andn2_b64 vcc, exec, s[52:53]
	s_cbranch_vccnz .LBB0_686
	v_mul_f32_e32 v4, 0x41800000, v102
	v_mul_f32_e32 v5, 0x41800000, v103
	v_med3_f32 v8, v4, s67, v206
	v_med3_f32 v5, v5, s67, v206
	v_cvt_pk_fp8_f32 v4, v8, v5
	v_mul_f32_e32 v6, 0x41800000, v104
	v_mul_f32_e32 v7, 0x41800000, v105
	v_med3_f32 v6, v6, s67, v206
	v_med3_f32 v7, v7, s67, v206
	v_cvt_pk_fp8_f32 v4, v6, v7 op_sel:[0,0,1]
	v_mul_f32_e32 v5, 0x41800000, v98
	v_mul_f32_e32 v6, 0x41800000, v99
	v_med3_f32 v9, v5, s67, v206
	v_med3_f32 v6, v6, s67, v206
	v_cvt_pk_fp8_f32 v5, v9, v6
	s_lshl_b32 s52, s41, 1
	v_readlane_b32 s54, v253, 46
	v_mul_f32_e32 v7, 0x41800000, v100
	v_mul_f32_e32 v8, 0x41800000, v101
	v_readlane_b32 s55, v253, 47
	s_add_u32 s52, s54, s52
	v_lshl_add_u64 v[2:3], v[146:147], 0, s[46:47]
	v_med3_f32 v7, v7, s67, v206
	v_med3_f32 v8, v8, s67, v206
	s_addc_u32 s53, s55, 0
	v_lshlrev_b64 v[2:3], 7, v[2:3]
	v_cvt_pk_fp8_f32 v5, v7, v8 op_sel:[0,0,1]
	v_lshl_add_u64 v[2:3], s[52:53], 0, v[2:3]
	v_lshl_add_u64 v[2:3], v[2:3], 0, s[28:29]
	v_lshl_add_u64 v[2:3], v[2:3], 0, v[170:171]
	global_store_dwordx2 v[2:3], v[4:5], off

; __device__ __forceinline__ unsigned pk4_fp8(float a, float b, float c, float d) {
;     a = fminf(fmaxf(a, -448.f), 448.f); b = fminf(fmaxf(b, -448.f), 448.f); c = fminf(fmaxf(c, -448.f), 448.f); d = fminf(fmaxf(d, -448.f), 448.f);
;     int w = 0; w = __builtin_amdgcn_cvt_pk_fp8_f32(a, b, w, false); w = __builtin_amdgcn_cvt_pk_fp8_f32(c, d, w, true); return (unsigned)w;
; }
;     __device__ __forceinline__ void operator()(const f32x4 (&acc)[2][2][4][2], const Unit& u, int wr, int wc, int fr, int fq) const {
;     ...
;                     if (g == 1) {
;                         unsigned char* d8 = (unsigned char*)(QKV + (size_t)g * 4 * 16 * 4096 * 128) + ((((size_t)b * 16 + head) * 4096 + s) * 128 + (wc >> 1) * 64 + (fq & 1) * 32 + ((wc & 1) * 2 + (fq >> 1)) * 8);
;                         u32x2 w8; w8.x = pk4_fp8(v0[0] * 16.f, v0[1] * 16.f, v0[2] * 16.f, v0[3] * 16.f); w8.y = pk4_fp8(v1[0] * 16.f, v1[1] * 16.f, v1[2] * 16.f, v1[3] * 16.f);
;                         *(u32x2*)d8 = w8;
;                     } else if (g == 3 || g == 4) {
;                         unsigned char* d8 = (unsigned char*)(QKV + (size_t)g * 4 * 16 * 4096 * 128) + ((((size_t)b * 16 + head) * 4096 + s) * 128 + wc * 32 + 8 * fq);
;                         u32x2 w8; w8.x = pk4_fp8(v0[0] * 16.f, v0[1] * 16.f, v0[2] * 16.f, v0[3] * 16.f); w8.y = pk4_fp8(v1[0] * 16.f, v1[1] * 16.f, v1[2] * 16.f, v1[3] * 16.f);
;                         *(u32x2*)d8 = w8;
.LBB0_687:
	s_andn2_b64 vcc, exec, s[52:53]
	s_cbranch_vccnz .LBB0_689
	v_mul_f32_e32 v4, 0x41800000, v102
	v_mul_f32_e32 v5, 0x41800000, v103
	v_med3_f32 v8, v4, s67, v206
	v_med3_f32 v5, v5, s67, v206
	v_cvt_pk_fp8_f32 v4, v8, v5
	v_mul_f32_e32 v6, 0x41800000, v104
	v_mul_f32_e32 v7, 0x41800000, v105
	v_med3_f32 v6, v6, s67, v206
	v_med3_f32 v7, v7, s67, v206
	v_cvt_pk_fp8_f32 v4, v6, v7 op_sel:[0,0,1]
	v_mul_f32_e32 v5, 0x41800000, v98
	v_mul_f32_e32 v6, 0x41800000, v99
	v_med3_f32 v9, v5, s67, v206
	v_med3_f32 v6, v6, s67, v206
	v_cvt_pk_fp8_f32 v5, v9, v6
	v_mul_f32_e32 v7, 0x41800000, v100
	v_mul_f32_e32 v8, 0x41800000, v101
	v_med3_f32 v7, v7, s67, v206
	v_med3_f32 v8, v8, s67, v206
	v_cvt_pk_fp8_f32 v5, v7, v8 op_sel:[0,0,1]
	v_lshl_add_u64 v[2:3], v[146:147], 0, s[46:47]
	v_lshlrev_b64 v[2:3], 7, v[2:3]
	v_lshl_add_u64 v[2:3], v[176:177], 0, v[2:3]
	global_store_dwordx2 v[2:3], v[4:5], off

; __device__ __forceinline__ unsigned pk4_fp8(float a, float b, float c, float d) {
;     a = fminf(fmaxf(a, -448.f), 448.f); b = fminf(fmaxf(b, -448.f), 448.f); c = fminf(fmaxf(c, -448.f), 448.f); d = fminf(fmaxf(d, -448.f), 448.f);
;     int w = 0; w = __builtin_amdgcn_cvt_pk_fp8_f32(a, b, w, false); w = __builtin_amdgcn_cvt_pk_fp8_f32(c, d, w, true); return (unsigned)w;
; }
;     __device__ __forceinline__ void operator()(const f32x4 (&acc)[2][2][4][2], const Unit& u, int wr, int wc, int fr, int fq) const {
;     ...
;                     } else if (g == 3 || g == 4) {
;                         unsigned char* d8 = (unsigned char*)(QKV + (size_t)g * 4 * 16 * 4096 * 128) + ((((size_t)b * 16 + head) * 4096 + s) * 128 + wc * 32 + 8 * fq);
;                         u32x2 w8; w8.x = pk4_fp8(v0[0] * 16.f, v0[1] * 16.f, v0[2] * 16.f, v0[3] * 16.f); w8.y = pk4_fp8(v1[0] * 16.f, v1[1] * 16.f, v1[2] * 16.f, v1[3] * 16.f);
;                         *(u32x2*)d8 = w8;
.LBB0_707:
	s_andn2_b64 vcc, exec, s[52:53]
	s_cbranch_vccnz .LBB0_709
	v_mul_f32_e32 v154, 0x41800000, v94
	v_mul_f32_e32 v155, 0x41800000, v95
	v_med3_f32 v158, v154, s67, v206
	v_med3_f32 v155, v155, s67, v206
	v_cvt_pk_fp8_f32 v154, v158, v155
	v_mul_f32_e32 v156, 0x41800000, v96
	v_mul_f32_e32 v157, 0x41800000, v97
	v_med3_f32 v156, v156, s67, v206
	v_med3_f32 v157, v157, s67, v206
	v_cvt_pk_fp8_f32 v154, v156, v157 op_sel:[0,0,1]
	v_mul_f32_e32 v155, 0x41800000, v90
	v_mul_f32_e32 v156, 0x41800000, v91
	v_med3_f32 v159, v155, s67, v206
	v_med3_f32 v156, v156, s67, v206
	v_cvt_pk_fp8_f32 v155, v159, v156
	s_lshl_b32 s52, s41, 1
	v_readlane_b32 s54, v253, 46
	v_mul_f32_e32 v157, 0x41800000, v92
	v_mul_f32_e32 v158, 0x41800000, v93
	v_readlane_b32 s55, v253, 47
	s_add_u32 s52, s54, s52
	v_lshl_add_u64 v[152:153], v[146:147], 0, s[24:25]
	v_med3_f32 v157, v157, s67, v206
	v_med3_f32 v158, v158, s67, v206
	s_addc_u32 s53, s55, 0
	v_lshlrev_b64 v[152:153], 7, v[152:153]
	v_cvt_pk_fp8_f32 v155, v157, v158 op_sel:[0,0,1]
	v_lshl_add_u64 v[152:153], s[52:53], 0, v[152:153]
	v_lshl_add_u64 v[152:153], v[152:153], 0, s[28:29]
	v_lshl_add_u64 v[152:153], v[152:153], 0, v[170:171]
	global_store_dwordx2 v[152:153], v[154:155], off

; __device__ __forceinline__ unsigned pk4_fp8(float a, float b, float c, float d) {
;     a = fminf(fmaxf(a, -448.f), 448.f); b = fminf(fmaxf(b, -448.f), 448.f); c = fminf(fmaxf(c, -448.f), 448.f); d = fminf(fmaxf(d, -448.f), 448.f);
;     int w = 0; w = __builtin_amdgcn_cvt_pk_fp8_f32(a, b, w, false); w = __builtin_amdgcn_cvt_pk_fp8_f32(c, d, w, true); return (unsigned)w;
; }
;     __device__ __forceinline__ void operator()(const f32x4 (&acc)[2][2][4][2], const Unit& u, int wr, int wc, int fr, int fq) const {
;     ...
;                     if (g == 1) {
;                         unsigned char* d8 = (unsigned char*)(QKV + (size_t)g * 4 * 16 * 4096 * 128) + ((((size_t)b * 16 + head) * 4096 + s) * 128 + (wc >> 1) * 64 + (fq & 1) * 32 + ((wc & 1) * 2 + (fq >> 1)) * 8);
;                         u32x2 w8; w8.x = pk4_fp8(v0[0] * 16.f, v0[1] * 16.f, v0[2] * 16.f, v0[3] * 16.f); w8.y = pk4_fp8(v1[0] * 16.f, v1[1] * 16.f, v1[2] * 16.f, v1[3] * 16.f);
;                         *(u32x2*)d8 = w8;
;                     } else if (g == 3 || g == 4) {
;                         unsigned char* d8 = (unsigned char*)(QKV + (size_t)g * 4 * 16 * 4096 * 128) + ((((size_t)b * 16 + head) * 4096 + s) * 128 + wc * 32 + 8 * fq);
;                         u32x2 w8; w8.x = pk4_fp8(v0[0] * 16.f, v0[1] * 16.f, v0[2] * 16.f, v0[3] * 16.f); w8.y = pk4_fp8(v1[0] * 16.f, v1[1] * 16.f, v1[2] * 16.f, v1[3] * 16.f);
;                         *(u32x2*)d8 = w8;
.LBB0_710:
	s_andn2_b64 vcc, exec, s[52:53]
	s_cbranch_vccnz .LBB0_712
	v_mul_f32_e32 v154, 0x41800000, v94
	v_mul_f32_e32 v155, 0x41800000, v95
	v_med3_f32 v158, v154, s67, v206
	v_med3_f32 v155, v155, s67, v206
	v_cvt_pk_fp8_f32 v154, v158, v155
	v_mul_f32_e32 v156, 0x41800000, v96
	v_mul_f32_e32 v157, 0x41800000, v97
	v_med3_f32 v156, v156, s67, v206
	v_med3_f32 v157, v157, s67, v206
	v_cvt_pk_fp8_f32 v154, v156, v157 op_sel:[0,0,1]
	v_mul_f32_e32 v155, 0x41800000, v90
	v_mul_f32_e32 v156, 0x41800000, v91
	v_med3_f32 v159, v155, s67, v206
	v_med3_f32 v156, v156, s67, v206
	v_cvt_pk_fp8_f32 v155, v159, v156
	v_mul_f32_e32 v157, 0x41800000, v92
	v_mul_f32_e32 v158, 0x41800000, v93
	v_med3_f32 v157, v157, s67, v206
	v_med3_f32 v158, v158, s67, v206
	v_cvt_pk_fp8_f32 v155, v157, v158 op_sel:[0,0,1]
	v_lshl_add_u64 v[152:153], v[146:147], 0, s[24:25]
	v_lshlrev_b64 v[152:153], 7, v[152:153]
	v_lshl_add_u64 v[152:153], v[176:177], 0, v[152:153]
	global_store_dwordx2 v[152:153], v[154:155], off

; __device__ __forceinline__ unsigned pk4_fp8(float a, float b, float c, float d) {
;     a = fminf(fmaxf(a, -448.f), 448.f); b = fminf(fmaxf(b, -448.f), 448.f); c = fminf(fmaxf(c, -448.f), 448.f); d = fminf(fmaxf(d, -448.f), 448.f);
;     int w = 0; w = __builtin_amdgcn_cvt_pk_fp8_f32(a, b, w, false); w = __builtin_amdgcn_cvt_pk_fp8_f32(c, d, w, true); return (unsigned)w;
; }
;     __device__ __forceinline__ void operator()(const f32x4 (&acc)[2][2][4][2], const Unit& u, int wr, int wc, int fr, int fq) const {
;     ...
;                     } else if (g == 3 || g == 4) {
;                         unsigned char* d8 = (unsigned char*)(QKV + (size_t)g * 4 * 16 * 4096 * 128) + ((((size_t)b * 16 + head) * 4096 + s) * 128 + wc * 32 + 8 * fq);
;                         u32x2 w8; w8.x = pk4_fp8(v0[0] * 16.f, v0[1] * 16.f, v0[2] * 16.f, v0[3] * 16.f); w8.y = pk4_fp8(v1[0] * 16.f, v1[1] * 16.f, v1[2] * 16.f, v1[3] * 16.f);
;                         *(u32x2*)d8 = w8;
.LBB0_722:
	s_andn2_b64 vcc, exec, s[52:53]
	s_cbranch_vccnz .LBB0_724
	v_mul_f32_e32 v4, 0x41800000, v86
	v_mul_f32_e32 v5, 0x41800000, v87
	v_med3_f32 v8, v4, s67, v206
	v_med3_f32 v5, v5, s67, v206
	v_cvt_pk_fp8_f32 v4, v8, v5
	v_mul_f32_e32 v6, 0x41800000, v88
	v_mul_f32_e32 v7, 0x41800000, v89
	v_med3_f32 v6, v6, s67, v206
	v_med3_f32 v7, v7, s67, v206
	v_cvt_pk_fp8_f32 v4, v6, v7 op_sel:[0,0,1]
	v_mul_f32_e32 v5, 0x41800000, v82
	v_mul_f32_e32 v6, 0x41800000, v83
	v_med3_f32 v9, v5, s67, v206
	v_med3_f32 v6, v6, s67, v206
	v_cvt_pk_fp8_f32 v5, v9, v6
	s_lshl_b32 s52, s41, 1
	v_readlane_b32 s54, v253, 46
	v_mul_f32_e32 v7, 0x41800000, v84
	v_mul_f32_e32 v8, 0x41800000, v85
	v_readlane_b32 s55, v253, 47
	s_add_u32 s52, s54, s52
	v_lshl_add_u64 v[2:3], v[146:147], 0, s[46:47]
	v_med3_f32 v7, v7, s67, v206
	v_med3_f32 v8, v8, s67, v206
	s_addc_u32 s53, s55, 0
	v_lshlrev_b64 v[2:3], 7, v[2:3]
	v_cvt_pk_fp8_f32 v5, v7, v8 op_sel:[0,0,1]
	v_lshl_add_u64 v[2:3], s[52:53], 0, v[2:3]
	v_lshl_add_u64 v[2:3], v[2:3], 0, s[28:29]
	v_lshl_add_u64 v[2:3], v[2:3], 0, v[170:171]
	global_store_dwordx2 v[2:3], v[4:5], off

; __device__ __forceinline__ unsigned pk4_fp8(float a, float b, float c, float d) {
;     a = fminf(fmaxf(a, -448.f), 448.f); b = fminf(fmaxf(b, -448.f), 448.f); c = fminf(fmaxf(c, -448.f), 448.f); d = fminf(fmaxf(d, -448.f), 448.f);
;     int w = 0; w = __builtin_amdgcn_cvt_pk_fp8_f32(a, b, w, false); w = __builtin_amdgcn_cvt_pk_fp8_f32(c, d, w, true); return (unsigned)w;
; }
;     __device__ __forceinline__ void operator()(const f32x4 (&acc)[2][2][4][2], const Unit& u, int wr, int wc, int fr, int fq) const {
;     ...
;                     if (g == 1) {
;                         unsigned char* d8 = (unsigned char*)(QKV + (size_t)g * 4 * 16 * 4096 * 128) + ((((size_t)b * 16 + head) * 4096 + s) * 128 + (wc >> 1) * 64 + (fq & 1) * 32 + ((wc & 1) * 2 + (fq >> 1)) * 8);
;                         u32x2 w8; w8.x = pk4_fp8(v0[0] * 16.f, v0[1] * 16.f, v0[2] * 16.f, v0[3] * 16.f); w8.y = pk4_fp8(v1[0] * 16.f, v1[1] * 16.f, v1[2] * 16.f, v1[3] * 16.f);
;                         *(u32x2*)d8 = w8;
;                     } else if (g == 3 || g == 4) {
;                         unsigned char* d8 = (unsigned char*)(QKV + (size_t)g * 4 * 16 * 4096 * 128) + ((((size_t)b * 16 + head) * 4096 + s) * 128 + wc * 32 + 8 * fq);
;                         u32x2 w8; w8.x = pk4_fp8(v0[0] * 16.f, v0[1] * 16.f, v0[2] * 16.f, v0[3] * 16.f); w8.y = pk4_fp8(v1[0] * 16.f, v1[1] * 16.f, v1[2] * 16.f, v1[3] * 16.f);
;                         *(u32x2*)d8 = w8;
.LBB0_725:
	s_andn2_b64 vcc, exec, s[52:53]
	s_cbranch_vccnz .LBB0_727
	v_mul_f32_e32 v4, 0x41800000, v86
	v_mul_f32_e32 v5, 0x41800000, v87
	v_med3_f32 v8, v4, s67, v206
	v_med3_f32 v5, v5, s67, v206
	v_cvt_pk_fp8_f32 v4, v8, v5
	v_mul_f32_e32 v6, 0x41800000, v88
	v_mul_f32_e32 v7, 0x41800000, v89
	v_med3_f32 v6, v6, s67, v206
	v_med3_f32 v7, v7, s67, v206
	v_cvt_pk_fp8_f32 v4, v6, v7 op_sel:[0,0,1]
	v_mul_f32_e32 v5, 0x41800000, v82
	v_mul_f32_e32 v6, 0x41800000, v83
	v_med3_f32 v9, v5, s67, v206
	v_med3_f32 v6, v6, s67, v206
	v_cvt_pk_fp8_f32 v5, v9, v6
	v_mul_f32_e32 v7, 0x41800000, v84
	v_mul_f32_e32 v8, 0x41800000, v85
	v_med3_f32 v7, v7, s67, v206
	v_med3_f32 v8, v8, s67, v206
	v_cvt_pk_fp8_f32 v5, v7, v8 op_sel:[0,0,1]
	v_lshl_add_u64 v[2:3], v[146:147], 0, s[46:47]
	v_lshlrev_b64 v[2:3], 7, v[2:3]
	v_lshl_add_u64 v[2:3], v[176:177], 0, v[2:3]
	global_store_dwordx2 v[2:3], v[4:5], off

; __device__ __forceinline__ unsigned pk4_fp8(float a, float b, float c, float d) {
;     a = fminf(fmaxf(a, -448.f), 448.f); b = fminf(fmaxf(b, -448.f), 448.f); c = fminf(fmaxf(c, -448.f), 448.f); d = fminf(fmaxf(d, -448.f), 448.f);
;     int w = 0; w = __builtin_amdgcn_cvt_pk_fp8_f32(a, b, w, false); w = __builtin_amdgcn_cvt_pk_fp8_f32(c, d, w, true); return (unsigned)w;
; }
;     __device__ __forceinline__ void operator()(const f32x4 (&acc)[2][2][4][2], const Unit& u, int wr, int wc, int fr, int fq) const {
;     ...
;                     } else if (g == 3 || g == 4) {
;                         unsigned char* d8 = (unsigned char*)(QKV + (size_t)g * 4 * 16 * 4096 * 128) + ((((size_t)b * 16 + head) * 4096 + s) * 128 + wc * 32 + 8 * fq);
;                         u32x2 w8; w8.x = pk4_fp8(v0[0] * 16.f, v0[1] * 16.f, v0[2] * 16.f, v0[3] * 16.f); w8.y = pk4_fp8(v1[0] * 16.f, v1[1] * 16.f, v1[2] * 16.f, v1[3] * 16.f);
;                         *(u32x2*)d8 = w8;
.LBB0_745:
	s_andn2_b64 vcc, exec, s[52:53]
	s_cbranch_vccnz .LBB0_747
	v_mul_f32_e32 v154, 0x41800000, v78
	v_mul_f32_e32 v155, 0x41800000, v79
	v_med3_f32 v158, v154, s67, v206
	v_med3_f32 v155, v155, s67, v206
	v_cvt_pk_fp8_f32 v154, v158, v155
	v_mul_f32_e32 v156, 0x41800000, v80
	v_mul_f32_e32 v157, 0x41800000, v81
	v_med3_f32 v156, v156, s67, v206
	v_med3_f32 v157, v157, s67, v206
	v_cvt_pk_fp8_f32 v154, v156, v157 op_sel:[0,0,1]
	v_mul_f32_e32 v155, 0x41800000, v74
	v_mul_f32_e32 v156, 0x41800000, v75
	v_med3_f32 v159, v155, s67, v206
	v_med3_f32 v156, v156, s67, v206
	v_cvt_pk_fp8_f32 v155, v159, v156
	s_lshl_b32 s52, s41, 1
	v_readlane_b32 s54, v253, 46
	v_mul_f32_e32 v157, 0x41800000, v76
	v_mul_f32_e32 v158, 0x41800000, v77
	v_readlane_b32 s55, v253, 47
	s_add_u32 s52, s54, s52
	v_lshl_add_u64 v[152:153], v[146:147], 0, s[24:25]
	v_med3_f32 v157, v157, s67, v206
	v_med3_f32 v158, v158, s67, v206
	s_addc_u32 s53, s55, 0
	v_lshlrev_b64 v[152:153], 7, v[152:153]
	v_cvt_pk_fp8_f32 v155, v157, v158 op_sel:[0,0,1]
	v_lshl_add_u64 v[152:153], s[52:53], 0, v[152:153]
	v_lshl_add_u64 v[152:153], v[152:153], 0, s[28:29]
	v_lshl_add_u64 v[152:153], v[152:153], 0, v[170:171]
	global_store_dwordx2 v[152:153], v[154:155], off

; __device__ __forceinline__ unsigned pk4_fp8(float a, float b, float c, float d) {
;     a = fminf(fmaxf(a, -448.f), 448.f); b = fminf(fmaxf(b, -448.f), 448.f); c = fminf(fmaxf(c, -448.f), 448.f); d = fminf(fmaxf(d, -448.f), 448.f);
;     int w = 0; w = __builtin_amdgcn_cvt_pk_fp8_f32(a, b, w, false); w = __builtin_amdgcn_cvt_pk_fp8_f32(c, d, w, true); return (unsigned)w;
; }
;     __device__ __forceinline__ void operator()(const f32x4 (&acc)[2][2][4][2], const Unit& u, int wr, int wc, int fr, int fq) const {
;     ...
;                     if (g == 1) {
;                         unsigned char* d8 = (unsigned char*)(QKV + (size_t)g * 4 * 16 * 4096 * 128) + ((((size_t)b * 16 + head) * 4096 + s) * 128 + (wc >> 1) * 64 + (fq & 1) * 32 + ((wc & 1) * 2 + (fq >> 1)) * 8);
;                         u32x2 w8; w8.x = pk4_fp8(v0[0] * 16.f, v0[1] * 16.f, v0[2] * 16.f, v0[3] * 16.f); w8.y = pk4_fp8(v1[0] * 16.f, v1[1] * 16.f, v1[2] * 16.f, v1[3] * 16.f);
;                         *(u32x2*)d8 = w8;
;                     } else if (g == 3 || g == 4) {
;                         unsigned char* d8 = (unsigned char*)(QKV + (size_t)g * 4 * 16 * 4096 * 128) + ((((size_t)b * 16 + head) * 4096 + s) * 128 + wc * 32 + 8 * fq);
;                         u32x2 w8; w8.x = pk4_fp8(v0[0] * 16.f, v0[1] * 16.f, v0[2] * 16.f, v0[3] * 16.f); w8.y = pk4_fp8(v1[0] * 16.f, v1[1] * 16.f, v1[2] * 16.f, v1[3] * 16.f);
;                         *(u32x2*)d8 = w8;
.LBB0_748:
	s_andn2_b64 vcc, exec, s[52:53]
	s_cbranch_vccnz .LBB0_750
	v_mul_f32_e32 v154, 0x41800000, v78
	v_mul_f32_e32 v155, 0x41800000, v79
	v_med3_f32 v158, v154, s67, v206
	v_med3_f32 v155, v155, s67, v206
	v_cvt_pk_fp8_f32 v154, v158, v155
	v_mul_f32_e32 v156, 0x41800000, v80
	v_mul_f32_e32 v157, 0x41800000, v81
	v_med3_f32 v156, v156, s67, v206
	v_med3_f32 v157, v157, s67, v206
	v_cvt_pk_fp8_f32 v154, v156, v157 op_sel:[0,0,1]
	v_mul_f32_e32 v155, 0x41800000, v74
	v_mul_f32_e32 v156, 0x41800000, v75
	v_med3_f32 v159, v155, s67, v206
	v_med3_f32 v156, v156, s67, v206
	v_cvt_pk_fp8_f32 v155, v159, v156
	v_mul_f32_e32 v157, 0x41800000, v76
	v_mul_f32_e32 v158, 0x41800000, v77
	v_med3_f32 v157, v157, s67, v206
	v_med3_f32 v158, v158, s67, v206
	v_cvt_pk_fp8_f32 v155, v157, v158 op_sel:[0,0,1]
	v_lshl_add_u64 v[152:153], v[146:147], 0, s[24:25]
	v_lshlrev_b64 v[152:153], 7, v[152:153]
	v_lshl_add_u64 v[152:153], v[176:177], 0, v[152:153]
	global_store_dwordx2 v[152:153], v[154:155], off

; __device__ __forceinline__ unsigned pk4_fp8(float a, float b, float c, float d) {
;     a = fminf(fmaxf(a, -448.f), 448.f); b = fminf(fmaxf(b, -448.f), 448.f); c = fminf(fmaxf(c, -448.f), 448.f); d = fminf(fmaxf(d, -448.f), 448.f);
;     int w = 0; w = __builtin_amdgcn_cvt_pk_fp8_f32(a, b, w, false); w = __builtin_amdgcn_cvt_pk_fp8_f32(c, d, w, true); return (unsigned)w;
; }
;     __device__ __forceinline__ void operator()(const f32x4 (&acc)[2][2][4][2], const Unit& u, int wr, int wc, int fr, int fq) const {
;     ...
;                     } else if (g == 3 || g == 4) {
;                         unsigned char* d8 = (unsigned char*)(QKV + (size_t)g * 4 * 16 * 4096 * 128) + ((((size_t)b * 16 + head) * 4096 + s) * 128 + wc * 32 + 8 * fq);
;                         u32x2 w8; w8.x = pk4_fp8(v0[0] * 16.f, v0[1] * 16.f, v0[2] * 16.f, v0[3] * 16.f); w8.y = pk4_fp8(v1[0] * 16.f, v1[1] * 16.f, v1[2] * 16.f, v1[3] * 16.f);
;                         *(u32x2*)d8 = w8;
.LBB0_760:
	s_andn2_b64 vcc, exec, s[52:53]
	s_cbranch_vccnz .LBB0_762
	v_mul_f32_e32 v4, 0x41800000, v70
	v_mul_f32_e32 v5, 0x41800000, v71
	v_med3_f32 v8, v4, s67, v206
	v_med3_f32 v5, v5, s67, v206
	v_cvt_pk_fp8_f32 v4, v8, v5
	v_mul_f32_e32 v6, 0x41800000, v72
	v_mul_f32_e32 v7, 0x41800000, v73
	v_med3_f32 v6, v6, s67, v206
	v_med3_f32 v7, v7, s67, v206
	v_cvt_pk_fp8_f32 v4, v6, v7 op_sel:[0,0,1]
	v_mul_f32_e32 v5, 0x41800000, v66
	v_mul_f32_e32 v6, 0x41800000, v67
	v_med3_f32 v9, v5, s67, v206
	v_med3_f32 v6, v6, s67, v206
	v_cvt_pk_fp8_f32 v5, v9, v6
	s_lshl_b32 s52, s41, 1
	v_readlane_b32 s54, v253, 46
	v_mul_f32_e32 v7, 0x41800000, v68
	v_mul_f32_e32 v8, 0x41800000, v69
	v_readlane_b32 s55, v253, 47
	s_add_u32 s52, s54, s52
	v_lshl_add_u64 v[2:3], v[146:147], 0, s[46:47]
	v_med3_f32 v7, v7, s67, v206
	v_med3_f32 v8, v8, s67, v206
	s_addc_u32 s53, s55, 0
	v_lshlrev_b64 v[2:3], 7, v[2:3]
	v_cvt_pk_fp8_f32 v5, v7, v8 op_sel:[0,0,1]
	v_lshl_add_u64 v[2:3], s[52:53], 0, v[2:3]
	v_lshl_add_u64 v[2:3], v[2:3], 0, s[28:29]
	v_lshl_add_u64 v[2:3], v[2:3], 0, v[170:171]
	global_store_dwordx2 v[2:3], v[4:5], off

; __device__ __forceinline__ unsigned pk4_fp8(float a, float b, float c, float d) {
;     a = fminf(fmaxf(a, -448.f), 448.f); b = fminf(fmaxf(b, -448.f), 448.f); c = fminf(fmaxf(c, -448.f), 448.f); d = fminf(fmaxf(d, -448.f), 448.f);
;     int w = 0; w = __builtin_amdgcn_cvt_pk_fp8_f32(a, b, w, false); w = __builtin_amdgcn_cvt_pk_fp8_f32(c, d, w, true); return (unsigned)w;
; }
;     __device__ __forceinline__ void operator()(const f32x4 (&acc)[2][2][4][2], const Unit& u, int wr, int wc, int fr, int fq) const {
;     ...
;                     if (g == 1) {
;                         unsigned char* d8 = (unsigned char*)(QKV + (size_t)g * 4 * 16 * 4096 * 128) + ((((size_t)b * 16 + head) * 4096 + s) * 128 + (wc >> 1) * 64 + (fq & 1) * 32 + ((wc & 1) * 2 + (fq >> 1)) * 8);
;                         u32x2 w8; w8.x = pk4_fp8(v0[0] * 16.f, v0[1] * 16.f, v0[2] * 16.f, v0[3] * 16.f); w8.y = pk4_fp8(v1[0] * 16.f, v1[1] * 16.f, v1[2] * 16.f, v1[3] * 16.f);
;                         *(u32x2*)d8 = w8;
;                     } else if (g == 3 || g == 4) {
;                         unsigned char* d8 = (unsigned char*)(QKV + (size_t)g * 4 * 16 * 4096 * 128) + ((((size_t)b * 16 + head) * 4096 + s) * 128 + wc * 32 + 8 * fq);
;                         u32x2 w8; w8.x = pk4_fp8(v0[0] * 16.f, v0[1] * 16.f, v0[2] * 16.f, v0[3] * 16.f); w8.y = pk4_fp8(v1[0] * 16.f, v1[1] * 16.f, v1[2] * 16.f, v1[3] * 16.f);
;                         *(u32x2*)d8 = w8;
.LBB0_763:
	s_andn2_b64 vcc, exec, s[52:53]
	s_cbranch_vccnz .LBB0_765
	v_mul_f32_e32 v4, 0x41800000, v70
	v_mul_f32_e32 v5, 0x41800000, v71
	v_med3_f32 v8, v4, s67, v206
	v_med3_f32 v5, v5, s67, v206
	v_cvt_pk_fp8_f32 v4, v8, v5
	v_mul_f32_e32 v6, 0x41800000, v72
	v_mul_f32_e32 v7, 0x41800000, v73
	v_med3_f32 v6, v6, s67, v206
	v_med3_f32 v7, v7, s67, v206
	v_cvt_pk_fp8_f32 v4, v6, v7 op_sel:[0,0,1]
	v_mul_f32_e32 v5, 0x41800000, v66
	v_mul_f32_e32 v6, 0x41800000, v67
	v_med3_f32 v9, v5, s67, v206
	v_med3_f32 v6, v6, s67, v206
	v_cvt_pk_fp8_f32 v5, v9, v6
	v_mul_f32_e32 v7, 0x41800000, v68
	v_mul_f32_e32 v8, 0x41800000, v69
	v_med3_f32 v7, v7, s67, v206
	v_med3_f32 v8, v8, s67, v206
	v_cvt_pk_fp8_f32 v5, v7, v8 op_sel:[0,0,1]
	v_lshl_add_u64 v[2:3], v[146:147], 0, s[46:47]
	v_lshlrev_b64 v[2:3], 7, v[2:3]
	v_lshl_add_u64 v[2:3], v[176:177], 0, v[2:3]
	global_store_dwordx2 v[2:3], v[4:5], off

; __device__ __forceinline__ unsigned pk4_fp8(float a, float b, float c, float d) {
;     a = fminf(fmaxf(a, -448.f), 448.f); b = fminf(fmaxf(b, -448.f), 448.f); c = fminf(fmaxf(c, -448.f), 448.f); d = fminf(fmaxf(d, -448.f), 448.f);
;     int w = 0; w = __builtin_amdgcn_cvt_pk_fp8_f32(a, b, w, false); w = __builtin_amdgcn_cvt_pk_fp8_f32(c, d, w, true); return (unsigned)w;
; }
;     __device__ __forceinline__ void operator()(const f32x4 (&acc)[2][2][4][2], const Unit& u, int wr, int wc, int fr, int fq) const {
;     ...
;                     } else if (g == 3 || g == 4) {
;                         unsigned char* d8 = (unsigned char*)(QKV + (size_t)g * 4 * 16 * 4096 * 128) + ((((size_t)b * 16 + head) * 4096 + s) * 128 + wc * 32 + 8 * fq);
;                         u32x2 w8; w8.x = pk4_fp8(v0[0] * 16.f, v0[1] * 16.f, v0[2] * 16.f, v0[3] * 16.f); w8.y = pk4_fp8(v1[0] * 16.f, v1[1] * 16.f, v1[2] * 16.f, v1[3] * 16.f);
;                         *(u32x2*)d8 = w8;
.LBB0_783:
	s_andn2_b64 vcc, exec, s[52:53]
	s_cbranch_vccnz .LBB0_785
	v_mul_f32_e32 v154, 0x41800000, v62
	v_mul_f32_e32 v155, 0x41800000, v63
	v_med3_f32 v158, v154, s67, v206
	v_med3_f32 v155, v155, s67, v206
	v_cvt_pk_fp8_f32 v154, v158, v155
	v_mul_f32_e32 v156, 0x41800000, v64
	v_mul_f32_e32 v157, 0x41800000, v65
	v_med3_f32 v156, v156, s67, v206
	v_med3_f32 v157, v157, s67, v206
	v_cvt_pk_fp8_f32 v154, v156, v157 op_sel:[0,0,1]
	v_mul_f32_e32 v155, 0x41800000, v58
	v_mul_f32_e32 v156, 0x41800000, v59
	v_med3_f32 v159, v155, s67, v206
	v_med3_f32 v156, v156, s67, v206
	v_cvt_pk_fp8_f32 v155, v159, v156
	s_lshl_b32 s52, s41, 1
	v_readlane_b32 s54, v253, 46
	v_mul_f32_e32 v157, 0x41800000, v60
	v_mul_f32_e32 v158, 0x41800000, v61
	v_readlane_b32 s55, v253, 47
	s_add_u32 s52, s54, s52
	v_lshl_add_u64 v[152:153], v[146:147], 0, s[24:25]
	v_med3_f32 v157, v157, s67, v206
	v_med3_f32 v158, v158, s67, v206
	s_addc_u32 s53, s55, 0
	v_lshlrev_b64 v[152:153], 7, v[152:153]
	v_cvt_pk_fp8_f32 v155, v157, v158 op_sel:[0,0,1]
	v_lshl_add_u64 v[152:153], s[52:53], 0, v[152:153]
	v_lshl_add_u64 v[152:153], v[152:153], 0, s[28:29]
	v_lshl_add_u64 v[152:153], v[152:153], 0, v[170:171]
	global_store_dwordx2 v[152:153], v[154:155], off

; __device__ __forceinline__ unsigned pk4_fp8(float a, float b, float c, float d) {
;     a = fminf(fmaxf(a, -448.f), 448.f); b = fminf(fmaxf(b, -448.f), 448.f); c = fminf(fmaxf(c, -448.f), 448.f); d = fminf(fmaxf(d, -448.f), 448.f);
;     int w = 0; w = __builtin_amdgcn_cvt_pk_fp8_f32(a, b, w, false); w = __builtin_amdgcn_cvt_pk_fp8_f32(c, d, w, true); return (unsigned)w;
; }
;     __device__ __forceinline__ void operator()(const f32x4 (&acc)[2][2][4][2], const Unit& u, int wr, int wc, int fr, int fq) const {
;     ...
;                     if (g == 1) {
;                         unsigned char* d8 = (unsigned char*)(QKV + (size_t)g * 4 * 16 * 4096 * 128) + ((((size_t)b * 16 + head) * 4096 + s) * 128 + (wc >> 1) * 64 + (fq & 1) * 32 + ((wc & 1) * 2 + (fq >> 1)) * 8);
;                         u32x2 w8; w8.x = pk4_fp8(v0[0] * 16.f, v0[1] * 16.f, v0[2] * 16.f, v0[3] * 16.f); w8.y = pk4_fp8(v1[0] * 16.f, v1[1] * 16.f, v1[2] * 16.f, v1[3] * 16.f);
;                         *(u32x2*)d8 = w8;
;                     } else if (g == 3 || g == 4) {
;                         unsigned char* d8 = (unsigned char*)(QKV + (size_t)g * 4 * 16 * 4096 * 128) + ((((size_t)b * 16 + head) * 4096 + s) * 128 + wc * 32 + 8 * fq);
;                         u32x2 w8; w8.x = pk4_fp8(v0[0] * 16.f, v0[1] * 16.f, v0[2] * 16.f, v0[3] * 16.f); w8.y = pk4_fp8(v1[0] * 16.f, v1[1] * 16.f, v1[2] * 16.f, v1[3] * 16.f);
;                         *(u32x2*)d8 = w8;
.LBB0_786:
	s_andn2_b64 vcc, exec, s[52:53]
	s_cbranch_vccnz .LBB0_788
	v_mul_f32_e32 v154, 0x41800000, v62
	v_mul_f32_e32 v155, 0x41800000, v63
	v_med3_f32 v158, v154, s67, v206
	v_med3_f32 v155, v155, s67, v206
	v_cvt_pk_fp8_f32 v154, v158, v155
	v_mul_f32_e32 v156, 0x41800000, v64
	v_mul_f32_e32 v157, 0x41800000, v65
	v_med3_f32 v156, v156, s67, v206
	v_med3_f32 v157, v157, s67, v206
	v_cvt_pk_fp8_f32 v154, v156, v157 op_sel:[0,0,1]
	v_mul_f32_e32 v155, 0x41800000, v58
	v_mul_f32_e32 v156, 0x41800000, v59
	v_med3_f32 v159, v155, s67, v206
	v_med3_f32 v156, v156, s67, v206
	v_cvt_pk_fp8_f32 v155, v159, v156
	v_mul_f32_e32 v157, 0x41800000, v60
	v_mul_f32_e32 v158, 0x41800000, v61
	v_med3_f32 v157, v157, s67, v206
	v_med3_f32 v158, v158, s67, v206
	v_cvt_pk_fp8_f32 v155, v157, v158 op_sel:[0,0,1]
	v_lshl_add_u64 v[152:153], v[146:147], 0, s[24:25]
	v_lshlrev_b64 v[152:153], 7, v[152:153]
	v_lshl_add_u64 v[152:153], v[176:177], 0, v[152:153]
	global_store_dwordx2 v[152:153], v[154:155], off

; __device__ __forceinline__ unsigned pk4_fp8(float a, float b, float c, float d) {
;     a = fminf(fmaxf(a, -448.f), 448.f); b = fminf(fmaxf(b, -448.f), 448.f); c = fminf(fmaxf(c, -448.f), 448.f); d = fminf(fmaxf(d, -448.f), 448.f);
;     int w = 0; w = __builtin_amdgcn_cvt_pk_fp8_f32(a, b, w, false); w = __builtin_amdgcn_cvt_pk_fp8_f32(c, d, w, true); return (unsigned)w;
; }
;     __device__ __forceinline__ void operator()(const f32x4 (&acc)[2][2][4][2], const Unit& u, int wr, int wc, int fr, int fq) const {
;     ...
;                     } else if (g == 3 || g == 4) {
;                         unsigned char* d8 = (unsigned char*)(QKV + (size_t)g * 4 * 16 * 4096 * 128) + ((((size_t)b * 16 + head) * 4096 + s) * 128 + wc * 32 + 8 * fq);
;                         u32x2 w8; w8.x = pk4_fp8(v0[0] * 16.f, v0[1] * 16.f, v0[2] * 16.f, v0[3] * 16.f); w8.y = pk4_fp8(v1[0] * 16.f, v1[1] * 16.f, v1[2] * 16.f, v1[3] * 16.f);
;                         *(u32x2*)d8 = w8;
.LBB0_798:
	s_andn2_b64 vcc, exec, s[52:53]
	s_cbranch_vccnz .LBB0_800
	v_mul_f32_e32 v4, 0x41800000, v54
	v_mul_f32_e32 v5, 0x41800000, v55
	v_med3_f32 v8, v4, s67, v206
	v_med3_f32 v5, v5, s67, v206
	v_cvt_pk_fp8_f32 v4, v8, v5
	v_mul_f32_e32 v6, 0x41800000, v56
	v_mul_f32_e32 v7, 0x41800000, v57
	v_med3_f32 v6, v6, s67, v206
	v_med3_f32 v7, v7, s67, v206
	v_cvt_pk_fp8_f32 v4, v6, v7 op_sel:[0,0,1]
	v_mul_f32_e32 v5, 0x41800000, v50
	v_mul_f32_e32 v6, 0x41800000, v51
	v_med3_f32 v9, v5, s67, v206
	v_med3_f32 v6, v6, s67, v206
	v_cvt_pk_fp8_f32 v5, v9, v6
	s_lshl_b32 s52, s41, 1
	v_readlane_b32 s54, v253, 46
	v_mul_f32_e32 v7, 0x41800000, v52
	v_mul_f32_e32 v8, 0x41800000, v53
	v_readlane_b32 s55, v253, 47
	s_add_u32 s52, s54, s52
	v_lshl_add_u64 v[2:3], v[146:147], 0, s[46:47]
	v_med3_f32 v7, v7, s67, v206
	v_med3_f32 v8, v8, s67, v206
	s_addc_u32 s53, s55, 0
	v_lshlrev_b64 v[2:3], 7, v[2:3]
	v_cvt_pk_fp8_f32 v5, v7, v8 op_sel:[0,0,1]
	v_lshl_add_u64 v[2:3], s[52:53], 0, v[2:3]
	v_lshl_add_u64 v[2:3], v[2:3], 0, s[28:29]
	v_lshl_add_u64 v[2:3], v[2:3], 0, v[170:171]
	global_store_dwordx2 v[2:3], v[4:5], off

; __device__ __forceinline__ unsigned pk4_fp8(float a, float b, float c, float d) {
;     a = fminf(fmaxf(a, -448.f), 448.f); b = fminf(fmaxf(b, -448.f), 448.f); c = fminf(fmaxf(c, -448.f), 448.f); d = fminf(fmaxf(d, -448.f), 448.f);
;     int w = 0; w = __builtin_amdgcn_cvt_pk_fp8_f32(a, b, w, false); w = __builtin_amdgcn_cvt_pk_fp8_f32(c, d, w, true); return (unsigned)w;
; }
;     __device__ __forceinline__ void operator()(const f32x4 (&acc)[2][2][4][2], const Unit& u, int wr, int wc, int fr, int fq) const {
;     ...
;                     if (g == 1) {
;                         unsigned char* d8 = (unsigned char*)(QKV + (size_t)g * 4 * 16 * 4096 * 128) + ((((size_t)b * 16 + head) * 4096 + s) * 128 + (wc >> 1) * 64 + (fq & 1) * 32 + ((wc & 1) * 2 + (fq >> 1)) * 8);
;                         u32x2 w8; w8.x = pk4_fp8(v0[0] * 16.f, v0[1] * 16.f, v0[2] * 16.f, v0[3] * 16.f); w8.y = pk4_fp8(v1[0] * 16.f, v1[1] * 16.f, v1[2] * 16.f, v1[3] * 16.f);
;                         *(u32x2*)d8 = w8;
;                     } else if (g == 3 || g == 4) {
;                         unsigned char* d8 = (unsigned char*)(QKV + (size_t)g * 4 * 16 * 4096 * 128) + ((((size_t)b * 16 + head) * 4096 + s) * 128 + wc * 32 + 8 * fq);
;                         u32x2 w8; w8.x = pk4_fp8(v0[0] * 16.f, v0[1] * 16.f, v0[2] * 16.f, v0[3] * 16.f); w8.y = pk4_fp8(v1[0] * 16.f, v1[1] * 16.f, v1[2] * 16.f, v1[3] * 16.f);
;                         *(u32x2*)d8 = w8;
.LBB0_801:
	s_andn2_b64 vcc, exec, s[52:53]
	s_cbranch_vccnz .LBB0_803
	v_mul_f32_e32 v4, 0x41800000, v54
	v_mul_f32_e32 v5, 0x41800000, v55
	v_med3_f32 v8, v4, s67, v206
	v_med3_f32 v5, v5, s67, v206
	v_cvt_pk_fp8_f32 v4, v8, v5
	v_mul_f32_e32 v6, 0x41800000, v56
	v_mul_f32_e32 v7, 0x41800000, v57
	v_med3_f32 v6, v6, s67, v206
	v_med3_f32 v7, v7, s67, v206
	v_cvt_pk_fp8_f32 v4, v6, v7 op_sel:[0,0,1]
	v_mul_f32_e32 v5, 0x41800000, v50
	v_mul_f32_e32 v6, 0x41800000, v51
	v_med3_f32 v9, v5, s67, v206
	v_med3_f32 v6, v6, s67, v206
	v_cvt_pk_fp8_f32 v5, v9, v6
	v_mul_f32_e32 v7, 0x41800000, v52
	v_mul_f32_e32 v8, 0x41800000, v53
	v_med3_f32 v7, v7, s67, v206
	v_med3_f32 v8, v8, s67, v206
	v_cvt_pk_fp8_f32 v5, v7, v8 op_sel:[0,0,1]
	v_lshl_add_u64 v[2:3], v[146:147], 0, s[46:47]
	v_lshlrev_b64 v[2:3], 7, v[2:3]
	v_lshl_add_u64 v[2:3], v[176:177], 0, v[2:3]
	global_store_dwordx2 v[2:3], v[4:5], off

; __device__ __forceinline__ unsigned pk4_fp8(float a, float b, float c, float d) {
;     a = fminf(fmaxf(a, -448.f), 448.f); b = fminf(fmaxf(b, -448.f), 448.f); c = fminf(fmaxf(c, -448.f), 448.f); d = fminf(fmaxf(d, -448.f), 448.f);
;     int w = 0; w = __builtin_amdgcn_cvt_pk_fp8_f32(a, b, w, false); w = __builtin_amdgcn_cvt_pk_fp8_f32(c, d, w, true); return (unsigned)w;
; }
;     __device__ __forceinline__ void operator()(const f32x4 (&acc)[2][2][4][2], const Unit& u, int wr, int wc, int fr, int fq) const {
;     ...
;                     } else if (g == 3 || g == 4) {
;                         unsigned char* d8 = (unsigned char*)(QKV + (size_t)g * 4 * 16 * 4096 * 128) + ((((size_t)b * 16 + head) * 4096 + s) * 128 + wc * 32 + 8 * fq);
;                         u32x2 w8; w8.x = pk4_fp8(v0[0] * 16.f, v0[1] * 16.f, v0[2] * 16.f, v0[3] * 16.f); w8.y = pk4_fp8(v1[0] * 16.f, v1[1] * 16.f, v1[2] * 16.f, v1[3] * 16.f);
;                         *(u32x2*)d8 = w8;
.LBB0_822:
	s_andn2_b64 vcc, exec, s[48:49]
	s_cbranch_vccnz .LBB0_824
	v_mul_f32_e32 v154, 0x41800000, v46
	v_mul_f32_e32 v155, 0x41800000, v47
	v_med3_f32 v158, v154, s67, v206
	v_med3_f32 v155, v155, s67, v206
	v_cvt_pk_fp8_f32 v154, v158, v155
	v_mul_f32_e32 v156, 0x41800000, v48
	v_mul_f32_e32 v157, 0x41800000, v49
	v_med3_f32 v156, v156, s67, v206
	v_med3_f32 v157, v157, s67, v206
	v_cvt_pk_fp8_f32 v154, v156, v157 op_sel:[0,0,1]
	v_mul_f32_e32 v155, 0x41800000, v42
	v_mul_f32_e32 v156, 0x41800000, v43
	v_med3_f32 v159, v155, s67, v206
	v_med3_f32 v156, v156, s67, v206
	v_cvt_pk_fp8_f32 v155, v159, v156
	s_lshl_b32 s48, s41, 1
	v_readlane_b32 s50, v253, 46
	v_mul_f32_e32 v157, 0x41800000, v44
	v_mul_f32_e32 v158, 0x41800000, v45
	v_readlane_b32 s51, v253, 47
	s_add_u32 s48, s50, s48
	v_lshl_add_u64 v[152:153], v[146:147], 0, s[24:25]
	v_med3_f32 v157, v157, s67, v206
	v_med3_f32 v158, v158, s67, v206
	s_addc_u32 s49, s51, 0
	v_lshlrev_b64 v[152:153], 7, v[152:153]
	v_cvt_pk_fp8_f32 v155, v157, v158 op_sel:[0,0,1]
	v_lshl_add_u64 v[152:153], s[48:49], 0, v[152:153]
	v_lshl_add_u64 v[152:153], v[152:153], 0, s[28:29]
	v_lshl_add_u64 v[152:153], v[152:153], 0, v[170:171]
	global_store_dwordx2 v[152:153], v[154:155], off

; __device__ __forceinline__ unsigned pk4_fp8(float a, float b, float c, float d) {
;     a = fminf(fmaxf(a, -448.f), 448.f); b = fminf(fmaxf(b, -448.f), 448.f); c = fminf(fmaxf(c, -448.f), 448.f); d = fminf(fmaxf(d, -448.f), 448.f);
;     int w = 0; w = __builtin_amdgcn_cvt_pk_fp8_f32(a, b, w, false); w = __builtin_amdgcn_cvt_pk_fp8_f32(c, d, w, true); return (unsigned)w;
; }
;     __device__ __forceinline__ void operator()(const f32x4 (&acc)[2][2][4][2], const Unit& u, int wr, int wc, int fr, int fq) const {
;     ...
;                     if (g == 1) {
;                         unsigned char* d8 = (unsigned char*)(QKV + (size_t)g * 4 * 16 * 4096 * 128) + ((((size_t)b * 16 + head) * 4096 + s) * 128 + (wc >> 1) * 64 + (fq & 1) * 32 + ((wc & 1) * 2 + (fq >> 1)) * 8);
;                         u32x2 w8; w8.x = pk4_fp8(v0[0] * 16.f, v0[1] * 16.f, v0[2] * 16.f, v0[3] * 16.f); w8.y = pk4_fp8(v1[0] * 16.f, v1[1] * 16.f, v1[2] * 16.f, v1[3] * 16.f);
;                         *(u32x2*)d8 = w8;
;                     } else if (g == 3 || g == 4) {
;                         unsigned char* d8 = (unsigned char*)(QKV + (size_t)g * 4 * 16 * 4096 * 128) + ((((size_t)b * 16 + head) * 4096 + s) * 128 + wc * 32 + 8 * fq);
;                         u32x2 w8; w8.x = pk4_fp8(v0[0] * 16.f, v0[1] * 16.f, v0[2] * 16.f, v0[3] * 16.f); w8.y = pk4_fp8(v1[0] * 16.f, v1[1] * 16.f, v1[2] * 16.f, v1[3] * 16.f);
;                         *(u32x2*)d8 = w8;
.LBB0_825:
	s_andn2_b64 vcc, exec, s[48:49]
	s_cbranch_vccnz .LBB0_827
	v_mul_f32_e32 v154, 0x41800000, v46
	v_mul_f32_e32 v155, 0x41800000, v47
	v_med3_f32 v158, v154, s67, v206
	v_med3_f32 v155, v155, s67, v206
	v_cvt_pk_fp8_f32 v154, v158, v155
	v_mul_f32_e32 v156, 0x41800000, v48
	v_mul_f32_e32 v157, 0x41800000, v49
	v_med3_f32 v156, v156, s67, v206
	v_med3_f32 v157, v157, s67, v206
	v_cvt_pk_fp8_f32 v154, v156, v157 op_sel:[0,0,1]
	v_mul_f32_e32 v155, 0x41800000, v42
	v_mul_f32_e32 v156, 0x41800000, v43
	v_med3_f32 v159, v155, s67, v206
	v_med3_f32 v156, v156, s67, v206
	v_cvt_pk_fp8_f32 v155, v159, v156
	v_mul_f32_e32 v157, 0x41800000, v44
	v_mul_f32_e32 v158, 0x41800000, v45
	v_med3_f32 v157, v157, s67, v206
	v_med3_f32 v158, v158, s67, v206
	v_cvt_pk_fp8_f32 v155, v157, v158 op_sel:[0,0,1]
	v_lshl_add_u64 v[152:153], v[146:147], 0, s[24:25]
	v_lshlrev_b64 v[152:153], 7, v[152:153]
	v_lshl_add_u64 v[152:153], v[176:177], 0, v[152:153]
	global_store_dwordx2 v[152:153], v[154:155], off

; __device__ __forceinline__ unsigned pk4_fp8(float a, float b, float c, float d) {
;     a = fminf(fmaxf(a, -448.f), 448.f); b = fminf(fmaxf(b, -448.f), 448.f); c = fminf(fmaxf(c, -448.f), 448.f); d = fminf(fmaxf(d, -448.f), 448.f);
;     int w = 0; w = __builtin_amdgcn_cvt_pk_fp8_f32(a, b, w, false); w = __builtin_amdgcn_cvt_pk_fp8_f32(c, d, w, true); return (unsigned)w;
; }
;     __device__ __forceinline__ void operator()(const f32x4 (&acc)[2][2][4][2], const Unit& u, int wr, int wc, int fr, int fq) const {
;     ...
;                     } else if (g == 3 || g == 4) {
;                         unsigned char* d8 = (unsigned char*)(QKV + (size_t)g * 4 * 16 * 4096 * 128) + ((((size_t)b * 16 + head) * 4096 + s) * 128 + wc * 32 + 8 * fq);
;                         u32x2 w8; w8.x = pk4_fp8(v0[0] * 16.f, v0[1] * 16.f, v0[2] * 16.f, v0[3] * 16.f); w8.y = pk4_fp8(v1[0] * 16.f, v1[1] * 16.f, v1[2] * 16.f, v1[3] * 16.f);
;                         *(u32x2*)d8 = w8;
.LBB0_840:
	s_andn2_b64 vcc, exec, s[10:11]
	s_cbranch_vccnz .LBB0_842
	v_mul_f32_e32 v4, 0x41800000, v38
	v_mul_f32_e32 v5, 0x41800000, v39
	v_med3_f32 v8, v4, s67, v206
	v_med3_f32 v5, v5, s67, v206
	v_cvt_pk_fp8_f32 v4, v8, v5
	v_mul_f32_e32 v6, 0x41800000, v40
	v_mul_f32_e32 v7, 0x41800000, v41
	v_med3_f32 v6, v6, s67, v206
	v_med3_f32 v7, v7, s67, v206
	v_cvt_pk_fp8_f32 v4, v6, v7 op_sel:[0,0,1]
	v_mul_f32_e32 v5, 0x41800000, v34
	v_mul_f32_e32 v6, 0x41800000, v35
	v_med3_f32 v9, v5, s67, v206
	v_med3_f32 v6, v6, s67, v206
	v_cvt_pk_fp8_f32 v5, v9, v6
	s_lshl_b32 s3, s41, 1
	v_readlane_b32 s10, v253, 46
	v_mul_f32_e32 v7, 0x41800000, v36
	v_mul_f32_e32 v8, 0x41800000, v37
	v_readlane_b32 s11, v253, 47
	s_add_u32 s10, s10, s3
	v_lshl_add_u64 v[2:3], v[146:147], 0, s[46:47]
	v_med3_f32 v7, v7, s67, v206
	v_med3_f32 v8, v8, s67, v206
	s_addc_u32 s11, s11, 0
	v_lshlrev_b64 v[2:3], 7, v[2:3]
	v_cvt_pk_fp8_f32 v5, v7, v8 op_sel:[0,0,1]
	v_lshl_add_u64 v[2:3], s[10:11], 0, v[2:3]
	v_lshl_add_u64 v[2:3], v[2:3], 0, s[28:29]
	v_lshl_add_u64 v[2:3], v[2:3], 0, v[170:171]
	global_store_dwordx2 v[2:3], v[4:5], off

; __device__ __forceinline__ unsigned pk4_fp8(float a, float b, float c, float d) {
;     a = fminf(fmaxf(a, -448.f), 448.f); b = fminf(fmaxf(b, -448.f), 448.f); c = fminf(fmaxf(c, -448.f), 448.f); d = fminf(fmaxf(d, -448.f), 448.f);
;     int w = 0; w = __builtin_amdgcn_cvt_pk_fp8_f32(a, b, w, false); w = __builtin_amdgcn_cvt_pk_fp8_f32(c, d, w, true); return (unsigned)w;
; }
;     __device__ __forceinline__ void operator()(const f32x4 (&acc)[2][2][4][2], const Unit& u, int wr, int wc, int fr, int fq) const {
;     ...
;                     if (g == 1) {
;                         unsigned char* d8 = (unsigned char*)(QKV + (size_t)g * 4 * 16 * 4096 * 128) + ((((size_t)b * 16 + head) * 4096 + s) * 128 + (wc >> 1) * 64 + (fq & 1) * 32 + ((wc & 1) * 2 + (fq >> 1)) * 8);
;                         u32x2 w8; w8.x = pk4_fp8(v0[0] * 16.f, v0[1] * 16.f, v0[2] * 16.f, v0[3] * 16.f); w8.y = pk4_fp8(v1[0] * 16.f, v1[1] * 16.f, v1[2] * 16.f, v1[3] * 16.f);
;                         *(u32x2*)d8 = w8;
;                     } else if (g == 3 || g == 4) {
;                         unsigned char* d8 = (unsigned char*)(QKV + (size_t)g * 4 * 16 * 4096 * 128) + ((((size_t)b * 16 + head) * 4096 + s) * 128 + wc * 32 + 8 * fq);
;                         u32x2 w8; w8.x = pk4_fp8(v0[0] * 16.f, v0[1] * 16.f, v0[2] * 16.f, v0[3] * 16.f); w8.y = pk4_fp8(v1[0] * 16.f, v1[1] * 16.f, v1[2] * 16.f, v1[3] * 16.f);
;                         *(u32x2*)d8 = w8;
.LBB0_843:
	v_mul_f32_e32 v4, 0x41800000, v38
	v_mul_f32_e32 v5, 0x41800000, v39
	v_med3_f32 v8, v4, s67, v206
	v_med3_f32 v5, v5, s67, v206
	v_cvt_pk_fp8_f32 v4, v8, v5
	v_mul_f32_e32 v6, 0x41800000, v40
	v_mul_f32_e32 v7, 0x41800000, v41
	v_med3_f32 v6, v6, s67, v206
	v_med3_f32 v7, v7, s67, v206
	v_cvt_pk_fp8_f32 v4, v6, v7 op_sel:[0,0,1]
	v_mul_f32_e32 v5, 0x41800000, v34
	v_mul_f32_e32 v6, 0x41800000, v35
	v_med3_f32 v9, v5, s67, v206
	v_med3_f32 v6, v6, s67, v206
	v_cvt_pk_fp8_f32 v5, v9, v6
	v_mul_f32_e32 v7, 0x41800000, v36
	v_mul_f32_e32 v8, 0x41800000, v37
	v_med3_f32 v7, v7, s67, v206
	v_med3_f32 v8, v8, s67, v206
	v_cvt_pk_fp8_f32 v5, v7, v8 op_sel:[0,0,1]
	v_lshl_add_u64 v[2:3], v[146:147], 0, s[46:47]
	v_lshlrev_b64 v[2:3], 7, v[2:3]
	v_lshl_add_u64 v[2:3], v[176:177], 0, v[2:3]
	global_store_dwordx2 v[2:3], v[4:5], off
	s_and_b64 vcc, exec, s[8:9]
	s_cbranch_vccz .LBB0_837

; __device__ __forceinline__ unsigned pk4_fp8(float a, float b, float c, float d) {
;     a = fminf(fmaxf(a, -448.f), 448.f); b = fminf(fmaxf(b, -448.f), 448.f); c = fminf(fmaxf(c, -448.f), 448.f); d = fminf(fmaxf(d, -448.f), 448.f);
;     int w = 0; w = __builtin_amdgcn_cvt_pk_fp8_f32(a, b, w, false); w = __builtin_amdgcn_cvt_pk_fp8_f32(c, d, w, true); return (unsigned)w;
; }
;     __device__ __forceinline__ void operator()(const f32x4 (&acc)[2][2][4][2], const Unit& u, int wr, int wc, int fr, int fq) const {
;         const int b = u.pm >> 4;
; #pragma unroll
;         for (int ai = 0; ai < 2; ++ai) { float rs4[4];
; #pragma unroll
;             for (int m = 0; m < 4; ++m) rs4[m] = rsqrtf(ss[u.pm * 256 + ai * HALF + wr * 64 + m * 16 + fr] * (1.0f / 4096.0f) + RMS_EPS) * (sc * 16.f);
;             const int T = (u.pm & 15) * 4 + ai * 2 + wr;
; #pragma unroll
;             for (int bj = 0; bj < 2; ++bj) { const int head = u.pn * 2 + bj;
;                 unsigned char* base = VT + (((size_t)b * 16 + head) * 64 + T) * 8192 + (wc * 32 + 8 * fq) * 64 + 32 * (fr >> 3) + 4 * (fr & 7);
; #pragma unroll
;                 for (int n = 0; n < 2; ++n)
; #pragma unroll
;                     for (int jj = 0; jj < 4; ++jj)
;                         *(unsigned*)(base + (4 * n + jj) * 64) = pk4_fp8(acc[ai][bj][0][n][jj] * rs4[0], acc[ai][bj][1][n][jj] * rs4[1], acc[ai][bj][2][n][jj] * rs4[2], acc[ai][bj][3][n][jj] * rs4[3]); } }
;     }
.LBB0_896:
	v_lshl_add_u32 v6, s26, 8, v1
	v_ashrrev_i32_e32 v7, 31, v6
	s_nop 15
	s_nop 15
	v_lshl_add_u64 v[2:3], v[6:7], 2, s[20:21]
	s_lshl_b32 s15, s26, 2
	s_lshl_b32 s28, s27, 1
	s_ashr_i32 s30, s26, 4
	s_and_b32 s15, s15, 60
	s_ashr_i32 s29, s28, 31
	s_add_i32 s26, s15, s39
	s_ashr_i32 s31, s30, 31
	s_lshl_b64 s[34:35], s[28:29], 19
	s_ashr_i32 s27, s26, 31
	s_lshl_b64 s[30:31], s[30:31], 23
	s_lshl_b64 s[26:27], s[26:27], 13
	v_mov_b32_e32 v17, 0
	s_or_b32 s28, s28, 1
	s_ashr_i32 s29, s28, 31
	s_lshl_b64 s[28:29], s[28:29], 19
	s_waitcnt vmcnt(0)
	v_fmamk_f32 v4, v234, 0x39800000, v192
	v_cmp_gt_f32_e32 vcc, s50, v4
	v_mul_f32_e32 v5, 0x4b800000, v4
	s_nop 0
	v_cndmask_b32_e32 v4, v4, v5, vcc
	v_rsq_f32_e32 v4, v4
	s_nop 0
	v_mul_f32_e32 v5, 0x45800000, v4
	v_cndmask_b32_e32 v4, v4, v5, vcc
	v_mul_f32_e32 v7, 0x3e800000, v4
	v_mul_f32_e32 v8, v158, v7
	v_med3_f32 v8, v8, s51, v193
	v_fmamk_f32 v4, v235, 0x39800000, v192
	v_cmp_gt_f32_e32 vcc, s50, v4
	v_mul_f32_e32 v5, 0x4b800000, v4
	s_nop 0
	v_cndmask_b32_e32 v4, v4, v5, vcc
	v_rsq_f32_e32 v4, v4
	s_nop 0
	v_mul_f32_e32 v5, 0x45800000, v4
	v_cndmask_b32_e32 v4, v4, v5, vcc
	v_mul_f32_e32 v10, 0x3e800000, v4
	v_mul_f32_e32 v9, v154, v10
	v_med3_f32 v9, v9, s51, v193
	v_cvt_pk_fp8_f32 v15, v8, v9
	v_mul_f32_e32 v8, v159, v7
	v_mul_f32_e32 v9, v155, v10
	v_med3_f32 v8, v8, s51, v193
	v_med3_f32 v9, v9, s51, v193
	v_fmamk_f32 v4, v236, 0x39800000, v192
	v_cmp_gt_f32_e32 vcc, s50, v4
	v_mul_f32_e32 v5, 0x4b800000, v4
	v_fmamk_f32 v2, v237, 0x39800000, v192
	v_cndmask_b32_e32 v4, v4, v5, vcc
	v_rsq_f32_e32 v4, v4
	v_mul_f32_e32 v3, 0x4b800000, v2
	v_mul_f32_e32 v5, 0x45800000, v4
	v_cndmask_b32_e32 v4, v4, v5, vcc
	v_cmp_gt_f32_e32 vcc, s50, v2
	v_mul_f32_e32 v11, 0x3e800000, v4
	v_mul_f32_e32 v13, v150, v11
	v_cndmask_b32_e32 v2, v2, v3, vcc
	v_rsq_f32_e32 v2, v2
	v_med3_f32 v13, v13, s51, v193
	v_mul_f32_e32 v3, 0x45800000, v2
	v_cndmask_b32_e32 v2, v2, v3, vcc
	v_mul_f32_e32 v12, 0x3e800000, v2
	v_mul_f32_e32 v14, v146, v12
	v_med3_f32 v14, v14, s51, v193
	v_cvt_pk_fp8_f32 v15, v13, v14 op_sel:[0,0,1]
	v_lshl_add_u64 v[2:3], v[170:171], 0, s[34:35]
	v_lshl_add_u64 v[4:5], v[2:3], 0, s[30:31]
	v_lshl_add_u64 v[2:3], v[4:5], 0, s[26:27]
	global_store_dword v[2:3], v15, off
	v_cvt_pk_fp8_f32 v15, v8, v9
	v_mul_f32_e32 v13, v151, v11
	v_mul_f32_e32 v14, v147, v12
	v_med3_f32 v13, v13, s51, v193
	v_med3_f32 v14, v14, s51, v193
	v_cvt_pk_fp8_f32 v15, v13, v14 op_sel:[0,0,1]
	v_mul_f32_e32 v8, v160, v7
	v_mul_f32_e32 v9, v156, v10
	v_med3_f32 v8, v8, s51, v193
	global_store_dword v[2:3], v15, off offset:64
	v_med3_f32 v9, v9, s51, v193
	v_cvt_pk_fp8_f32 v15, v8, v9
	v_mul_f32_e32 v13, v152, v11
	v_mul_f32_e32 v14, v148, v12
	v_med3_f32 v13, v13, s51, v193
	v_med3_f32 v14, v14, s51, v193
	v_cvt_pk_fp8_f32 v15, v13, v14 op_sel:[0,0,1]
	v_mul_f32_e32 v8, v161, v7
	v_mul_f32_e32 v9, v157, v10
	v_med3_f32 v8, v8, s51, v193
	global_store_dword v[2:3], v15, off offset:128
	v_med3_f32 v9, v9, s51, v193
	v_cvt_pk_fp8_f32 v15, v8, v9
	v_mul_f32_e32 v13, v153, v11
	v_mul_f32_e32 v14, v149, v12
	v_med3_f32 v13, v13, s51, v193
	v_med3_f32 v14, v14, s51, v193
	v_cvt_pk_fp8_f32 v15, v13, v14 op_sel:[0,0,1]
	v_mul_f32_e32 v8, v142, v7
	v_mul_f32_e32 v9, v138, v10
	v_med3_f32 v8, v8, s51, v193
	global_store_dword v[2:3], v15, off offset:192
	v_med3_f32 v9, v9, s51, v193
	v_cvt_pk_fp8_f32 v15, v8, v9
	v_mul_f32_e32 v13, v134, v11
	v_mul_f32_e32 v14, v130, v12
	v_med3_f32 v13, v13, s51, v193
	v_med3_f32 v14, v14, s51, v193
	v_cvt_pk_fp8_f32 v15, v13, v14 op_sel:[0,0,1]
	v_mul_f32_e32 v8, v143, v7
	v_mul_f32_e32 v9, v139, v10
	v_med3_f32 v8, v8, s51, v193
	global_store_dword v[2:3], v15, off offset:256
	v_med3_f32 v9, v9, s51, v193
	v_cvt_pk_fp8_f32 v15, v8, v9
	v_mul_f32_e32 v13, v135, v11
	v_mul_f32_e32 v14, v131, v12
	v_med3_f32 v13, v13, s51, v193
	v_med3_f32 v14, v14, s51, v193
	v_cvt_pk_fp8_f32 v15, v13, v14 op_sel:[0,0,1]
	v_mul_f32_e32 v8, v144, v7
	v_mul_f32_e32 v9, v140, v10
	v_med3_f32 v8, v8, s51, v193
	global_store_dword v[2:3], v15, off offset:320
	v_med3_f32 v9, v9, s51, v193
	v_cvt_pk_fp8_f32 v15, v8, v9
	v_mul_f32_e32 v13, v136, v11
	v_mul_f32_e32 v14, v132, v12
	v_med3_f32 v13, v13, s51, v193
	v_med3_f32 v14, v14, s51, v193
	v_cvt_pk_fp8_f32 v15, v13, v14 op_sel:[0,0,1]
	v_mul_f32_e32 v8, v145, v7
	v_mul_f32_e32 v9, v141, v10
	v_med3_f32 v8, v8, s51, v193
	global_store_dword v[2:3], v15, off offset:384
	v_med3_f32 v9, v9, s51, v193
	v_cvt_pk_fp8_f32 v15, v8, v9
	v_mul_f32_e32 v13, v137, v11
	v_mul_f32_e32 v14, v133, v12
	v_med3_f32 v13, v13, s51, v193
	v_med3_f32 v14, v14, s51, v193
	v_cvt_pk_fp8_f32 v15, v13, v14 op_sel:[0,0,1]
	v_mul_f32_e32 v13, v126, v7
	v_mul_f32_e32 v14, v122, v10
	v_med3_f32 v13, v13, s51, v193
	v_med3_f32 v14, v14, s51, v193
	v_cvt_pk_fp8_f32 v17, v13, v14
	global_store_dword v[2:3], v15, off offset:448
	v_mul_f32_e32 v15, v118, v11
	v_mul_f32_e32 v16, v114, v12
	v_med3_f32 v15, v15, s51, v193
	v_med3_f32 v16, v16, s51, v193
	v_cvt_pk_fp8_f32 v17, v15, v16 op_sel:[0,0,1]
	v_lshl_add_u64 v[2:3], v[170:171], 0, s[28:29]
	v_lshl_add_u64 v[2:3], v[2:3], 0, s[30:31]
	v_lshl_add_u64 v[8:9], v[2:3], 0, s[26:27]
	v_mul_f32_e32 v13, v127, v7
	v_mul_f32_e32 v14, v123, v10
	global_store_dword v[8:9], v17, off
	v_med3_f32 v13, v13, s51, v193
	v_med3_f32 v14, v14, s51, v193
	v_cvt_pk_fp8_f32 v17, v13, v14
	v_mul_f32_e32 v15, v119, v11
	v_mul_f32_e32 v16, v115, v12
	v_med3_f32 v15, v15, s51, v193
	v_med3_f32 v16, v16, s51, v193
	v_cvt_pk_fp8_f32 v17, v15, v16 op_sel:[0,0,1]
	v_mul_f32_e32 v13, v128, v7
	v_mul_f32_e32 v14, v124, v10
	v_med3_f32 v13, v13, s51, v193
; __device__ __forceinline__ unsigned pk4_fp8(float a, float b, float c, float d) {
;     a = fminf(fmaxf(a, -448.f), 448.f); b = fminf(fmaxf(b, -448.f), 448.f); c = fminf(fmaxf(c, -448.f), 448.f); d = fminf(fmaxf(d, -448.f), 448.f);
;     int w = 0; w = __builtin_amdgcn_cvt_pk_fp8_f32(a, b, w, false); w = __builtin_amdgcn_cvt_pk_fp8_f32(c, d, w, true); return (unsigned)w;
; }
;     __device__ __forceinline__ void operator()(const f32x4 (&acc)[2][2][4][2], const Unit& u, int wr, int wc, int fr, int fq) const {
;         const int b = u.pm >> 4;
; #pragma unroll
;         for (int ai = 0; ai < 2; ++ai) { float rs4[4];
; #pragma unroll
;             for (int m = 0; m < 4; ++m) rs4[m] = rsqrtf(ss[u.pm * 256 + ai * HALF + wr * 64 + m * 16 + fr] * (1.0f / 4096.0f) + RMS_EPS) * (sc * 16.f);
;             const int T = (u.pm & 15) * 4 + ai * 2 + wr;
; #pragma unroll
;             for (int bj = 0; bj < 2; ++bj) { const int head = u.pn * 2 + bj;
;                 unsigned char* base = VT + (((size_t)b * 16 + head) * 64 + T) * 8192 + (wc * 32 + 8 * fq) * 64 + 32 * (fr >> 3) + 4 * (fr & 7);
; #pragma unroll
;                 for (int n = 0; n < 2; ++n)
; #pragma unroll
;                     for (int jj = 0; jj < 4; ++jj)
;                         *(unsigned*)(base + (4 * n + jj) * 64) = pk4_fp8(acc[ai][bj][0][n][jj] * rs4[0], acc[ai][bj][1][n][jj] * rs4[1], acc[ai][bj][2][n][jj] * rs4[2], acc[ai][bj][3][n][jj] * rs4[3]); } }
;     }
	global_store_dword v[8:9], v17, off offset:64
	v_med3_f32 v14, v14, s51, v193
	v_cvt_pk_fp8_f32 v17, v13, v14
	v_mul_f32_e32 v15, v120, v11
	v_mul_f32_e32 v16, v116, v12
	v_med3_f32 v15, v15, s51, v193
	v_med3_f32 v16, v16, s51, v193
	v_cvt_pk_fp8_f32 v17, v15, v16 op_sel:[0,0,1]
	v_mul_f32_e32 v13, v129, v7
	v_mul_f32_e32 v14, v125, v10
	v_med3_f32 v13, v13, s51, v193
	global_store_dword v[8:9], v17, off offset:128
	v_med3_f32 v14, v14, s51, v193
	v_cvt_pk_fp8_f32 v17, v13, v14
	v_mul_f32_e32 v15, v121, v11
	v_mul_f32_e32 v16, v117, v12
	v_med3_f32 v15, v15, s51, v193
	v_med3_f32 v16, v16, s51, v193
	v_cvt_pk_fp8_f32 v17, v15, v16 op_sel:[0,0,1]
	v_mul_f32_e32 v13, v110, v7
	v_mul_f32_e32 v14, v106, v10
	v_med3_f32 v13, v13, s51, v193
	global_store_dword v[8:9], v17, off offset:192
	v_med3_f32 v14, v14, s51, v193
	v_cvt_pk_fp8_f32 v17, v13, v14
	v_mul_f32_e32 v15, v102, v11
	v_mul_f32_e32 v16, v98, v12
	v_med3_f32 v15, v15, s51, v193
	v_med3_f32 v16, v16, s51, v193
	v_cvt_pk_fp8_f32 v17, v15, v16 op_sel:[0,0,1]
	v_mul_f32_e32 v13, v111, v7
	v_mul_f32_e32 v14, v107, v10
	v_med3_f32 v13, v13, s51, v193
	global_store_dword v[8:9], v17, off offset:256
	v_med3_f32 v14, v14, s51, v193
	v_cvt_pk_fp8_f32 v17, v13, v14
	v_mul_f32_e32 v15, v103, v11
	v_mul_f32_e32 v16, v99, v12
	v_med3_f32 v15, v15, s51, v193
	v_med3_f32 v16, v16, s51, v193
	v_cvt_pk_fp8_f32 v17, v15, v16 op_sel:[0,0,1]
	v_mul_f32_e32 v13, v112, v7
	v_mul_f32_e32 v14, v108, v10
	v_med3_f32 v13, v13, s51, v193
	global_store_dword v[8:9], v17, off offset:320
	v_med3_f32 v14, v14, s51, v193
	v_mul_f32_e32 v7, v113, v7
	v_mul_f32_e32 v10, v109, v10
	v_cvt_pk_fp8_f32 v17, v13, v14
	v_med3_f32 v7, v7, s51, v193
	v_med3_f32 v10, v10, s51, v193
	v_cvt_pk_fp8_f32 v13, v7, v10
	v_mul_f32_e32 v15, v104, v11
	v_mul_f32_e32 v16, v100, v12
	v_mul_f32_e32 v11, v105, v11
	v_mul_f32_e32 v12, v101, v12
	v_med3_f32 v15, v15, s51, v193
	v_med3_f32 v16, v16, s51, v193
	v_med3_f32 v11, v11, s51, v193
	v_med3_f32 v12, v12, s51, v193
	v_cvt_pk_fp8_f32 v17, v15, v16 op_sel:[0,0,1]
	v_cvt_pk_fp8_f32 v13, v11, v12 op_sel:[0,0,1]
	v_add_u32_e32 v10, 0xa0, v6
	v_ashrrev_i32_e32 v11, 31, v10
	global_store_dword v[8:9], v17, off offset:384
	global_store_dword v[8:9], v13, off offset:448
	v_add_u32_e32 v8, 0x80, v6
	v_ashrrev_i32_e32 v9, 31, v8
	v_lshl_add_u64 v[8:9], v[8:9], 2, s[20:21]
	v_lshl_add_u64 v[10:11], v[10:11], 2, s[20:21]
	s_add_u32 s26, s26, 0x4000
	s_addc_u32 s27, s27, 0
	v_lshl_add_u64 v[4:5], v[4:5], 0, s[26:27]
	v_lshl_add_u64 v[2:3], v[2:3], 0, s[26:27]
	s_mov_b64 s[26:27], -1
	v_fmamk_f32 v7, v238, 0x39800000, v192
	v_cmp_gt_f32_e32 vcc, s50, v7
	v_mul_f32_e32 v8, 0x4b800000, v7
	s_nop 0
	v_cndmask_b32_e32 v7, v7, v8, vcc
	v_rsq_f32_e32 v7, v7
	s_nop 0
	v_mul_f32_e32 v8, 0x45800000, v7
	v_cndmask_b32_e32 v7, v7, v8, vcc
	v_add_u32_e32 v8, 0x90, v6
	v_ashrrev_i32_e32 v9, 31, v8
	v_lshl_add_u64 v[8:9], v[8:9], 2, s[20:21]
	v_mul_f32_e32 v7, 0x3e800000, v7
	v_fmamk_f32 v8, v239, 0x39800000, v192
	v_cmp_gt_f32_e32 vcc, s50, v8
	v_mul_f32_e32 v9, 0x4b800000, v8
	s_nop 0
	v_cndmask_b32_e32 v8, v8, v9, vcc
	v_rsq_f32_e32 v8, v8
	s_nop 0
	v_mul_f32_e32 v9, 0x45800000, v8
	v_cndmask_b32_e32 v8, v8, v9, vcc
	v_mul_f32_e32 v8, 0x3e800000, v8
	v_fmamk_f32 v9, v240, 0x39800000, v192
	v_cmp_gt_f32_e32 vcc, s50, v9
	v_mul_f32_e32 v10, 0x4b800000, v9
	s_nop 0
	v_cndmask_b32_e32 v9, v9, v10, vcc
	v_rsq_f32_e32 v9, v9
	s_nop 0
	v_mul_f32_e32 v10, 0x45800000, v9
	v_cndmask_b32_e32 v9, v9, v10, vcc
	v_add_u32_e32 v10, 0xb0, v6
	v_ashrrev_i32_e32 v11, 31, v10
	v_lshl_add_u64 v[10:11], v[10:11], 2, s[20:21]
	v_mul_f32_e32 v11, v90, v8
	v_med3_f32 v11, v11, s51, v193
	v_mul_f32_e32 v9, 0x3e800000, v9
	v_mul_f32_e32 v12, v86, v9
	v_med3_f32 v12, v12, s51, v193
	v_fmamk_f32 v6, v241, 0x39800000, v192
	v_cmp_gt_f32_e32 vcc, s50, v6
	v_mul_f32_e32 v10, 0x4b800000, v6
	s_nop 0
	v_cndmask_b32_e32 v6, v6, v10, vcc
	v_rsq_f32_e32 v6, v6
	s_nop 0
	v_mul_f32_e32 v10, 0x45800000, v6
	v_cndmask_b32_e32 v6, v6, v10, vcc
	v_mul_f32_e32 v10, v94, v7
	v_med3_f32 v10, v10, s51, v193
	v_cvt_pk_fp8_f32 v14, v10, v11
	v_mul_f32_e32 v6, 0x3e800000, v6
	v_mul_f32_e32 v13, v82, v6
	v_med3_f32 v13, v13, s51, v193
	v_cvt_pk_fp8_f32 v14, v12, v13 op_sel:[0,0,1]
	v_mul_f32_e32 v10, v95, v7
	v_mul_f32_e32 v11, v91, v8
	v_med3_f32 v10, v10, s51, v193
	global_store_dword v[4:5], v14, off
	v_med3_f32 v11, v11, s51, v193
	v_cvt_pk_fp8_f32 v14, v10, v11
	v_mul_f32_e32 v12, v87, v9
	v_mul_f32_e32 v13, v83, v6
	v_med3_f32 v12, v12, s51, v193
	v_med3_f32 v13, v13, s51, v193
	v_cvt_pk_fp8_f32 v14, v12, v13 op_sel:[0,0,1]
	v_mul_f32_e32 v10, v96, v7
	v_mul_f32_e32 v11, v92, v8
	v_med3_f32 v10, v10, s51, v193
	global_store_dword v[4:5], v14, off offset:64
	v_med3_f32 v11, v11, s51, v193
	v_cvt_pk_fp8_f32 v14, v10, v11
	v_mul_f32_e32 v12, v88, v9
	v_mul_f32_e32 v13, v84, v6
	v_med3_f32 v12, v12, s51, v193
	v_med3_f32 v13, v13, s51, v193
; __device__ __forceinline__ unsigned pk4_fp8(float a, float b, float c, float d) {
;     a = fminf(fmaxf(a, -448.f), 448.f); b = fminf(fmaxf(b, -448.f), 448.f); c = fminf(fmaxf(c, -448.f), 448.f); d = fminf(fmaxf(d, -448.f), 448.f);
;     int w = 0; w = __builtin_amdgcn_cvt_pk_fp8_f32(a, b, w, false); w = __builtin_amdgcn_cvt_pk_fp8_f32(c, d, w, true); return (unsigned)w;
; }
;     __device__ __forceinline__ void operator()(const f32x4 (&acc)[2][2][4][2], const Unit& u, int wr, int wc, int fr, int fq) const {
;         const int b = u.pm >> 4;
; #pragma unroll
;         for (int ai = 0; ai < 2; ++ai) { float rs4[4];
; #pragma unroll
;             for (int m = 0; m < 4; ++m) rs4[m] = rsqrtf(ss[u.pm * 256 + ai * HALF + wr * 64 + m * 16 + fr] * (1.0f / 4096.0f) + RMS_EPS) * (sc * 16.f);
;             const int T = (u.pm & 15) * 4 + ai * 2 + wr;
; #pragma unroll
;             for (int bj = 0; bj < 2; ++bj) { const int head = u.pn * 2 + bj;
;                 unsigned char* base = VT + (((size_t)b * 16 + head) * 64 + T) * 8192 + (wc * 32 + 8 * fq) * 64 + 32 * (fr >> 3) + 4 * (fr & 7);
; #pragma unroll
;                 for (int n = 0; n < 2; ++n)
; #pragma unroll
;                     for (int jj = 0; jj < 4; ++jj)
;                         *(unsigned*)(base + (4 * n + jj) * 64) = pk4_fp8(acc[ai][bj][0][n][jj] * rs4[0], acc[ai][bj][1][n][jj] * rs4[1], acc[ai][bj][2][n][jj] * rs4[2], acc[ai][bj][3][n][jj] * rs4[3]); } }
;     }
	v_cvt_pk_fp8_f32 v14, v12, v13 op_sel:[0,0,1]
	v_mul_f32_e32 v10, v97, v7
	v_mul_f32_e32 v11, v93, v8
	v_med3_f32 v10, v10, s51, v193
	global_store_dword v[4:5], v14, off offset:128
	v_med3_f32 v11, v11, s51, v193
	v_cvt_pk_fp8_f32 v14, v10, v11
	v_mul_f32_e32 v12, v89, v9
	v_mul_f32_e32 v13, v85, v6
	v_med3_f32 v12, v12, s51, v193
	v_med3_f32 v13, v13, s51, v193
	v_cvt_pk_fp8_f32 v14, v12, v13 op_sel:[0,0,1]
	v_mul_f32_e32 v10, v78, v7
	v_mul_f32_e32 v11, v74, v8
	v_med3_f32 v10, v10, s51, v193
	global_store_dword v[4:5], v14, off offset:192
	v_med3_f32 v11, v11, s51, v193
	v_cvt_pk_fp8_f32 v14, v10, v11
	v_mul_f32_e32 v12, v70, v9
	v_mul_f32_e32 v13, v66, v6
	v_med3_f32 v12, v12, s51, v193
	v_med3_f32 v13, v13, s51, v193
	v_cvt_pk_fp8_f32 v14, v12, v13 op_sel:[0,0,1]
	v_mul_f32_e32 v10, v79, v7
	v_mul_f32_e32 v11, v75, v8
	v_med3_f32 v10, v10, s51, v193
	global_store_dword v[4:5], v14, off offset:256
	v_med3_f32 v11, v11, s51, v193
	v_cvt_pk_fp8_f32 v14, v10, v11
	v_mul_f32_e32 v12, v71, v9
	v_mul_f32_e32 v13, v67, v6
	v_med3_f32 v12, v12, s51, v193
	v_med3_f32 v13, v13, s51, v193
	v_cvt_pk_fp8_f32 v14, v12, v13 op_sel:[0,0,1]
	v_mul_f32_e32 v10, v80, v7
	v_mul_f32_e32 v11, v76, v8
	v_med3_f32 v10, v10, s51, v193
	global_store_dword v[4:5], v14, off offset:320
	v_med3_f32 v11, v11, s51, v193
	v_cvt_pk_fp8_f32 v14, v10, v11
	v_mul_f32_e32 v12, v72, v9
	v_mul_f32_e32 v13, v68, v6
	v_med3_f32 v12, v12, s51, v193
	v_med3_f32 v13, v13, s51, v193
	v_cvt_pk_fp8_f32 v14, v12, v13 op_sel:[0,0,1]
	v_mul_f32_e32 v10, v81, v7
	v_mul_f32_e32 v11, v77, v8
	v_med3_f32 v10, v10, s51, v193
	global_store_dword v[4:5], v14, off offset:384
	v_med3_f32 v11, v11, s51, v193
	v_cvt_pk_fp8_f32 v14, v10, v11
	v_mul_f32_e32 v12, v73, v9
	v_mul_f32_e32 v13, v69, v6
	v_med3_f32 v12, v12, s51, v193
	v_med3_f32 v13, v13, s51, v193
	v_cvt_pk_fp8_f32 v14, v12, v13 op_sel:[0,0,1]
	v_mul_f32_e32 v10, v54, v9
	v_mul_f32_e32 v11, v50, v6
	global_store_dword v[4:5], v14, off offset:448
	v_mul_f32_e32 v4, v62, v7
	v_mul_f32_e32 v5, v58, v8
	v_med3_f32 v4, v4, s51, v193
	v_med3_f32 v5, v5, s51, v193
	v_cvt_pk_fp8_f32 v12, v4, v5
	v_med3_f32 v10, v10, s51, v193
	v_med3_f32 v11, v11, s51, v193
	v_mul_f32_e32 v4, v63, v7
	v_cvt_pk_fp8_f32 v12, v10, v11 op_sel:[0,0,1]
	v_mul_f32_e32 v5, v59, v8
	v_med3_f32 v4, v4, s51, v193
	v_med3_f32 v5, v5, s51, v193
	global_store_dword v[2:3], v12, off
	v_cvt_pk_fp8_f32 v12, v4, v5
	v_mul_f32_e32 v10, v55, v9
	v_mul_f32_e32 v11, v51, v6
	v_med3_f32 v10, v10, s51, v193
	v_med3_f32 v11, v11, s51, v193
	v_cvt_pk_fp8_f32 v12, v10, v11 op_sel:[0,0,1]
	v_mul_f32_e32 v4, v64, v7
	v_mul_f32_e32 v5, v60, v8
	v_med3_f32 v4, v4, s51, v193
	global_store_dword v[2:3], v12, off offset:64
	v_med3_f32 v5, v5, s51, v193
	v_cvt_pk_fp8_f32 v12, v4, v5
	v_mul_f32_e32 v10, v56, v9
	v_mul_f32_e32 v11, v52, v6
	v_med3_f32 v10, v10, s51, v193
	v_med3_f32 v11, v11, s51, v193
	v_cvt_pk_fp8_f32 v12, v10, v11 op_sel:[0,0,1]
	v_mul_f32_e32 v4, v65, v7
	v_mul_f32_e32 v5, v61, v8
	v_med3_f32 v4, v4, s51, v193
	global_store_dword v[2:3], v12, off offset:128
	v_med3_f32 v5, v5, s51, v193
	v_cvt_pk_fp8_f32 v12, v4, v5
	v_mul_f32_e32 v10, v57, v9
	v_mul_f32_e32 v11, v53, v6
	v_med3_f32 v10, v10, s51, v193
	v_med3_f32 v11, v11, s51, v193
	v_cvt_pk_fp8_f32 v12, v10, v11 op_sel:[0,0,1]
	v_mul_f32_e32 v4, v46, v7
	v_mul_f32_e32 v5, v42, v8
	v_med3_f32 v4, v4, s51, v193
	global_store_dword v[2:3], v12, off offset:192
	v_med3_f32 v5, v5, s51, v193
	v_cvt_pk_fp8_f32 v12, v4, v5
	v_mul_f32_e32 v10, v38, v9
	v_mul_f32_e32 v11, v34, v6
	v_med3_f32 v10, v10, s51, v193
	v_med3_f32 v11, v11, s51, v193
	v_cvt_pk_fp8_f32 v12, v10, v11 op_sel:[0,0,1]
	v_mul_f32_e32 v4, v47, v7
	v_mul_f32_e32 v5, v43, v8
	v_med3_f32 v4, v4, s51, v193
	global_store_dword v[2:3], v12, off offset:256
	v_med3_f32 v5, v5, s51, v193
	v_cvt_pk_fp8_f32 v12, v4, v5
	v_mul_f32_e32 v10, v39, v9
	v_mul_f32_e32 v11, v35, v6
	v_med3_f32 v10, v10, s51, v193
	v_med3_f32 v11, v11, s51, v193
	v_cvt_pk_fp8_f32 v12, v10, v11 op_sel:[0,0,1]
	v_mul_f32_e32 v4, v48, v7
	v_mul_f32_e32 v5, v44, v8
	v_med3_f32 v4, v4, s51, v193
	global_store_dword v[2:3], v12, off offset:320
	v_med3_f32 v5, v5, s51, v193
	v_cvt_pk_fp8_f32 v12, v4, v5
	v_mul_f32_e32 v4, v49, v7
	v_mul_f32_e32 v5, v45, v8
	v_med3_f32 v4, v4, s51, v193
	v_med3_f32 v5, v5, s51, v193
	v_cvt_pk_fp8_f32 v8, v4, v5
	v_mul_f32_e32 v10, v40, v9
	v_mul_f32_e32 v11, v36, v6
	v_mul_f32_e32 v7, v41, v9
	v_mul_f32_e32 v6, v37, v6
	v_med3_f32 v10, v10, s51, v193
	v_med3_f32 v11, v11, s51, v193
	v_med3_f32 v7, v7, s51, v193
	v_med3_f32 v6, v6, s51, v193
	v_cvt_pk_fp8_f32 v12, v10, v11 op_sel:[0,0,1]
	v_cvt_pk_fp8_f32 v8, v7, v6 op_sel:[0,0,1]
	s_andn2_b64 vcc, exec, s[0:1]
	global_store_dword v[2:3], v12, off offset:384
	global_store_dword v[2:3], v8, off offset:448
	s_cbranch_vccnz .LBB0_885
	s_andn2_b64 vcc, exec, s[6:7]
	s_cbranch_vccnz .LBB0_884
	s_barrier
	s_branch .LBB0_884

; __device__ __forceinline__ unsigned pk4_fp8(float a, float b, float c, float d) {
;     a = fminf(fmaxf(a, -448.f), 448.f); b = fminf(fmaxf(b, -448.f), 448.f); c = fminf(fmaxf(c, -448.f), 448.f); d = fminf(fmaxf(d, -448.f), 448.f);
;     int w = 0; w = __builtin_amdgcn_cvt_pk_fp8_f32(a, b, w, false); w = __builtin_amdgcn_cvt_pk_fp8_f32(c, d, w, true); return (unsigned)w;
; }
;     __device__ __forceinline__ void operator()(const f32x4 (&acc)[2][2][4][2], const Unit& u, int wr, int wc, int fr, int fq) const {
;         const int b = u.pm >> 4;
; #pragma unroll
;         for (int ai = 0; ai < 2; ++ai) { float rs4[4];
; #pragma unroll
;             for (int m = 0; m < 4; ++m) rs4[m] = rsqrtf(ss[u.pm * 256 + ai * HALF + wr * 64 + m * 16 + fr] * (1.0f / 4096.0f) + RMS_EPS) * (sc * 16.f);
;             const int T = (u.pm & 15) * 4 + ai * 2 + wr;
; #pragma unroll
;             for (int bj = 0; bj < 2; ++bj) { const int head = u.pn * 2 + bj;
;                 unsigned char* base = VT + (((size_t)b * 16 + head) * 64 + T) * 8192 + (wc * 32 + 8 * fq) * 64 + 32 * (fr >> 3) + 4 * (fr & 7);
; #pragma unroll
;                 for (int n = 0; n < 2; ++n)
; #pragma unroll
;                     for (int jj = 0; jj < 4; ++jj)
;                         *(unsigned*)(base + (4 * n + jj) * 64) = pk4_fp8(acc[ai][bj][0][n][jj] * rs4[0], acc[ai][bj][1][n][jj] * rs4[1], acc[ai][bj][2][n][jj] * rs4[2], acc[ai][bj][3][n][jj] * rs4[3]); } }
;     }
.LBB0_916:
	v_lshl_add_u32 v6, s18, 8, v1
	v_ashrrev_i32_e32 v7, 31, v6
	s_nop 15
	s_nop 15
	v_lshl_add_u64 v[2:3], v[6:7], 2, s[20:21]
	s_lshl_b32 s11, s18, 2
	s_lshl_b32 s22, s19, 1
	s_ashr_i32 s24, s18, 4
	s_and_b32 s11, s11, 60
	s_ashr_i32 s23, s22, 31
	s_add_i32 s18, s11, s30
	s_ashr_i32 s25, s24, 31
	s_lshl_b64 s[26:27], s[22:23], 19
	s_ashr_i32 s19, s18, 31
	s_lshl_b64 s[24:25], s[24:25], 23
	s_lshl_b64 s[18:19], s[18:19], 13
	v_mov_b32_e32 v17, 0
	s_or_b32 s22, s22, 1
	s_ashr_i32 s23, s22, 31
	s_lshl_b64 s[22:23], s[22:23], 19
	s_waitcnt vmcnt(0)
	v_fmamk_f32 v4, v234, 0x39800000, v192
	v_cmp_gt_f32_e32 vcc, s43, v4
	v_mul_f32_e32 v5, 0x4b800000, v4
	s_nop 0
	v_cndmask_b32_e32 v4, v4, v5, vcc
	v_rsq_f32_e32 v4, v4
	s_nop 0
	v_mul_f32_e32 v5, 0x45800000, v4
	v_cndmask_b32_e32 v4, v4, v5, vcc
	v_mul_f32_e32 v7, 0x3e800000, v4
	v_mul_f32_e32 v8, v158, v7
	v_med3_f32 v8, v8, s44, v193
	v_fmamk_f32 v4, v235, 0x39800000, v192
	v_cmp_gt_f32_e32 vcc, s43, v4
	v_mul_f32_e32 v5, 0x4b800000, v4
	s_nop 0
	v_cndmask_b32_e32 v4, v4, v5, vcc
	v_rsq_f32_e32 v4, v4
	s_nop 0
	v_mul_f32_e32 v5, 0x45800000, v4
	v_cndmask_b32_e32 v4, v4, v5, vcc
	v_mul_f32_e32 v10, 0x3e800000, v4
	v_mul_f32_e32 v9, v154, v10
	v_med3_f32 v9, v9, s44, v193
	v_cvt_pk_fp8_f32 v15, v8, v9
	v_mul_f32_e32 v8, v159, v7
	v_mul_f32_e32 v9, v155, v10
	v_med3_f32 v8, v8, s44, v193
	v_med3_f32 v9, v9, s44, v193
	v_fmamk_f32 v4, v236, 0x39800000, v192
	v_cmp_gt_f32_e32 vcc, s43, v4
	v_mul_f32_e32 v5, 0x4b800000, v4
	v_fmamk_f32 v2, v237, 0x39800000, v192
	v_cndmask_b32_e32 v4, v4, v5, vcc
	v_rsq_f32_e32 v4, v4
	v_mul_f32_e32 v3, 0x4b800000, v2
	v_mul_f32_e32 v5, 0x45800000, v4
	v_cndmask_b32_e32 v4, v4, v5, vcc
	v_cmp_gt_f32_e32 vcc, s43, v2
	v_mul_f32_e32 v11, 0x3e800000, v4
	v_mul_f32_e32 v13, v150, v11
	v_cndmask_b32_e32 v2, v2, v3, vcc
	v_rsq_f32_e32 v2, v2
	v_med3_f32 v13, v13, s44, v193
	v_mul_f32_e32 v3, 0x45800000, v2
	v_cndmask_b32_e32 v2, v2, v3, vcc
	v_mul_f32_e32 v12, 0x3e800000, v2
	v_mul_f32_e32 v14, v146, v12
	v_med3_f32 v14, v14, s44, v193
	v_cvt_pk_fp8_f32 v15, v13, v14 op_sel:[0,0,1]
	v_lshl_add_u64 v[2:3], v[170:171], 0, s[26:27]
	v_lshl_add_u64 v[4:5], v[2:3], 0, s[24:25]
	v_lshl_add_u64 v[2:3], v[4:5], 0, s[18:19]
	global_store_dword v[2:3], v15, off
	v_cvt_pk_fp8_f32 v15, v8, v9
	v_mul_f32_e32 v13, v151, v11
	v_mul_f32_e32 v14, v147, v12
	v_med3_f32 v13, v13, s44, v193
	v_med3_f32 v14, v14, s44, v193
	v_cvt_pk_fp8_f32 v15, v13, v14 op_sel:[0,0,1]
	v_mul_f32_e32 v8, v160, v7
	v_mul_f32_e32 v9, v156, v10
	v_med3_f32 v8, v8, s44, v193
	global_store_dword v[2:3], v15, off offset:64
	v_med3_f32 v9, v9, s44, v193
	v_cvt_pk_fp8_f32 v15, v8, v9
	v_mul_f32_e32 v13, v152, v11
	v_mul_f32_e32 v14, v148, v12
	v_med3_f32 v13, v13, s44, v193
	v_med3_f32 v14, v14, s44, v193
	v_cvt_pk_fp8_f32 v15, v13, v14 op_sel:[0,0,1]
	v_mul_f32_e32 v8, v161, v7
	v_mul_f32_e32 v9, v157, v10
	v_med3_f32 v8, v8, s44, v193
	global_store_dword v[2:3], v15, off offset:128
	v_med3_f32 v9, v9, s44, v193
	v_cvt_pk_fp8_f32 v15, v8, v9
	v_mul_f32_e32 v13, v153, v11
	v_mul_f32_e32 v14, v149, v12
	v_med3_f32 v13, v13, s44, v193
	v_med3_f32 v14, v14, s44, v193
	v_cvt_pk_fp8_f32 v15, v13, v14 op_sel:[0,0,1]
	v_mul_f32_e32 v8, v142, v7
	v_mul_f32_e32 v9, v138, v10
	v_med3_f32 v8, v8, s44, v193
	global_store_dword v[2:3], v15, off offset:192
	v_med3_f32 v9, v9, s44, v193
	v_cvt_pk_fp8_f32 v15, v8, v9
	v_mul_f32_e32 v13, v134, v11
	v_mul_f32_e32 v14, v130, v12
	v_med3_f32 v13, v13, s44, v193
	v_med3_f32 v14, v14, s44, v193
	v_cvt_pk_fp8_f32 v15, v13, v14 op_sel:[0,0,1]
	v_mul_f32_e32 v8, v143, v7
	v_mul_f32_e32 v9, v139, v10
	v_med3_f32 v8, v8, s44, v193
	global_store_dword v[2:3], v15, off offset:256
	v_med3_f32 v9, v9, s44, v193
	v_cvt_pk_fp8_f32 v15, v8, v9
	v_mul_f32_e32 v13, v135, v11
	v_mul_f32_e32 v14, v131, v12
	v_med3_f32 v13, v13, s44, v193
	v_med3_f32 v14, v14, s44, v193
	v_cvt_pk_fp8_f32 v15, v13, v14 op_sel:[0,0,1]
	v_mul_f32_e32 v8, v144, v7
	v_mul_f32_e32 v9, v140, v10
	v_med3_f32 v8, v8, s44, v193
	global_store_dword v[2:3], v15, off offset:320
	v_med3_f32 v9, v9, s44, v193
	v_cvt_pk_fp8_f32 v15, v8, v9
	v_mul_f32_e32 v13, v136, v11
	v_mul_f32_e32 v14, v132, v12
	v_med3_f32 v13, v13, s44, v193
	v_med3_f32 v14, v14, s44, v193
	v_cvt_pk_fp8_f32 v15, v13, v14 op_sel:[0,0,1]
	v_mul_f32_e32 v8, v145, v7
	v_mul_f32_e32 v9, v141, v10
	v_med3_f32 v8, v8, s44, v193
	global_store_dword v[2:3], v15, off offset:384
	v_med3_f32 v9, v9, s44, v193
	v_cvt_pk_fp8_f32 v15, v8, v9
	v_mul_f32_e32 v13, v137, v11
	v_mul_f32_e32 v14, v133, v12
	v_med3_f32 v13, v13, s44, v193
	v_med3_f32 v14, v14, s44, v193
	v_cvt_pk_fp8_f32 v15, v13, v14 op_sel:[0,0,1]
	v_mul_f32_e32 v13, v126, v7
	v_mul_f32_e32 v14, v122, v10
	v_med3_f32 v13, v13, s44, v193
	v_med3_f32 v14, v14, s44, v193
	v_cvt_pk_fp8_f32 v17, v13, v14
	global_store_dword v[2:3], v15, off offset:448
	v_mul_f32_e32 v15, v118, v11
	v_mul_f32_e32 v16, v114, v12
	v_med3_f32 v15, v15, s44, v193
	v_med3_f32 v16, v16, s44, v193
	v_cvt_pk_fp8_f32 v17, v15, v16 op_sel:[0,0,1]
	v_lshl_add_u64 v[2:3], v[170:171], 0, s[22:23]
	v_lshl_add_u64 v[2:3], v[2:3], 0, s[24:25]
	v_lshl_add_u64 v[8:9], v[2:3], 0, s[18:19]
	v_mul_f32_e32 v13, v127, v7
	v_mul_f32_e32 v14, v123, v10
	global_store_dword v[8:9], v17, off
	v_med3_f32 v13, v13, s44, v193
	v_med3_f32 v14, v14, s44, v193
	v_cvt_pk_fp8_f32 v17, v13, v14
	v_mul_f32_e32 v15, v119, v11
	v_mul_f32_e32 v16, v115, v12
	v_med3_f32 v15, v15, s44, v193
	v_med3_f32 v16, v16, s44, v193
	v_cvt_pk_fp8_f32 v17, v15, v16 op_sel:[0,0,1]
	v_mul_f32_e32 v13, v128, v7
	v_mul_f32_e32 v14, v124, v10
	v_med3_f32 v13, v13, s44, v193
; __device__ __forceinline__ unsigned pk4_fp8(float a, float b, float c, float d) {
;     a = fminf(fmaxf(a, -448.f), 448.f); b = fminf(fmaxf(b, -448.f), 448.f); c = fminf(fmaxf(c, -448.f), 448.f); d = fminf(fmaxf(d, -448.f), 448.f);
;     int w = 0; w = __builtin_amdgcn_cvt_pk_fp8_f32(a, b, w, false); w = __builtin_amdgcn_cvt_pk_fp8_f32(c, d, w, true); return (unsigned)w;
; }
;     __device__ __forceinline__ void operator()(const f32x4 (&acc)[2][2][4][2], const Unit& u, int wr, int wc, int fr, int fq) const {
;         const int b = u.pm >> 4;
; #pragma unroll
;         for (int ai = 0; ai < 2; ++ai) { float rs4[4];
; #pragma unroll
;             for (int m = 0; m < 4; ++m) rs4[m] = rsqrtf(ss[u.pm * 256 + ai * HALF + wr * 64 + m * 16 + fr] * (1.0f / 4096.0f) + RMS_EPS) * (sc * 16.f);
;             const int T = (u.pm & 15) * 4 + ai * 2 + wr;
; #pragma unroll
;             for (int bj = 0; bj < 2; ++bj) { const int head = u.pn * 2 + bj;
;                 unsigned char* base = VT + (((size_t)b * 16 + head) * 64 + T) * 8192 + (wc * 32 + 8 * fq) * 64 + 32 * (fr >> 3) + 4 * (fr & 7);
; #pragma unroll
;                 for (int n = 0; n < 2; ++n)
; #pragma unroll
;                     for (int jj = 0; jj < 4; ++jj)
;                         *(unsigned*)(base + (4 * n + jj) * 64) = pk4_fp8(acc[ai][bj][0][n][jj] * rs4[0], acc[ai][bj][1][n][jj] * rs4[1], acc[ai][bj][2][n][jj] * rs4[2], acc[ai][bj][3][n][jj] * rs4[3]); } }
;     }
	global_store_dword v[8:9], v17, off offset:64
	v_med3_f32 v14, v14, s44, v193
	v_cvt_pk_fp8_f32 v17, v13, v14
	v_mul_f32_e32 v15, v120, v11
	v_mul_f32_e32 v16, v116, v12
	v_med3_f32 v15, v15, s44, v193
	v_med3_f32 v16, v16, s44, v193
	v_cvt_pk_fp8_f32 v17, v15, v16 op_sel:[0,0,1]
	v_mul_f32_e32 v13, v129, v7
	v_mul_f32_e32 v14, v125, v10
	v_med3_f32 v13, v13, s44, v193
	global_store_dword v[8:9], v17, off offset:128
	v_med3_f32 v14, v14, s44, v193
	v_cvt_pk_fp8_f32 v17, v13, v14
	v_mul_f32_e32 v15, v121, v11
	v_mul_f32_e32 v16, v117, v12
	v_med3_f32 v15, v15, s44, v193
	v_med3_f32 v16, v16, s44, v193
	v_cvt_pk_fp8_f32 v17, v15, v16 op_sel:[0,0,1]
	v_mul_f32_e32 v13, v110, v7
	v_mul_f32_e32 v14, v106, v10
	v_med3_f32 v13, v13, s44, v193
	global_store_dword v[8:9], v17, off offset:192
	v_med3_f32 v14, v14, s44, v193
	v_cvt_pk_fp8_f32 v17, v13, v14
	v_mul_f32_e32 v15, v102, v11
	v_mul_f32_e32 v16, v98, v12
	v_med3_f32 v15, v15, s44, v193
	v_med3_f32 v16, v16, s44, v193
	v_cvt_pk_fp8_f32 v17, v15, v16 op_sel:[0,0,1]
	v_mul_f32_e32 v13, v111, v7
	v_mul_f32_e32 v14, v107, v10
	v_med3_f32 v13, v13, s44, v193
	global_store_dword v[8:9], v17, off offset:256
	v_med3_f32 v14, v14, s44, v193
	v_cvt_pk_fp8_f32 v17, v13, v14
	v_mul_f32_e32 v15, v103, v11
	v_mul_f32_e32 v16, v99, v12
	v_med3_f32 v15, v15, s44, v193
	v_med3_f32 v16, v16, s44, v193
	v_cvt_pk_fp8_f32 v17, v15, v16 op_sel:[0,0,1]
	v_mul_f32_e32 v13, v112, v7
	v_mul_f32_e32 v14, v108, v10
	v_med3_f32 v13, v13, s44, v193
	global_store_dword v[8:9], v17, off offset:320
	v_med3_f32 v14, v14, s44, v193
	v_mul_f32_e32 v7, v113, v7
	v_mul_f32_e32 v10, v109, v10
	v_cvt_pk_fp8_f32 v17, v13, v14
	v_med3_f32 v7, v7, s44, v193
	v_med3_f32 v10, v10, s44, v193
	v_cvt_pk_fp8_f32 v13, v7, v10
	v_mul_f32_e32 v15, v104, v11
	v_mul_f32_e32 v16, v100, v12
	v_mul_f32_e32 v11, v105, v11
	v_mul_f32_e32 v12, v101, v12
	v_med3_f32 v15, v15, s44, v193
	v_med3_f32 v16, v16, s44, v193
	v_med3_f32 v11, v11, s44, v193
	v_med3_f32 v12, v12, s44, v193
	v_cvt_pk_fp8_f32 v17, v15, v16 op_sel:[0,0,1]
	v_cvt_pk_fp8_f32 v13, v11, v12 op_sel:[0,0,1]
	v_add_u32_e32 v10, 0xa0, v6
	v_ashrrev_i32_e32 v11, 31, v10
	global_store_dword v[8:9], v17, off offset:384
	global_store_dword v[8:9], v13, off offset:448
	v_add_u32_e32 v8, 0x80, v6
	v_ashrrev_i32_e32 v9, 31, v8
	v_lshl_add_u64 v[8:9], v[8:9], 2, s[20:21]
	v_lshl_add_u64 v[10:11], v[10:11], 2, s[20:21]
	s_add_u32 s18, s18, 0x4000
	s_addc_u32 s19, s19, 0
	v_lshl_add_u64 v[4:5], v[4:5], 0, s[18:19]
	v_lshl_add_u64 v[2:3], v[2:3], 0, s[18:19]
	s_mov_b64 s[18:19], -1
	v_fmamk_f32 v7, v238, 0x39800000, v192
	v_cmp_gt_f32_e32 vcc, s43, v7
	v_mul_f32_e32 v8, 0x4b800000, v7
	s_nop 0
	v_cndmask_b32_e32 v7, v7, v8, vcc
	v_rsq_f32_e32 v7, v7
	s_nop 0
	v_mul_f32_e32 v8, 0x45800000, v7
	v_cndmask_b32_e32 v7, v7, v8, vcc
	v_add_u32_e32 v8, 0x90, v6
	v_ashrrev_i32_e32 v9, 31, v8
	v_lshl_add_u64 v[8:9], v[8:9], 2, s[20:21]
	v_mul_f32_e32 v7, 0x3e800000, v7
	v_fmamk_f32 v8, v239, 0x39800000, v192
	v_cmp_gt_f32_e32 vcc, s43, v8
	v_mul_f32_e32 v9, 0x4b800000, v8
	s_nop 0
	v_cndmask_b32_e32 v8, v8, v9, vcc
	v_rsq_f32_e32 v8, v8
	s_nop 0
	v_mul_f32_e32 v9, 0x45800000, v8
	v_cndmask_b32_e32 v8, v8, v9, vcc
	v_mul_f32_e32 v8, 0x3e800000, v8
	v_fmamk_f32 v9, v240, 0x39800000, v192
	v_cmp_gt_f32_e32 vcc, s43, v9
	v_mul_f32_e32 v10, 0x4b800000, v9
	s_nop 0
	v_cndmask_b32_e32 v9, v9, v10, vcc
	v_rsq_f32_e32 v9, v9
	s_nop 0
	v_mul_f32_e32 v10, 0x45800000, v9
	v_cndmask_b32_e32 v9, v9, v10, vcc
	v_add_u32_e32 v10, 0xb0, v6
	v_ashrrev_i32_e32 v11, 31, v10
	v_lshl_add_u64 v[10:11], v[10:11], 2, s[20:21]
	v_mul_f32_e32 v11, v90, v8
	v_med3_f32 v11, v11, s44, v193
	v_mul_f32_e32 v9, 0x3e800000, v9
	v_mul_f32_e32 v12, v86, v9
	v_med3_f32 v12, v12, s44, v193
	v_fmamk_f32 v6, v241, 0x39800000, v192
	v_cmp_gt_f32_e32 vcc, s43, v6
	v_mul_f32_e32 v10, 0x4b800000, v6
	s_nop 0
	v_cndmask_b32_e32 v6, v6, v10, vcc
	v_rsq_f32_e32 v6, v6
	s_nop 0
	v_mul_f32_e32 v10, 0x45800000, v6
	v_cndmask_b32_e32 v6, v6, v10, vcc
	v_mul_f32_e32 v10, v94, v7
	v_med3_f32 v10, v10, s44, v193
	v_cvt_pk_fp8_f32 v14, v10, v11
	v_mul_f32_e32 v6, 0x3e800000, v6
	v_mul_f32_e32 v13, v82, v6
	v_med3_f32 v13, v13, s44, v193
	v_cvt_pk_fp8_f32 v14, v12, v13 op_sel:[0,0,1]
	v_mul_f32_e32 v10, v95, v7
	v_mul_f32_e32 v11, v91, v8
	v_med3_f32 v10, v10, s44, v193
	global_store_dword v[4:5], v14, off
	v_med3_f32 v11, v11, s44, v193
	v_cvt_pk_fp8_f32 v14, v10, v11
	v_mul_f32_e32 v12, v87, v9
	v_mul_f32_e32 v13, v83, v6
	v_med3_f32 v12, v12, s44, v193
	v_med3_f32 v13, v13, s44, v193
	v_cvt_pk_fp8_f32 v14, v12, v13 op_sel:[0,0,1]
	v_mul_f32_e32 v10, v96, v7
	v_mul_f32_e32 v11, v92, v8
	v_med3_f32 v10, v10, s44, v193
	global_store_dword v[4:5], v14, off offset:64
	v_med3_f32 v11, v11, s44, v193
	v_cvt_pk_fp8_f32 v14, v10, v11
	v_mul_f32_e32 v12, v88, v9
	v_mul_f32_e32 v13, v84, v6
	v_med3_f32 v12, v12, s44, v193
	v_med3_f32 v13, v13, s44, v193
; __device__ __forceinline__ unsigned pk4_fp8(float a, float b, float c, float d) {
;     a = fminf(fmaxf(a, -448.f), 448.f); b = fminf(fmaxf(b, -448.f), 448.f); c = fminf(fmaxf(c, -448.f), 448.f); d = fminf(fmaxf(d, -448.f), 448.f);
;     int w = 0; w = __builtin_amdgcn_cvt_pk_fp8_f32(a, b, w, false); w = __builtin_amdgcn_cvt_pk_fp8_f32(c, d, w, true); return (unsigned)w;
; }
;     __device__ __forceinline__ void operator()(const f32x4 (&acc)[2][2][4][2], const Unit& u, int wr, int wc, int fr, int fq) const {
;         const int b = u.pm >> 4;
; #pragma unroll
;         for (int ai = 0; ai < 2; ++ai) { float rs4[4];
; #pragma unroll
;             for (int m = 0; m < 4; ++m) rs4[m] = rsqrtf(ss[u.pm * 256 + ai * HALF + wr * 64 + m * 16 + fr] * (1.0f / 4096.0f) + RMS_EPS) * (sc * 16.f);
;             const int T = (u.pm & 15) * 4 + ai * 2 + wr;
; #pragma unroll
;             for (int bj = 0; bj < 2; ++bj) { const int head = u.pn * 2 + bj;
;                 unsigned char* base = VT + (((size_t)b * 16 + head) * 64 + T) * 8192 + (wc * 32 + 8 * fq) * 64 + 32 * (fr >> 3) + 4 * (fr & 7);
; #pragma unroll
;                 for (int n = 0; n < 2; ++n)
; #pragma unroll
;                     for (int jj = 0; jj < 4; ++jj)
;                         *(unsigned*)(base + (4 * n + jj) * 64) = pk4_fp8(acc[ai][bj][0][n][jj] * rs4[0], acc[ai][bj][1][n][jj] * rs4[1], acc[ai][bj][2][n][jj] * rs4[2], acc[ai][bj][3][n][jj] * rs4[3]); } }
;     }
	v_cvt_pk_fp8_f32 v14, v12, v13 op_sel:[0,0,1]
	v_mul_f32_e32 v10, v97, v7
	v_mul_f32_e32 v11, v93, v8
	v_med3_f32 v10, v10, s44, v193
	global_store_dword v[4:5], v14, off offset:128
	v_med3_f32 v11, v11, s44, v193
	v_cvt_pk_fp8_f32 v14, v10, v11
	v_mul_f32_e32 v12, v89, v9
	v_mul_f32_e32 v13, v85, v6
	v_med3_f32 v12, v12, s44, v193
	v_med3_f32 v13, v13, s44, v193
	v_cvt_pk_fp8_f32 v14, v12, v13 op_sel:[0,0,1]
	v_mul_f32_e32 v10, v78, v7
	v_mul_f32_e32 v11, v74, v8
	v_med3_f32 v10, v10, s44, v193
	global_store_dword v[4:5], v14, off offset:192
	v_med3_f32 v11, v11, s44, v193
	v_cvt_pk_fp8_f32 v14, v10, v11
	v_mul_f32_e32 v12, v70, v9
	v_mul_f32_e32 v13, v66, v6
	v_med3_f32 v12, v12, s44, v193
	v_med3_f32 v13, v13, s44, v193
	v_cvt_pk_fp8_f32 v14, v12, v13 op_sel:[0,0,1]
	v_mul_f32_e32 v10, v79, v7
	v_mul_f32_e32 v11, v75, v8
	v_med3_f32 v10, v10, s44, v193
	global_store_dword v[4:5], v14, off offset:256
	v_med3_f32 v11, v11, s44, v193
	v_cvt_pk_fp8_f32 v14, v10, v11
	v_mul_f32_e32 v12, v71, v9
	v_mul_f32_e32 v13, v67, v6
	v_med3_f32 v12, v12, s44, v193
	v_med3_f32 v13, v13, s44, v193
	v_cvt_pk_fp8_f32 v14, v12, v13 op_sel:[0,0,1]
	v_mul_f32_e32 v10, v80, v7
	v_mul_f32_e32 v11, v76, v8
	v_med3_f32 v10, v10, s44, v193
	global_store_dword v[4:5], v14, off offset:320
	v_med3_f32 v11, v11, s44, v193
	v_cvt_pk_fp8_f32 v14, v10, v11
	v_mul_f32_e32 v12, v72, v9
	v_mul_f32_e32 v13, v68, v6
	v_med3_f32 v12, v12, s44, v193
	v_med3_f32 v13, v13, s44, v193
	v_cvt_pk_fp8_f32 v14, v12, v13 op_sel:[0,0,1]
	v_mul_f32_e32 v10, v81, v7
	v_mul_f32_e32 v11, v77, v8
	v_med3_f32 v10, v10, s44, v193
	global_store_dword v[4:5], v14, off offset:384
	v_med3_f32 v11, v11, s44, v193
	v_cvt_pk_fp8_f32 v14, v10, v11
	v_mul_f32_e32 v12, v73, v9
	v_mul_f32_e32 v13, v69, v6
	v_med3_f32 v12, v12, s44, v193
	v_med3_f32 v13, v13, s44, v193
	v_cvt_pk_fp8_f32 v14, v12, v13 op_sel:[0,0,1]
	v_mul_f32_e32 v10, v54, v9
	v_mul_f32_e32 v11, v50, v6
	global_store_dword v[4:5], v14, off offset:448
	v_mul_f32_e32 v4, v62, v7
	v_mul_f32_e32 v5, v58, v8
	v_med3_f32 v4, v4, s44, v193
	v_med3_f32 v5, v5, s44, v193
	v_cvt_pk_fp8_f32 v12, v4, v5
	v_med3_f32 v10, v10, s44, v193
	v_med3_f32 v11, v11, s44, v193
	v_mul_f32_e32 v4, v63, v7
	v_cvt_pk_fp8_f32 v12, v10, v11 op_sel:[0,0,1]
	v_mul_f32_e32 v5, v59, v8
	v_med3_f32 v4, v4, s44, v193
	v_med3_f32 v5, v5, s44, v193
	global_store_dword v[2:3], v12, off
	v_cvt_pk_fp8_f32 v12, v4, v5
	v_mul_f32_e32 v10, v55, v9
	v_mul_f32_e32 v11, v51, v6
	v_med3_f32 v10, v10, s44, v193
	v_med3_f32 v11, v11, s44, v193
	v_cvt_pk_fp8_f32 v12, v10, v11 op_sel:[0,0,1]
	v_mul_f32_e32 v4, v64, v7
	v_mul_f32_e32 v5, v60, v8
	v_med3_f32 v4, v4, s44, v193
	global_store_dword v[2:3], v12, off offset:64
	v_med3_f32 v5, v5, s44, v193
	v_cvt_pk_fp8_f32 v12, v4, v5
	v_mul_f32_e32 v10, v56, v9
	v_mul_f32_e32 v11, v52, v6
	v_med3_f32 v10, v10, s44, v193
	v_med3_f32 v11, v11, s44, v193
	v_cvt_pk_fp8_f32 v12, v10, v11 op_sel:[0,0,1]
	v_mul_f32_e32 v4, v65, v7
	v_mul_f32_e32 v5, v61, v8
	v_med3_f32 v4, v4, s44, v193
	global_store_dword v[2:3], v12, off offset:128
	v_med3_f32 v5, v5, s44, v193
	v_cvt_pk_fp8_f32 v12, v4, v5
	v_mul_f32_e32 v10, v57, v9
	v_mul_f32_e32 v11, v53, v6
	v_med3_f32 v10, v10, s44, v193
	v_med3_f32 v11, v11, s44, v193
	v_cvt_pk_fp8_f32 v12, v10, v11 op_sel:[0,0,1]
	v_mul_f32_e32 v4, v46, v7
	v_mul_f32_e32 v5, v42, v8
	v_med3_f32 v4, v4, s44, v193
	global_store_dword v[2:3], v12, off offset:192
	v_med3_f32 v5, v5, s44, v193
	v_cvt_pk_fp8_f32 v12, v4, v5
	v_mul_f32_e32 v10, v38, v9
	v_mul_f32_e32 v11, v34, v6
	v_med3_f32 v10, v10, s44, v193
	v_med3_f32 v11, v11, s44, v193
	v_cvt_pk_fp8_f32 v12, v10, v11 op_sel:[0,0,1]
	v_mul_f32_e32 v4, v47, v7
	v_mul_f32_e32 v5, v43, v8
	v_med3_f32 v4, v4, s44, v193
	global_store_dword v[2:3], v12, off offset:256
	v_med3_f32 v5, v5, s44, v193
	v_cvt_pk_fp8_f32 v12, v4, v5
	v_mul_f32_e32 v10, v39, v9
	v_mul_f32_e32 v11, v35, v6
	v_med3_f32 v10, v10, s44, v193
	v_med3_f32 v11, v11, s44, v193
	v_cvt_pk_fp8_f32 v12, v10, v11 op_sel:[0,0,1]
	v_mul_f32_e32 v4, v48, v7
	v_mul_f32_e32 v5, v44, v8
	v_med3_f32 v4, v4, s44, v193
	global_store_dword v[2:3], v12, off offset:320
	v_med3_f32 v5, v5, s44, v193
	v_cvt_pk_fp8_f32 v12, v4, v5
	v_mul_f32_e32 v4, v49, v7
	v_mul_f32_e32 v5, v45, v8
	v_med3_f32 v4, v4, s44, v193
	v_med3_f32 v5, v5, s44, v193
	v_cvt_pk_fp8_f32 v8, v4, v5
	v_mul_f32_e32 v10, v40, v9
	v_mul_f32_e32 v11, v36, v6
	v_mul_f32_e32 v7, v41, v9
	v_mul_f32_e32 v6, v37, v6
	v_med3_f32 v10, v10, s44, v193
	v_med3_f32 v11, v11, s44, v193
	v_med3_f32 v7, v7, s44, v193
	v_med3_f32 v6, v6, s44, v193
	v_cvt_pk_fp8_f32 v12, v10, v11 op_sel:[0,0,1]
	v_cvt_pk_fp8_f32 v8, v7, v6 op_sel:[0,0,1]
	s_and_b64 vcc, exec, s[0:1]
	global_store_dword v[2:3], v12, off offset:384
	global_store_dword v[2:3], v8, off offset:448
	s_cbranch_vccz .LBB0_905
	s_andn2_b64 vcc, exec, s[2:3]
	s_cbranch_vccnz .LBB0_904
	s_barrier
	s_branch .LBB0_904

; __device__ __forceinline__ unsigned cvt_pk_bf16(float lo, float hi) { unsigned r; asm volatile("v_cvt_pk_bf16_f32 %0, %1, %2" : "=v"(r) : "v"(lo), "v"(hi)); return r; }
;     __device__ __forceinline__ void operator()(const f32x4 (&acc)[2][2][4][2], const Unit& u, int wr, int wc, int fr, int fq) const {
;     ...
;                 for (int bj = 0; bj < 2; ++bj) { const size_t o2 = (size_t)(row0 + ai * HALF + m * 16) * DM + col0 + bj * HALF;
;                     if constexpr (XF32) { a[m][bj][0] = *(const f32x4*)((const float*)xin + o2); a[m][bj][1] = *(const f32x4*)((const float*)xin + o2 + 4); }
;                     else { const u32x4 w = *(const u32x4*)((const bf16_t*)xin + o2); a[m][bj][0] = __builtin_bit_cast(f32x4, w); } }
; #pragma unroll
;             for (int m = 0; m < 4; ++m) {
;                 const int row = row0 + ai * HALF + m * 16; const size_t off = (size_t)row * DM + col0; float q = 0.f;
; #pragma unroll
;                 for (int bj = 0; bj < 2; ++bj) { const size_t o2 = off + bj * HALF;
;                     f32x4 a0, a1;
;                     if constexpr (XF32) { a0 = a[m][bj][0]; a1 = a[m][bj][1]; }
;                     else { const u32x4 w = __builtin_bit_cast(u32x4, a[m][bj][0]);
;                         a0 = (f32x4){__uint_as_float(w.x << 16), __uint_as_float(w.x & 0xffff0000u), __uint_as_float(w.y << 16), __uint_as_float(w.y & 0xffff0000u)};
;                         a1 = (f32x4){__uint_as_float(w.z << 16), __uint_as_float(w.z & 0xffff0000u), __uint_as_float(w.w << 16), __uint_as_float(w.w & 0xffff0000u)}; }
;                     const f32x4 v0 = a0 + acc[ai][bj][m][0] * sc, v1 = a1 + acc[ai][bj][m][1] * sc;
;                     q += ((v0[0] * v0[0] + v0[1] * v0[1]) + (v0[2] * v0[2] + v0[3] * v0[3])) + ((v1[0] * v1[0] + v1[1] * v1[1]) + (v1[2] * v1[2] + v1[3] * v1[3]));
;                     u32x4 wo; wo.x = cvt_pk_bf16(v0[0], v0[1]); wo.y = cvt_pk_bf16(v0[2], v0[3]); wo.z = cvt_pk_bf16(v1[0], v1[1]); wo.w = cvt_pk_bf16(v1[2], v1[3]);
;                     *(u32x4*)(xb + o2) = wo;
;                     if (x8) { u32x2 w8; w8.x = pk4_fp8(v0[0], v0[1], v0[2], v0[3]); w8.y = pk4_fp8(v1[0], v1[1], v1[2], v1[3]); *(u32x2*)(x8 + o2) = w8; } }
.LBB0_1678:
	v_lshl_add_u32 v178, s6, 8, v1
	v_lshl_or_b32 v30, s28, 8, v195
	v_ashrrev_i32_e32 v31, 31, v30
	v_ashrrev_i32_e32 v179, 31, v178
	v_or_b32_e32 v188, 16, v178
	v_lshl_add_u64 v[32:33], v[30:31], 1, s[66:67]
	v_lshlrev_b64 v[2:3], 13, v[178:179]
	v_ashrrev_i32_e32 v189, 31, v188
	v_or_b32_e32 v184, 32, v178
	v_lshl_add_u64 v[206:207], v[32:33], 0, v[2:3]
	v_lshlrev_b64 v[2:3], 13, v[188:189]
	v_ashrrev_i32_e32 v185, 31, v184
	v_or_b32_e32 v180, 48, v178
	v_lshl_add_u64 v[190:191], v[32:33], 0, v[2:3]
	v_lshlrev_b64 v[2:3], 13, v[184:185]
	v_ashrrev_i32_e32 v181, 31, v180
	s_nop 15
	s_nop 15
	v_lshl_add_u64 v[186:187], v[32:33], 0, v[2:3]
	v_lshlrev_b64 v[2:3], 13, v[180:181]
	global_load_dwordx4 v[202:205], v[206:207], off
	global_load_dwordx4 v[26:29], v[206:207], off offset:256
	v_lshl_add_u64 v[182:183], v[32:33], 0, v[2:3]
	global_load_dwordx4 v[22:25], v[190:191], off
	global_load_dwordx4 v[18:21], v[190:191], off offset:256
	global_load_dwordx4 v[14:17], v[186:187], off
	global_load_dwordx4 v[10:13], v[186:187], off offset:256
	global_load_dwordx4 v[6:9], v[182:183], off
	global_load_dwordx4 v[2:5], v[182:183], off offset:256
	v_cndmask_b32_e64 v192, 0, 1, s[16:17]
	v_cmp_ne_u32_e64 s[6:7], 1, v192
	v_lshlrev_b64 v[192:193], 12, v[178:179]
	v_lshl_add_u64 v[192:193], v[192:193], 0, v[30:31]
	s_andn2_b64 vcc, exec, s[16:17]
	s_waitcnt vmcnt(0)
	v_lshlrev_b32_e32 v208, 16, v202
	v_and_b32_e32 v209, 0xffff0000, v202
	v_lshlrev_b32_e32 v202, 16, v203
	v_and_b32_e32 v203, 0xffff0000, v203
	v_lshlrev_b32_e32 v210, 16, v204
	v_and_b32_e32 v211, 0xffff0000, v204
	v_lshlrev_b32_e32 v204, 16, v205
	v_and_b32_e32 v205, 0xffff0000, v205
	v_pk_fma_f32 v[160:161], v[160:161], s[18:19], v[202:203] op_sel_hi:[1,0,1]
	v_pk_fma_f32 v[158:159], v[158:159], s[18:19], v[208:209] op_sel_hi:[1,0,1]
	v_pk_fma_f32 v[156:157], v[156:157], s[18:19], v[204:205] op_sel_hi:[1,0,1]
	v_pk_fma_f32 v[154:155], v[154:155], s[18:19], v[210:211] op_sel_hi:[1,0,1]
	v_cvt_pk_bf16_f32 v202, v158, v159
	v_cvt_pk_bf16_f32 v203, v160, v161
	s_nop 0
	v_cvt_pk_bf16_f32 v204, v154, v155
	v_cvt_pk_bf16_f32 v205, v156, v157
	global_store_dwordx4 v[206:207], v[202:205], off
	s_cbranch_vccnz .LBB0_1680
	v_max_f32_e32 v201, v158, v158
	v_max_f32_e32 v202, v159, v159
	v_med3_f32 v201, v201, s48, v200
	v_med3_f32 v203, v202, s48, v200
	v_cvt_pk_fp8_f32 v202, v201, v203
	v_max_f32_e32 v204, v160, v160
	v_max_f32_e32 v203, v161, v161
	v_med3_f32 v201, v204, s48, v200
	v_med3_f32 v203, v203, s48, v200
	v_cvt_pk_fp8_f32 v202, v201, v203 op_sel:[0,0,1]
	v_max_f32_e32 v201, v154, v154
	v_max_f32_e32 v203, v155, v155
	v_med3_f32 v201, v201, s48, v200
	v_med3_f32 v204, v203, s48, v200
	v_cvt_pk_fp8_f32 v203, v201, v204
	v_max_f32_e32 v205, v156, v156
	v_max_f32_e32 v204, v157, v157
	v_med3_f32 v201, v205, s48, v200
	v_med3_f32 v204, v204, s48, v200
	v_cvt_pk_fp8_f32 v203, v201, v204 op_sel:[0,0,1]
	v_lshl_add_u64 v[204:205], s[70:71], 0, v[192:193]
	global_store_dwordx2 v[204:205], v[202:203], off
.LBB0_1680:
	v_or_b32_e32 v192, 0x80, v192
	v_lshlrev_b32_e32 v202, 16, v26
	v_and_b32_e32 v203, 0xffff0000, v26
	v_lshlrev_b32_e32 v26, 16, v27
	v_and_b32_e32 v27, 0xffff0000, v27
	v_lshlrev_b32_e32 v204, 16, v28
	v_and_b32_e32 v205, 0xffff0000, v28
	v_lshlrev_b32_e32 v28, 16, v29
	v_and_b32_e32 v29, 0xffff0000, v29
	v_pk_fma_f32 v[26:27], v[152:153], s[18:19], v[26:27] op_sel_hi:[1,0,1]
	v_pk_fma_f32 v[150:151], v[150:151], s[18:19], v[202:203] op_sel_hi:[1,0,1]
	v_pk_fma_f32 v[28:29], v[148:149], s[18:19], v[28:29] op_sel_hi:[1,0,1]
	v_pk_fma_f32 v[146:147], v[146:147], s[18:19], v[204:205] op_sel_hi:[1,0,1]
	v_lshl_add_u64 v[148:149], v[192:193], 1, s[66:67]
	s_and_b64 vcc, exec, s[6:7]
	v_cvt_pk_bf16_f32 v202, v150, v151
	v_cvt_pk_bf16_f32 v203, v26, v27
	v_cvt_pk_bf16_f32 v204, v146, v147
	v_cvt_pk_bf16_f32 v205, v28, v29
	global_store_dwordx4 v[148:149], v[202:205], off
	s_cbranch_vccnz .LBB0_1682
	v_max_f32_e32 v148, v150, v150
	v_med3_f32 v149, v148, s48, v200
	v_max_f32_e32 v148, v151, v151
	v_med3_f32 v152, v148, s48, v200
	v_cvt_pk_fp8_f32 v148, v149, v152
	v_max_f32_e32 v153, v26, v26
	v_max_f32_e32 v152, v27, v27
	v_med3_f32 v149, v153, s48, v200
	v_med3_f32 v152, v152, s48, v200
	v_cvt_pk_fp8_f32 v148, v149, v152 op_sel:[0,0,1]
	v_max_f32_e32 v149, v146, v146
	v_med3_f32 v152, v149, s48, v200
	v_max_f32_e32 v149, v147, v147
	v_med3_f32 v153, v149, s48, v200
	v_cvt_pk_fp8_f32 v149, v152, v153
	v_max_f32_e32 v201, v28, v28
	v_max_f32_e32 v153, v29, v29
	v_med3_f32 v152, v201, s48, v200
	v_med3_f32 v153, v153, s48, v200
	v_cvt_pk_fp8_f32 v149, v152, v153 op_sel:[0,0,1]
	v_lshl_add_u64 v[152:153], s[70:71], 0, v[192:193]
	global_store_dwordx2 v[152:153], v[148:149], off

; __device__ __forceinline__ unsigned cvt_pk_bf16(float lo, float hi) { unsigned r; asm volatile("v_cvt_pk_bf16_f32 %0, %1, %2" : "=v"(r) : "v"(lo), "v"(hi)); return r; }
;     __device__ __forceinline__ void operator()(const f32x4 (&acc)[2][2][4][2], const Unit& u, int wr, int wc, int fr, int fq) const {
;     ...
;                 for (int bj = 0; bj < 2; ++bj) { const size_t o2 = (size_t)(row0 + ai * HALF + m * 16) * DM + col0 + bj * HALF;
;                     if constexpr (XF32) { a[m][bj][0] = *(const f32x4*)((const float*)xin + o2); a[m][bj][1] = *(const f32x4*)((const float*)xin + o2 + 4); }
;                     else { const u32x4 w = *(const u32x4*)((const bf16_t*)xin + o2); a[m][bj][0] = __builtin_bit_cast(f32x4, w); } }
; #pragma unroll
;             for (int m = 0; m < 4; ++m) {
;                 const int row = row0 + ai * HALF + m * 16; const size_t off = (size_t)row * DM + col0; float q = 0.f;
; #pragma unroll
;                 for (int bj = 0; bj < 2; ++bj) { const size_t o2 = off + bj * HALF;
;                     f32x4 a0, a1;
;                     if constexpr (XF32) { a0 = a[m][bj][0]; a1 = a[m][bj][1]; }
;                     else { const u32x4 w = __builtin_bit_cast(u32x4, a[m][bj][0]);
;                         a0 = (f32x4){__uint_as_float(w.x << 16), __uint_as_float(w.x & 0xffff0000u), __uint_as_float(w.y << 16), __uint_as_float(w.y & 0xffff0000u)};
;                         a1 = (f32x4){__uint_as_float(w.z << 16), __uint_as_float(w.z & 0xffff0000u), __uint_as_float(w.w << 16), __uint_as_float(w.w & 0xffff0000u)}; }
;                     const f32x4 v0 = a0 + acc[ai][bj][m][0] * sc, v1 = a1 + acc[ai][bj][m][1] * sc;
;                     q += ((v0[0] * v0[0] + v0[1] * v0[1]) + (v0[2] * v0[2] + v0[3] * v0[3])) + ((v1[0] * v1[0] + v1[1] * v1[1]) + (v1[2] * v1[2] + v1[3] * v1[3]));
;                     u32x4 wo; wo.x = cvt_pk_bf16(v0[0], v0[1]); wo.y = cvt_pk_bf16(v0[2], v0[3]); wo.z = cvt_pk_bf16(v1[0], v1[1]); wo.w = cvt_pk_bf16(v1[2], v1[3]);
;                     *(u32x4*)(xb + o2) = wo;
;                     if (x8) { u32x2 w8; w8.x = pk4_fp8(v0[0], v0[1], v0[2], v0[3]); w8.y = pk4_fp8(v1[0], v1[1], v1[2], v1[3]); *(u32x2*)(x8 + o2) = w8; } }
.LBB0_1684:
	s_or_b64 exec, exec, s[28:29]
	s_waitcnt lgkmcnt(0)
	v_lshlrev_b64 v[26:27], 12, v[188:189]
	v_lshlrev_b32_e32 v28, 16, v22
	v_and_b32_e32 v29, 0xffff0000, v22
	v_lshlrev_b32_e32 v22, 16, v23
	v_and_b32_e32 v23, 0xffff0000, v23
	v_lshlrev_b32_e32 v148, 16, v24
	v_and_b32_e32 v149, 0xffff0000, v24
	v_lshlrev_b32_e32 v24, 16, v25
	v_and_b32_e32 v25, 0xffff0000, v25
	v_lshl_add_u64 v[26:27], v[26:27], 0, v[30:31]
	v_pk_fma_f32 v[22:23], v[144:145], s[18:19], v[22:23] op_sel_hi:[1,0,1]
	v_pk_fma_f32 v[28:29], v[142:143], s[18:19], v[28:29] op_sel_hi:[1,0,1]
	v_pk_fma_f32 v[24:25], v[140:141], s[18:19], v[24:25] op_sel_hi:[1,0,1]
	v_pk_fma_f32 v[138:139], v[138:139], s[18:19], v[148:149] op_sel_hi:[1,0,1]
	s_and_b64 vcc, exec, s[6:7]
	v_cvt_pk_bf16_f32 v140, v28, v29
	v_cvt_pk_bf16_f32 v141, v22, v23
	v_cvt_pk_bf16_f32 v142, v138, v139
	v_cvt_pk_bf16_f32 v143, v24, v25
	global_store_dwordx4 v[190:191], v[140:143], off
	s_cbranch_vccnz .LBB0_1686
	s_nop 0
	v_max_f32_e32 v140, v28, v28
	v_med3_f32 v141, v140, s48, v200
	v_max_f32_e32 v140, v29, v29
	v_med3_f32 v142, v140, s48, v200
	v_cvt_pk_fp8_f32 v140, v141, v142
	v_max_f32_e32 v143, v22, v22
	v_max_f32_e32 v142, v23, v23
	v_med3_f32 v141, v143, s48, v200
	v_med3_f32 v142, v142, s48, v200
	v_cvt_pk_fp8_f32 v140, v141, v142 op_sel:[0,0,1]
	v_max_f32_e32 v141, v138, v138
	v_med3_f32 v142, v141, s48, v200
	v_max_f32_e32 v141, v139, v139
	v_med3_f32 v143, v141, s48, v200
	v_cvt_pk_fp8_f32 v141, v142, v143
	v_max_f32_e32 v144, v24, v24
	v_max_f32_e32 v143, v25, v25
	v_med3_f32 v142, v144, s48, v200
	v_med3_f32 v143, v143, s48, v200
	v_cvt_pk_fp8_f32 v141, v142, v143 op_sel:[0,0,1]
	v_lshl_add_u64 v[142:143], s[70:71], 0, v[26:27]
	global_store_dwordx2 v[142:143], v[140:141], off
.LBB0_1686:
	v_or_b32_e32 v26, 0x80, v26
	v_lshlrev_b32_e32 v140, 16, v18
	v_and_b32_e32 v141, 0xffff0000, v18
	v_lshlrev_b32_e32 v18, 16, v19
	v_and_b32_e32 v19, 0xffff0000, v19
	v_lshlrev_b32_e32 v142, 16, v20
	v_and_b32_e32 v143, 0xffff0000, v20
	v_lshlrev_b32_e32 v20, 16, v21
	v_and_b32_e32 v21, 0xffff0000, v21
	v_pk_fma_f32 v[18:19], v[136:137], s[18:19], v[18:19] op_sel_hi:[1,0,1]
	v_pk_fma_f32 v[134:135], v[134:135], s[18:19], v[140:141] op_sel_hi:[1,0,1]
	v_pk_fma_f32 v[20:21], v[132:133], s[18:19], v[20:21] op_sel_hi:[1,0,1]
	v_pk_fma_f32 v[130:131], v[130:131], s[18:19], v[142:143] op_sel_hi:[1,0,1]
	v_lshl_add_u64 v[132:133], v[26:27], 1, s[66:67]
	s_and_b64 vcc, exec, s[6:7]
	v_cvt_pk_bf16_f32 v140, v134, v135
	v_cvt_pk_bf16_f32 v141, v18, v19
	v_cvt_pk_bf16_f32 v142, v130, v131
	v_cvt_pk_bf16_f32 v143, v20, v21
	global_store_dwordx4 v[132:133], v[140:143], off
	s_cbranch_vccnz .LBB0_1688
	v_max_f32_e32 v132, v134, v134
	v_med3_f32 v133, v132, s48, v200
	v_max_f32_e32 v132, v135, v135
	v_med3_f32 v136, v132, s48, v200
	v_cvt_pk_fp8_f32 v132, v133, v136
	v_max_f32_e32 v137, v18, v18
	v_max_f32_e32 v136, v19, v19
	v_med3_f32 v133, v137, s48, v200
	v_med3_f32 v136, v136, s48, v200
	v_cvt_pk_fp8_f32 v132, v133, v136 op_sel:[0,0,1]
	v_max_f32_e32 v133, v130, v130
	v_med3_f32 v136, v133, s48, v200
	v_max_f32_e32 v133, v131, v131
	v_med3_f32 v137, v133, s48, v200
	v_cvt_pk_fp8_f32 v133, v136, v137
	v_max_f32_e32 v140, v20, v20
	v_max_f32_e32 v137, v21, v21
	v_med3_f32 v136, v140, s48, v200
	v_med3_f32 v137, v137, s48, v200
	v_cvt_pk_fp8_f32 v133, v136, v137 op_sel:[0,0,1]
	v_lshl_add_u64 v[26:27], s[70:71], 0, v[26:27]
	global_store_dwordx2 v[26:27], v[132:133], off

; __device__ __forceinline__ unsigned cvt_pk_bf16(float lo, float hi) { unsigned r; asm volatile("v_cvt_pk_bf16_f32 %0, %1, %2" : "=v"(r) : "v"(lo), "v"(hi)); return r; }
;     __device__ __forceinline__ void operator()(const f32x4 (&acc)[2][2][4][2], const Unit& u, int wr, int wc, int fr, int fq) const {
;     ...
;                 for (int bj = 0; bj < 2; ++bj) { const size_t o2 = (size_t)(row0 + ai * HALF + m * 16) * DM + col0 + bj * HALF;
;                     if constexpr (XF32) { a[m][bj][0] = *(const f32x4*)((const float*)xin + o2); a[m][bj][1] = *(const f32x4*)((const float*)xin + o2 + 4); }
;                     else { const u32x4 w = *(const u32x4*)((const bf16_t*)xin + o2); a[m][bj][0] = __builtin_bit_cast(f32x4, w); } }
; #pragma unroll
;             for (int m = 0; m < 4; ++m) {
;                 const int row = row0 + ai * HALF + m * 16; const size_t off = (size_t)row * DM + col0; float q = 0.f;
; #pragma unroll
;                 for (int bj = 0; bj < 2; ++bj) { const size_t o2 = off + bj * HALF;
;                     f32x4 a0, a1;
;                     if constexpr (XF32) { a0 = a[m][bj][0]; a1 = a[m][bj][1]; }
;                     else { const u32x4 w = __builtin_bit_cast(u32x4, a[m][bj][0]);
;                         a0 = (f32x4){__uint_as_float(w.x << 16), __uint_as_float(w.x & 0xffff0000u), __uint_as_float(w.y << 16), __uint_as_float(w.y & 0xffff0000u)};
;                         a1 = (f32x4){__uint_as_float(w.z << 16), __uint_as_float(w.z & 0xffff0000u), __uint_as_float(w.w << 16), __uint_as_float(w.w & 0xffff0000u)}; }
;                     const f32x4 v0 = a0 + acc[ai][bj][m][0] * sc, v1 = a1 + acc[ai][bj][m][1] * sc;
;                     q += ((v0[0] * v0[0] + v0[1] * v0[1]) + (v0[2] * v0[2] + v0[3] * v0[3])) + ((v1[0] * v1[0] + v1[1] * v1[1]) + (v1[2] * v1[2] + v1[3] * v1[3]));
;                     u32x4 wo; wo.x = cvt_pk_bf16(v0[0], v0[1]); wo.y = cvt_pk_bf16(v0[2], v0[3]); wo.z = cvt_pk_bf16(v1[0], v1[1]); wo.w = cvt_pk_bf16(v1[2], v1[3]);
;                     *(u32x4*)(xb + o2) = wo;
;                     if (x8) { u32x2 w8; w8.x = pk4_fp8(v0[0], v0[1], v0[2], v0[3]); w8.y = pk4_fp8(v1[0], v1[1], v1[2], v1[3]); *(u32x2*)(x8 + o2) = w8; } }
.LBB0_1690:
	s_or_b64 exec, exec, s[28:29]
	s_waitcnt lgkmcnt(0)
	v_lshlrev_b64 v[18:19], 12, v[184:185]
	v_lshlrev_b32_e32 v20, 16, v14
	v_and_b32_e32 v21, 0xffff0000, v14
	v_lshlrev_b32_e32 v14, 16, v15
	v_and_b32_e32 v15, 0xffff0000, v15
	v_lshlrev_b32_e32 v22, 16, v16
	v_and_b32_e32 v23, 0xffff0000, v16
	v_lshlrev_b32_e32 v16, 16, v17
	v_and_b32_e32 v17, 0xffff0000, v17
	v_lshl_add_u64 v[18:19], v[18:19], 0, v[30:31]
	v_pk_fma_f32 v[14:15], v[128:129], s[18:19], v[14:15] op_sel_hi:[1,0,1]
	v_pk_fma_f32 v[20:21], v[126:127], s[18:19], v[20:21] op_sel_hi:[1,0,1]
	v_pk_fma_f32 v[16:17], v[124:125], s[18:19], v[16:17] op_sel_hi:[1,0,1]
	v_pk_fma_f32 v[22:23], v[122:123], s[18:19], v[22:23] op_sel_hi:[1,0,1]
	s_and_b64 vcc, exec, s[6:7]
	v_cvt_pk_bf16_f32 v24, v20, v21
	v_cvt_pk_bf16_f32 v25, v14, v15
	v_cvt_pk_bf16_f32 v26, v22, v23
	v_cvt_pk_bf16_f32 v27, v16, v17
	global_store_dwordx4 v[186:187], v[24:27], off
	s_cbranch_vccnz .LBB0_1692
	s_nop 0
	v_max_f32_e32 v24, v20, v20
	v_med3_f32 v25, v24, s48, v200
	v_max_f32_e32 v24, v21, v21
	v_med3_f32 v26, v24, s48, v200
	v_cvt_pk_fp8_f32 v24, v25, v26
	v_max_f32_e32 v27, v14, v14
	v_max_f32_e32 v26, v15, v15
	v_med3_f32 v25, v27, s48, v200
	v_med3_f32 v26, v26, s48, v200
	v_cvt_pk_fp8_f32 v24, v25, v26 op_sel:[0,0,1]
	v_max_f32_e32 v25, v22, v22
	v_med3_f32 v26, v25, s48, v200
	v_max_f32_e32 v25, v23, v23
	v_med3_f32 v27, v25, s48, v200
	v_cvt_pk_fp8_f32 v25, v26, v27
	v_max_f32_e32 v28, v16, v16
	v_max_f32_e32 v27, v17, v17
	v_med3_f32 v26, v28, s48, v200
	v_med3_f32 v27, v27, s48, v200
	v_cvt_pk_fp8_f32 v25, v26, v27 op_sel:[0,0,1]
	v_lshl_add_u64 v[26:27], s[70:71], 0, v[18:19]
	global_store_dwordx2 v[26:27], v[24:25], off
.LBB0_1692:
	v_or_b32_e32 v18, 0x80, v18
	v_lshlrev_b32_e32 v24, 16, v10
	v_and_b32_e32 v25, 0xffff0000, v10
	v_lshlrev_b32_e32 v10, 16, v11
	v_and_b32_e32 v11, 0xffff0000, v11
	v_lshlrev_b32_e32 v26, 16, v12
	v_and_b32_e32 v27, 0xffff0000, v12
	v_lshlrev_b32_e32 v12, 16, v13
	v_and_b32_e32 v13, 0xffff0000, v13
	v_pk_fma_f32 v[10:11], v[120:121], s[18:19], v[10:11] op_sel_hi:[1,0,1]
	v_pk_fma_f32 v[24:25], v[118:119], s[18:19], v[24:25] op_sel_hi:[1,0,1]
	v_pk_fma_f32 v[12:13], v[116:117], s[18:19], v[12:13] op_sel_hi:[1,0,1]
	v_pk_fma_f32 v[26:27], v[114:115], s[18:19], v[26:27] op_sel_hi:[1,0,1]
	v_lshl_add_u64 v[28:29], v[18:19], 1, s[66:67]
	s_and_b64 vcc, exec, s[6:7]
	v_cvt_pk_bf16_f32 v114, v24, v25
	v_cvt_pk_bf16_f32 v115, v10, v11
	v_cvt_pk_bf16_f32 v116, v26, v27
	v_cvt_pk_bf16_f32 v117, v12, v13
	global_store_dwordx4 v[28:29], v[114:117], off
	s_cbranch_vccnz .LBB0_1694
	v_max_f32_e32 v28, v24, v24
	v_med3_f32 v29, v28, s48, v200
	v_max_f32_e32 v28, v25, v25
	v_med3_f32 v114, v28, s48, v200
	v_cvt_pk_fp8_f32 v28, v29, v114
	v_max_f32_e32 v115, v10, v10
	v_max_f32_e32 v114, v11, v11
	v_med3_f32 v29, v115, s48, v200
	v_med3_f32 v114, v114, s48, v200
	v_cvt_pk_fp8_f32 v28, v29, v114 op_sel:[0,0,1]
	v_max_f32_e32 v29, v26, v26
	v_med3_f32 v114, v29, s48, v200
	v_max_f32_e32 v29, v27, v27
	v_med3_f32 v115, v29, s48, v200
	v_cvt_pk_fp8_f32 v29, v114, v115
	v_max_f32_e32 v116, v12, v12
	v_max_f32_e32 v115, v13, v13
	v_med3_f32 v114, v116, s48, v200
	v_med3_f32 v115, v115, s48, v200
	v_cvt_pk_fp8_f32 v29, v114, v115 op_sel:[0,0,1]
	v_lshl_add_u64 v[18:19], s[70:71], 0, v[18:19]
	global_store_dwordx2 v[18:19], v[28:29], off

; __device__ __forceinline__ unsigned cvt_pk_bf16(float lo, float hi) { unsigned r; asm volatile("v_cvt_pk_bf16_f32 %0, %1, %2" : "=v"(r) : "v"(lo), "v"(hi)); return r; }
;     __device__ __forceinline__ void operator()(const f32x4 (&acc)[2][2][4][2], const Unit& u, int wr, int wc, int fr, int fq) const {
;     ...
;                 for (int bj = 0; bj < 2; ++bj) { const size_t o2 = (size_t)(row0 + ai * HALF + m * 16) * DM + col0 + bj * HALF;
;                     if constexpr (XF32) { a[m][bj][0] = *(const f32x4*)((const float*)xin + o2); a[m][bj][1] = *(const f32x4*)((const float*)xin + o2 + 4); }
;                     else { const u32x4 w = *(const u32x4*)((const bf16_t*)xin + o2); a[m][bj][0] = __builtin_bit_cast(f32x4, w); } }
; #pragma unroll
;             for (int m = 0; m < 4; ++m) {
;                 const int row = row0 + ai * HALF + m * 16; const size_t off = (size_t)row * DM + col0; float q = 0.f;
; #pragma unroll
;                 for (int bj = 0; bj < 2; ++bj) { const size_t o2 = off + bj * HALF;
;                     f32x4 a0, a1;
;                     if constexpr (XF32) { a0 = a[m][bj][0]; a1 = a[m][bj][1]; }
;                     else { const u32x4 w = __builtin_bit_cast(u32x4, a[m][bj][0]);
;                         a0 = (f32x4){__uint_as_float(w.x << 16), __uint_as_float(w.x & 0xffff0000u), __uint_as_float(w.y << 16), __uint_as_float(w.y & 0xffff0000u)};
;                         a1 = (f32x4){__uint_as_float(w.z << 16), __uint_as_float(w.z & 0xffff0000u), __uint_as_float(w.w << 16), __uint_as_float(w.w & 0xffff0000u)}; }
;                     const f32x4 v0 = a0 + acc[ai][bj][m][0] * sc, v1 = a1 + acc[ai][bj][m][1] * sc;
;                     q += ((v0[0] * v0[0] + v0[1] * v0[1]) + (v0[2] * v0[2] + v0[3] * v0[3])) + ((v1[0] * v1[0] + v1[1] * v1[1]) + (v1[2] * v1[2] + v1[3] * v1[3]));
;                     u32x4 wo; wo.x = cvt_pk_bf16(v0[0], v0[1]); wo.y = cvt_pk_bf16(v0[2], v0[3]); wo.z = cvt_pk_bf16(v1[0], v1[1]); wo.w = cvt_pk_bf16(v1[2], v1[3]);
;                     *(u32x4*)(xb + o2) = wo;
;                     if (x8) { u32x2 w8; w8.x = pk4_fp8(v0[0], v0[1], v0[2], v0[3]); w8.y = pk4_fp8(v1[0], v1[1], v1[2], v1[3]); *(u32x2*)(x8 + o2) = w8; } }
.LBB0_1696:
	s_or_b64 exec, exec, s[28:29]
	s_waitcnt lgkmcnt(0)
	v_lshlrev_b64 v[10:11], 12, v[180:181]
	v_lshlrev_b32_e32 v12, 16, v6
	v_and_b32_e32 v13, 0xffff0000, v6
	v_lshlrev_b32_e32 v6, 16, v7
	v_and_b32_e32 v7, 0xffff0000, v7
	v_lshlrev_b32_e32 v14, 16, v8
	v_and_b32_e32 v15, 0xffff0000, v8
	v_lshlrev_b32_e32 v8, 16, v9
	v_and_b32_e32 v9, 0xffff0000, v9
	v_lshl_add_u64 v[10:11], v[10:11], 0, v[30:31]
	v_pk_fma_f32 v[6:7], v[112:113], s[18:19], v[6:7] op_sel_hi:[1,0,1]
	v_pk_fma_f32 v[12:13], v[110:111], s[18:19], v[12:13] op_sel_hi:[1,0,1]
	v_pk_fma_f32 v[8:9], v[108:109], s[18:19], v[8:9] op_sel_hi:[1,0,1]
	v_pk_fma_f32 v[14:15], v[106:107], s[18:19], v[14:15] op_sel_hi:[1,0,1]
	s_and_b64 vcc, exec, s[6:7]
	v_cvt_pk_bf16_f32 v16, v12, v13
	v_cvt_pk_bf16_f32 v17, v6, v7
	v_cvt_pk_bf16_f32 v18, v14, v15
	v_cvt_pk_bf16_f32 v19, v8, v9
	global_store_dwordx4 v[182:183], v[16:19], off
	s_cbranch_vccnz .LBB0_1698
	s_nop 0
	v_max_f32_e32 v16, v12, v12
	v_med3_f32 v17, v16, s48, v200
	v_max_f32_e32 v16, v13, v13
	v_med3_f32 v18, v16, s48, v200
	v_cvt_pk_fp8_f32 v16, v17, v18
	v_max_f32_e32 v19, v6, v6
	v_max_f32_e32 v18, v7, v7
	v_med3_f32 v17, v19, s48, v200
	v_med3_f32 v18, v18, s48, v200
	v_cvt_pk_fp8_f32 v16, v17, v18 op_sel:[0,0,1]
	v_max_f32_e32 v17, v14, v14
	v_med3_f32 v18, v17, s48, v200
	v_max_f32_e32 v17, v15, v15
	v_med3_f32 v19, v17, s48, v200
	v_cvt_pk_fp8_f32 v17, v18, v19
	v_max_f32_e32 v20, v8, v8
	v_max_f32_e32 v19, v9, v9
	v_med3_f32 v18, v20, s48, v200
	v_med3_f32 v19, v19, s48, v200
	v_cvt_pk_fp8_f32 v17, v18, v19 op_sel:[0,0,1]
	v_lshl_add_u64 v[18:19], s[70:71], 0, v[10:11]
	global_store_dwordx2 v[18:19], v[16:17], off
.LBB0_1698:
	v_or_b32_e32 v10, 0x80, v10
	v_lshlrev_b32_e32 v16, 16, v2
	v_and_b32_e32 v17, 0xffff0000, v2
	v_lshlrev_b32_e32 v2, 16, v3
	v_and_b32_e32 v3, 0xffff0000, v3
	v_lshlrev_b32_e32 v18, 16, v4
	v_and_b32_e32 v19, 0xffff0000, v4
	v_lshlrev_b32_e32 v4, 16, v5
	v_and_b32_e32 v5, 0xffff0000, v5
	v_pk_fma_f32 v[2:3], v[104:105], s[18:19], v[2:3] op_sel_hi:[1,0,1]
	v_pk_fma_f32 v[16:17], v[102:103], s[18:19], v[16:17] op_sel_hi:[1,0,1]
	v_pk_fma_f32 v[4:5], v[100:101], s[18:19], v[4:5] op_sel_hi:[1,0,1]
	v_pk_fma_f32 v[18:19], v[98:99], s[18:19], v[18:19] op_sel_hi:[1,0,1]
	v_lshl_add_u64 v[24:25], v[10:11], 1, s[66:67]
	s_and_b64 vcc, exec, s[6:7]
	v_cvt_pk_bf16_f32 v20, v16, v17
	v_cvt_pk_bf16_f32 v21, v2, v3
	v_cvt_pk_bf16_f32 v22, v18, v19
	v_cvt_pk_bf16_f32 v23, v4, v5
	global_store_dwordx4 v[24:25], v[20:23], off
	s_cbranch_vccnz .LBB0_1700
	s_nop 0
	v_max_f32_e32 v20, v16, v16
	v_med3_f32 v21, v20, s48, v200
	v_max_f32_e32 v20, v17, v17
	v_med3_f32 v22, v20, s48, v200
	v_cvt_pk_fp8_f32 v20, v21, v22
	v_max_f32_e32 v23, v2, v2
	v_max_f32_e32 v22, v3, v3
	v_med3_f32 v21, v23, s48, v200
	v_med3_f32 v22, v22, s48, v200
	v_cvt_pk_fp8_f32 v20, v21, v22 op_sel:[0,0,1]
	v_max_f32_e32 v21, v18, v18
	v_med3_f32 v22, v21, s48, v200
	v_max_f32_e32 v21, v19, v19
	v_med3_f32 v23, v21, s48, v200
	v_cvt_pk_fp8_f32 v21, v22, v23
	v_max_f32_e32 v24, v4, v4
	v_max_f32_e32 v23, v5, v5
	v_med3_f32 v22, v24, s48, v200
	v_med3_f32 v23, v23, s48, v200
	v_cvt_pk_fp8_f32 v21, v22, v23 op_sel:[0,0,1]
	v_lshl_add_u64 v[10:11], s[70:71], 0, v[10:11]
	global_store_dwordx2 v[10:11], v[20:21], off

; __device__ __forceinline__ unsigned cvt_pk_bf16(float lo, float hi) { unsigned r; asm volatile("v_cvt_pk_bf16_f32 %0, %1, %2" : "=v"(r) : "v"(lo), "v"(hi)); return r; }
;     __device__ __forceinline__ void operator()(const f32x4 (&acc)[2][2][4][2], const Unit& u, int wr, int wc, int fr, int fq) const {
;     ...
;                 for (int bj = 0; bj < 2; ++bj) { const size_t o2 = (size_t)(row0 + ai * HALF + m * 16) * DM + col0 + bj * HALF;
;                     if constexpr (XF32) { a[m][bj][0] = *(const f32x4*)((const float*)xin + o2); a[m][bj][1] = *(const f32x4*)((const float*)xin + o2 + 4); }
;                     else { const u32x4 w = *(const u32x4*)((const bf16_t*)xin + o2); a[m][bj][0] = __builtin_bit_cast(f32x4, w); } }
; #pragma unroll
;             for (int m = 0; m < 4; ++m) {
;                 const int row = row0 + ai * HALF + m * 16; const size_t off = (size_t)row * DM + col0; float q = 0.f;
; #pragma unroll
;                 for (int bj = 0; bj < 2; ++bj) { const size_t o2 = off + bj * HALF;
;                     f32x4 a0, a1;
;                     if constexpr (XF32) { a0 = a[m][bj][0]; a1 = a[m][bj][1]; }
;                     else { const u32x4 w = __builtin_bit_cast(u32x4, a[m][bj][0]);
;                         a0 = (f32x4){__uint_as_float(w.x << 16), __uint_as_float(w.x & 0xffff0000u), __uint_as_float(w.y << 16), __uint_as_float(w.y & 0xffff0000u)};
;                         a1 = (f32x4){__uint_as_float(w.z << 16), __uint_as_float(w.z & 0xffff0000u), __uint_as_float(w.w << 16), __uint_as_float(w.w & 0xffff0000u)}; }
;                     const f32x4 v0 = a0 + acc[ai][bj][m][0] * sc, v1 = a1 + acc[ai][bj][m][1] * sc;
;                     q += ((v0[0] * v0[0] + v0[1] * v0[1]) + (v0[2] * v0[2] + v0[3] * v0[3])) + ((v1[0] * v1[0] + v1[1] * v1[1]) + (v1[2] * v1[2] + v1[3] * v1[3]));
;                     u32x4 wo; wo.x = cvt_pk_bf16(v0[0], v0[1]); wo.y = cvt_pk_bf16(v0[2], v0[3]); wo.z = cvt_pk_bf16(v1[0], v1[1]); wo.w = cvt_pk_bf16(v1[2], v1[3]);
;                     *(u32x4*)(xb + o2) = wo;
;                     if (x8) { u32x2 w8; w8.x = pk4_fp8(v0[0], v0[1], v0[2], v0[3]); w8.y = pk4_fp8(v1[0], v1[1], v1[2], v1[3]); *(u32x2*)(x8 + o2) = w8; } }
.LBB0_1702:
	s_or_b64 exec, exec, s[28:29]
	v_add_u32_e32 v108, 0x80, v178
	v_ashrrev_i32_e32 v109, 31, v108
	v_add_u32_e32 v104, 0x90, v178
	s_waitcnt lgkmcnt(0)
	v_lshlrev_b64 v[2:3], 13, v[108:109]
	v_ashrrev_i32_e32 v105, 31, v104
	v_add_u32_e32 v100, 0xa0, v178
	v_lshl_add_u64 v[116:117], v[32:33], 0, v[2:3]
	v_lshlrev_b64 v[2:3], 13, v[104:105]
	v_ashrrev_i32_e32 v101, 31, v100
	v_add_u32_e32 v98, 0xb0, v178
	v_lshl_add_u64 v[106:107], v[32:33], 0, v[2:3]
	v_lshlrev_b64 v[2:3], 13, v[100:101]
	v_ashrrev_i32_e32 v99, 31, v98
	v_lshl_add_u64 v[102:103], v[32:33], 0, v[2:3]
	v_lshlrev_b64 v[2:3], 13, v[98:99]
	global_load_dwordx4 v[112:115], v[116:117], off
	global_load_dwordx4 v[26:29], v[116:117], off offset:256
	v_lshl_add_u64 v[32:33], v[32:33], 0, v[2:3]
	global_load_dwordx4 v[22:25], v[106:107], off
	global_load_dwordx4 v[18:21], v[106:107], off offset:256
	global_load_dwordx4 v[14:17], v[102:103], off
	global_load_dwordx4 v[10:13], v[102:103], off offset:256
	global_load_dwordx4 v[6:9], v[32:33], off
	global_load_dwordx4 v[2:5], v[32:33], off offset:256
	v_lshlrev_b64 v[110:111], 12, v[108:109]
	v_lshl_add_u64 v[110:111], v[110:111], 0, v[30:31]
	s_and_b64 vcc, exec, s[6:7]
	s_waitcnt vmcnt(7)
	v_lshlrev_b32_e32 v118, 16, v112
	v_and_b32_e32 v119, 0xffff0000, v112
	v_lshlrev_b32_e32 v112, 16, v113
	v_and_b32_e32 v113, 0xffff0000, v113
	v_lshlrev_b32_e32 v120, 16, v114
	v_and_b32_e32 v121, 0xffff0000, v114
	v_lshlrev_b32_e32 v114, 16, v115
	v_and_b32_e32 v115, 0xffff0000, v115
	v_pk_fma_f32 v[96:97], v[96:97], s[18:19], v[112:113] op_sel_hi:[1,0,1]
	v_pk_fma_f32 v[94:95], v[94:95], s[18:19], v[118:119] op_sel_hi:[1,0,1]
	v_pk_fma_f32 v[92:93], v[92:93], s[18:19], v[114:115] op_sel_hi:[1,0,1]
	v_pk_fma_f32 v[90:91], v[90:91], s[18:19], v[120:121] op_sel_hi:[1,0,1]
	v_cvt_pk_bf16_f32 v112, v94, v95
	v_cvt_pk_bf16_f32 v113, v96, v97
	s_nop 0
	v_cvt_pk_bf16_f32 v114, v90, v91
	v_cvt_pk_bf16_f32 v115, v92, v93
	global_store_dwordx4 v[116:117], v[112:115], off
	s_cbranch_vccnz .LBB0_1704
	s_nop 0
	v_max_f32_e32 v112, v94, v94
	v_med3_f32 v113, v112, s48, v200
	v_max_f32_e32 v112, v95, v95
	v_med3_f32 v114, v112, s48, v200
	v_cvt_pk_fp8_f32 v112, v113, v114
	v_max_f32_e32 v115, v96, v96
	v_max_f32_e32 v114, v97, v97
	v_med3_f32 v113, v115, s48, v200
	v_med3_f32 v114, v114, s48, v200
	v_cvt_pk_fp8_f32 v112, v113, v114 op_sel:[0,0,1]
	v_max_f32_e32 v113, v90, v90
	v_med3_f32 v114, v113, s48, v200
	v_max_f32_e32 v113, v91, v91
	v_med3_f32 v115, v113, s48, v200
	v_cvt_pk_fp8_f32 v113, v114, v115
	v_max_f32_e32 v116, v92, v92
	v_max_f32_e32 v115, v93, v93
	v_med3_f32 v114, v116, s48, v200
	v_med3_f32 v115, v115, s48, v200
	v_cvt_pk_fp8_f32 v113, v114, v115 op_sel:[0,0,1]
	v_lshl_add_u64 v[114:115], s[70:71], 0, v[110:111]
	global_store_dwordx2 v[114:115], v[112:113], off
.LBB0_1704:
	v_or_b32_e32 v110, 0x80, v110
	s_waitcnt vmcnt(7)
	v_lshlrev_b32_e32 v112, 16, v26
	v_and_b32_e32 v113, 0xffff0000, v26
	v_lshlrev_b32_e32 v26, 16, v27
	v_and_b32_e32 v27, 0xffff0000, v27
	v_lshlrev_b32_e32 v114, 16, v28
	v_and_b32_e32 v115, 0xffff0000, v28
	v_lshlrev_b32_e32 v28, 16, v29
	v_and_b32_e32 v29, 0xffff0000, v29
	v_pk_fma_f32 v[26:27], v[88:89], s[18:19], v[26:27] op_sel_hi:[1,0,1]
	v_pk_fma_f32 v[86:87], v[86:87], s[18:19], v[112:113] op_sel_hi:[1,0,1]
	v_pk_fma_f32 v[28:29], v[84:85], s[18:19], v[28:29] op_sel_hi:[1,0,1]
	v_pk_fma_f32 v[82:83], v[82:83], s[18:19], v[114:115] op_sel_hi:[1,0,1]
	v_lshl_add_u64 v[84:85], v[110:111], 1, s[66:67]
	s_and_b64 vcc, exec, s[6:7]
	v_cvt_pk_bf16_f32 v112, v86, v87
	v_cvt_pk_bf16_f32 v113, v26, v27
	v_cvt_pk_bf16_f32 v114, v82, v83
	v_cvt_pk_bf16_f32 v115, v28, v29
	global_store_dwordx4 v[84:85], v[112:115], off
	s_cbranch_vccnz .LBB0_1706
	v_max_f32_e32 v84, v86, v86
	v_med3_f32 v85, v84, s48, v200
	v_max_f32_e32 v84, v87, v87
	v_med3_f32 v88, v84, s48, v200
	v_cvt_pk_fp8_f32 v84, v85, v88
	v_max_f32_e32 v89, v26, v26
	v_max_f32_e32 v88, v27, v27
	v_med3_f32 v85, v89, s48, v200
	v_med3_f32 v88, v88, s48, v200
	v_cvt_pk_fp8_f32 v84, v85, v88 op_sel:[0,0,1]
	v_max_f32_e32 v85, v82, v82
	v_med3_f32 v88, v85, s48, v200
	v_max_f32_e32 v85, v83, v83
	v_med3_f32 v89, v85, s48, v200
	v_cvt_pk_fp8_f32 v85, v88, v89
	v_max_f32_e32 v112, v28, v28
	v_max_f32_e32 v89, v29, v29
	v_med3_f32 v88, v112, s48, v200
	v_med3_f32 v89, v89, s48, v200
	v_cvt_pk_fp8_f32 v85, v88, v89 op_sel:[0,0,1]
	v_lshl_add_u64 v[88:89], s[70:71], 0, v[110:111]
	global_store_dwordx2 v[88:89], v[84:85], off

; __device__ __forceinline__ unsigned cvt_pk_bf16(float lo, float hi) { unsigned r; asm volatile("v_cvt_pk_bf16_f32 %0, %1, %2" : "=v"(r) : "v"(lo), "v"(hi)); return r; }
;     __device__ __forceinline__ void operator()(const f32x4 (&acc)[2][2][4][2], const Unit& u, int wr, int wc, int fr, int fq) const {
;     ...
;                 for (int bj = 0; bj < 2; ++bj) { const size_t o2 = (size_t)(row0 + ai * HALF + m * 16) * DM + col0 + bj * HALF;
;                     if constexpr (XF32) { a[m][bj][0] = *(const f32x4*)((const float*)xin + o2); a[m][bj][1] = *(const f32x4*)((const float*)xin + o2 + 4); }
;                     else { const u32x4 w = *(const u32x4*)((const bf16_t*)xin + o2); a[m][bj][0] = __builtin_bit_cast(f32x4, w); } }
; #pragma unroll
;             for (int m = 0; m < 4; ++m) {
;                 const int row = row0 + ai * HALF + m * 16; const size_t off = (size_t)row * DM + col0; float q = 0.f;
; #pragma unroll
;                 for (int bj = 0; bj < 2; ++bj) { const size_t o2 = off + bj * HALF;
;                     f32x4 a0, a1;
;                     if constexpr (XF32) { a0 = a[m][bj][0]; a1 = a[m][bj][1]; }
;                     else { const u32x4 w = __builtin_bit_cast(u32x4, a[m][bj][0]);
;                         a0 = (f32x4){__uint_as_float(w.x << 16), __uint_as_float(w.x & 0xffff0000u), __uint_as_float(w.y << 16), __uint_as_float(w.y & 0xffff0000u)};
;                         a1 = (f32x4){__uint_as_float(w.z << 16), __uint_as_float(w.z & 0xffff0000u), __uint_as_float(w.w << 16), __uint_as_float(w.w & 0xffff0000u)}; }
;                     const f32x4 v0 = a0 + acc[ai][bj][m][0] * sc, v1 = a1 + acc[ai][bj][m][1] * sc;
;                     q += ((v0[0] * v0[0] + v0[1] * v0[1]) + (v0[2] * v0[2] + v0[3] * v0[3])) + ((v1[0] * v1[0] + v1[1] * v1[1]) + (v1[2] * v1[2] + v1[3] * v1[3]));
;                     u32x4 wo; wo.x = cvt_pk_bf16(v0[0], v0[1]); wo.y = cvt_pk_bf16(v0[2], v0[3]); wo.z = cvt_pk_bf16(v1[0], v1[1]); wo.w = cvt_pk_bf16(v1[2], v1[3]);
;                     *(u32x4*)(xb + o2) = wo;
;                     if (x8) { u32x2 w8; w8.x = pk4_fp8(v0[0], v0[1], v0[2], v0[3]); w8.y = pk4_fp8(v1[0], v1[1], v1[2], v1[3]); *(u32x2*)(x8 + o2) = w8; } }
.LBB0_1708:
	s_or_b64 exec, exec, s[28:29]
	s_waitcnt lgkmcnt(0)
	v_lshlrev_b64 v[26:27], 12, v[104:105]
	s_waitcnt vmcnt(7)
	v_lshlrev_b32_e32 v28, 16, v22
	v_and_b32_e32 v29, 0xffff0000, v22
	v_lshlrev_b32_e32 v22, 16, v23
	v_and_b32_e32 v23, 0xffff0000, v23
	v_lshlrev_b32_e32 v82, 16, v24
	v_and_b32_e32 v83, 0xffff0000, v24
	v_lshlrev_b32_e32 v24, 16, v25
	v_and_b32_e32 v25, 0xffff0000, v25
	v_lshl_add_u64 v[26:27], v[26:27], 0, v[30:31]
	v_pk_fma_f32 v[22:23], v[80:81], s[18:19], v[22:23] op_sel_hi:[1,0,1]
	v_pk_fma_f32 v[28:29], v[78:79], s[18:19], v[28:29] op_sel_hi:[1,0,1]
	v_pk_fma_f32 v[24:25], v[76:77], s[18:19], v[24:25] op_sel_hi:[1,0,1]
	v_pk_fma_f32 v[74:75], v[74:75], s[18:19], v[82:83] op_sel_hi:[1,0,1]
	s_and_b64 vcc, exec, s[6:7]
	v_cvt_pk_bf16_f32 v76, v28, v29
	v_cvt_pk_bf16_f32 v77, v22, v23
	v_cvt_pk_bf16_f32 v78, v74, v75
	v_cvt_pk_bf16_f32 v79, v24, v25
	global_store_dwordx4 v[106:107], v[76:79], off
	s_cbranch_vccnz .LBB0_1710
	s_nop 0
	v_max_f32_e32 v76, v28, v28
	v_med3_f32 v77, v76, s48, v200
	v_max_f32_e32 v76, v29, v29
	v_med3_f32 v78, v76, s48, v200
	v_cvt_pk_fp8_f32 v76, v77, v78
	v_max_f32_e32 v79, v22, v22
	v_max_f32_e32 v78, v23, v23
	v_med3_f32 v77, v79, s48, v200
	v_med3_f32 v78, v78, s48, v200
	v_cvt_pk_fp8_f32 v76, v77, v78 op_sel:[0,0,1]
	v_max_f32_e32 v77, v74, v74
	v_med3_f32 v78, v77, s48, v200
	v_max_f32_e32 v77, v75, v75
	v_med3_f32 v79, v77, s48, v200
	v_cvt_pk_fp8_f32 v77, v78, v79
	v_max_f32_e32 v80, v24, v24
	v_max_f32_e32 v79, v25, v25
	v_med3_f32 v78, v80, s48, v200
	v_med3_f32 v79, v79, s48, v200
	v_cvt_pk_fp8_f32 v77, v78, v79 op_sel:[0,0,1]
	v_lshl_add_u64 v[78:79], s[70:71], 0, v[26:27]
	global_store_dwordx2 v[78:79], v[76:77], off
.LBB0_1710:
	v_or_b32_e32 v26, 0x80, v26
	s_waitcnt vmcnt(7)
	v_lshlrev_b32_e32 v76, 16, v18
	v_and_b32_e32 v77, 0xffff0000, v18
	v_lshlrev_b32_e32 v18, 16, v19
	v_and_b32_e32 v19, 0xffff0000, v19
	v_lshlrev_b32_e32 v78, 16, v20
	v_and_b32_e32 v79, 0xffff0000, v20
	v_lshlrev_b32_e32 v20, 16, v21
	v_and_b32_e32 v21, 0xffff0000, v21
	v_pk_fma_f32 v[18:19], v[72:73], s[18:19], v[18:19] op_sel_hi:[1,0,1]
	v_pk_fma_f32 v[70:71], v[70:71], s[18:19], v[76:77] op_sel_hi:[1,0,1]
	v_pk_fma_f32 v[20:21], v[68:69], s[18:19], v[20:21] op_sel_hi:[1,0,1]
	v_pk_fma_f32 v[66:67], v[66:67], s[18:19], v[78:79] op_sel_hi:[1,0,1]
	v_lshl_add_u64 v[68:69], v[26:27], 1, s[66:67]
	s_and_b64 vcc, exec, s[6:7]
	v_cvt_pk_bf16_f32 v76, v70, v71
	v_cvt_pk_bf16_f32 v77, v18, v19
	v_cvt_pk_bf16_f32 v78, v66, v67
	v_cvt_pk_bf16_f32 v79, v20, v21
	global_store_dwordx4 v[68:69], v[76:79], off
	s_cbranch_vccnz .LBB0_1712
	v_max_f32_e32 v68, v70, v70
	v_med3_f32 v69, v68, s48, v200
	v_max_f32_e32 v68, v71, v71
	v_med3_f32 v72, v68, s48, v200
	v_cvt_pk_fp8_f32 v68, v69, v72
	v_max_f32_e32 v73, v18, v18
	v_max_f32_e32 v72, v19, v19
	v_med3_f32 v69, v73, s48, v200
	v_med3_f32 v72, v72, s48, v200
	v_cvt_pk_fp8_f32 v68, v69, v72 op_sel:[0,0,1]
	v_max_f32_e32 v69, v66, v66
	v_med3_f32 v72, v69, s48, v200
	v_max_f32_e32 v69, v67, v67
	v_med3_f32 v73, v69, s48, v200
	v_cvt_pk_fp8_f32 v69, v72, v73
	v_max_f32_e32 v76, v20, v20
	v_max_f32_e32 v73, v21, v21
	v_med3_f32 v72, v76, s48, v200
	v_med3_f32 v73, v73, s48, v200
	v_cvt_pk_fp8_f32 v69, v72, v73 op_sel:[0,0,1]
	v_lshl_add_u64 v[26:27], s[70:71], 0, v[26:27]
	global_store_dwordx2 v[26:27], v[68:69], off

; __device__ __forceinline__ unsigned cvt_pk_bf16(float lo, float hi) { unsigned r; asm volatile("v_cvt_pk_bf16_f32 %0, %1, %2" : "=v"(r) : "v"(lo), "v"(hi)); return r; }
;     __device__ __forceinline__ void operator()(const f32x4 (&acc)[2][2][4][2], const Unit& u, int wr, int wc, int fr, int fq) const {
;     ...
;                 for (int bj = 0; bj < 2; ++bj) { const size_t o2 = (size_t)(row0 + ai * HALF + m * 16) * DM + col0 + bj * HALF;
;                     if constexpr (XF32) { a[m][bj][0] = *(const f32x4*)((const float*)xin + o2); a[m][bj][1] = *(const f32x4*)((const float*)xin + o2 + 4); }
;                     else { const u32x4 w = *(const u32x4*)((const bf16_t*)xin + o2); a[m][bj][0] = __builtin_bit_cast(f32x4, w); } }
; #pragma unroll
;             for (int m = 0; m < 4; ++m) {
;                 const int row = row0 + ai * HALF + m * 16; const size_t off = (size_t)row * DM + col0; float q = 0.f;
; #pragma unroll
;                 for (int bj = 0; bj < 2; ++bj) { const size_t o2 = off + bj * HALF;
;                     f32x4 a0, a1;
;                     if constexpr (XF32) { a0 = a[m][bj][0]; a1 = a[m][bj][1]; }
;                     else { const u32x4 w = __builtin_bit_cast(u32x4, a[m][bj][0]);
;                         a0 = (f32x4){__uint_as_float(w.x << 16), __uint_as_float(w.x & 0xffff0000u), __uint_as_float(w.y << 16), __uint_as_float(w.y & 0xffff0000u)};
;                         a1 = (f32x4){__uint_as_float(w.z << 16), __uint_as_float(w.z & 0xffff0000u), __uint_as_float(w.w << 16), __uint_as_float(w.w & 0xffff0000u)}; }
;                     const f32x4 v0 = a0 + acc[ai][bj][m][0] * sc, v1 = a1 + acc[ai][bj][m][1] * sc;
;                     q += ((v0[0] * v0[0] + v0[1] * v0[1]) + (v0[2] * v0[2] + v0[3] * v0[3])) + ((v1[0] * v1[0] + v1[1] * v1[1]) + (v1[2] * v1[2] + v1[3] * v1[3]));
;                     u32x4 wo; wo.x = cvt_pk_bf16(v0[0], v0[1]); wo.y = cvt_pk_bf16(v0[2], v0[3]); wo.z = cvt_pk_bf16(v1[0], v1[1]); wo.w = cvt_pk_bf16(v1[2], v1[3]);
;                     *(u32x4*)(xb + o2) = wo;
;                     if (x8) { u32x2 w8; w8.x = pk4_fp8(v0[0], v0[1], v0[2], v0[3]); w8.y = pk4_fp8(v1[0], v1[1], v1[2], v1[3]); *(u32x2*)(x8 + o2) = w8; } }
.LBB0_1714:
	s_or_b64 exec, exec, s[28:29]
	s_waitcnt lgkmcnt(0)
	v_lshlrev_b64 v[18:19], 12, v[100:101]
	s_waitcnt vmcnt(7)
	v_lshlrev_b32_e32 v20, 16, v14
	v_and_b32_e32 v21, 0xffff0000, v14
	v_lshlrev_b32_e32 v14, 16, v15
	v_and_b32_e32 v15, 0xffff0000, v15
	v_lshlrev_b32_e32 v22, 16, v16
	v_and_b32_e32 v23, 0xffff0000, v16
	v_lshlrev_b32_e32 v16, 16, v17
	v_and_b32_e32 v17, 0xffff0000, v17
	v_lshl_add_u64 v[18:19], v[18:19], 0, v[30:31]
	v_pk_fma_f32 v[14:15], v[64:65], s[18:19], v[14:15] op_sel_hi:[1,0,1]
	v_pk_fma_f32 v[20:21], v[62:63], s[18:19], v[20:21] op_sel_hi:[1,0,1]
	v_pk_fma_f32 v[16:17], v[60:61], s[18:19], v[16:17] op_sel_hi:[1,0,1]
	v_pk_fma_f32 v[22:23], v[58:59], s[18:19], v[22:23] op_sel_hi:[1,0,1]
	s_and_b64 vcc, exec, s[6:7]
	v_cvt_pk_bf16_f32 v24, v20, v21
	v_cvt_pk_bf16_f32 v25, v14, v15
	v_cvt_pk_bf16_f32 v26, v22, v23
	v_cvt_pk_bf16_f32 v27, v16, v17
	global_store_dwordx4 v[102:103], v[24:27], off
	s_cbranch_vccnz .LBB0_1716
	s_nop 0
	v_max_f32_e32 v24, v20, v20
	v_med3_f32 v25, v24, s48, v200
	v_max_f32_e32 v24, v21, v21
	v_med3_f32 v26, v24, s48, v200
	v_cvt_pk_fp8_f32 v24, v25, v26
	v_max_f32_e32 v27, v14, v14
	v_max_f32_e32 v26, v15, v15
	v_med3_f32 v25, v27, s48, v200
	v_med3_f32 v26, v26, s48, v200
	v_cvt_pk_fp8_f32 v24, v25, v26 op_sel:[0,0,1]
	v_max_f32_e32 v25, v22, v22
	v_med3_f32 v26, v25, s48, v200
	v_max_f32_e32 v25, v23, v23
	v_med3_f32 v27, v25, s48, v200
	v_cvt_pk_fp8_f32 v25, v26, v27
	v_max_f32_e32 v28, v16, v16
	v_max_f32_e32 v27, v17, v17
	v_med3_f32 v26, v28, s48, v200
	v_med3_f32 v27, v27, s48, v200
	v_cvt_pk_fp8_f32 v25, v26, v27 op_sel:[0,0,1]
	v_lshl_add_u64 v[26:27], s[70:71], 0, v[18:19]
	global_store_dwordx2 v[26:27], v[24:25], off
.LBB0_1716:
	v_or_b32_e32 v18, 0x80, v18
	s_waitcnt vmcnt(7)
	v_lshlrev_b32_e32 v24, 16, v10
	v_and_b32_e32 v25, 0xffff0000, v10
	v_lshlrev_b32_e32 v10, 16, v11
	v_and_b32_e32 v11, 0xffff0000, v11
	v_lshlrev_b32_e32 v26, 16, v12
	v_and_b32_e32 v27, 0xffff0000, v12
	v_lshlrev_b32_e32 v12, 16, v13
	v_and_b32_e32 v13, 0xffff0000, v13
	v_pk_fma_f32 v[10:11], v[56:57], s[18:19], v[10:11] op_sel_hi:[1,0,1]
	v_pk_fma_f32 v[24:25], v[54:55], s[18:19], v[24:25] op_sel_hi:[1,0,1]
	v_pk_fma_f32 v[12:13], v[52:53], s[18:19], v[12:13] op_sel_hi:[1,0,1]
	v_pk_fma_f32 v[26:27], v[50:51], s[18:19], v[26:27] op_sel_hi:[1,0,1]
	v_lshl_add_u64 v[28:29], v[18:19], 1, s[66:67]
	s_and_b64 vcc, exec, s[6:7]
	v_cvt_pk_bf16_f32 v50, v24, v25
	v_cvt_pk_bf16_f32 v51, v10, v11
	v_cvt_pk_bf16_f32 v52, v26, v27
	v_cvt_pk_bf16_f32 v53, v12, v13
	global_store_dwordx4 v[28:29], v[50:53], off
	s_cbranch_vccnz .LBB0_1718
	v_max_f32_e32 v28, v24, v24
	v_med3_f32 v29, v28, s48, v200
	v_max_f32_e32 v28, v25, v25
	v_med3_f32 v50, v28, s48, v200
	v_cvt_pk_fp8_f32 v28, v29, v50
	v_max_f32_e32 v51, v10, v10
	v_max_f32_e32 v50, v11, v11
	v_med3_f32 v29, v51, s48, v200
	v_med3_f32 v50, v50, s48, v200
	v_cvt_pk_fp8_f32 v28, v29, v50 op_sel:[0,0,1]
	v_max_f32_e32 v29, v26, v26
	v_med3_f32 v50, v29, s48, v200
	v_max_f32_e32 v29, v27, v27
	v_med3_f32 v51, v29, s48, v200
	v_cvt_pk_fp8_f32 v29, v50, v51
	v_max_f32_e32 v52, v12, v12
	v_max_f32_e32 v51, v13, v13
	v_med3_f32 v50, v52, s48, v200
	v_med3_f32 v51, v51, s48, v200
	v_cvt_pk_fp8_f32 v29, v50, v51 op_sel:[0,0,1]
	v_lshl_add_u64 v[18:19], s[70:71], 0, v[18:19]
	global_store_dwordx2 v[18:19], v[28:29], off

; __device__ __forceinline__ unsigned cvt_pk_bf16(float lo, float hi) { unsigned r; asm volatile("v_cvt_pk_bf16_f32 %0, %1, %2" : "=v"(r) : "v"(lo), "v"(hi)); return r; }
;     __device__ __forceinline__ void operator()(const f32x4 (&acc)[2][2][4][2], const Unit& u, int wr, int wc, int fr, int fq) const {
;     ...
;                 for (int bj = 0; bj < 2; ++bj) { const size_t o2 = (size_t)(row0 + ai * HALF + m * 16) * DM + col0 + bj * HALF;
;                     if constexpr (XF32) { a[m][bj][0] = *(const f32x4*)((const float*)xin + o2); a[m][bj][1] = *(const f32x4*)((const float*)xin + o2 + 4); }
;                     else { const u32x4 w = *(const u32x4*)((const bf16_t*)xin + o2); a[m][bj][0] = __builtin_bit_cast(f32x4, w); } }
; #pragma unroll
;             for (int m = 0; m < 4; ++m) {
;                 const int row = row0 + ai * HALF + m * 16; const size_t off = (size_t)row * DM + col0; float q = 0.f;
; #pragma unroll
;                 for (int bj = 0; bj < 2; ++bj) { const size_t o2 = off + bj * HALF;
;                     f32x4 a0, a1;
;                     if constexpr (XF32) { a0 = a[m][bj][0]; a1 = a[m][bj][1]; }
;                     else { const u32x4 w = __builtin_bit_cast(u32x4, a[m][bj][0]);
;                         a0 = (f32x4){__uint_as_float(w.x << 16), __uint_as_float(w.x & 0xffff0000u), __uint_as_float(w.y << 16), __uint_as_float(w.y & 0xffff0000u)};
;                         a1 = (f32x4){__uint_as_float(w.z << 16), __uint_as_float(w.z & 0xffff0000u), __uint_as_float(w.w << 16), __uint_as_float(w.w & 0xffff0000u)}; }
;                     const f32x4 v0 = a0 + acc[ai][bj][m][0] * sc, v1 = a1 + acc[ai][bj][m][1] * sc;
;                     q += ((v0[0] * v0[0] + v0[1] * v0[1]) + (v0[2] * v0[2] + v0[3] * v0[3])) + ((v1[0] * v1[0] + v1[1] * v1[1]) + (v1[2] * v1[2] + v1[3] * v1[3]));
;                     u32x4 wo; wo.x = cvt_pk_bf16(v0[0], v0[1]); wo.y = cvt_pk_bf16(v0[2], v0[3]); wo.z = cvt_pk_bf16(v1[0], v1[1]); wo.w = cvt_pk_bf16(v1[2], v1[3]);
;                     *(u32x4*)(xb + o2) = wo;
;                     if (x8) { u32x2 w8; w8.x = pk4_fp8(v0[0], v0[1], v0[2], v0[3]); w8.y = pk4_fp8(v1[0], v1[1], v1[2], v1[3]); *(u32x2*)(x8 + o2) = w8; } }
.LBB0_1720:
	s_or_b64 exec, exec, s[28:29]
	s_waitcnt lgkmcnt(0)
	v_lshlrev_b64 v[10:11], 12, v[98:99]
	s_waitcnt vmcnt(7)
	v_lshlrev_b32_e32 v12, 16, v6
	v_and_b32_e32 v13, 0xffff0000, v6
	v_lshlrev_b32_e32 v6, 16, v7
	v_and_b32_e32 v7, 0xffff0000, v7
	v_lshlrev_b32_e32 v14, 16, v8
	v_and_b32_e32 v15, 0xffff0000, v8
	v_lshlrev_b32_e32 v8, 16, v9
	v_and_b32_e32 v9, 0xffff0000, v9
	v_lshl_add_u64 v[10:11], v[10:11], 0, v[30:31]
	v_pk_fma_f32 v[6:7], v[48:49], s[18:19], v[6:7] op_sel_hi:[1,0,1]
	v_pk_fma_f32 v[12:13], v[46:47], s[18:19], v[12:13] op_sel_hi:[1,0,1]
	v_pk_fma_f32 v[8:9], v[44:45], s[18:19], v[8:9] op_sel_hi:[1,0,1]
	v_pk_fma_f32 v[14:15], v[42:43], s[18:19], v[14:15] op_sel_hi:[1,0,1]
	s_and_b64 vcc, exec, s[6:7]
	v_cvt_pk_bf16_f32 v16, v12, v13
	v_cvt_pk_bf16_f32 v17, v6, v7
	v_cvt_pk_bf16_f32 v18, v14, v15
	v_cvt_pk_bf16_f32 v19, v8, v9
	global_store_dwordx4 v[32:33], v[16:19], off
	s_cbranch_vccnz .LBB0_1722
	s_nop 0
	v_max_f32_e32 v16, v12, v12
	v_med3_f32 v17, v16, s48, v200
	v_max_f32_e32 v16, v13, v13
	v_med3_f32 v18, v16, s48, v200
	v_cvt_pk_fp8_f32 v16, v17, v18
	v_max_f32_e32 v19, v6, v6
	v_max_f32_e32 v18, v7, v7
	v_med3_f32 v17, v19, s48, v200
	v_med3_f32 v18, v18, s48, v200
	v_cvt_pk_fp8_f32 v16, v17, v18 op_sel:[0,0,1]
	v_max_f32_e32 v17, v14, v14
	v_med3_f32 v18, v17, s48, v200
	v_max_f32_e32 v17, v15, v15
	v_med3_f32 v19, v17, s48, v200
	v_cvt_pk_fp8_f32 v17, v18, v19
	v_max_f32_e32 v20, v8, v8
	v_max_f32_e32 v19, v9, v9
	v_med3_f32 v18, v20, s48, v200
	v_med3_f32 v19, v19, s48, v200
	v_cvt_pk_fp8_f32 v17, v18, v19 op_sel:[0,0,1]
	v_lshl_add_u64 v[18:19], s[70:71], 0, v[10:11]
	global_store_dwordx2 v[18:19], v[16:17], off
.LBB0_1722:
	v_or_b32_e32 v10, 0x80, v10
	s_waitcnt vmcnt(7)
	v_lshlrev_b32_e32 v16, 16, v2
	v_and_b32_e32 v17, 0xffff0000, v2
	v_lshlrev_b32_e32 v2, 16, v3
	v_and_b32_e32 v3, 0xffff0000, v3
	v_lshlrev_b32_e32 v18, 16, v4
	v_and_b32_e32 v19, 0xffff0000, v4
	v_lshlrev_b32_e32 v4, 16, v5
	v_and_b32_e32 v5, 0xffff0000, v5
	v_pk_fma_f32 v[2:3], v[40:41], s[18:19], v[2:3] op_sel_hi:[1,0,1]
	v_pk_fma_f32 v[16:17], v[38:39], s[18:19], v[16:17] op_sel_hi:[1,0,1]
	v_pk_fma_f32 v[4:5], v[36:37], s[18:19], v[4:5] op_sel_hi:[1,0,1]
	v_pk_fma_f32 v[18:19], v[34:35], s[18:19], v[18:19] op_sel_hi:[1,0,1]
	v_lshl_add_u64 v[24:25], v[10:11], 1, s[66:67]
	s_and_b64 vcc, exec, s[6:7]
	v_cvt_pk_bf16_f32 v20, v16, v17
	v_cvt_pk_bf16_f32 v21, v2, v3
	v_cvt_pk_bf16_f32 v22, v18, v19
	v_cvt_pk_bf16_f32 v23, v4, v5
	global_store_dwordx4 v[24:25], v[20:23], off
	s_cbranch_vccnz .LBB0_1724
	s_nop 0
	v_max_f32_e32 v20, v16, v16
	v_med3_f32 v21, v20, s48, v200
	v_max_f32_e32 v20, v17, v17
	v_med3_f32 v22, v20, s48, v200
	v_cvt_pk_fp8_f32 v20, v21, v22
	v_max_f32_e32 v23, v2, v2
	v_max_f32_e32 v22, v3, v3
	v_med3_f32 v21, v23, s48, v200
	v_med3_f32 v22, v22, s48, v200
	v_cvt_pk_fp8_f32 v20, v21, v22 op_sel:[0,0,1]
	v_max_f32_e32 v21, v18, v18
	v_med3_f32 v22, v21, s48, v200
	v_max_f32_e32 v21, v19, v19
	v_med3_f32 v23, v21, s48, v200
	v_cvt_pk_fp8_f32 v21, v22, v23
	v_max_f32_e32 v24, v4, v4
	v_max_f32_e32 v23, v5, v5
	v_med3_f32 v22, v24, s48, v200
	v_med3_f32 v23, v23, s48, v200
	v_cvt_pk_fp8_f32 v21, v22, v23 op_sel:[0,0,1]
	v_lshl_add_u64 v[10:11], s[70:71], 0, v[10:11]
	global_store_dwordx2 v[10:11], v[20:21], off

; __device__ __forceinline__ unsigned cvt_pk_bf16(float lo, float hi) { unsigned r; asm volatile("v_cvt_pk_bf16_f32 %0, %1, %2" : "=v"(r) : "v"(lo), "v"(hi)); return r; }
;     __device__ __forceinline__ void operator()(const f32x4 (&acc)[2][2][4][2], const Unit& u, int wr, int wc, int fr, int fq) const {
;     ...
;                 for (int bj = 0; bj < 2; ++bj) { const size_t o2 = (size_t)(row0 + ai * HALF + m * 16) * DM + col0 + bj * HALF;
;                     if constexpr (XF32) { a[m][bj][0] = *(const f32x4*)((const float*)xin + o2); a[m][bj][1] = *(const f32x4*)((const float*)xin + o2 + 4); }
;                     else { const u32x4 w = *(const u32x4*)((const bf16_t*)xin + o2); a[m][bj][0] = __builtin_bit_cast(f32x4, w); } }
; #pragma unroll
;             for (int m = 0; m < 4; ++m) {
;                 const int row = row0 + ai * HALF + m * 16; const size_t off = (size_t)row * DM + col0; float q = 0.f;
; #pragma unroll
;                 for (int bj = 0; bj < 2; ++bj) { const size_t o2 = off + bj * HALF;
;                     f32x4 a0, a1;
;                     if constexpr (XF32) { a0 = a[m][bj][0]; a1 = a[m][bj][1]; }
;                     else { const u32x4 w = __builtin_bit_cast(u32x4, a[m][bj][0]);
;                         a0 = (f32x4){__uint_as_float(w.x << 16), __uint_as_float(w.x & 0xffff0000u), __uint_as_float(w.y << 16), __uint_as_float(w.y & 0xffff0000u)};
;                         a1 = (f32x4){__uint_as_float(w.z << 16), __uint_as_float(w.z & 0xffff0000u), __uint_as_float(w.w << 16), __uint_as_float(w.w & 0xffff0000u)}; }
;                     const f32x4 v0 = a0 + acc[ai][bj][m][0] * sc, v1 = a1 + acc[ai][bj][m][1] * sc;
;                     q += ((v0[0] * v0[0] + v0[1] * v0[1]) + (v0[2] * v0[2] + v0[3] * v0[3])) + ((v1[0] * v1[0] + v1[1] * v1[1]) + (v1[2] * v1[2] + v1[3] * v1[3]));
;                     u32x4 wo; wo.x = cvt_pk_bf16(v0[0], v0[1]); wo.y = cvt_pk_bf16(v0[2], v0[3]); wo.z = cvt_pk_bf16(v1[0], v1[1]); wo.w = cvt_pk_bf16(v1[2], v1[3]);
;                     *(u32x4*)(xb + o2) = wo;
;                     if (x8) { u32x2 w8; w8.x = pk4_fp8(v0[0], v0[1], v0[2], v0[3]); w8.y = pk4_fp8(v1[0], v1[1], v1[2], v1[3]); *(u32x2*)(x8 + o2) = w8; } }
.LBB0_2162:
	v_lshl_add_u32 v32, s6, 8, v1
	v_lshl_or_b32 v30, s30, 8, v191
	v_readlane_b32 s66, v253, 52
	v_ashrrev_i32_e32 v31, 31, v30
	v_readlane_b32 s67, v253, 53
	v_ashrrev_i32_e32 v33, 31, v32
	v_or_b32_e32 v184, 16, v32
	v_lshl_add_u64 v[174:175], v[30:31], 1, s[66:67]
	v_lshlrev_b64 v[2:3], 13, v[32:33]
	v_ashrrev_i32_e32 v185, 31, v184
	v_or_b32_e32 v180, 32, v32
	v_lshl_add_u64 v[202:203], v[174:175], 0, v[2:3]
	v_lshlrev_b64 v[2:3], 13, v[184:185]
	v_ashrrev_i32_e32 v181, 31, v180
	v_or_b32_e32 v176, 48, v32
	v_lshl_add_u64 v[186:187], v[174:175], 0, v[2:3]
	v_lshlrev_b64 v[2:3], 13, v[180:181]
	v_ashrrev_i32_e32 v177, 31, v176
	s_nop 15
	s_nop 15
	v_lshl_add_u64 v[182:183], v[174:175], 0, v[2:3]
	v_lshlrev_b64 v[2:3], 13, v[176:177]
	global_load_dwordx4 v[198:201], v[202:203], off
	global_load_dwordx4 v[26:29], v[202:203], off offset:256
	v_lshl_add_u64 v[178:179], v[174:175], 0, v[2:3]
	global_load_dwordx4 v[22:25], v[186:187], off
	global_load_dwordx4 v[18:21], v[186:187], off offset:256
	global_load_dwordx4 v[14:17], v[182:183], off
	global_load_dwordx4 v[10:13], v[182:183], off offset:256
	global_load_dwordx4 v[6:9], v[178:179], off
	global_load_dwordx4 v[2:5], v[178:179], off offset:256
	v_cndmask_b32_e64 v188, 0, 1, s[18:19]
	v_cmp_ne_u32_e64 s[6:7], 1, v188
	v_lshlrev_b64 v[188:189], 12, v[32:33]
	v_readlane_b32 s70, v253, 50
	v_lshl_add_u64 v[188:189], v[188:189], 0, v[30:31]
	s_andn2_b64 vcc, exec, s[18:19]
	v_readlane_b32 s71, v253, 51
	s_waitcnt vmcnt(0)
	v_lshlrev_b32_e32 v204, 16, v198
	v_and_b32_e32 v205, 0xffff0000, v198
	v_lshlrev_b32_e32 v198, 16, v199
	v_and_b32_e32 v199, 0xffff0000, v199
	v_lshlrev_b32_e32 v206, 16, v200
	v_and_b32_e32 v207, 0xffff0000, v200
	v_lshlrev_b32_e32 v200, 16, v201
	v_and_b32_e32 v201, 0xffff0000, v201
	v_pk_fma_f32 v[160:161], v[160:161], s[20:21], v[198:199] op_sel_hi:[1,0,1]
	v_pk_fma_f32 v[158:159], v[158:159], s[20:21], v[204:205] op_sel_hi:[1,0,1]
	v_pk_fma_f32 v[156:157], v[156:157], s[20:21], v[200:201] op_sel_hi:[1,0,1]
	v_pk_fma_f32 v[154:155], v[154:155], s[20:21], v[206:207] op_sel_hi:[1,0,1]
	v_cvt_pk_bf16_f32 v198, v158, v159
	v_cvt_pk_bf16_f32 v199, v160, v161
	s_nop 0
	v_cvt_pk_bf16_f32 v200, v154, v155
	v_cvt_pk_bf16_f32 v201, v156, v157
	global_store_dwordx4 v[202:203], v[198:201], off
	s_cbranch_vccnz .LBB0_2164
	v_max_f32_e32 v197, v158, v158
	v_max_f32_e32 v198, v159, v159
	v_med3_f32 v197, v197, s63, v196
	v_med3_f32 v199, v198, s63, v196
	v_cvt_pk_fp8_f32 v198, v197, v199
	v_max_f32_e32 v200, v160, v160
	v_max_f32_e32 v199, v161, v161
	v_med3_f32 v197, v200, s63, v196
	v_med3_f32 v199, v199, s63, v196
	v_cvt_pk_fp8_f32 v198, v197, v199 op_sel:[0,0,1]
	v_max_f32_e32 v197, v154, v154
	v_max_f32_e32 v199, v155, v155
	v_med3_f32 v197, v197, s63, v196
	v_med3_f32 v200, v199, s63, v196
	v_cvt_pk_fp8_f32 v199, v197, v200
	v_max_f32_e32 v201, v156, v156
	v_max_f32_e32 v200, v157, v157
	v_med3_f32 v197, v201, s63, v196
	v_med3_f32 v200, v200, s63, v196
	v_cvt_pk_fp8_f32 v199, v197, v200 op_sel:[0,0,1]
	v_lshl_add_u64 v[200:201], s[70:71], 0, v[188:189]
	global_store_dwordx2 v[200:201], v[198:199], off
.LBB0_2164:
	v_or_b32_e32 v188, 0x80, v188
	v_lshlrev_b32_e32 v198, 16, v26
	v_and_b32_e32 v199, 0xffff0000, v26
	v_lshlrev_b32_e32 v26, 16, v27
	v_and_b32_e32 v27, 0xffff0000, v27
	v_lshlrev_b32_e32 v200, 16, v28
	v_and_b32_e32 v201, 0xffff0000, v28
	v_lshlrev_b32_e32 v28, 16, v29
	v_and_b32_e32 v29, 0xffff0000, v29
	v_pk_fma_f32 v[26:27], v[152:153], s[20:21], v[26:27] op_sel_hi:[1,0,1]
	v_pk_fma_f32 v[150:151], v[150:151], s[20:21], v[198:199] op_sel_hi:[1,0,1]
	v_pk_fma_f32 v[28:29], v[148:149], s[20:21], v[28:29] op_sel_hi:[1,0,1]
	v_pk_fma_f32 v[146:147], v[146:147], s[20:21], v[200:201] op_sel_hi:[1,0,1]
	v_lshl_add_u64 v[148:149], v[188:189], 1, s[66:67]
	s_and_b64 vcc, exec, s[6:7]
	v_cvt_pk_bf16_f32 v198, v150, v151
	v_cvt_pk_bf16_f32 v199, v26, v27
	v_cvt_pk_bf16_f32 v200, v146, v147
	v_cvt_pk_bf16_f32 v201, v28, v29
	global_store_dwordx4 v[148:149], v[198:201], off
	s_cbranch_vccnz .LBB0_2166
	v_max_f32_e32 v148, v150, v150
	v_med3_f32 v149, v148, s63, v196
	v_max_f32_e32 v148, v151, v151
	v_med3_f32 v152, v148, s63, v196
	v_cvt_pk_fp8_f32 v148, v149, v152
	v_max_f32_e32 v153, v26, v26
	v_max_f32_e32 v152, v27, v27
	v_med3_f32 v149, v153, s63, v196
	v_med3_f32 v152, v152, s63, v196
	v_cvt_pk_fp8_f32 v148, v149, v152 op_sel:[0,0,1]
	v_max_f32_e32 v149, v146, v146
	v_med3_f32 v152, v149, s63, v196
	v_max_f32_e32 v149, v147, v147
	v_med3_f32 v153, v149, s63, v196
	v_cvt_pk_fp8_f32 v149, v152, v153
	v_max_f32_e32 v197, v28, v28
	v_max_f32_e32 v153, v29, v29
	v_med3_f32 v152, v197, s63, v196
	v_med3_f32 v153, v153, s63, v196
	v_cvt_pk_fp8_f32 v149, v152, v153 op_sel:[0,0,1]
	v_lshl_add_u64 v[152:153], s[70:71], 0, v[188:189]
	global_store_dwordx2 v[152:153], v[148:149], off

; __device__ __forceinline__ unsigned cvt_pk_bf16(float lo, float hi) { unsigned r; asm volatile("v_cvt_pk_bf16_f32 %0, %1, %2" : "=v"(r) : "v"(lo), "v"(hi)); return r; }
;     __device__ __forceinline__ void operator()(const f32x4 (&acc)[2][2][4][2], const Unit& u, int wr, int wc, int fr, int fq) const {
;     ...
;                 for (int bj = 0; bj < 2; ++bj) { const size_t o2 = (size_t)(row0 + ai * HALF + m * 16) * DM + col0 + bj * HALF;
;                     if constexpr (XF32) { a[m][bj][0] = *(const f32x4*)((const float*)xin + o2); a[m][bj][1] = *(const f32x4*)((const float*)xin + o2 + 4); }
;                     else { const u32x4 w = *(const u32x4*)((const bf16_t*)xin + o2); a[m][bj][0] = __builtin_bit_cast(f32x4, w); } }
; #pragma unroll
;             for (int m = 0; m < 4; ++m) {
;                 const int row = row0 + ai * HALF + m * 16; const size_t off = (size_t)row * DM + col0; float q = 0.f;
; #pragma unroll
;                 for (int bj = 0; bj < 2; ++bj) { const size_t o2 = off + bj * HALF;
;                     f32x4 a0, a1;
;                     if constexpr (XF32) { a0 = a[m][bj][0]; a1 = a[m][bj][1]; }
;                     else { const u32x4 w = __builtin_bit_cast(u32x4, a[m][bj][0]);
;                         a0 = (f32x4){__uint_as_float(w.x << 16), __uint_as_float(w.x & 0xffff0000u), __uint_as_float(w.y << 16), __uint_as_float(w.y & 0xffff0000u)};
;                         a1 = (f32x4){__uint_as_float(w.z << 16), __uint_as_float(w.z & 0xffff0000u), __uint_as_float(w.w << 16), __uint_as_float(w.w & 0xffff0000u)}; }
;                     const f32x4 v0 = a0 + acc[ai][bj][m][0] * sc, v1 = a1 + acc[ai][bj][m][1] * sc;
;                     q += ((v0[0] * v0[0] + v0[1] * v0[1]) + (v0[2] * v0[2] + v0[3] * v0[3])) + ((v1[0] * v1[0] + v1[1] * v1[1]) + (v1[2] * v1[2] + v1[3] * v1[3]));
;                     u32x4 wo; wo.x = cvt_pk_bf16(v0[0], v0[1]); wo.y = cvt_pk_bf16(v0[2], v0[3]); wo.z = cvt_pk_bf16(v1[0], v1[1]); wo.w = cvt_pk_bf16(v1[2], v1[3]);
;                     *(u32x4*)(xb + o2) = wo;
;                     if (x8) { u32x2 w8; w8.x = pk4_fp8(v0[0], v0[1], v0[2], v0[3]); w8.y = pk4_fp8(v1[0], v1[1], v1[2], v1[3]); *(u32x2*)(x8 + o2) = w8; } }
.LBB0_2168:
	s_or_b64 exec, exec, s[30:31]
	s_waitcnt lgkmcnt(0)
	v_lshlrev_b64 v[26:27], 12, v[184:185]
	v_lshlrev_b32_e32 v28, 16, v22
	v_and_b32_e32 v29, 0xffff0000, v22
	v_lshlrev_b32_e32 v22, 16, v23
	v_and_b32_e32 v23, 0xffff0000, v23
	v_lshlrev_b32_e32 v148, 16, v24
	v_and_b32_e32 v149, 0xffff0000, v24
	v_lshlrev_b32_e32 v24, 16, v25
	v_and_b32_e32 v25, 0xffff0000, v25
	v_lshl_add_u64 v[26:27], v[26:27], 0, v[30:31]
	v_pk_fma_f32 v[22:23], v[144:145], s[20:21], v[22:23] op_sel_hi:[1,0,1]
	v_pk_fma_f32 v[28:29], v[142:143], s[20:21], v[28:29] op_sel_hi:[1,0,1]
	v_pk_fma_f32 v[24:25], v[140:141], s[20:21], v[24:25] op_sel_hi:[1,0,1]
	v_pk_fma_f32 v[138:139], v[138:139], s[20:21], v[148:149] op_sel_hi:[1,0,1]
	s_and_b64 vcc, exec, s[6:7]
	v_cvt_pk_bf16_f32 v140, v28, v29
	v_cvt_pk_bf16_f32 v141, v22, v23
	v_cvt_pk_bf16_f32 v142, v138, v139
	v_cvt_pk_bf16_f32 v143, v24, v25
	global_store_dwordx4 v[186:187], v[140:143], off
	s_cbranch_vccnz .LBB0_2170
	v_max_f32_e32 v33, v28, v28
	v_max_f32_e32 v140, v29, v29
	v_med3_f32 v33, v33, s63, v196
	v_med3_f32 v141, v140, s63, v196
	v_cvt_pk_fp8_f32 v140, v33, v141
	v_max_f32_e32 v142, v22, v22
	v_max_f32_e32 v141, v23, v23
	v_med3_f32 v33, v142, s63, v196
	v_med3_f32 v141, v141, s63, v196
	v_cvt_pk_fp8_f32 v140, v33, v141 op_sel:[0,0,1]
	v_max_f32_e32 v33, v138, v138
	v_max_f32_e32 v141, v139, v139
	v_med3_f32 v33, v33, s63, v196
	v_med3_f32 v142, v141, s63, v196
	v_cvt_pk_fp8_f32 v141, v33, v142
	v_max_f32_e32 v143, v24, v24
	v_max_f32_e32 v142, v25, v25
	v_med3_f32 v33, v143, s63, v196
	v_med3_f32 v142, v142, s63, v196
	v_cvt_pk_fp8_f32 v141, v33, v142 op_sel:[0,0,1]
	v_lshl_add_u64 v[142:143], s[70:71], 0, v[26:27]
	global_store_dwordx2 v[142:143], v[140:141], off
.LBB0_2170:
	v_or_b32_e32 v26, 0x80, v26
	v_lshlrev_b32_e32 v140, 16, v18
	v_and_b32_e32 v141, 0xffff0000, v18
	v_lshlrev_b32_e32 v18, 16, v19
	v_and_b32_e32 v19, 0xffff0000, v19
	v_lshlrev_b32_e32 v142, 16, v20
	v_and_b32_e32 v143, 0xffff0000, v20
	v_lshlrev_b32_e32 v20, 16, v21
	v_and_b32_e32 v21, 0xffff0000, v21
	v_pk_fma_f32 v[18:19], v[136:137], s[20:21], v[18:19] op_sel_hi:[1,0,1]
	v_pk_fma_f32 v[134:135], v[134:135], s[20:21], v[140:141] op_sel_hi:[1,0,1]
	v_pk_fma_f32 v[20:21], v[132:133], s[20:21], v[20:21] op_sel_hi:[1,0,1]
	v_pk_fma_f32 v[130:131], v[130:131], s[20:21], v[142:143] op_sel_hi:[1,0,1]
	v_lshl_add_u64 v[132:133], v[26:27], 1, s[66:67]
	s_and_b64 vcc, exec, s[6:7]
	v_cvt_pk_bf16_f32 v140, v134, v135
	v_cvt_pk_bf16_f32 v141, v18, v19
	v_cvt_pk_bf16_f32 v142, v130, v131
	v_cvt_pk_bf16_f32 v143, v20, v21
	global_store_dwordx4 v[132:133], v[140:143], off
	s_cbranch_vccnz .LBB0_2172
	v_max_f32_e32 v33, v134, v134
	v_max_f32_e32 v132, v135, v135
	v_med3_f32 v33, v33, s63, v196
	v_med3_f32 v133, v132, s63, v196
	v_cvt_pk_fp8_f32 v132, v33, v133
	v_max_f32_e32 v136, v18, v18
	v_max_f32_e32 v133, v19, v19
	v_med3_f32 v33, v136, s63, v196
	v_med3_f32 v133, v133, s63, v196
	v_cvt_pk_fp8_f32 v132, v33, v133 op_sel:[0,0,1]
	v_max_f32_e32 v33, v130, v130
	v_max_f32_e32 v133, v131, v131
	v_med3_f32 v33, v33, s63, v196
	v_med3_f32 v136, v133, s63, v196
	v_cvt_pk_fp8_f32 v133, v33, v136
	v_max_f32_e32 v137, v20, v20
	v_max_f32_e32 v136, v21, v21
	v_med3_f32 v33, v137, s63, v196
	v_med3_f32 v136, v136, s63, v196
	v_cvt_pk_fp8_f32 v133, v33, v136 op_sel:[0,0,1]
	v_lshl_add_u64 v[26:27], s[70:71], 0, v[26:27]
	global_store_dwordx2 v[26:27], v[132:133], off

; __device__ __forceinline__ unsigned cvt_pk_bf16(float lo, float hi) { unsigned r; asm volatile("v_cvt_pk_bf16_f32 %0, %1, %2" : "=v"(r) : "v"(lo), "v"(hi)); return r; }
;     __device__ __forceinline__ void operator()(const f32x4 (&acc)[2][2][4][2], const Unit& u, int wr, int wc, int fr, int fq) const {
;     ...
;                 for (int bj = 0; bj < 2; ++bj) { const size_t o2 = (size_t)(row0 + ai * HALF + m * 16) * DM + col0 + bj * HALF;
;                     if constexpr (XF32) { a[m][bj][0] = *(const f32x4*)((const float*)xin + o2); a[m][bj][1] = *(const f32x4*)((const float*)xin + o2 + 4); }
;                     else { const u32x4 w = *(const u32x4*)((const bf16_t*)xin + o2); a[m][bj][0] = __builtin_bit_cast(f32x4, w); } }
; #pragma unroll
;             for (int m = 0; m < 4; ++m) {
;                 const int row = row0 + ai * HALF + m * 16; const size_t off = (size_t)row * DM + col0; float q = 0.f;
; #pragma unroll
;                 for (int bj = 0; bj < 2; ++bj) { const size_t o2 = off + bj * HALF;
;                     f32x4 a0, a1;
;                     if constexpr (XF32) { a0 = a[m][bj][0]; a1 = a[m][bj][1]; }
;                     else { const u32x4 w = __builtin_bit_cast(u32x4, a[m][bj][0]);
;                         a0 = (f32x4){__uint_as_float(w.x << 16), __uint_as_float(w.x & 0xffff0000u), __uint_as_float(w.y << 16), __uint_as_float(w.y & 0xffff0000u)};
;                         a1 = (f32x4){__uint_as_float(w.z << 16), __uint_as_float(w.z & 0xffff0000u), __uint_as_float(w.w << 16), __uint_as_float(w.w & 0xffff0000u)}; }
;                     const f32x4 v0 = a0 + acc[ai][bj][m][0] * sc, v1 = a1 + acc[ai][bj][m][1] * sc;
;                     q += ((v0[0] * v0[0] + v0[1] * v0[1]) + (v0[2] * v0[2] + v0[3] * v0[3])) + ((v1[0] * v1[0] + v1[1] * v1[1]) + (v1[2] * v1[2] + v1[3] * v1[3]));
;                     u32x4 wo; wo.x = cvt_pk_bf16(v0[0], v0[1]); wo.y = cvt_pk_bf16(v0[2], v0[3]); wo.z = cvt_pk_bf16(v1[0], v1[1]); wo.w = cvt_pk_bf16(v1[2], v1[3]);
;                     *(u32x4*)(xb + o2) = wo;
;                     if (x8) { u32x2 w8; w8.x = pk4_fp8(v0[0], v0[1], v0[2], v0[3]); w8.y = pk4_fp8(v1[0], v1[1], v1[2], v1[3]); *(u32x2*)(x8 + o2) = w8; } }
.LBB0_2174:
	s_or_b64 exec, exec, s[30:31]
	s_waitcnt lgkmcnt(0)
	v_lshlrev_b64 v[18:19], 12, v[180:181]
	v_lshlrev_b32_e32 v20, 16, v14
	v_and_b32_e32 v21, 0xffff0000, v14
	v_lshlrev_b32_e32 v14, 16, v15
	v_and_b32_e32 v15, 0xffff0000, v15
	v_lshlrev_b32_e32 v22, 16, v16
	v_and_b32_e32 v23, 0xffff0000, v16
	v_lshlrev_b32_e32 v16, 16, v17
	v_and_b32_e32 v17, 0xffff0000, v17
	v_lshl_add_u64 v[18:19], v[18:19], 0, v[30:31]
	v_pk_fma_f32 v[14:15], v[128:129], s[20:21], v[14:15] op_sel_hi:[1,0,1]
	v_pk_fma_f32 v[20:21], v[126:127], s[20:21], v[20:21] op_sel_hi:[1,0,1]
	v_pk_fma_f32 v[16:17], v[124:125], s[20:21], v[16:17] op_sel_hi:[1,0,1]
	v_pk_fma_f32 v[22:23], v[122:123], s[20:21], v[22:23] op_sel_hi:[1,0,1]
	s_and_b64 vcc, exec, s[6:7]
	v_cvt_pk_bf16_f32 v24, v20, v21
	v_cvt_pk_bf16_f32 v25, v14, v15
	v_cvt_pk_bf16_f32 v26, v22, v23
	v_cvt_pk_bf16_f32 v27, v16, v17
	global_store_dwordx4 v[182:183], v[24:27], off
	s_cbranch_vccnz .LBB0_2176
	s_nop 0
	v_max_f32_e32 v24, v20, v20
	v_med3_f32 v25, v24, s63, v196
	v_max_f32_e32 v24, v21, v21
	v_med3_f32 v26, v24, s63, v196
	v_cvt_pk_fp8_f32 v24, v25, v26
	v_max_f32_e32 v27, v14, v14
	v_max_f32_e32 v26, v15, v15
	v_med3_f32 v25, v27, s63, v196
	v_med3_f32 v26, v26, s63, v196
	v_cvt_pk_fp8_f32 v24, v25, v26 op_sel:[0,0,1]
	v_max_f32_e32 v25, v22, v22
	v_med3_f32 v26, v25, s63, v196
	v_max_f32_e32 v25, v23, v23
	v_med3_f32 v27, v25, s63, v196
	v_cvt_pk_fp8_f32 v25, v26, v27
	v_max_f32_e32 v28, v16, v16
	v_max_f32_e32 v27, v17, v17
	v_med3_f32 v26, v28, s63, v196
	v_med3_f32 v27, v27, s63, v196
	v_cvt_pk_fp8_f32 v25, v26, v27 op_sel:[0,0,1]
	v_lshl_add_u64 v[26:27], s[70:71], 0, v[18:19]
	global_store_dwordx2 v[26:27], v[24:25], off
.LBB0_2176:
	v_or_b32_e32 v18, 0x80, v18
	v_lshlrev_b32_e32 v24, 16, v10
	v_and_b32_e32 v25, 0xffff0000, v10
	v_lshlrev_b32_e32 v10, 16, v11
	v_and_b32_e32 v11, 0xffff0000, v11
	v_lshlrev_b32_e32 v26, 16, v12
	v_and_b32_e32 v27, 0xffff0000, v12
	v_lshlrev_b32_e32 v12, 16, v13
	v_and_b32_e32 v13, 0xffff0000, v13
	v_pk_fma_f32 v[10:11], v[120:121], s[20:21], v[10:11] op_sel_hi:[1,0,1]
	v_pk_fma_f32 v[24:25], v[118:119], s[20:21], v[24:25] op_sel_hi:[1,0,1]
	v_pk_fma_f32 v[12:13], v[116:117], s[20:21], v[12:13] op_sel_hi:[1,0,1]
	v_pk_fma_f32 v[26:27], v[114:115], s[20:21], v[26:27] op_sel_hi:[1,0,1]
	v_lshl_add_u64 v[28:29], v[18:19], 1, s[66:67]
	s_and_b64 vcc, exec, s[6:7]
	v_cvt_pk_bf16_f32 v114, v24, v25
	v_cvt_pk_bf16_f32 v115, v10, v11
	v_cvt_pk_bf16_f32 v116, v26, v27
	v_cvt_pk_bf16_f32 v117, v12, v13
	global_store_dwordx4 v[28:29], v[114:117], off
	s_cbranch_vccnz .LBB0_2178
	v_max_f32_e32 v28, v24, v24
	v_med3_f32 v29, v28, s63, v196
	v_max_f32_e32 v28, v25, v25
	v_med3_f32 v33, v28, s63, v196
	v_cvt_pk_fp8_f32 v28, v29, v33
	v_max_f32_e32 v114, v10, v10
	v_max_f32_e32 v33, v11, v11
	v_med3_f32 v29, v114, s63, v196
	v_med3_f32 v33, v33, s63, v196
	v_cvt_pk_fp8_f32 v28, v29, v33 op_sel:[0,0,1]
	v_max_f32_e32 v29, v26, v26
	v_med3_f32 v33, v29, s63, v196
	v_max_f32_e32 v29, v27, v27
	v_med3_f32 v114, v29, s63, v196
	v_cvt_pk_fp8_f32 v29, v33, v114
	v_max_f32_e32 v115, v12, v12
	v_max_f32_e32 v114, v13, v13
	v_med3_f32 v33, v115, s63, v196
	v_med3_f32 v114, v114, s63, v196
	v_cvt_pk_fp8_f32 v29, v33, v114 op_sel:[0,0,1]
	v_lshl_add_u64 v[18:19], s[70:71], 0, v[18:19]
	global_store_dwordx2 v[18:19], v[28:29], off

; __device__ __forceinline__ unsigned cvt_pk_bf16(float lo, float hi) { unsigned r; asm volatile("v_cvt_pk_bf16_f32 %0, %1, %2" : "=v"(r) : "v"(lo), "v"(hi)); return r; }
;     __device__ __forceinline__ void operator()(const f32x4 (&acc)[2][2][4][2], const Unit& u, int wr, int wc, int fr, int fq) const {
;     ...
;                 for (int bj = 0; bj < 2; ++bj) { const size_t o2 = (size_t)(row0 + ai * HALF + m * 16) * DM + col0 + bj * HALF;
;                     if constexpr (XF32) { a[m][bj][0] = *(const f32x4*)((const float*)xin + o2); a[m][bj][1] = *(const f32x4*)((const float*)xin + o2 + 4); }
;                     else { const u32x4 w = *(const u32x4*)((const bf16_t*)xin + o2); a[m][bj][0] = __builtin_bit_cast(f32x4, w); } }
; #pragma unroll
;             for (int m = 0; m < 4; ++m) {
;                 const int row = row0 + ai * HALF + m * 16; const size_t off = (size_t)row * DM + col0; float q = 0.f;
; #pragma unroll
;                 for (int bj = 0; bj < 2; ++bj) { const size_t o2 = off + bj * HALF;
;                     f32x4 a0, a1;
;                     if constexpr (XF32) { a0 = a[m][bj][0]; a1 = a[m][bj][1]; }
;                     else { const u32x4 w = __builtin_bit_cast(u32x4, a[m][bj][0]);
;                         a0 = (f32x4){__uint_as_float(w.x << 16), __uint_as_float(w.x & 0xffff0000u), __uint_as_float(w.y << 16), __uint_as_float(w.y & 0xffff0000u)};
;                         a1 = (f32x4){__uint_as_float(w.z << 16), __uint_as_float(w.z & 0xffff0000u), __uint_as_float(w.w << 16), __uint_as_float(w.w & 0xffff0000u)}; }
;                     const f32x4 v0 = a0 + acc[ai][bj][m][0] * sc, v1 = a1 + acc[ai][bj][m][1] * sc;
;                     q += ((v0[0] * v0[0] + v0[1] * v0[1]) + (v0[2] * v0[2] + v0[3] * v0[3])) + ((v1[0] * v1[0] + v1[1] * v1[1]) + (v1[2] * v1[2] + v1[3] * v1[3]));
;                     u32x4 wo; wo.x = cvt_pk_bf16(v0[0], v0[1]); wo.y = cvt_pk_bf16(v0[2], v0[3]); wo.z = cvt_pk_bf16(v1[0], v1[1]); wo.w = cvt_pk_bf16(v1[2], v1[3]);
;                     *(u32x4*)(xb + o2) = wo;
;                     if (x8) { u32x2 w8; w8.x = pk4_fp8(v0[0], v0[1], v0[2], v0[3]); w8.y = pk4_fp8(v1[0], v1[1], v1[2], v1[3]); *(u32x2*)(x8 + o2) = w8; } }
.LBB0_2180:
	s_or_b64 exec, exec, s[30:31]
	s_waitcnt lgkmcnt(0)
	v_lshlrev_b64 v[10:11], 12, v[176:177]
	v_lshlrev_b32_e32 v12, 16, v6
	v_and_b32_e32 v13, 0xffff0000, v6
	v_lshlrev_b32_e32 v6, 16, v7
	v_and_b32_e32 v7, 0xffff0000, v7
	v_lshlrev_b32_e32 v14, 16, v8
	v_and_b32_e32 v15, 0xffff0000, v8
	v_lshlrev_b32_e32 v8, 16, v9
	v_and_b32_e32 v9, 0xffff0000, v9
	v_lshl_add_u64 v[10:11], v[10:11], 0, v[30:31]
	v_pk_fma_f32 v[6:7], v[112:113], s[20:21], v[6:7] op_sel_hi:[1,0,1]
	v_pk_fma_f32 v[12:13], v[110:111], s[20:21], v[12:13] op_sel_hi:[1,0,1]
	v_pk_fma_f32 v[8:9], v[108:109], s[20:21], v[8:9] op_sel_hi:[1,0,1]
	v_pk_fma_f32 v[14:15], v[106:107], s[20:21], v[14:15] op_sel_hi:[1,0,1]
	s_and_b64 vcc, exec, s[6:7]
	v_cvt_pk_bf16_f32 v16, v12, v13
	v_cvt_pk_bf16_f32 v17, v6, v7
	v_cvt_pk_bf16_f32 v18, v14, v15
	v_cvt_pk_bf16_f32 v19, v8, v9
	global_store_dwordx4 v[178:179], v[16:19], off
	s_cbranch_vccnz .LBB0_2182
	s_nop 0
	v_max_f32_e32 v16, v12, v12
	v_med3_f32 v17, v16, s63, v196
	v_max_f32_e32 v16, v13, v13
	v_med3_f32 v18, v16, s63, v196
	v_cvt_pk_fp8_f32 v16, v17, v18
	v_max_f32_e32 v19, v6, v6
	v_max_f32_e32 v18, v7, v7
	v_med3_f32 v17, v19, s63, v196
	v_med3_f32 v18, v18, s63, v196
	v_cvt_pk_fp8_f32 v16, v17, v18 op_sel:[0,0,1]
	v_max_f32_e32 v17, v14, v14
	v_med3_f32 v18, v17, s63, v196
	v_max_f32_e32 v17, v15, v15
	v_med3_f32 v19, v17, s63, v196
	v_cvt_pk_fp8_f32 v17, v18, v19
	v_max_f32_e32 v20, v8, v8
	v_max_f32_e32 v19, v9, v9
	v_med3_f32 v18, v20, s63, v196
	v_med3_f32 v19, v19, s63, v196
	v_cvt_pk_fp8_f32 v17, v18, v19 op_sel:[0,0,1]
	v_lshl_add_u64 v[18:19], s[70:71], 0, v[10:11]
	global_store_dwordx2 v[18:19], v[16:17], off
.LBB0_2182:
	v_or_b32_e32 v10, 0x80, v10
	v_lshlrev_b32_e32 v16, 16, v2
	v_and_b32_e32 v17, 0xffff0000, v2
	v_lshlrev_b32_e32 v2, 16, v3
	v_and_b32_e32 v3, 0xffff0000, v3
	v_lshlrev_b32_e32 v18, 16, v4
	v_and_b32_e32 v19, 0xffff0000, v4
	v_lshlrev_b32_e32 v4, 16, v5
	v_and_b32_e32 v5, 0xffff0000, v5
	v_pk_fma_f32 v[2:3], v[104:105], s[20:21], v[2:3] op_sel_hi:[1,0,1]
	v_pk_fma_f32 v[16:17], v[102:103], s[20:21], v[16:17] op_sel_hi:[1,0,1]
	v_pk_fma_f32 v[4:5], v[100:101], s[20:21], v[4:5] op_sel_hi:[1,0,1]
	v_pk_fma_f32 v[18:19], v[98:99], s[20:21], v[18:19] op_sel_hi:[1,0,1]
	v_lshl_add_u64 v[24:25], v[10:11], 1, s[66:67]
	s_and_b64 vcc, exec, s[6:7]
	v_cvt_pk_bf16_f32 v20, v16, v17
	v_cvt_pk_bf16_f32 v21, v2, v3
	v_cvt_pk_bf16_f32 v22, v18, v19
	v_cvt_pk_bf16_f32 v23, v4, v5
	global_store_dwordx4 v[24:25], v[20:23], off
	s_cbranch_vccnz .LBB0_2184
	s_nop 0
	v_max_f32_e32 v20, v16, v16
	v_med3_f32 v21, v20, s63, v196
	v_max_f32_e32 v20, v17, v17
	v_med3_f32 v22, v20, s63, v196
	v_cvt_pk_fp8_f32 v20, v21, v22
	v_max_f32_e32 v23, v2, v2
	v_max_f32_e32 v22, v3, v3
	v_med3_f32 v21, v23, s63, v196
	v_med3_f32 v22, v22, s63, v196
	v_cvt_pk_fp8_f32 v20, v21, v22 op_sel:[0,0,1]
	v_max_f32_e32 v21, v18, v18
	v_med3_f32 v22, v21, s63, v196
	v_max_f32_e32 v21, v19, v19
	v_med3_f32 v23, v21, s63, v196
	v_cvt_pk_fp8_f32 v21, v22, v23
	v_max_f32_e32 v24, v4, v4
	v_max_f32_e32 v23, v5, v5
	v_med3_f32 v22, v24, s63, v196
	v_med3_f32 v23, v23, s63, v196
	v_cvt_pk_fp8_f32 v21, v22, v23 op_sel:[0,0,1]
	v_lshl_add_u64 v[10:11], s[70:71], 0, v[10:11]
	global_store_dwordx2 v[10:11], v[20:21], off

; __device__ __forceinline__ unsigned pk4_fp8(float a, float b, float c, float d) {
;     a = fminf(fmaxf(a, -448.f), 448.f); b = fminf(fmaxf(b, -448.f), 448.f); c = fminf(fmaxf(c, -448.f), 448.f); d = fminf(fmaxf(d, -448.f), 448.f);
;     __device__ __forceinline__ void operator()(const f32x4 (&acc)[2][2][4][2], const Unit& u, int wr, int wc, int fr, int fq) const {
;     ...
;                 for (int bj = 0; bj < 2; ++bj) { const size_t o2 = (size_t)(row0 + ai * HALF + m * 16) * DM + col0 + bj * HALF;
;                     if constexpr (XF32) { a[m][bj][0] = *(const f32x4*)((const float*)xin + o2); a[m][bj][1] = *(const f32x4*)((const float*)xin + o2 + 4); }
;                     else { const u32x4 w = *(const u32x4*)((const bf16_t*)xin + o2); a[m][bj][0] = __builtin_bit_cast(f32x4, w); } }
; #pragma unroll
;             for (int m = 0; m < 4; ++m) {
;                 const int row = row0 + ai * HALF + m * 16; const size_t off = (size_t)row * DM + col0; float q = 0.f;
; #pragma unroll
;                 for (int bj = 0; bj < 2; ++bj) { const size_t o2 = off + bj * HALF;
;                     f32x4 a0, a1;
;                     if constexpr (XF32) { a0 = a[m][bj][0]; a1 = a[m][bj][1]; }
;                     else { const u32x4 w = __builtin_bit_cast(u32x4, a[m][bj][0]);
;                         a0 = (f32x4){__uint_as_float(w.x << 16), __uint_as_float(w.x & 0xffff0000u), __uint_as_float(w.y << 16), __uint_as_float(w.y & 0xffff0000u)};
;                         a1 = (f32x4){__uint_as_float(w.z << 16), __uint_as_float(w.z & 0xffff0000u), __uint_as_float(w.w << 16), __uint_as_float(w.w & 0xffff0000u)}; }
;                     const f32x4 v0 = a0 + acc[ai][bj][m][0] * sc, v1 = a1 + acc[ai][bj][m][1] * sc;
;                     q += ((v0[0] * v0[0] + v0[1] * v0[1]) + (v0[2] * v0[2] + v0[3] * v0[3])) + ((v1[0] * v1[0] + v1[1] * v1[1]) + (v1[2] * v1[2] + v1[3] * v1[3]));
;                     u32x4 wo; wo.x = cvt_pk_bf16(v0[0], v0[1]); wo.y = cvt_pk_bf16(v0[2], v0[3]); wo.z = cvt_pk_bf16(v1[0], v1[1]); wo.w = cvt_pk_bf16(v1[2], v1[3]);
;                     *(u32x4*)(xb + o2) = wo;
;                     if (x8) { u32x2 w8; w8.x = pk4_fp8(v0[0], v0[1], v0[2], v0[3]); w8.y = pk4_fp8(v1[0], v1[1], v1[2], v1[3]); *(u32x2*)(x8 + o2) = w8; } }
.LBB0_2186:
	s_or_b64 exec, exec, s[30:31]
	v_add_u32_e32 v108, 0x80, v32
	v_ashrrev_i32_e32 v109, 31, v108
	v_add_u32_e32 v104, 0x90, v32
	s_waitcnt lgkmcnt(0)
	v_lshlrev_b64 v[2:3], 13, v[108:109]
	v_ashrrev_i32_e32 v105, 31, v104
	v_add_u32_e32 v100, 0xa0, v32
	v_lshl_add_u64 v[116:117], v[174:175], 0, v[2:3]
	v_lshlrev_b64 v[2:3], 13, v[104:105]
	v_ashrrev_i32_e32 v101, 31, v100
	v_add_u32_e32 v32, 0xb0, v32
	v_lshl_add_u64 v[106:107], v[174:175], 0, v[2:3]
	v_lshlrev_b64 v[2:3], 13, v[100:101]
	v_ashrrev_i32_e32 v33, 31, v32
	v_lshl_add_u64 v[102:103], v[174:175], 0, v[2:3]
	v_lshlrev_b64 v[2:3], 13, v[32:33]
	global_load_dwordx4 v[112:115], v[116:117], off
	global_load_dwordx4 v[26:29], v[116:117], off offset:256
	v_lshl_add_u64 v[98:99], v[174:175], 0, v[2:3]
	global_load_dwordx4 v[22:25], v[106:107], off
	global_load_dwordx4 v[18:21], v[106:107], off offset:256
	global_load_dwordx4 v[14:17], v[102:103], off
	global_load_dwordx4 v[10:13], v[102:103], off offset:256
	global_load_dwordx4 v[6:9], v[98:99], off
	global_load_dwordx4 v[2:5], v[98:99], off offset:256
	v_lshlrev_b64 v[110:111], 12, v[108:109]
	v_lshl_add_u64 v[110:111], v[110:111], 0, v[30:31]
	s_and_b64 vcc, exec, s[6:7]
	s_waitcnt vmcnt(7)
	v_lshlrev_b32_e32 v118, 16, v112
	v_and_b32_e32 v119, 0xffff0000, v112
	v_lshlrev_b32_e32 v112, 16, v113
	v_and_b32_e32 v113, 0xffff0000, v113
	v_lshlrev_b32_e32 v120, 16, v114
	v_and_b32_e32 v121, 0xffff0000, v114
	v_lshlrev_b32_e32 v114, 16, v115
	v_and_b32_e32 v115, 0xffff0000, v115
	v_pk_fma_f32 v[96:97], v[96:97], s[20:21], v[112:113] op_sel_hi:[1,0,1]
	v_pk_fma_f32 v[94:95], v[94:95], s[20:21], v[118:119] op_sel_hi:[1,0,1]
	v_pk_fma_f32 v[92:93], v[92:93], s[20:21], v[114:115] op_sel_hi:[1,0,1]
	v_pk_fma_f32 v[90:91], v[90:91], s[20:21], v[120:121] op_sel_hi:[1,0,1]
	v_cvt_pk_bf16_f32 v112, v94, v95
	v_cvt_pk_bf16_f32 v113, v96, v97
	s_nop 0
	v_cvt_pk_bf16_f32 v114, v90, v91
	v_cvt_pk_bf16_f32 v115, v92, v93
	global_store_dwordx4 v[116:117], v[112:115], off
	s_cbranch_vccnz .LBB0_2188
	s_nop 0
	v_max_f32_e32 v112, v94, v94
	v_med3_f32 v113, v112, s63, v196
	v_max_f32_e32 v112, v95, v95
	v_med3_f32 v114, v112, s63, v196
	v_cvt_pk_fp8_f32 v112, v113, v114
	v_max_f32_e32 v115, v96, v96
	v_max_f32_e32 v114, v97, v97
	v_med3_f32 v113, v115, s63, v196
	v_med3_f32 v114, v114, s63, v196
	v_cvt_pk_fp8_f32 v112, v113, v114 op_sel:[0,0,1]
	v_max_f32_e32 v113, v90, v90
	v_med3_f32 v114, v113, s63, v196
	v_max_f32_e32 v113, v91, v91
	v_med3_f32 v115, v113, s63, v196
	v_cvt_pk_fp8_f32 v113, v114, v115
	v_max_f32_e32 v116, v92, v92
	v_max_f32_e32 v115, v93, v93
	v_med3_f32 v114, v116, s63, v196
	v_med3_f32 v115, v115, s63, v196
	v_cvt_pk_fp8_f32 v113, v114, v115 op_sel:[0,0,1]
	v_lshl_add_u64 v[114:115], s[70:71], 0, v[110:111]
	global_store_dwordx2 v[114:115], v[112:113], off
.LBB0_2188:
	v_or_b32_e32 v110, 0x80, v110
	s_waitcnt vmcnt(7)
	v_lshlrev_b32_e32 v112, 16, v26
	v_and_b32_e32 v113, 0xffff0000, v26
	v_lshlrev_b32_e32 v26, 16, v27
	v_and_b32_e32 v27, 0xffff0000, v27
	v_lshlrev_b32_e32 v114, 16, v28
	v_and_b32_e32 v115, 0xffff0000, v28
	v_lshlrev_b32_e32 v28, 16, v29
	v_and_b32_e32 v29, 0xffff0000, v29
	v_pk_fma_f32 v[26:27], v[88:89], s[20:21], v[26:27] op_sel_hi:[1,0,1]
	v_pk_fma_f32 v[86:87], v[86:87], s[20:21], v[112:113] op_sel_hi:[1,0,1]
	v_pk_fma_f32 v[28:29], v[84:85], s[20:21], v[28:29] op_sel_hi:[1,0,1]
	v_pk_fma_f32 v[82:83], v[82:83], s[20:21], v[114:115] op_sel_hi:[1,0,1]
	v_lshl_add_u64 v[84:85], v[110:111], 1, s[66:67]
	s_and_b64 vcc, exec, s[6:7]
	v_cvt_pk_bf16_f32 v112, v86, v87
	v_cvt_pk_bf16_f32 v113, v26, v27
	v_cvt_pk_bf16_f32 v114, v82, v83
	v_cvt_pk_bf16_f32 v115, v28, v29
	global_store_dwordx4 v[84:85], v[112:115], off
	s_cbranch_vccnz .LBB0_2190
	v_max_f32_e32 v84, v86, v86
	v_med3_f32 v85, v84, s63, v196
	v_max_f32_e32 v84, v87, v87
	v_med3_f32 v88, v84, s63, v196
	v_cvt_pk_fp8_f32 v84, v85, v88
	v_max_f32_e32 v89, v26, v26
	v_max_f32_e32 v88, v27, v27
	v_med3_f32 v85, v89, s63, v196
	v_med3_f32 v88, v88, s63, v196
	v_cvt_pk_fp8_f32 v84, v85, v88 op_sel:[0,0,1]
	v_max_f32_e32 v85, v82, v82
	v_med3_f32 v88, v85, s63, v196
	v_max_f32_e32 v85, v83, v83
	v_med3_f32 v89, v85, s63, v196
	v_cvt_pk_fp8_f32 v85, v88, v89
	v_max_f32_e32 v112, v28, v28
	v_max_f32_e32 v89, v29, v29
	v_med3_f32 v88, v112, s63, v196
	v_med3_f32 v89, v89, s63, v196
	v_cvt_pk_fp8_f32 v85, v88, v89 op_sel:[0,0,1]
	v_lshl_add_u64 v[88:89], s[70:71], 0, v[110:111]
	global_store_dwordx2 v[88:89], v[84:85], off

; __device__ __forceinline__ unsigned cvt_pk_bf16(float lo, float hi) { unsigned r; asm volatile("v_cvt_pk_bf16_f32 %0, %1, %2" : "=v"(r) : "v"(lo), "v"(hi)); return r; }
; __device__ __forceinline__ unsigned pk4_fp8(float a, float b, float c, float d) {
;     a = fminf(fmaxf(a, -448.f), 448.f); b = fminf(fmaxf(b, -448.f), 448.f); c = fminf(fmaxf(c, -448.f), 448.f); d = fminf(fmaxf(d, -448.f), 448.f);
;     int w = 0; w = __builtin_amdgcn_cvt_pk_fp8_f32(a, b, w, false); w = __builtin_amdgcn_cvt_pk_fp8_f32(c, d, w, true); return (unsigned)w;
;     __device__ __forceinline__ void operator()(const f32x4 (&acc)[2][2][4][2], const Unit& u, int wr, int wc, int fr, int fq) const {
;     ...
;                 for (int bj = 0; bj < 2; ++bj) { const size_t o2 = off + bj * HALF;
;                     f32x4 a0, a1;
;                     if constexpr (XF32) { a0 = a[m][bj][0]; a1 = a[m][bj][1]; }
;                     else { const u32x4 w = __builtin_bit_cast(u32x4, a[m][bj][0]);
;                         a0 = (f32x4){__uint_as_float(w.x << 16), __uint_as_float(w.x & 0xffff0000u), __uint_as_float(w.y << 16), __uint_as_float(w.y & 0xffff0000u)};
;                         a1 = (f32x4){__uint_as_float(w.z << 16), __uint_as_float(w.z & 0xffff0000u), __uint_as_float(w.w << 16), __uint_as_float(w.w & 0xffff0000u)}; }
;                     const f32x4 v0 = a0 + acc[ai][bj][m][0] * sc, v1 = a1 + acc[ai][bj][m][1] * sc;
;                     q += ((v0[0] * v0[0] + v0[1] * v0[1]) + (v0[2] * v0[2] + v0[3] * v0[3])) + ((v1[0] * v1[0] + v1[1] * v1[1]) + (v1[2] * v1[2] + v1[3] * v1[3]));
;                     u32x4 wo; wo.x = cvt_pk_bf16(v0[0], v0[1]); wo.y = cvt_pk_bf16(v0[2], v0[3]); wo.z = cvt_pk_bf16(v1[0], v1[1]); wo.w = cvt_pk_bf16(v1[2], v1[3]);
;                     *(u32x4*)(xb + o2) = wo;
;                     if (x8) { u32x2 w8; w8.x = pk4_fp8(v0[0], v0[1], v0[2], v0[3]); w8.y = pk4_fp8(v1[0], v1[1], v1[2], v1[3]); *(u32x2*)(x8 + o2) = w8; } }
.LBB0_2192:
	s_or_b64 exec, exec, s[30:31]
	s_waitcnt lgkmcnt(0)
	v_lshlrev_b64 v[26:27], 12, v[104:105]
	s_waitcnt vmcnt(7)
	v_lshlrev_b32_e32 v28, 16, v22
	v_and_b32_e32 v29, 0xffff0000, v22
	v_lshlrev_b32_e32 v22, 16, v23
	v_and_b32_e32 v23, 0xffff0000, v23
	v_lshlrev_b32_e32 v82, 16, v24
	v_and_b32_e32 v83, 0xffff0000, v24
	v_lshlrev_b32_e32 v24, 16, v25
	v_and_b32_e32 v25, 0xffff0000, v25
	v_lshl_add_u64 v[26:27], v[26:27], 0, v[30:31]
	v_pk_fma_f32 v[22:23], v[80:81], s[20:21], v[22:23] op_sel_hi:[1,0,1]
	v_pk_fma_f32 v[28:29], v[78:79], s[20:21], v[28:29] op_sel_hi:[1,0,1]
	v_pk_fma_f32 v[24:25], v[76:77], s[20:21], v[24:25] op_sel_hi:[1,0,1]
	v_pk_fma_f32 v[74:75], v[74:75], s[20:21], v[82:83] op_sel_hi:[1,0,1]
	s_and_b64 vcc, exec, s[6:7]
	v_cvt_pk_bf16_f32 v76, v28, v29
	v_cvt_pk_bf16_f32 v77, v22, v23
	v_cvt_pk_bf16_f32 v78, v74, v75
	v_cvt_pk_bf16_f32 v79, v24, v25
	global_store_dwordx4 v[106:107], v[76:79], off
	s_cbranch_vccnz .LBB0_2194
	s_nop 0
	v_max_f32_e32 v76, v28, v28
	v_med3_f32 v77, v76, s63, v196
	v_max_f32_e32 v76, v29, v29
	v_med3_f32 v78, v76, s63, v196
	v_cvt_pk_fp8_f32 v76, v77, v78
	v_max_f32_e32 v79, v22, v22
	v_max_f32_e32 v78, v23, v23
	v_med3_f32 v77, v79, s63, v196
	v_med3_f32 v78, v78, s63, v196
	v_cvt_pk_fp8_f32 v76, v77, v78 op_sel:[0,0,1]
	v_max_f32_e32 v77, v74, v74
	v_med3_f32 v78, v77, s63, v196
	v_max_f32_e32 v77, v75, v75
	v_med3_f32 v79, v77, s63, v196
	v_cvt_pk_fp8_f32 v77, v78, v79
	v_max_f32_e32 v80, v24, v24
	v_max_f32_e32 v79, v25, v25
	v_med3_f32 v78, v80, s63, v196
	v_med3_f32 v79, v79, s63, v196
	v_cvt_pk_fp8_f32 v77, v78, v79 op_sel:[0,0,1]
	v_lshl_add_u64 v[78:79], s[70:71], 0, v[26:27]
	global_store_dwordx2 v[78:79], v[76:77], off
.LBB0_2194:
	v_or_b32_e32 v26, 0x80, v26
	s_waitcnt vmcnt(7)
	v_lshlrev_b32_e32 v76, 16, v18
	v_and_b32_e32 v77, 0xffff0000, v18
	v_lshlrev_b32_e32 v18, 16, v19
	v_and_b32_e32 v19, 0xffff0000, v19
	v_lshlrev_b32_e32 v78, 16, v20
	v_and_b32_e32 v79, 0xffff0000, v20
	v_lshlrev_b32_e32 v20, 16, v21
	v_and_b32_e32 v21, 0xffff0000, v21
	v_pk_fma_f32 v[18:19], v[72:73], s[20:21], v[18:19] op_sel_hi:[1,0,1]
	v_pk_fma_f32 v[70:71], v[70:71], s[20:21], v[76:77] op_sel_hi:[1,0,1]
	v_pk_fma_f32 v[20:21], v[68:69], s[20:21], v[20:21] op_sel_hi:[1,0,1]
	v_pk_fma_f32 v[66:67], v[66:67], s[20:21], v[78:79] op_sel_hi:[1,0,1]
	v_lshl_add_u64 v[68:69], v[26:27], 1, s[66:67]
	s_and_b64 vcc, exec, s[6:7]
	v_cvt_pk_bf16_f32 v76, v70, v71
	v_cvt_pk_bf16_f32 v77, v18, v19
	v_cvt_pk_bf16_f32 v78, v66, v67
	v_cvt_pk_bf16_f32 v79, v20, v21
	global_store_dwordx4 v[68:69], v[76:79], off
	s_cbranch_vccnz .LBB0_2196
	v_max_f32_e32 v68, v70, v70
	v_med3_f32 v69, v68, s63, v196
	v_max_f32_e32 v68, v71, v71
	v_med3_f32 v72, v68, s63, v196
	v_cvt_pk_fp8_f32 v68, v69, v72
	v_max_f32_e32 v73, v18, v18
	v_max_f32_e32 v72, v19, v19
	v_med3_f32 v69, v73, s63, v196
	v_med3_f32 v72, v72, s63, v196
	v_cvt_pk_fp8_f32 v68, v69, v72 op_sel:[0,0,1]
	v_max_f32_e32 v69, v66, v66
	v_med3_f32 v72, v69, s63, v196
	v_max_f32_e32 v69, v67, v67
	v_med3_f32 v73, v69, s63, v196
	v_cvt_pk_fp8_f32 v69, v72, v73
	v_max_f32_e32 v76, v20, v20
	v_max_f32_e32 v73, v21, v21
	v_med3_f32 v72, v76, s63, v196
	v_med3_f32 v73, v73, s63, v196
	v_cvt_pk_fp8_f32 v69, v72, v73 op_sel:[0,0,1]
	v_lshl_add_u64 v[26:27], s[70:71], 0, v[26:27]
	global_store_dwordx2 v[26:27], v[68:69], off

; __device__ __forceinline__ unsigned cvt_pk_bf16(float lo, float hi) { unsigned r; asm volatile("v_cvt_pk_bf16_f32 %0, %1, %2" : "=v"(r) : "v"(lo), "v"(hi)); return r; }
; __device__ __forceinline__ unsigned pk4_fp8(float a, float b, float c, float d) {
;     a = fminf(fmaxf(a, -448.f), 448.f); b = fminf(fmaxf(b, -448.f), 448.f); c = fminf(fmaxf(c, -448.f), 448.f); d = fminf(fmaxf(d, -448.f), 448.f);
;     int w = 0; w = __builtin_amdgcn_cvt_pk_fp8_f32(a, b, w, false); w = __builtin_amdgcn_cvt_pk_fp8_f32(c, d, w, true); return (unsigned)w;
;     __device__ __forceinline__ void operator()(const f32x4 (&acc)[2][2][4][2], const Unit& u, int wr, int wc, int fr, int fq) const {
;     ...
;                 for (int bj = 0; bj < 2; ++bj) { const size_t o2 = off + bj * HALF;
;                     f32x4 a0, a1;
;                     if constexpr (XF32) { a0 = a[m][bj][0]; a1 = a[m][bj][1]; }
;                     else { const u32x4 w = __builtin_bit_cast(u32x4, a[m][bj][0]);
;                         a0 = (f32x4){__uint_as_float(w.x << 16), __uint_as_float(w.x & 0xffff0000u), __uint_as_float(w.y << 16), __uint_as_float(w.y & 0xffff0000u)};
;                         a1 = (f32x4){__uint_as_float(w.z << 16), __uint_as_float(w.z & 0xffff0000u), __uint_as_float(w.w << 16), __uint_as_float(w.w & 0xffff0000u)}; }
;                     const f32x4 v0 = a0 + acc[ai][bj][m][0] * sc, v1 = a1 + acc[ai][bj][m][1] * sc;
;                     q += ((v0[0] * v0[0] + v0[1] * v0[1]) + (v0[2] * v0[2] + v0[3] * v0[3])) + ((v1[0] * v1[0] + v1[1] * v1[1]) + (v1[2] * v1[2] + v1[3] * v1[3]));
;                     u32x4 wo; wo.x = cvt_pk_bf16(v0[0], v0[1]); wo.y = cvt_pk_bf16(v0[2], v0[3]); wo.z = cvt_pk_bf16(v1[0], v1[1]); wo.w = cvt_pk_bf16(v1[2], v1[3]);
;                     *(u32x4*)(xb + o2) = wo;
;                     if (x8) { u32x2 w8; w8.x = pk4_fp8(v0[0], v0[1], v0[2], v0[3]); w8.y = pk4_fp8(v1[0], v1[1], v1[2], v1[3]); *(u32x2*)(x8 + o2) = w8; } }
.LBB0_2198:
	s_or_b64 exec, exec, s[30:31]
	s_waitcnt lgkmcnt(0)
	v_lshlrev_b64 v[18:19], 12, v[100:101]
	s_waitcnt vmcnt(7)
	v_lshlrev_b32_e32 v20, 16, v14
	v_and_b32_e32 v21, 0xffff0000, v14
	v_lshlrev_b32_e32 v14, 16, v15
	v_and_b32_e32 v15, 0xffff0000, v15
	v_lshlrev_b32_e32 v22, 16, v16
	v_and_b32_e32 v23, 0xffff0000, v16
	v_lshlrev_b32_e32 v16, 16, v17
	v_and_b32_e32 v17, 0xffff0000, v17
	v_lshl_add_u64 v[18:19], v[18:19], 0, v[30:31]
	v_pk_fma_f32 v[14:15], v[64:65], s[20:21], v[14:15] op_sel_hi:[1,0,1]
	v_pk_fma_f32 v[20:21], v[62:63], s[20:21], v[20:21] op_sel_hi:[1,0,1]
	v_pk_fma_f32 v[16:17], v[60:61], s[20:21], v[16:17] op_sel_hi:[1,0,1]
	v_pk_fma_f32 v[22:23], v[58:59], s[20:21], v[22:23] op_sel_hi:[1,0,1]
	s_and_b64 vcc, exec, s[6:7]
	v_cvt_pk_bf16_f32 v24, v20, v21
	v_cvt_pk_bf16_f32 v25, v14, v15
	v_cvt_pk_bf16_f32 v26, v22, v23
	v_cvt_pk_bf16_f32 v27, v16, v17
	global_store_dwordx4 v[102:103], v[24:27], off
	s_cbranch_vccnz .LBB0_2200
	s_nop 0
	v_max_f32_e32 v24, v20, v20
	v_med3_f32 v25, v24, s63, v196
	v_max_f32_e32 v24, v21, v21
	v_med3_f32 v26, v24, s63, v196
	v_cvt_pk_fp8_f32 v24, v25, v26
	v_max_f32_e32 v27, v14, v14
	v_max_f32_e32 v26, v15, v15
	v_med3_f32 v25, v27, s63, v196
	v_med3_f32 v26, v26, s63, v196
	v_cvt_pk_fp8_f32 v24, v25, v26 op_sel:[0,0,1]
	v_max_f32_e32 v25, v22, v22
	v_med3_f32 v26, v25, s63, v196
	v_max_f32_e32 v25, v23, v23
	v_med3_f32 v27, v25, s63, v196
	v_cvt_pk_fp8_f32 v25, v26, v27
	v_max_f32_e32 v28, v16, v16
	v_max_f32_e32 v27, v17, v17
	v_med3_f32 v26, v28, s63, v196
	v_med3_f32 v27, v27, s63, v196
	v_cvt_pk_fp8_f32 v25, v26, v27 op_sel:[0,0,1]
	v_lshl_add_u64 v[26:27], s[70:71], 0, v[18:19]
	global_store_dwordx2 v[26:27], v[24:25], off
.LBB0_2200:
	v_or_b32_e32 v18, 0x80, v18
	s_waitcnt vmcnt(7)
	v_lshlrev_b32_e32 v24, 16, v10
	v_and_b32_e32 v25, 0xffff0000, v10
	v_lshlrev_b32_e32 v10, 16, v11
	v_and_b32_e32 v11, 0xffff0000, v11
	v_lshlrev_b32_e32 v26, 16, v12
	v_and_b32_e32 v27, 0xffff0000, v12
	v_lshlrev_b32_e32 v12, 16, v13
	v_and_b32_e32 v13, 0xffff0000, v13
	v_pk_fma_f32 v[10:11], v[56:57], s[20:21], v[10:11] op_sel_hi:[1,0,1]
	v_pk_fma_f32 v[24:25], v[54:55], s[20:21], v[24:25] op_sel_hi:[1,0,1]
	v_pk_fma_f32 v[12:13], v[52:53], s[20:21], v[12:13] op_sel_hi:[1,0,1]
	v_pk_fma_f32 v[26:27], v[50:51], s[20:21], v[26:27] op_sel_hi:[1,0,1]
	v_lshl_add_u64 v[28:29], v[18:19], 1, s[66:67]
	s_and_b64 vcc, exec, s[6:7]
	v_cvt_pk_bf16_f32 v50, v24, v25
	v_cvt_pk_bf16_f32 v51, v10, v11
	v_cvt_pk_bf16_f32 v52, v26, v27
	v_cvt_pk_bf16_f32 v53, v12, v13
	global_store_dwordx4 v[28:29], v[50:53], off
	s_cbranch_vccnz .LBB0_2202
	v_max_f32_e32 v28, v24, v24
	v_med3_f32 v29, v28, s63, v196
	v_max_f32_e32 v28, v25, v25
	v_med3_f32 v50, v28, s63, v196
	v_cvt_pk_fp8_f32 v28, v29, v50
	v_max_f32_e32 v51, v10, v10
	v_max_f32_e32 v50, v11, v11
	v_med3_f32 v29, v51, s63, v196
	v_med3_f32 v50, v50, s63, v196
	v_cvt_pk_fp8_f32 v28, v29, v50 op_sel:[0,0,1]
	v_max_f32_e32 v29, v26, v26
	v_med3_f32 v50, v29, s63, v196
	v_max_f32_e32 v29, v27, v27
	v_med3_f32 v51, v29, s63, v196
	v_cvt_pk_fp8_f32 v29, v50, v51
	v_max_f32_e32 v52, v12, v12
	v_max_f32_e32 v51, v13, v13
	v_med3_f32 v50, v52, s63, v196
	v_med3_f32 v51, v51, s63, v196
	v_cvt_pk_fp8_f32 v29, v50, v51 op_sel:[0,0,1]
	v_lshl_add_u64 v[18:19], s[70:71], 0, v[18:19]
	global_store_dwordx2 v[18:19], v[28:29], off

; __device__ __forceinline__ unsigned cvt_pk_bf16(float lo, float hi) { unsigned r; asm volatile("v_cvt_pk_bf16_f32 %0, %1, %2" : "=v"(r) : "v"(lo), "v"(hi)); return r; }
; __device__ __forceinline__ unsigned pk4_fp8(float a, float b, float c, float d) {
;     a = fminf(fmaxf(a, -448.f), 448.f); b = fminf(fmaxf(b, -448.f), 448.f); c = fminf(fmaxf(c, -448.f), 448.f); d = fminf(fmaxf(d, -448.f), 448.f);
;     int w = 0; w = __builtin_amdgcn_cvt_pk_fp8_f32(a, b, w, false); w = __builtin_amdgcn_cvt_pk_fp8_f32(c, d, w, true); return (unsigned)w;
;     __device__ __forceinline__ void operator()(const f32x4 (&acc)[2][2][4][2], const Unit& u, int wr, int wc, int fr, int fq) const {
;     ...
;                 for (int bj = 0; bj < 2; ++bj) { const size_t o2 = off + bj * HALF;
;                     f32x4 a0, a1;
;                     if constexpr (XF32) { a0 = a[m][bj][0]; a1 = a[m][bj][1]; }
;                     else { const u32x4 w = __builtin_bit_cast(u32x4, a[m][bj][0]);
;                         a0 = (f32x4){__uint_as_float(w.x << 16), __uint_as_float(w.x & 0xffff0000u), __uint_as_float(w.y << 16), __uint_as_float(w.y & 0xffff0000u)};
;                         a1 = (f32x4){__uint_as_float(w.z << 16), __uint_as_float(w.z & 0xffff0000u), __uint_as_float(w.w << 16), __uint_as_float(w.w & 0xffff0000u)}; }
;                     const f32x4 v0 = a0 + acc[ai][bj][m][0] * sc, v1 = a1 + acc[ai][bj][m][1] * sc;
;                     q += ((v0[0] * v0[0] + v0[1] * v0[1]) + (v0[2] * v0[2] + v0[3] * v0[3])) + ((v1[0] * v1[0] + v1[1] * v1[1]) + (v1[2] * v1[2] + v1[3] * v1[3]));
;                     u32x4 wo; wo.x = cvt_pk_bf16(v0[0], v0[1]); wo.y = cvt_pk_bf16(v0[2], v0[3]); wo.z = cvt_pk_bf16(v1[0], v1[1]); wo.w = cvt_pk_bf16(v1[2], v1[3]);
;                     *(u32x4*)(xb + o2) = wo;
;                     if (x8) { u32x2 w8; w8.x = pk4_fp8(v0[0], v0[1], v0[2], v0[3]); w8.y = pk4_fp8(v1[0], v1[1], v1[2], v1[3]); *(u32x2*)(x8 + o2) = w8; } }
.LBB0_2204:
	s_or_b64 exec, exec, s[30:31]
	s_waitcnt lgkmcnt(0)
	v_lshlrev_b64 v[10:11], 12, v[32:33]
	s_waitcnt vmcnt(7)
	v_lshlrev_b32_e32 v12, 16, v6
	v_and_b32_e32 v13, 0xffff0000, v6
	v_lshlrev_b32_e32 v6, 16, v7
	v_and_b32_e32 v7, 0xffff0000, v7
	v_lshlrev_b32_e32 v14, 16, v8
	v_and_b32_e32 v15, 0xffff0000, v8
	v_lshlrev_b32_e32 v8, 16, v9
	v_and_b32_e32 v9, 0xffff0000, v9
	v_lshl_add_u64 v[10:11], v[10:11], 0, v[30:31]
	v_pk_fma_f32 v[6:7], v[48:49], s[20:21], v[6:7] op_sel_hi:[1,0,1]
	v_pk_fma_f32 v[12:13], v[46:47], s[20:21], v[12:13] op_sel_hi:[1,0,1]
	v_pk_fma_f32 v[8:9], v[44:45], s[20:21], v[8:9] op_sel_hi:[1,0,1]
	v_pk_fma_f32 v[14:15], v[42:43], s[20:21], v[14:15] op_sel_hi:[1,0,1]
	s_and_b64 vcc, exec, s[6:7]
	v_cvt_pk_bf16_f32 v16, v12, v13
	v_cvt_pk_bf16_f32 v17, v6, v7
	v_cvt_pk_bf16_f32 v18, v14, v15
	v_cvt_pk_bf16_f32 v19, v8, v9
	global_store_dwordx4 v[98:99], v[16:19], off
	s_cbranch_vccnz .LBB0_2206
	s_nop 0
	v_max_f32_e32 v16, v12, v12
	v_med3_f32 v17, v16, s63, v196
	v_max_f32_e32 v16, v13, v13
	v_med3_f32 v18, v16, s63, v196
	v_cvt_pk_fp8_f32 v16, v17, v18
	v_max_f32_e32 v19, v6, v6
	v_max_f32_e32 v18, v7, v7
	v_med3_f32 v17, v19, s63, v196
	v_med3_f32 v18, v18, s63, v196
	v_cvt_pk_fp8_f32 v16, v17, v18 op_sel:[0,0,1]
	v_max_f32_e32 v17, v14, v14
	v_med3_f32 v18, v17, s63, v196
	v_max_f32_e32 v17, v15, v15
	v_med3_f32 v19, v17, s63, v196
	v_cvt_pk_fp8_f32 v17, v18, v19
	v_max_f32_e32 v20, v8, v8
	v_max_f32_e32 v19, v9, v9
	v_med3_f32 v18, v20, s63, v196
	v_med3_f32 v19, v19, s63, v196
	v_cvt_pk_fp8_f32 v17, v18, v19 op_sel:[0,0,1]
	v_lshl_add_u64 v[18:19], s[70:71], 0, v[10:11]
	global_store_dwordx2 v[18:19], v[16:17], off
.LBB0_2206:
	v_or_b32_e32 v10, 0x80, v10
	s_waitcnt vmcnt(7)
	v_lshlrev_b32_e32 v16, 16, v2
	v_and_b32_e32 v17, 0xffff0000, v2
	v_lshlrev_b32_e32 v2, 16, v3
	v_and_b32_e32 v3, 0xffff0000, v3
	v_lshlrev_b32_e32 v18, 16, v4
	v_and_b32_e32 v19, 0xffff0000, v4
	v_lshlrev_b32_e32 v4, 16, v5
	v_and_b32_e32 v5, 0xffff0000, v5
	v_pk_fma_f32 v[2:3], v[40:41], s[20:21], v[2:3] op_sel_hi:[1,0,1]
	v_pk_fma_f32 v[16:17], v[38:39], s[20:21], v[16:17] op_sel_hi:[1,0,1]
	v_pk_fma_f32 v[4:5], v[36:37], s[20:21], v[4:5] op_sel_hi:[1,0,1]
	v_pk_fma_f32 v[18:19], v[34:35], s[20:21], v[18:19] op_sel_hi:[1,0,1]
	v_lshl_add_u64 v[24:25], v[10:11], 1, s[66:67]
	s_and_b64 vcc, exec, s[6:7]
	v_cvt_pk_bf16_f32 v20, v16, v17
	v_cvt_pk_bf16_f32 v21, v2, v3
	v_cvt_pk_bf16_f32 v22, v18, v19
	v_cvt_pk_bf16_f32 v23, v4, v5
	global_store_dwordx4 v[24:25], v[20:23], off
	s_cbranch_vccnz .LBB0_2208
	s_nop 0
	v_max_f32_e32 v20, v16, v16
	v_med3_f32 v21, v20, s63, v196
	v_max_f32_e32 v20, v17, v17
	v_med3_f32 v22, v20, s63, v196
	v_cvt_pk_fp8_f32 v20, v21, v22
	v_max_f32_e32 v23, v2, v2
	v_max_f32_e32 v22, v3, v3
	v_med3_f32 v21, v23, s63, v196
	v_med3_f32 v22, v22, s63, v196
	v_cvt_pk_fp8_f32 v20, v21, v22 op_sel:[0,0,1]
	v_max_f32_e32 v21, v18, v18
	v_med3_f32 v22, v21, s63, v196
	v_max_f32_e32 v21, v19, v19
	v_med3_f32 v23, v21, s63, v196
	v_cvt_pk_fp8_f32 v21, v22, v23
	v_max_f32_e32 v24, v4, v4
	v_max_f32_e32 v23, v5, v5
	v_med3_f32 v22, v24, s63, v196
	v_med3_f32 v23, v23, s63, v196
	v_cvt_pk_fp8_f32 v21, v22, v23 op_sel:[0,0,1]
	v_lshl_add_u64 v[10:11], s[70:71], 0, v[10:11]
	global_store_dwordx2 v[10:11], v[20:21], off

; __device__ __forceinline__ unsigned pk4_fp8(float a, float b, float c, float d) {
;     a = fminf(fmaxf(a, -448.f), 448.f); b = fminf(fmaxf(b, -448.f), 448.f); c = fminf(fmaxf(c, -448.f), 448.f); d = fminf(fmaxf(d, -448.f), 448.f);
;     int w = 0; w = __builtin_amdgcn_cvt_pk_fp8_f32(a, b, w, false); w = __builtin_amdgcn_cvt_pk_fp8_f32(c, d, w, true); return (unsigned)w;
;     __device__ __forceinline__ void operator()(const f32x4 (&acc)[2][2][4][2], const Unit& u, int wr, int wc, int fr, int fq) const {
;         const int row0 = u.pm * BM + wr * 64 + fr, col0 = u.pn * BM + wc * 32 + 8 * fq;
; #pragma unroll
;         for (int ai = 0; ai < 2; ++ai)
; #pragma unroll
;             for (int m = 0; m < 4; ++m) {
;                 const int row = row0 + ai * HALF + m * 16;
;                 const float rs = rsqrtf(ss[row] * (1.0f / 4096.0f) + RMS_EPS) * (1.0f / 64.0f);
;                 unsigned char* rowp = U + ((size_t)(row >> 4) * 512 + (col0 >> 5)) * 512 + (row & 15) * 32 + (col0 & 31);
; #pragma unroll
;                 for (int bj = 0; bj < 2; ++bj) {
;                     f32x4 v0 = acc[ai][bj][m][0] * rs, v1 = acc[ai][bj][m][1] * rs;
; #pragma unroll
;                     for (int j = 0; j < 4; ++j) { const float a = fmaxf(v0[j], 0.f), b = fmaxf(v1[j], 0.f); v0[j] = a * a * 4.f; v1[j] = b * b * 4.f; }
;                     u32x2 w; w.x = pk4_fp8(v0[0], v0[1], v0[2], v0[3]); w.y = pk4_fp8(v1[0], v1[1], v1[2], v1[3]);
;                     *(u32x2*)(rowp + bj * (HALF / 32) * 512) = w;
;                 }
.LBB0_2284:
	s_lshl_b32 s13, s20, 8
	s_add_i32 s13, s13, s36
	v_or_b32_e32 v2, s13, v1
	v_ashrrev_i32_e32 v3, 31, v2
	s_nop 15
	s_nop 15
	v_lshl_add_u64 v[4:5], v[2:3], 2, s[2:3]
	s_lshl_b32 s15, s21, 8
	s_or_b32 s15, s15, s37
	s_ashr_i32 s20, s15, 5
	s_ashr_i32 s22, s13, 4
	s_ashr_i32 s21, s20, 31
	s_ashr_i32 s23, s22, 31
	s_lshl_b64 s[20:21], s[20:21], 9
	s_lshl_b64 s[22:23], s[22:23], 18
	v_readlane_b32 s24, v253, 46
	v_readlane_b32 s25, v253, 47
	s_add_u32 s13, s24, s22
	s_addc_u32 s15, s25, s23
	s_add_u32 s22, s13, s20
	s_addc_u32 s23, s15, s21
	s_waitcnt vmcnt(0)
	v_fmamk_f32 v3, v234, 0x39800000, v194
	v_mul_f32_e32 v9, 0x4b800000, v3
	v_cmp_gt_f32_e32 vcc, s43, v3
	s_nop 1
	v_cndmask_b32_e32 v3, v3, v9, vcc
	v_rsq_f32_e32 v3, v3
	s_nop 0
	v_mul_f32_e32 v9, 0x45800000, v3
	v_cndmask_b32_e32 v3, v3, v9, vcc
	v_mul_f32_e32 v10, 0x3d000000, v3
	v_pk_mul_f32 v[14:15], v[158:159], v[10:11] op_sel_hi:[1,0]
	v_pk_mul_f32 v[18:19], v[154:155], v[10:11] op_sel_hi:[1,0]
	v_pk_mul_f32 v[12:13], v[160:161], v[10:11] op_sel_hi:[1,0]
	v_pk_mul_f32 v[16:17], v[156:157], v[10:11] op_sel_hi:[1,0]
	v_pk_mul_f32 v[20:21], v[152:153], v[10:11] op_sel_hi:[1,0]
	v_pk_mul_f32 v[22:23], v[150:151], v[10:11] op_sel_hi:[1,0]
	v_pk_mul_f32 v[24:25], v[148:149], v[10:11] op_sel_hi:[1,0]
	v_pk_mul_f32 v[10:11], v[146:147], v[10:11] op_sel_hi:[1,0]
	v_max_f32_e32 v3, 0, v14
	v_max_f32_e32 v9, 0, v18
	v_max_f32_e32 v14, 0, v15
	v_max_f32_e32 v15, 0, v19
	v_max_f32_e32 v18, 0, v22
	v_max_f32_e32 v10, 0, v10
	v_max_f32_e32 v19, 0, v23
	v_max_f32_e32 v11, 0, v11
	v_mul_f32_e32 v3, v3, v3
	v_mul_f32_e32 v9, v9, v9
	v_mul_f32_e32 v14, v14, v14
	v_mul_f32_e32 v15, v15, v15
	v_mul_f32_e32 v18, v18, v18
	v_mul_f32_e32 v10, v10, v10
	v_mul_f32_e32 v19, v19, v19
	v_mul_f32_e32 v11, v11, v11
	v_med3_f32 v3, v3, s44, v195
	v_med3_f32 v14, v14, s44, v195
	v_med3_f32 v9, v9, s44, v195
	v_med3_f32 v15, v15, s44, v195
	v_max_f32_e32 v12, 0, v12
	v_max_f32_e32 v16, 0, v16
	v_max_f32_e32 v13, 0, v13
	v_max_f32_e32 v17, 0, v17
	v_med3_f32 v18, v18, s44, v195
	v_med3_f32 v19, v19, s44, v195
	v_med3_f32 v10, v10, s44, v195
	v_cvt_pk_fp8_f32 v6, v3, v14
	v_cvt_pk_fp8_f32 v7, v9, v15
	v_med3_f32 v3, v11, s44, v195
	v_max_f32_e32 v20, 0, v20
	v_max_f32_e32 v22, 0, v24
	v_max_f32_e32 v21, 0, v21
	v_max_f32_e32 v23, 0, v25
	v_mul_f32_e32 v12, v12, v12
	v_mul_f32_e32 v16, v16, v16
	v_mul_f32_e32 v13, v13, v13
	v_mul_f32_e32 v17, v17, v17
	v_cvt_pk_fp8_f32 v8, v18, v19
	v_cvt_pk_fp8_f32 v9, v10, v3
	v_mul_f32_e32 v20, v20, v20
	v_mul_f32_e32 v22, v22, v22
	v_mul_f32_e32 v21, v21, v21
	v_mul_f32_e32 v23, v23, v23
	v_med3_f32 v12, v12, s44, v195
	v_med3_f32 v13, v13, s44, v195
	v_med3_f32 v16, v16, s44, v195
	v_med3_f32 v17, v17, s44, v195
	v_med3_f32 v20, v20, s44, v195
	v_med3_f32 v21, v21, s44, v195
	v_cvt_pk_fp8_f32 v6, v12, v13 op_sel:[0,0,1]
	v_cvt_pk_fp8_f32 v7, v16, v17 op_sel:[0,0,1]
	v_med3_f32 v3, v22, s44, v195
	v_med3_f32 v10, v23, s44, v195
	v_cvt_pk_fp8_f32 v8, v20, v21 op_sel:[0,0,1]
	v_cvt_pk_fp8_f32 v9, v3, v10 op_sel:[0,0,1]
	v_lshl_add_u64 v[10:11], s[22:23], 0, v[172:173]
	v_lshl_add_u64 v[10:11], v[10:11], 0, v[170:171]
	global_store_dwordx2 v[10:11], v[6:7], off
	global_store_dwordx2 v[10:11], v[8:9], off offset:2048
	v_or_b32_e32 v6, 16, v2
	v_ashrrev_i32_e32 v7, 31, v6
	v_lshl_add_u64 v[8:9], v[6:7], 2, s[2:3]
	v_ashrrev_i32_e32 v6, 4, v6
	v_ashrrev_i32_e32 v7, 31, v6
	v_lshlrev_b64 v[6:7], 18, v[6:7]
	v_lshl_add_u64 v[6:7], s[24:25], 0, v[6:7]
	v_lshl_add_u64 v[6:7], v[6:7], 0, s[20:21]
	v_lshl_add_u64 v[6:7], v[6:7], 0, v[172:173]
	v_lshl_add_u64 v[6:7], v[6:7], 0, v[170:171]
	v_fmamk_f32 v3, v235, 0x39800000, v194
	v_mul_f32_e32 v11, 0x4b800000, v3
	v_cmp_gt_f32_e32 vcc, s43, v3
	s_nop 1
	v_cndmask_b32_e32 v3, v3, v11, vcc
	v_rsq_f32_e32 v3, v3
	s_nop 0
	v_mul_f32_e32 v11, 0x45800000, v3
	v_cndmask_b32_e32 v3, v3, v11, vcc
	v_mul_f32_e32 v12, 0x3d000000, v3
	v_pk_mul_f32 v[16:17], v[142:143], v[12:13] op_sel_hi:[1,0]
	v_pk_mul_f32 v[20:21], v[138:139], v[12:13] op_sel_hi:[1,0]
	v_pk_mul_f32 v[14:15], v[144:145], v[12:13] op_sel_hi:[1,0]
	v_pk_mul_f32 v[18:19], v[140:141], v[12:13] op_sel_hi:[1,0]
	v_pk_mul_f32 v[22:23], v[136:137], v[12:13] op_sel_hi:[1,0]
	v_pk_mul_f32 v[24:25], v[134:135], v[12:13] op_sel_hi:[1,0]
	v_pk_mul_f32 v[26:27], v[132:133], v[12:13] op_sel_hi:[1,0]
	v_pk_mul_f32 v[12:13], v[130:131], v[12:13] op_sel_hi:[1,0]
	v_max_f32_e32 v3, 0, v16
	v_max_f32_e32 v11, 0, v20
	v_max_f32_e32 v16, 0, v17
	v_max_f32_e32 v17, 0, v21
	v_max_f32_e32 v20, 0, v24
	v_max_f32_e32 v12, 0, v12
	v_max_f32_e32 v21, 0, v25
	v_max_f32_e32 v13, 0, v13
	v_mul_f32_e32 v3, v3, v3
	v_mul_f32_e32 v11, v11, v11
	v_mul_f32_e32 v16, v16, v16
	v_mul_f32_e32 v17, v17, v17
	v_mul_f32_e32 v20, v20, v20
	v_mul_f32_e32 v12, v12, v12
	v_mul_f32_e32 v21, v21, v21
	v_mul_f32_e32 v13, v13, v13
	v_med3_f32 v3, v3, s44, v195
	v_med3_f32 v16, v16, s44, v195
	v_med3_f32 v11, v11, s44, v195
	v_med3_f32 v17, v17, s44, v195
	v_max_f32_e32 v14, 0, v14
	v_max_f32_e32 v18, 0, v18
	v_max_f32_e32 v15, 0, v15
	v_max_f32_e32 v19, 0, v19
	v_med3_f32 v20, v20, s44, v195
	v_med3_f32 v21, v21, s44, v195
	v_cvt_pk_fp8_f32 v8, v3, v16
	v_cvt_pk_fp8_f32 v9, v11, v17
	v_med3_f32 v3, v12, s44, v195
	v_med3_f32 v12, v13, s44, v195
	v_max_f32_e32 v22, 0, v22
	v_max_f32_e32 v24, 0, v26
	v_max_f32_e32 v23, 0, v23
	v_max_f32_e32 v25, 0, v27
	v_mul_f32_e32 v14, v14, v14
	v_mul_f32_e32 v18, v18, v18
	v_mul_f32_e32 v15, v15, v15
	v_mul_f32_e32 v19, v19, v19
	v_cvt_pk_fp8_f32 v10, v20, v21
	v_cvt_pk_fp8_f32 v11, v3, v12
	v_mul_f32_e32 v22, v22, v22
	v_mul_f32_e32 v24, v24, v24
	v_mul_f32_e32 v23, v23, v23
; __device__ __forceinline__ unsigned pk4_fp8(float a, float b, float c, float d) {
;     a = fminf(fmaxf(a, -448.f), 448.f); b = fminf(fmaxf(b, -448.f), 448.f); c = fminf(fmaxf(c, -448.f), 448.f); d = fminf(fmaxf(d, -448.f), 448.f);
;     int w = 0; w = __builtin_amdgcn_cvt_pk_fp8_f32(a, b, w, false); w = __builtin_amdgcn_cvt_pk_fp8_f32(c, d, w, true); return (unsigned)w;
;     __device__ __forceinline__ void operator()(const f32x4 (&acc)[2][2][4][2], const Unit& u, int wr, int wc, int fr, int fq) const {
;         const int row0 = u.pm * BM + wr * 64 + fr, col0 = u.pn * BM + wc * 32 + 8 * fq;
; #pragma unroll
;         for (int ai = 0; ai < 2; ++ai)
; #pragma unroll
;             for (int m = 0; m < 4; ++m) {
;                 const int row = row0 + ai * HALF + m * 16;
;                 const float rs = rsqrtf(ss[row] * (1.0f / 4096.0f) + RMS_EPS) * (1.0f / 64.0f);
;                 unsigned char* rowp = U + ((size_t)(row >> 4) * 512 + (col0 >> 5)) * 512 + (row & 15) * 32 + (col0 & 31);
; #pragma unroll
;                 for (int bj = 0; bj < 2; ++bj) {
;                     f32x4 v0 = acc[ai][bj][m][0] * rs, v1 = acc[ai][bj][m][1] * rs;
; #pragma unroll
;                     for (int j = 0; j < 4; ++j) { const float a = fmaxf(v0[j], 0.f), b = fmaxf(v1[j], 0.f); v0[j] = a * a * 4.f; v1[j] = b * b * 4.f; }
;                     u32x2 w; w.x = pk4_fp8(v0[0], v0[1], v0[2], v0[3]); w.y = pk4_fp8(v1[0], v1[1], v1[2], v1[3]);
;                     *(u32x2*)(rowp + bj * (HALF / 32) * 512) = w;
;                 }
	v_mul_f32_e32 v25, v25, v25
	v_med3_f32 v14, v14, s44, v195
	v_med3_f32 v15, v15, s44, v195
	v_med3_f32 v18, v18, s44, v195
	v_med3_f32 v19, v19, s44, v195
	v_med3_f32 v22, v22, s44, v195
	v_med3_f32 v23, v23, s44, v195
	v_cvt_pk_fp8_f32 v8, v14, v15 op_sel:[0,0,1]
	v_cvt_pk_fp8_f32 v9, v18, v19 op_sel:[0,0,1]
	v_med3_f32 v3, v24, s44, v195
	v_med3_f32 v12, v25, s44, v195
	v_cvt_pk_fp8_f32 v10, v22, v23 op_sel:[0,0,1]
	v_cvt_pk_fp8_f32 v11, v3, v12 op_sel:[0,0,1]
	global_store_dwordx2 v[6:7], v[8:9], off
	global_store_dwordx2 v[6:7], v[10:11], off offset:2048
	v_or_b32_e32 v6, 32, v2
	v_ashrrev_i32_e32 v7, 31, v6
	v_lshl_add_u64 v[8:9], v[6:7], 2, s[2:3]
	v_ashrrev_i32_e32 v6, 4, v6
	v_ashrrev_i32_e32 v7, 31, v6
	v_lshlrev_b64 v[6:7], 18, v[6:7]
	v_lshl_add_u64 v[6:7], s[24:25], 0, v[6:7]
	v_lshl_add_u64 v[6:7], v[6:7], 0, s[20:21]
	v_lshl_add_u64 v[6:7], v[6:7], 0, v[172:173]
	v_lshl_add_u64 v[6:7], v[6:7], 0, v[170:171]
	v_fmamk_f32 v3, v236, 0x39800000, v194
	v_mul_f32_e32 v11, 0x4b800000, v3
	v_cmp_gt_f32_e32 vcc, s43, v3
	s_nop 1
	v_cndmask_b32_e32 v3, v3, v11, vcc
	v_rsq_f32_e32 v3, v3
	s_nop 0
	v_mul_f32_e32 v11, 0x45800000, v3
	v_cndmask_b32_e32 v3, v3, v11, vcc
	v_mul_f32_e32 v12, 0x3d000000, v3
	v_pk_mul_f32 v[16:17], v[126:127], v[12:13] op_sel_hi:[1,0]
	v_pk_mul_f32 v[20:21], v[122:123], v[12:13] op_sel_hi:[1,0]
	v_pk_mul_f32 v[24:25], v[118:119], v[12:13] op_sel_hi:[1,0]
	v_pk_mul_f32 v[14:15], v[128:129], v[12:13] op_sel_hi:[1,0]
	v_pk_mul_f32 v[18:19], v[124:125], v[12:13] op_sel_hi:[1,0]
	v_pk_mul_f32 v[22:23], v[120:121], v[12:13] op_sel_hi:[1,0]
	v_pk_mul_f32 v[26:27], v[116:117], v[12:13] op_sel_hi:[1,0]
	v_pk_mul_f32 v[12:13], v[114:115], v[12:13] op_sel_hi:[1,0]
	v_max_f32_e32 v3, 0, v16
	v_max_f32_e32 v11, 0, v20
	v_max_f32_e32 v16, 0, v17
	v_max_f32_e32 v17, 0, v21
	v_max_f32_e32 v20, 0, v24
	v_max_f32_e32 v21, 0, v25
	v_max_f32_e32 v12, 0, v12
	v_max_f32_e32 v13, 0, v13
	v_mul_f32_e32 v3, v3, v3
	v_mul_f32_e32 v11, v11, v11
	v_mul_f32_e32 v16, v16, v16
	v_mul_f32_e32 v17, v17, v17
	v_mul_f32_e32 v20, v20, v20
	v_mul_f32_e32 v21, v21, v21
	v_mul_f32_e32 v12, v12, v12
	v_mul_f32_e32 v13, v13, v13
	v_med3_f32 v3, v3, s44, v195
	v_med3_f32 v16, v16, s44, v195
	v_med3_f32 v11, v11, s44, v195
	v_med3_f32 v17, v17, s44, v195
	v_med3_f32 v20, v20, s44, v195
	v_med3_f32 v21, v21, s44, v195
	v_max_f32_e32 v14, 0, v14
	v_max_f32_e32 v18, 0, v18
	v_max_f32_e32 v15, 0, v15
	v_max_f32_e32 v19, 0, v19
	v_max_f32_e32 v22, 0, v22
	v_max_f32_e32 v23, 0, v23
	v_cvt_pk_fp8_f32 v8, v3, v16
	v_cvt_pk_fp8_f32 v9, v11, v17
	v_cvt_pk_fp8_f32 v10, v20, v21
	v_med3_f32 v12, v12, s44, v195
	v_med3_f32 v13, v13, s44, v195
	v_max_f32_e32 v24, 0, v26
	v_max_f32_e32 v25, 0, v27
	v_mul_f32_e32 v14, v14, v14
	v_mul_f32_e32 v18, v18, v18
	v_mul_f32_e32 v15, v15, v15
	v_mul_f32_e32 v19, v19, v19
	v_mul_f32_e32 v22, v22, v22
	v_mul_f32_e32 v23, v23, v23
	v_cvt_pk_fp8_f32 v11, v12, v13
	v_mul_f32_e32 v24, v24, v24
	v_mul_f32_e32 v25, v25, v25
	v_med3_f32 v14, v14, s44, v195
	v_med3_f32 v15, v15, s44, v195
	v_med3_f32 v18, v18, s44, v195
	v_med3_f32 v19, v19, s44, v195
	v_med3_f32 v22, v22, s44, v195
	v_med3_f32 v3, v23, s44, v195
	v_cvt_pk_fp8_f32 v8, v14, v15 op_sel:[0,0,1]
	v_cvt_pk_fp8_f32 v9, v18, v19 op_sel:[0,0,1]
	v_cvt_pk_fp8_f32 v10, v22, v3 op_sel:[0,0,1]
	v_med3_f32 v3, v24, s44, v195
	v_med3_f32 v12, v25, s44, v195
	v_cvt_pk_fp8_f32 v11, v3, v12 op_sel:[0,0,1]
	global_store_dwordx2 v[6:7], v[8:9], off
	global_store_dwordx2 v[6:7], v[10:11], off offset:2048
	v_or_b32_e32 v6, 48, v2
	v_ashrrev_i32_e32 v7, 31, v6
	v_lshl_add_u64 v[8:9], v[6:7], 2, s[2:3]
	v_ashrrev_i32_e32 v6, 4, v6
	v_ashrrev_i32_e32 v7, 31, v6
	v_lshlrev_b64 v[6:7], 18, v[6:7]
	v_lshl_add_u64 v[6:7], s[24:25], 0, v[6:7]
	v_lshl_add_u64 v[6:7], v[6:7], 0, s[20:21]
	v_lshl_add_u64 v[6:7], v[6:7], 0, v[172:173]
	v_lshl_add_u64 v[6:7], v[6:7], 0, v[170:171]
	v_fmamk_f32 v3, v237, 0x39800000, v194
	v_mul_f32_e32 v11, 0x4b800000, v3
	v_cmp_gt_f32_e32 vcc, s43, v3
	s_nop 1
	v_cndmask_b32_e32 v3, v3, v11, vcc
	v_rsq_f32_e32 v3, v3
	s_nop 0
	v_mul_f32_e32 v11, 0x45800000, v3
	v_cndmask_b32_e32 v3, v3, v11, vcc
	v_mul_f32_e32 v12, 0x3d000000, v3
	v_pk_mul_f32 v[16:17], v[110:111], v[12:13] op_sel_hi:[1,0]
	v_pk_mul_f32 v[20:21], v[106:107], v[12:13] op_sel_hi:[1,0]
	v_pk_mul_f32 v[24:25], v[102:103], v[12:13] op_sel_hi:[1,0]
	v_pk_mul_f32 v[14:15], v[112:113], v[12:13] op_sel_hi:[1,0]
	v_pk_mul_f32 v[18:19], v[108:109], v[12:13] op_sel_hi:[1,0]
	v_pk_mul_f32 v[22:23], v[104:105], v[12:13] op_sel_hi:[1,0]
	v_pk_mul_f32 v[26:27], v[100:101], v[12:13] op_sel_hi:[1,0]
	v_pk_mul_f32 v[12:13], v[98:99], v[12:13] op_sel_hi:[1,0]
	v_max_f32_e32 v3, 0, v16
	v_max_f32_e32 v11, 0, v20
	v_max_f32_e32 v16, 0, v17
	v_max_f32_e32 v17, 0, v21
	v_max_f32_e32 v20, 0, v24
	v_max_f32_e32 v21, 0, v25
	v_max_f32_e32 v12, 0, v12
	v_max_f32_e32 v13, 0, v13
	v_mul_f32_e32 v3, v3, v3
	v_mul_f32_e32 v11, v11, v11
	v_mul_f32_e32 v16, v16, v16
	v_mul_f32_e32 v17, v17, v17
	v_mul_f32_e32 v20, v20, v20
	v_mul_f32_e32 v21, v21, v21
	v_mul_f32_e32 v12, v12, v12
	v_mul_f32_e32 v13, v13, v13
	v_med3_f32 v3, v3, s44, v195
	v_med3_f32 v16, v16, s44, v195
	v_med3_f32 v11, v11, s44, v195
	v_med3_f32 v17, v17, s44, v195
	v_med3_f32 v20, v20, s44, v195
	v_med3_f32 v21, v21, s44, v195
	v_max_f32_e32 v14, 0, v14
	v_max_f32_e32 v18, 0, v18
	v_max_f32_e32 v15, 0, v15
	v_max_f32_e32 v19, 0, v19
	v_max_f32_e32 v22, 0, v22
	v_max_f32_e32 v23, 0, v23
	v_cvt_pk_fp8_f32 v8, v3, v16
	v_cvt_pk_fp8_f32 v9, v11, v17
	v_cvt_pk_fp8_f32 v10, v20, v21
	v_med3_f32 v12, v12, s44, v195
	v_med3_f32 v13, v13, s44, v195
	v_max_f32_e32 v24, 0, v26
; __device__ __forceinline__ unsigned pk4_fp8(float a, float b, float c, float d) {
;     a = fminf(fmaxf(a, -448.f), 448.f); b = fminf(fmaxf(b, -448.f), 448.f); c = fminf(fmaxf(c, -448.f), 448.f); d = fminf(fmaxf(d, -448.f), 448.f);
;     int w = 0; w = __builtin_amdgcn_cvt_pk_fp8_f32(a, b, w, false); w = __builtin_amdgcn_cvt_pk_fp8_f32(c, d, w, true); return (unsigned)w;
;     __device__ __forceinline__ void operator()(const f32x4 (&acc)[2][2][4][2], const Unit& u, int wr, int wc, int fr, int fq) const {
;         const int row0 = u.pm * BM + wr * 64 + fr, col0 = u.pn * BM + wc * 32 + 8 * fq;
; #pragma unroll
;         for (int ai = 0; ai < 2; ++ai)
; #pragma unroll
;             for (int m = 0; m < 4; ++m) {
;                 const int row = row0 + ai * HALF + m * 16;
;                 const float rs = rsqrtf(ss[row] * (1.0f / 4096.0f) + RMS_EPS) * (1.0f / 64.0f);
;                 unsigned char* rowp = U + ((size_t)(row >> 4) * 512 + (col0 >> 5)) * 512 + (row & 15) * 32 + (col0 & 31);
; #pragma unroll
;                 for (int bj = 0; bj < 2; ++bj) {
;                     f32x4 v0 = acc[ai][bj][m][0] * rs, v1 = acc[ai][bj][m][1] * rs;
; #pragma unroll
;                     for (int j = 0; j < 4; ++j) { const float a = fmaxf(v0[j], 0.f), b = fmaxf(v1[j], 0.f); v0[j] = a * a * 4.f; v1[j] = b * b * 4.f; }
;                     u32x2 w; w.x = pk4_fp8(v0[0], v0[1], v0[2], v0[3]); w.y = pk4_fp8(v1[0], v1[1], v1[2], v1[3]);
;                     *(u32x2*)(rowp + bj * (HALF / 32) * 512) = w;
;                 }
	v_max_f32_e32 v25, 0, v27
	v_mul_f32_e32 v14, v14, v14
	v_mul_f32_e32 v18, v18, v18
	v_mul_f32_e32 v15, v15, v15
	v_mul_f32_e32 v19, v19, v19
	v_mul_f32_e32 v22, v22, v22
	v_mul_f32_e32 v23, v23, v23
	v_cvt_pk_fp8_f32 v11, v12, v13
	v_mul_f32_e32 v24, v24, v24
	v_mul_f32_e32 v25, v25, v25
	v_med3_f32 v14, v14, s44, v195
	v_med3_f32 v15, v15, s44, v195
	v_med3_f32 v18, v18, s44, v195
	v_med3_f32 v19, v19, s44, v195
	v_med3_f32 v3, v22, s44, v195
	v_med3_f32 v16, v23, s44, v195
	v_cvt_pk_fp8_f32 v8, v14, v15 op_sel:[0,0,1]
	v_cvt_pk_fp8_f32 v9, v18, v19 op_sel:[0,0,1]
	v_cvt_pk_fp8_f32 v10, v3, v16 op_sel:[0,0,1]
	v_med3_f32 v3, v24, s44, v195
	v_med3_f32 v12, v25, s44, v195
	v_cvt_pk_fp8_f32 v11, v3, v12 op_sel:[0,0,1]
	global_store_dwordx2 v[6:7], v[8:9], off
	global_store_dwordx2 v[6:7], v[10:11], off offset:2048
	v_add_u32_e32 v9, 0x80, v2
	v_ashrrev_i32_e32 v10, 4, v9
	v_ashrrev_i32_e32 v11, 31, v10
	v_lshlrev_b64 v[10:11], 18, v[10:11]
	v_lshl_add_u64 v[10:11], s[24:25], 0, v[10:11]
	v_lshl_add_u64 v[10:11], v[10:11], 0, s[20:21]
	v_lshl_add_u64 v[10:11], v[10:11], 0, v[172:173]
	v_lshl_add_u64 v[10:11], v[10:11], 0, v[170:171]
	v_fmamk_f32 v3, v238, 0x39800000, v194
	v_mul_f32_e32 v9, 0x4b800000, v3
	v_cmp_gt_f32_e32 vcc, s43, v3
	s_nop 1
	v_cndmask_b32_e32 v3, v3, v9, vcc
	v_rsq_f32_e32 v3, v3
	s_nop 0
	v_mul_f32_e32 v9, 0x45800000, v3
	v_cndmask_b32_e32 v3, v3, v9, vcc
	v_mul_f32_e32 v12, 0x3d000000, v3
	v_pk_mul_f32 v[16:17], v[94:95], v[12:13] op_sel_hi:[1,0]
	v_pk_mul_f32 v[20:21], v[90:91], v[12:13] op_sel_hi:[1,0]
	v_pk_mul_f32 v[24:25], v[86:87], v[12:13] op_sel_hi:[1,0]
	v_pk_mul_f32 v[14:15], v[96:97], v[12:13] op_sel_hi:[1,0]
	v_pk_mul_f32 v[18:19], v[92:93], v[12:13] op_sel_hi:[1,0]
	v_pk_mul_f32 v[22:23], v[88:89], v[12:13] op_sel_hi:[1,0]
	v_pk_mul_f32 v[26:27], v[84:85], v[12:13] op_sel_hi:[1,0]
	v_pk_mul_f32 v[12:13], v[82:83], v[12:13] op_sel_hi:[1,0]
	v_max_f32_e32 v3, 0, v16
	v_max_f32_e32 v9, 0, v20
	v_max_f32_e32 v16, 0, v17
	v_max_f32_e32 v17, 0, v21
	v_max_f32_e32 v20, 0, v24
	v_max_f32_e32 v21, 0, v25
	v_max_f32_e32 v12, 0, v12
	v_max_f32_e32 v13, 0, v13
	v_mul_f32_e32 v3, v3, v3
	v_mul_f32_e32 v9, v9, v9
	v_mul_f32_e32 v16, v16, v16
	v_mul_f32_e32 v17, v17, v17
	v_mul_f32_e32 v20, v20, v20
	v_mul_f32_e32 v21, v21, v21
	v_mul_f32_e32 v12, v12, v12
	v_mul_f32_e32 v13, v13, v13
	v_med3_f32 v3, v3, s44, v195
	v_med3_f32 v16, v16, s44, v195
	v_med3_f32 v9, v9, s44, v195
	v_med3_f32 v17, v17, s44, v195
	v_med3_f32 v20, v20, s44, v195
	v_med3_f32 v21, v21, s44, v195
	v_max_f32_e32 v14, 0, v14
	v_max_f32_e32 v18, 0, v18
	v_max_f32_e32 v15, 0, v15
	v_max_f32_e32 v19, 0, v19
	v_max_f32_e32 v22, 0, v22
	v_max_f32_e32 v23, 0, v23
	v_cvt_pk_fp8_f32 v6, v3, v16
	v_cvt_pk_fp8_f32 v7, v9, v17
	v_cvt_pk_fp8_f32 v8, v20, v21
	v_med3_f32 v12, v12, s44, v195
	v_med3_f32 v13, v13, s44, v195
	v_max_f32_e32 v24, 0, v26
	v_max_f32_e32 v25, 0, v27
	v_mul_f32_e32 v14, v14, v14
	v_mul_f32_e32 v18, v18, v18
	v_mul_f32_e32 v15, v15, v15
	v_mul_f32_e32 v19, v19, v19
	v_mul_f32_e32 v22, v22, v22
	v_mul_f32_e32 v23, v23, v23
	v_cvt_pk_fp8_f32 v9, v12, v13
	v_mul_f32_e32 v24, v24, v24
	v_mul_f32_e32 v25, v25, v25
	v_med3_f32 v14, v14, s44, v195
	v_med3_f32 v15, v15, s44, v195
	v_med3_f32 v18, v18, s44, v195
	v_med3_f32 v19, v19, s44, v195
	v_med3_f32 v22, v22, s44, v195
	v_med3_f32 v3, v23, s44, v195
	v_cvt_pk_fp8_f32 v6, v14, v15 op_sel:[0,0,1]
	v_cvt_pk_fp8_f32 v7, v18, v19 op_sel:[0,0,1]
	v_cvt_pk_fp8_f32 v8, v22, v3 op_sel:[0,0,1]
	v_med3_f32 v3, v24, s44, v195
	v_med3_f32 v12, v25, s44, v195
	v_cvt_pk_fp8_f32 v9, v3, v12 op_sel:[0,0,1]
	global_store_dwordx2 v[10:11], v[6:7], off
	global_store_dwordx2 v[10:11], v[8:9], off offset:2048
	v_add_u32_e32 v9, 0x90, v2
	v_ashrrev_i32_e32 v10, 4, v9
	v_ashrrev_i32_e32 v11, 31, v10
	v_lshlrev_b64 v[10:11], 18, v[10:11]
	v_lshl_add_u64 v[10:11], s[24:25], 0, v[10:11]
	v_lshl_add_u64 v[10:11], v[10:11], 0, s[20:21]
	v_lshl_add_u64 v[10:11], v[10:11], 0, v[172:173]
	v_lshl_add_u64 v[10:11], v[10:11], 0, v[170:171]
	v_fmamk_f32 v3, v239, 0x39800000, v194
	v_mul_f32_e32 v9, 0x4b800000, v3
	v_cmp_gt_f32_e32 vcc, s43, v3
	s_nop 1
	v_cndmask_b32_e32 v3, v3, v9, vcc
	v_rsq_f32_e32 v3, v3
	s_nop 0
	v_mul_f32_e32 v9, 0x45800000, v3
	v_cndmask_b32_e32 v3, v3, v9, vcc
	v_mul_f32_e32 v12, 0x3d000000, v3
	v_pk_mul_f32 v[16:17], v[78:79], v[12:13] op_sel_hi:[1,0]
	v_pk_mul_f32 v[20:21], v[74:75], v[12:13] op_sel_hi:[1,0]
	v_pk_mul_f32 v[14:15], v[80:81], v[12:13] op_sel_hi:[1,0]
	v_pk_mul_f32 v[18:19], v[76:77], v[12:13] op_sel_hi:[1,0]
	v_pk_mul_f32 v[22:23], v[72:73], v[12:13] op_sel_hi:[1,0]
	v_pk_mul_f32 v[24:25], v[70:71], v[12:13] op_sel_hi:[1,0]
	v_pk_mul_f32 v[26:27], v[68:69], v[12:13] op_sel_hi:[1,0]
	v_pk_mul_f32 v[12:13], v[66:67], v[12:13] op_sel_hi:[1,0]
	v_max_f32_e32 v3, 0, v16
	v_max_f32_e32 v9, 0, v20
	v_max_f32_e32 v16, 0, v17
	v_max_f32_e32 v17, 0, v21
	v_max_f32_e32 v20, 0, v24
	v_max_f32_e32 v12, 0, v12
	v_max_f32_e32 v21, 0, v25
	v_max_f32_e32 v13, 0, v13
	v_mul_f32_e32 v3, v3, v3
	v_mul_f32_e32 v9, v9, v9
	v_mul_f32_e32 v16, v16, v16
	v_mul_f32_e32 v17, v17, v17
	v_mul_f32_e32 v20, v20, v20
	v_mul_f32_e32 v12, v12, v12
	v_mul_f32_e32 v21, v21, v21
	v_mul_f32_e32 v13, v13, v13
	v_med3_f32 v3, v3, s44, v195
	v_med3_f32 v16, v16, s44, v195
	v_med3_f32 v9, v9, s44, v195
	v_med3_f32 v17, v17, s44, v195
	v_max_f32_e32 v14, 0, v14
	v_max_f32_e32 v18, 0, v18
	v_max_f32_e32 v15, 0, v15
	v_max_f32_e32 v19, 0, v19
	v_med3_f32 v20, v20, s44, v195
	v_med3_f32 v21, v21, s44, v195
	v_cvt_pk_fp8_f32 v6, v3, v16
	v_cvt_pk_fp8_f32 v7, v9, v17
	v_med3_f32 v3, v12, s44, v195
	v_med3_f32 v12, v13, s44, v195
; __device__ __forceinline__ unsigned pk4_fp8(float a, float b, float c, float d) {
;     a = fminf(fmaxf(a, -448.f), 448.f); b = fminf(fmaxf(b, -448.f), 448.f); c = fminf(fmaxf(c, -448.f), 448.f); d = fminf(fmaxf(d, -448.f), 448.f);
;     int w = 0; w = __builtin_amdgcn_cvt_pk_fp8_f32(a, b, w, false); w = __builtin_amdgcn_cvt_pk_fp8_f32(c, d, w, true); return (unsigned)w;
;     __device__ __forceinline__ void operator()(const f32x4 (&acc)[2][2][4][2], const Unit& u, int wr, int wc, int fr, int fq) const {
;         const int row0 = u.pm * BM + wr * 64 + fr, col0 = u.pn * BM + wc * 32 + 8 * fq;
; #pragma unroll
;         for (int ai = 0; ai < 2; ++ai)
; #pragma unroll
;             for (int m = 0; m < 4; ++m) {
;                 const int row = row0 + ai * HALF + m * 16;
;                 const float rs = rsqrtf(ss[row] * (1.0f / 4096.0f) + RMS_EPS) * (1.0f / 64.0f);
;                 unsigned char* rowp = U + ((size_t)(row >> 4) * 512 + (col0 >> 5)) * 512 + (row & 15) * 32 + (col0 & 31);
; #pragma unroll
;                 for (int bj = 0; bj < 2; ++bj) {
;                     f32x4 v0 = acc[ai][bj][m][0] * rs, v1 = acc[ai][bj][m][1] * rs;
; #pragma unroll
;                     for (int j = 0; j < 4; ++j) { const float a = fmaxf(v0[j], 0.f), b = fmaxf(v1[j], 0.f); v0[j] = a * a * 4.f; v1[j] = b * b * 4.f; }
;                     u32x2 w; w.x = pk4_fp8(v0[0], v0[1], v0[2], v0[3]); w.y = pk4_fp8(v1[0], v1[1], v1[2], v1[3]);
;                     *(u32x2*)(rowp + bj * (HALF / 32) * 512) = w;
;                 }
	v_max_f32_e32 v22, 0, v22
	v_max_f32_e32 v24, 0, v26
	v_max_f32_e32 v23, 0, v23
	v_max_f32_e32 v25, 0, v27
	v_mul_f32_e32 v14, v14, v14
	v_mul_f32_e32 v18, v18, v18
	v_mul_f32_e32 v15, v15, v15
	v_mul_f32_e32 v19, v19, v19
	v_cvt_pk_fp8_f32 v8, v20, v21
	v_cvt_pk_fp8_f32 v9, v3, v12
	v_mul_f32_e32 v22, v22, v22
	v_mul_f32_e32 v24, v24, v24
	v_mul_f32_e32 v23, v23, v23
	v_mul_f32_e32 v25, v25, v25
	v_med3_f32 v14, v14, s44, v195
	v_med3_f32 v15, v15, s44, v195
	v_med3_f32 v18, v18, s44, v195
	v_med3_f32 v19, v19, s44, v195
	v_med3_f32 v22, v22, s44, v195
	v_med3_f32 v23, v23, s44, v195
	v_cvt_pk_fp8_f32 v6, v14, v15 op_sel:[0,0,1]
	v_cvt_pk_fp8_f32 v7, v18, v19 op_sel:[0,0,1]
	v_med3_f32 v3, v24, s44, v195
	v_med3_f32 v12, v25, s44, v195
	v_cvt_pk_fp8_f32 v8, v22, v23 op_sel:[0,0,1]
	v_cvt_pk_fp8_f32 v9, v3, v12 op_sel:[0,0,1]
	global_store_dwordx2 v[10:11], v[6:7], off
	global_store_dwordx2 v[10:11], v[8:9], off offset:2048
	v_add_u32_e32 v9, 0xa0, v2
	v_ashrrev_i32_e32 v10, 4, v9
	v_ashrrev_i32_e32 v11, 31, v10
	v_lshlrev_b64 v[10:11], 18, v[10:11]
	v_lshl_add_u64 v[10:11], s[24:25], 0, v[10:11]
	v_lshl_add_u64 v[10:11], v[10:11], 0, s[20:21]
	v_lshl_add_u64 v[10:11], v[10:11], 0, v[172:173]
	v_lshl_add_u64 v[10:11], v[10:11], 0, v[170:171]
	v_add_u32_e32 v2, 0xb0, v2
	v_ashrrev_i32_e32 v2, 4, v2
	v_fmamk_f32 v3, v240, 0x39800000, v194
	v_mul_f32_e32 v9, 0x4b800000, v3
	v_cmp_gt_f32_e32 vcc, s43, v3
	s_nop 1
	v_cndmask_b32_e32 v3, v3, v9, vcc
	v_rsq_f32_e32 v3, v3
	s_nop 0
	v_mul_f32_e32 v9, 0x45800000, v3
	v_cndmask_b32_e32 v3, v3, v9, vcc
	v_mul_f32_e32 v12, 0x3d000000, v3
	v_pk_mul_f32 v[16:17], v[62:63], v[12:13] op_sel_hi:[1,0]
	v_pk_mul_f32 v[20:21], v[58:59], v[12:13] op_sel_hi:[1,0]
	v_pk_mul_f32 v[14:15], v[64:65], v[12:13] op_sel_hi:[1,0]
	v_pk_mul_f32 v[18:19], v[60:61], v[12:13] op_sel_hi:[1,0]
	v_pk_mul_f32 v[22:23], v[56:57], v[12:13] op_sel_hi:[1,0]
	v_pk_mul_f32 v[24:25], v[54:55], v[12:13] op_sel_hi:[1,0]
	v_pk_mul_f32 v[26:27], v[52:53], v[12:13] op_sel_hi:[1,0]
	v_pk_mul_f32 v[12:13], v[50:51], v[12:13] op_sel_hi:[1,0]
	v_max_f32_e32 v3, 0, v16
	v_max_f32_e32 v9, 0, v20
	v_max_f32_e32 v16, 0, v17
	v_max_f32_e32 v17, 0, v21
	v_max_f32_e32 v20, 0, v24
	v_max_f32_e32 v12, 0, v12
	v_max_f32_e32 v21, 0, v25
	v_max_f32_e32 v13, 0, v13
	v_mul_f32_e32 v3, v3, v3
	v_mul_f32_e32 v9, v9, v9
	v_mul_f32_e32 v16, v16, v16
	v_mul_f32_e32 v17, v17, v17
	v_mul_f32_e32 v20, v20, v20
	v_mul_f32_e32 v12, v12, v12
	v_mul_f32_e32 v21, v21, v21
	v_mul_f32_e32 v13, v13, v13
	v_med3_f32 v3, v3, s44, v195
	v_med3_f32 v16, v16, s44, v195
	v_med3_f32 v9, v9, s44, v195
	v_med3_f32 v17, v17, s44, v195
	v_max_f32_e32 v14, 0, v14
	v_max_f32_e32 v18, 0, v18
	v_max_f32_e32 v15, 0, v15
	v_max_f32_e32 v19, 0, v19
	v_med3_f32 v20, v20, s44, v195
	v_med3_f32 v21, v21, s44, v195
	v_med3_f32 v12, v12, s44, v195
	v_cvt_pk_fp8_f32 v6, v3, v16
	v_cvt_pk_fp8_f32 v7, v9, v17
	v_med3_f32 v3, v13, s44, v195
	v_max_f32_e32 v22, 0, v22
	v_max_f32_e32 v24, 0, v26
	v_max_f32_e32 v23, 0, v23
	v_max_f32_e32 v25, 0, v27
	v_mul_f32_e32 v14, v14, v14
	v_mul_f32_e32 v18, v18, v18
	v_mul_f32_e32 v15, v15, v15
	v_mul_f32_e32 v19, v19, v19
	v_cvt_pk_fp8_f32 v8, v20, v21
	v_cvt_pk_fp8_f32 v9, v12, v3
	v_mul_f32_e32 v22, v22, v22
	v_mul_f32_e32 v24, v24, v24
	v_mul_f32_e32 v23, v23, v23
	v_mul_f32_e32 v25, v25, v25
	v_med3_f32 v14, v14, s44, v195
	v_med3_f32 v15, v15, s44, v195
	v_med3_f32 v18, v18, s44, v195
	v_med3_f32 v19, v19, s44, v195
	v_med3_f32 v22, v22, s44, v195
	v_med3_f32 v23, v23, s44, v195
	v_cvt_pk_fp8_f32 v6, v14, v15 op_sel:[0,0,1]
	v_cvt_pk_fp8_f32 v7, v18, v19 op_sel:[0,0,1]
	v_med3_f32 v3, v24, s44, v195
	v_med3_f32 v12, v25, s44, v195
	v_cvt_pk_fp8_f32 v8, v22, v23 op_sel:[0,0,1]
	v_cvt_pk_fp8_f32 v9, v3, v12 op_sel:[0,0,1]
	global_store_dwordx2 v[10:11], v[6:7], off
	global_store_dwordx2 v[10:11], v[8:9], off offset:2048
	v_ashrrev_i32_e32 v3, 31, v2
	v_lshlrev_b64 v[2:3], 18, v[2:3]
	v_lshl_add_u64 v[2:3], s[24:25], 0, v[2:3]
	v_lshl_add_u64 v[2:3], v[2:3], 0, s[20:21]
	v_lshl_add_u64 v[2:3], v[2:3], 0, v[172:173]
	v_lshl_add_u64 v[2:3], v[2:3], 0, v[170:171]
	v_fmamk_f32 v8, v241, 0x39800000, v194
	v_mul_f32_e32 v9, 0x4b800000, v8
	v_cmp_gt_f32_e32 vcc, s43, v8
	s_nop 1
	v_cndmask_b32_e32 v8, v8, v9, vcc
	v_rsq_f32_e32 v8, v8
	s_nop 0
	v_mul_f32_e32 v9, 0x45800000, v8
	v_cndmask_b32_e32 v8, v8, v9, vcc
	v_mul_f32_e32 v8, 0x3d000000, v8
	v_pk_mul_f32 v[12:13], v[46:47], v[8:9] op_sel_hi:[1,0]
	v_pk_mul_f32 v[16:17], v[42:43], v[8:9] op_sel_hi:[1,0]
	v_pk_mul_f32 v[10:11], v[48:49], v[8:9] op_sel_hi:[1,0]
	v_pk_mul_f32 v[14:15], v[44:45], v[8:9] op_sel_hi:[1,0]
	v_pk_mul_f32 v[18:19], v[40:41], v[8:9] op_sel_hi:[1,0]
	v_pk_mul_f32 v[20:21], v[38:39], v[8:9] op_sel_hi:[1,0]
	v_pk_mul_f32 v[22:23], v[36:37], v[8:9] op_sel_hi:[1,0]
	v_pk_mul_f32 v[8:9], v[34:35], v[8:9] op_sel_hi:[1,0]
	v_max_f32_e32 v12, 0, v12
	v_max_f32_e32 v16, 0, v16
	v_max_f32_e32 v13, 0, v13
	v_max_f32_e32 v17, 0, v17
	v_max_f32_e32 v20, 0, v20
	v_max_f32_e32 v8, 0, v8
	v_max_f32_e32 v21, 0, v21
	v_max_f32_e32 v9, 0, v9
	v_mul_f32_e32 v12, v12, v12
	v_mul_f32_e32 v16, v16, v16
	v_mul_f32_e32 v13, v13, v13
	v_mul_f32_e32 v17, v17, v17
	v_mul_f32_e32 v20, v20, v20
	v_mul_f32_e32 v8, v8, v8
	v_mul_f32_e32 v21, v21, v21
	v_mul_f32_e32 v9, v9, v9
	v_med3_f32 v12, v12, s44, v195
	v_med3_f32 v13, v13, s44, v195
	v_med3_f32 v16, v16, s44, v195
	v_med3_f32 v17, v17, s44, v195
	v_max_f32_e32 v10, 0, v10
	v_max_f32_e32 v14, 0, v14
	v_max_f32_e32 v11, 0, v11
	v_max_f32_e32 v15, 0, v15
	v_med3_f32 v20, v20, s44, v195
	v_med3_f32 v21, v21, s44, v195
	v_med3_f32 v8, v8, s44, v195
	v_cvt_pk_fp8_f32 v4, v12, v13
	v_cvt_pk_fp8_f32 v5, v16, v17
	v_med3_f32 v9, v9, s44, v195
	v_max_f32_e32 v18, 0, v18
	v_max_f32_e32 v22, 0, v22
	v_max_f32_e32 v19, 0, v19
	v_max_f32_e32 v23, 0, v23
	v_mul_f32_e32 v10, v10, v10
	v_mul_f32_e32 v14, v14, v14
	v_mul_f32_e32 v11, v11, v11
	v_mul_f32_e32 v15, v15, v15
	v_cvt_pk_fp8_f32 v6, v20, v21
	v_cvt_pk_fp8_f32 v7, v8, v9
	v_mul_f32_e32 v18, v18, v18
	v_mul_f32_e32 v22, v22, v22
	v_mul_f32_e32 v19, v19, v19
	v_mul_f32_e32 v23, v23, v23
	v_med3_f32 v10, v10, s44, v195
	v_med3_f32 v11, v11, s44, v195
	v_med3_f32 v14, v14, s44, v195
	v_med3_f32 v15, v15, s44, v195
	v_med3_f32 v18, v18, s44, v195
	v_med3_f32 v19, v19, s44, v195
	v_cvt_pk_fp8_f32 v4, v10, v11 op_sel:[0,0,1]
	v_cvt_pk_fp8_f32 v5, v14, v15 op_sel:[0,0,1]
	v_med3_f32 v8, v22, s44, v195
	v_med3_f32 v9, v23, s44, v195
	v_cvt_pk_fp8_f32 v6, v18, v19 op_sel:[0,0,1]
	v_cvt_pk_fp8_f32 v7, v8, v9 op_sel:[0,0,1]
	s_andn2_b64 vcc, exec, s[0:1]
	s_mov_b64 s[0:1], -1
	global_store_dwordx2 v[2:3], v[4:5], off
	global_store_dwordx2 v[2:3], v[6:7], off offset:2048
	s_cbranch_vccnz .LBB0_2273
	s_andn2_b64 vcc, exec, s[4:5]
	s_cbranch_vccnz .LBB0_2272
	s_barrier
	s_branch .LBB0_2272
